# stack: adaLN GEMV pipelining + LDS-DMA m0 save/restore removed + P8 LN params from LDS + attention queue index prefetch (3 queues/layer)
# speedup vs baseline: 1.0053x; 1.0001x over previous
; #define PG8_STAGE(bufoff, gbase, voff) do { _Pragma("unroll") for (int _i = 0; _i < 2; ++_i) { unsigned keep_; \
;         asm volatile("s_mov_b32 %0, m0\n\ts_mov_b32 m0, %3\n\ts_nop 0\n\tglobal_load_lds_dwordx4 %1, %2\n\ts_mov_b32 m0, %0" : "=&s"(keep_) : "v"((voff)[_i]), "s"((const char*)(gbase)), "s"(ldsb + (unsigned)((bufoff) + _i * 8192)) : "memory"); } } while (0)
; #define PG8_WAIT_V(n) asm volatile("s_waitcnt vmcnt(" #n ")" ::: "memory")
; #define PG8_BAR __builtin_amdgcn_s_barrier()
; template <class Epi, class Sched, bool ALIGN_EPI, bool FP8 = false>
; __device__ __forceinline__ void gemm_phase(PG8_LAS unsigned char* lds, const Gemm g, const Sched& S, const Epi& E, const int wid, const int lane) {
;     ...
;     for (int i = 0; i < 2; ++i) { int R, C; stage_rc(tid * 16 + i * 8192, R, C); const int Rb = Epi::PERM ? ((R & ~31) + perm32(R & 31)) : R;
;         rA[i] = R; cA2[i] = (unsigned)C * 2u; voffA[i] = (unsigned)(R * KB + C * 2); voffB[i] = (unsigned)(Rb * KB + C * 2); }
;     ...
;     const char* cA = GA ? (const char*)g.A : (const char*)g.A + (size_t)cur.pm * tstep; const char* cB = (const char*)g.Bt + (size_t)cur.pn * tstep;
;     PG8_STAGE(PG8_SB(0, 0), cB, voffB); PG8_STAGE(PG8_SB(0, 1), cB + hstep, voffB); PG8_STAGE(PG8_SA(0, 0), cA, vc0); PG8_STAGE(PG8_SA(0, 1), cA + hstepA, vc1);
;     if (wr == 1) PG8_BAR;
;     PG8_WAIT_V(2); PG8_BAR;
;     PG8_STAGE(PG8_SB(1, 0), cB + kstep, voffB); PG8_STAGE(PG8_SA(1, 0), cA + kstep, vc0); PG8_STAGE(PG8_SB(1, 1), cB + hstep + kstep, voffB);
;     PG8_WAIT_V(6); PG8_BAR;
.LBB0_211:
	v_lshlrev_b32_e32 v0, 4, v7
	v_add_u32_e32 v1, s10, v0
	v_ashrrev_i32_e32 v2, 31, v1
	v_lshrrev_b32_e32 v2, 22, v2
	v_add_u32_e32 v2, v1, v2
	v_ashrrev_i32_e32 v2, 10, v2
	v_mul_i32_i24_e32 v3, 0x400, v2
	v_sub_u32_e32 v3, v1, v3
	v_lshrrev_b32_e32 v4, 4, v3
	v_bitop3_b32 v3, v4, v3, 32 bitop3:0x6c
	v_ashrrev_i32_e32 v5, 31, v3
	v_lshrrev_b32_e32 v5, 26, v5
	v_lshlrev_b32_e32 v4, 3, v2
	v_add_u32_e32 v5, v3, v5
	v_and_b32_e32 v4, -16, v4
	v_ashrrev_i32_e32 v6, 6, v5
	v_and_b32_e32 v5, 0xc0, v5
	v_add_u32_e32 v4, v6, v4
	v_sub_u32_e32 v3, v3, v5
	v_mov_b32_e32 v5, 1
	v_lshlrev_b32_e32 v2, 5, v2
	v_ashrrev_i16_sdwa v3, v5, sext(v3) dst_sel:DWORD dst_unused:UNUSED_PAD src0_sel:DWORD src1_sel:BYTE_0
	v_lshlrev_b32_e32 v8, 1, v4
	v_lshrrev_b32_e32 v9, 2, v4
	v_and_b32_e32 v6, 3, v6
	s_movk_i32 s1, 0xffe0
	v_and_b32_e32 v2, 32, v2
	v_bfe_i32 v3, v3, 0, 16
	v_and_b32_e32 v8, 24, v8
	v_and_b32_e32 v9, 4, v9
	v_and_or_b32 v6, v4, s1, v6
	v_or3_b32 v6, v6, v9, v8
	v_add_lshl_u32 v2, v2, v3, 1
	v_add_u32_e32 v1, 0x2000, v1
	v_mad_u64_u32 v[132:133], s[4:5], s0, v4, v[2:3]
	v_mad_u64_u32 v[134:135], s[4:5], s0, v6, v[2:3]
	v_ashrrev_i32_e32 v2, 31, v1
	v_lshrrev_b32_e32 v2, 22, v2
	v_add_u32_e32 v2, v1, v2
	v_ashrrev_i32_e32 v2, 10, v2
	v_mul_i32_i24_e32 v3, 0x400, v2
	v_sub_u32_e32 v1, v1, v3
	v_lshrrev_b32_e32 v3, 4, v1
	v_bitop3_b32 v1, v3, v1, 32 bitop3:0x6c
	v_ashrrev_i32_e32 v4, 31, v1
	v_lshrrev_b32_e32 v4, 26, v4
	v_add_u32_e32 v4, v1, v4
	v_ashrrev_i32_e32 v6, 6, v4
	v_and_b32_e32 v4, 0xffc0, v4
	v_lshlrev_b32_e32 v3, 3, v2
	v_sub_u32_e32 v1, v1, v4
	v_and_b32_e32 v3, -16, v3
	v_lshrrev_b16_e32 v4, 7, v1
	v_add_u32_e32 v3, v6, v3
	v_and_b32_e32 v4, 1, v4
	v_and_b32_e32 v6, 3, v6
	v_add_u16_e32 v1, v1, v4
	v_and_or_b32 v6, v3, s1, v6
	s_ashr_i32 s1, s0, 31
	v_lshlrev_b32_e32 v2, 5, v2
	v_ashrrev_i16_sdwa v1, v5, sext(v1) dst_sel:DWORD dst_unused:UNUSED_PAD src0_sel:DWORD src1_sel:BYTE_0
	v_lshlrev_b32_e32 v4, 1, v3
	v_lshrrev_b32_e32 v5, 2, v3
	s_lshr_b32 s12, s90, 8
	s_lshl_b64 s[6:7], s[0:1], 7
	s_lshl_b64 s[8:9], s[0:1], 8
	s_add_i32 s34, s10, 0
	v_and_b32_e32 v2, 32, v2
	v_bfe_i32 v1, v1, 0, 16
	v_and_b32_e32 v4, 24, v4
	v_and_b32_e32 v5, 4, v5
	s_add_u32 s35, s56, 0x1000000
	v_or3_b32 v4, v6, v5, v4
	v_add_lshl_u32 v2, v2, v1, 1
	s_addc_u32 s36, s57, 0
	v_mad_u64_u32 v[136:137], s[4:5], s0, v3, v[2:3]
	v_mad_u64_u32 v[138:139], s[4:5], s0, v4, v[2:3]
	s_add_u32 s37, s56, 0x35c00000
	s_addc_u32 s38, s57, 0
	s_ashr_i32 s4, s83, 31
	s_mul_i32 s4, s8, s4
	s_mul_hi_u32 s5, s8, s83
	s_add_i32 s10, s5, s4
	s_lshr_b64 s[4:5], s[0:1], 24
	s_mul_i32 s5, s4, s83
	s_add_i32 s10, s10, s5
	s_ashr_i32 s5, s82, 31
	s_mul_i32 s5, s8, s5
	s_mul_hi_u32 s13, s8, s82
	s_add_i32 s5, s13, s5
	s_mul_i32 s4, s4, s82
	s_add_i32 s5, s5, s4
	s_mul_i32 s4, s8, s82
	s_add_u32 s26, s35, s4
	s_addc_u32 s27, s36, s5
	s_add_i32 s39, s34, 0x10000
	s_mov_b32 m0, s39
	s_nop 0
	global_load_lds_dwordx4 v134, s[26:27]
	s_add_i32 s40, s34, 0x12000
	s_mov_b32 m0, s40
	s_nop 0
	global_load_lds_dwordx4 v138, s[26:27]
	s_add_u32 s4, s26, s6
	s_mul_i32 s11, s8, s83
	s_addc_u32 s5, s27, s7
	s_add_i32 s41, s34, 0x14000
	s_mov_b32 m0, s41
	s_nop 0
	global_load_lds_dwordx4 v134, s[4:5]
	s_add_i32 s42, s34, 0x16000
	s_mov_b32 m0, s42
	s_nop 0
	global_load_lds_dwordx4 v138, s[4:5]
	s_add_u32 s28, s37, s11
	s_addc_u32 s29, s38, s10
	s_mov_b32 m0, s34
	s_nop 0
	global_load_lds_dwordx4 v132, s[28:29]
	s_add_i32 s43, s34, 0x2000
	s_mov_b32 m0, s43
	s_nop 0
	global_load_lds_dwordx4 v136, s[28:29]
	s_add_u32 s14, s28, s6
	s_addc_u32 s15, s29, s7
	s_add_i32 s44, s34, 0x4000
	s_mov_b32 m0, s44
	s_nop 0
	global_load_lds_dwordx4 v132, s[14:15]
	s_add_i32 s45, s34, 0x6000
	s_mov_b32 m0, s45
	s_nop 0
	global_load_lds_dwordx4 v136, s[14:15]
	s_cmp_eq_u32 s12, 1
	s_mov_b32 s3, 0
	s_cselect_b64 s[10:11], -1, 0
	s_cmp_lg_u32 s12, 1
	s_cbranch_scc1 .LBB0_213
	s_barrier
.LBB0_213:
	s_lshr_b32 s1, s1, 25
	s_bfe_u32 s13, s90, 0x20006
	s_add_i32 s1, s0, s1
	s_ashr_i32 s46, s1, 7
	s_lshl_b32 s47, s12, 6
	v_and_b32_e32 v0, 0xfffffc00, v0
	s_lshl_b32 s1, s13, 5
	v_lshl_add_u32 v3, s12, 13, v0
	s_add_u32 s12, s56, 0x45c00000
	v_lshl_add_u32 v0, s13, 12, v0
	s_addc_u32 s13, s57, 0
	s_ashr_i32 s48, s2, 31
	s_add_u32 s14, s26, 0x80
	s_waitcnt vmcnt(2)
	s_barrier
	s_addc_u32 s15, s27, 0
	s_add_i32 s49, s34, 0x18000
	s_mov_b32 m0, s49
	s_nop 0
	global_load_lds_dwordx4 v134, s[14:15]
	s_add_i32 s50, s34, 0x1a000
	s_mov_b32 m0, s50
	s_nop 0
	global_load_lds_dwordx4 v138, s[14:15]
	s_add_u32 s14, s28, 0x80
	s_addc_u32 s15, s29, 0
	s_add_i32 s51, s34, 0x8000
	s_mov_b32 m0, s51
	s_nop 0
	global_load_lds_dwordx4 v132, s[14:15]
	s_add_i32 s52, s34, 0xa000
	v_and_b32_e32 v133, 15, v7
	v_ashrrev_i32_e32 v4, 1, v7
	v_and_b32_e32 v1, 48, v7
	v_lshlrev_b32_e32 v5, 2, v7
	s_mov_b32 m0, s52
	s_nop 0
	global_load_lds_dwordx4 v136, s[14:15]
	s_add_u32 s4, s4, 0x80
	v_and_b32_e32 v2, -8, v4
	v_lshl_or_b32 v1, v133, 6, v1
	v_and_b32_e32 v5, 32, v5
	s_addc_u32 s5, s5, 0
	s_add_i32 s53, s34, 0x1c000
	s_mov_b32 m0, s53
	s_nop 0
	global_load_lds_dwordx4 v134, s[4:5]
	s_add_i32 s54, s34, 0x1e000
	v_bitop3_b32 v6, v1, v3, v5 bitop3:0xde
	s_mov_b32 m0, s54
	s_nop 0
	global_load_lds_dwordx4 v138, s[4:5]
	s_cmpk_gt_i32 s0, 0x7f
	v_add_u32_e32 v135, s1, v2
	v_ashrrev_i32_e32 v3, 31, v2
	v_bitop3_b32 v5, v1, v0, v5 bitop3:0xde
	s_waitcnt vmcnt(6)
	s_cselect_b64 s[14:15], -1, 0
	s_add_i32 s55, s46, -2
	s_add_i32 s64, s34, 0xc000
	v_add_u32_e32 v137, s1, v135
	v_lshl_add_u64 v[0:1], v[2:3], 2, s[56:57]
	s_mov_b64 s[0:1], 0x200000
	s_cmpk_lt_u32 s90, 0x100
	v_lshl_add_u64 v[140:141], v[0:1], 0, s[0:1]
	v_and_b32_e32 v0, 56, v4
	v_add_u32_e32 v1, 0, v5
	s_cselect_b64 s[16:17], -1, 0
	v_mov_b32_e32 v143, 0
	s_add_i32 s65, s34, 0xe000
	v_and_b32_e32 v144, 56, v135
	s_ashr_i32 s66, s76, 31
	v_mov_b64_e32 v[146:147], 0x600
	v_mov_b64_e32 v[148:149], 0x5ff
	s_movk_i32 s67, 0xc1
	v_add_u32_e32 v139, 0x10000, v1
	v_add_u32_e32 v164, 0x14000, v1
	v_add_u32_e32 v165, 0, v6
	v_add_u32_e32 v166, 0x18000, v1
	v_add_u32_e32 v167, 0x1c000, v1
	s_movk_i32 s68, 0x5ff
	s_mov_b32 s69, 0xaaaaaaab
	s_movk_i32 s70, 0x600
	s_movk_i32 s71, 0x300
	s_movk_i32 s72, 0x57f
	v_lshlrev_b32_e32 v150, 1, v0
	s_mov_b64 s[18:19], 0x1000
	s_movk_i32 s73, 0x1000
	s_mov_b64 s[20:21], 0x1800
	v_mov_b32_e32 v168, 0x3e38aa3b
	v_mov_b32_e32 v169, 0x600
	s_barrier
	s_branch .LBB0_216

; #define PG8_STAGE(bufoff, gbase, voff) do { _Pragma("unroll") for (int _i = 0; _i < 2; ++_i) { unsigned keep_; \
;         asm volatile("s_mov_b32 %0, m0\n\ts_mov_b32 m0, %3\n\ts_nop 0\n\tglobal_load_lds_dwordx4 %1, %2\n\ts_mov_b32 m0, %0" : "=&s"(keep_) : "v"((voff)[_i]), "s"((const char*)(gbase)), "s"(ldsb + (unsigned)((bufoff) + _i * 8192)) : "memory"); } } while (0)
; #define PG8_LDA(dst, b, h) do { _Pragma("unroll") for (int m = 0; m < 4; ++m) _Pragma("unroll") for (int k = 0; k < 2; ++k) dst[m][k] = *(const PG8_LAS bf16x8*)(lds + PG8_SA(b, h) + aoff + m * 2048 + k * 1024); } while (0)
; #define PG8_LDB(dst, b, h) do { _Pragma("unroll") for (int n = 0; n < 2; ++n) _Pragma("unroll") for (int k = 0; k < 2; ++k) dst[n][k] = *(const PG8_LAS bf16x8*)(lds + PG8_SB(b, h) + boff + n * 2048 + k * 1024); } while (0)
; #define PG8_WAIT_V(n) asm volatile("s_waitcnt vmcnt(" #n ")" ::: "memory")
; #define PG8_WAIT_L(n) asm volatile("s_waitcnt lgkmcnt(" #n ")" ::: "memory")
; #define PG8_BAR __builtin_amdgcn_s_barrier()
; #define PG8_SCHED __builtin_amdgcn_sched_barrier(0)
; template <class Epi, class Sched, bool ALIGN_EPI, bool FP8 = false>
; __device__ __forceinline__ void gemm_phase(PG8_LAS unsigned char* lds, const Gemm g, const Sched& S, const Epi& E, const int wid, const int lane) {
;     ...
;             PG8_LDB(B0, 0, 0); PG8_LDB(B1, 0, 1); PG8_SCHED; PG8_LDA(At, 0, 0); PG8_STAGE(PG8_SA(1, 1), a1 + hstepA, vc1);
;             if (GA && last && has_next) { const u32x4 q = *gslot; vc0[0] = q.x; vc0[1] = q.y; vc1[0] = q.z; vc1[1] = q.w; }
;             PG8_WAIT_V(8); PG8_WAIT_L(0); PG8_BAR; PG8_MMA(0, 0, At, B0); PG8_MMA(0, 1, At, B1); PG8_BAR; PG8_SCHED;
;             PG8_LDA(At, 0, 1); PG8_STAGE(PG8_SB(0, 0), b2, voffB); PG8_STAGE(PG8_SB(0, 1), b2 + hstep, voffB); PG8_STAGE(PG8_SA(0, 0), a2, vc0);
;             PG8_WAIT_V(8); PG8_WAIT_L(0); PG8_BAR; PG8_MMA(1, 0, At, B0); PG8_MMA(1, 1, At, B1); PG8_BAR; PG8_SCHED;
.LBB0_224:
	ds_read_b128 v[128:131], v139
	ds_read_b128 v[152:155], v139 offset:1024
	ds_read_b128 v[156:159], v139 offset:2048
	ds_read_b128 v[160:163], v139 offset:3072
	ds_read_b128 v[170:173], v164
	ds_read_b128 v[174:177], v164 offset:1024
	ds_read_b128 v[178:181], v164 offset:2048
	ds_read_b128 v[182:185], v164 offset:3072
	s_add_i32 s33, s26, 2
	s_cmp_eq_u32 s55, s26
	s_cselect_b32 s30, s22, s60
	s_cselect_b32 s31, s23, s61
	s_cselect_b32 s28, s24, s62
	s_cselect_b32 s29, s25, s63
	s_add_u32 s26, s30, 0x80
	s_addc_u32 s27, s31, 0
	ds_read_b128 v[186:189], v165
	ds_read_b128 v[190:193], v165 offset:1024
	ds_read_b128 v[194:197], v165 offset:2048
	ds_read_b128 v[198:201], v165 offset:3072
	ds_read_b128 v[202:205], v165 offset:4096
	ds_read_b128 v[206:209], v165 offset:5120
	ds_read_b128 v[210:213], v165 offset:6144
	ds_read_b128 v[218:221], v165 offset:7168
	s_mov_b32 m0, s64
	s_nop 0
	global_load_lds_dwordx4 v132, s[4:5]
	s_mov_b32 m0, s65
	s_nop 0
	global_load_lds_dwordx4 v136, s[4:5]
	s_waitcnt vmcnt(8)
	s_waitcnt lgkmcnt(0)
	s_barrier
	s_setprio 1
	s_waitcnt lgkmcnt(7)
	v_mfma_f32_16x16x32_bf16 v[124:127], v[128:131], v[186:189], v[124:127]
	v_mfma_f32_16x16x32_bf16 v[120:123], v[156:159], v[186:189], v[120:123]
	s_waitcnt lgkmcnt(5)
	v_mfma_f32_16x16x32_bf16 v[108:111], v[128:131], v[194:197], v[108:111]
	v_mfma_f32_16x16x32_bf16 v[104:107], v[156:159], v[194:197], v[104:107]
	s_waitcnt lgkmcnt(3)
	v_mfma_f32_16x16x32_bf16 v[92:95], v[128:131], v[202:205], v[92:95]
	v_mfma_f32_16x16x32_bf16 v[88:91], v[156:159], v[202:205], v[88:91]
	s_waitcnt lgkmcnt(1)
	v_mfma_f32_16x16x32_bf16 v[76:79], v[128:131], v[210:213], v[76:79]
	v_mfma_f32_16x16x32_bf16 v[72:75], v[156:159], v[210:213], v[72:75]
	v_mfma_f32_16x16x32_bf16 v[124:127], v[152:155], v[190:193], v[124:127]
	v_mfma_f32_16x16x32_bf16 v[120:123], v[160:163], v[190:193], v[120:123]
	v_mfma_f32_16x16x32_bf16 v[108:111], v[152:155], v[198:201], v[108:111]
	v_mfma_f32_16x16x32_bf16 v[104:107], v[160:163], v[198:201], v[104:107]
	v_mfma_f32_16x16x32_bf16 v[92:95], v[152:155], v[206:209], v[92:95]
	v_mfma_f32_16x16x32_bf16 v[88:91], v[160:163], v[206:209], v[88:91]
	s_waitcnt lgkmcnt(0)
	v_mfma_f32_16x16x32_bf16 v[76:79], v[152:155], v[218:221], v[76:79]
	v_mfma_f32_16x16x32_bf16 v[72:75], v[160:163], v[218:221], v[72:75]
	s_setprio 0
	s_setprio 1
	v_mfma_f32_16x16x32_bf16 v[116:119], v[170:173], v[186:189], v[116:119]
	v_mfma_f32_16x16x32_bf16 v[112:115], v[178:181], v[186:189], v[112:115]
	v_mfma_f32_16x16x32_bf16 v[100:103], v[170:173], v[194:197], v[100:103]
	v_mfma_f32_16x16x32_bf16 v[96:99], v[178:181], v[194:197], v[96:99]
	v_mfma_f32_16x16x32_bf16 v[84:87], v[170:173], v[202:205], v[84:87]
	v_mfma_f32_16x16x32_bf16 v[80:83], v[178:181], v[202:205], v[80:83]
	v_mfma_f32_16x16x32_bf16 v[68:71], v[170:173], v[210:213], v[68:71]
	v_mfma_f32_16x16x32_bf16 v[64:67], v[178:181], v[210:213], v[64:67]
	v_mfma_f32_16x16x32_bf16 v[116:119], v[174:177], v[190:193], v[116:119]
	v_mfma_f32_16x16x32_bf16 v[112:115], v[182:185], v[190:193], v[112:115]
	v_mfma_f32_16x16x32_bf16 v[100:103], v[174:177], v[198:201], v[100:103]
	v_mfma_f32_16x16x32_bf16 v[96:99], v[182:185], v[198:201], v[96:99]
	v_mfma_f32_16x16x32_bf16 v[84:87], v[174:177], v[206:209], v[84:87]
	v_mfma_f32_16x16x32_bf16 v[80:83], v[182:185], v[206:209], v[80:83]
	v_mfma_f32_16x16x32_bf16 v[68:71], v[174:177], v[218:221], v[68:71]
	v_mfma_f32_16x16x32_bf16 v[64:67], v[182:185], v[218:221], v[64:67]
	s_setprio 0
	s_barrier
	ds_read_b128 v[186:189], v165 offset:16384
	ds_read_b128 v[190:193], v165 offset:17408
	ds_read_b128 v[194:197], v165 offset:18432
	ds_read_b128 v[198:201], v165 offset:19456
	ds_read_b128 v[202:205], v165 offset:20480
	ds_read_b128 v[206:209], v165 offset:21504
	ds_read_b128 v[210:213], v165 offset:22528
	ds_read_b128 v[218:221], v165 offset:23552
	s_mov_b32 m0, s39
	s_nop 0
	global_load_lds_dwordx4 v134, s[28:29]
	s_mov_b32 m0, s40
	s_nop 0
	global_load_lds_dwordx4 v138, s[28:29]
	s_add_u32 s58, s28, s6
	s_addc_u32 s59, s29, s7
	s_mov_b32 m0, s41
	s_nop 0
	global_load_lds_dwordx4 v134, s[58:59]
	s_mov_b32 m0, s42
	s_nop 0
	global_load_lds_dwordx4 v138, s[58:59]
	s_mov_b32 m0, s34
	s_nop 0
	global_load_lds_dwordx4 v132, s[30:31]
	s_mov_b32 m0, s43
	s_nop 0
	global_load_lds_dwordx4 v136, s[30:31]
	s_waitcnt vmcnt(8)
	s_waitcnt lgkmcnt(0)
	s_barrier
	s_setprio 1
	s_waitcnt lgkmcnt(7)
	v_mfma_f32_16x16x32_bf16 v[60:63], v[128:131], v[186:189], v[60:63]
	v_mfma_f32_16x16x32_bf16 v[56:59], v[156:159], v[186:189], v[56:59]
	s_waitcnt lgkmcnt(5)
	v_mfma_f32_16x16x32_bf16 v[44:47], v[128:131], v[194:197], v[44:47]
	v_mfma_f32_16x16x32_bf16 v[40:43], v[156:159], v[194:197], v[40:43]
	s_waitcnt lgkmcnt(3)
	v_mfma_f32_16x16x32_bf16 v[28:31], v[128:131], v[202:205], v[28:31]
	v_mfma_f32_16x16x32_bf16 v[24:27], v[156:159], v[202:205], v[24:27]
	s_waitcnt lgkmcnt(1)
	v_mfma_f32_16x16x32_bf16 v[12:15], v[128:131], v[210:213], v[12:15]
	v_mfma_f32_16x16x32_bf16 v[8:11], v[156:159], v[210:213], v[8:11]
	v_mfma_f32_16x16x32_bf16 v[60:63], v[152:155], v[190:193], v[60:63]
	v_mfma_f32_16x16x32_bf16 v[56:59], v[160:163], v[190:193], v[56:59]
	v_mfma_f32_16x16x32_bf16 v[44:47], v[152:155], v[198:201], v[44:47]
	v_mfma_f32_16x16x32_bf16 v[40:43], v[160:163], v[198:201], v[40:43]
	v_mfma_f32_16x16x32_bf16 v[28:31], v[152:155], v[206:209], v[28:31]
	v_mfma_f32_16x16x32_bf16 v[24:27], v[160:163], v[206:209], v[24:27]
	s_waitcnt lgkmcnt(0)
	v_mfma_f32_16x16x32_bf16 v[12:15], v[152:155], v[218:221], v[12:15]
	v_mfma_f32_16x16x32_bf16 v[8:11], v[160:163], v[218:221], v[8:11]
	s_setprio 0
	s_setprio 1
	v_mfma_f32_16x16x32_bf16 v[52:55], v[170:173], v[186:189], v[52:55]
	v_mfma_f32_16x16x32_bf16 v[48:51], v[178:181], v[186:189], v[48:51]
	v_mfma_f32_16x16x32_bf16 v[36:39], v[170:173], v[194:197], v[36:39]
	v_mfma_f32_16x16x32_bf16 v[32:35], v[178:181], v[194:197], v[32:35]
	v_mfma_f32_16x16x32_bf16 v[20:23], v[170:173], v[202:205], v[20:23]
	v_mfma_f32_16x16x32_bf16 v[16:19], v[178:181], v[202:205], v[16:19]
	v_mfma_f32_16x16x32_bf16 v[4:7], v[170:173], v[210:213], v[4:7]
	v_mfma_f32_16x16x32_bf16 v[0:3], v[178:181], v[210:213], v[0:3]
	v_mfma_f32_16x16x32_bf16 v[52:55], v[174:177], v[190:193], v[52:55]
	v_mfma_f32_16x16x32_bf16 v[48:51], v[182:185], v[190:193], v[48:51]
	v_mfma_f32_16x16x32_bf16 v[36:39], v[174:177], v[198:201], v[36:39]
	v_mfma_f32_16x16x32_bf16 v[32:35], v[182:185], v[198:201], v[32:35]
	v_mfma_f32_16x16x32_bf16 v[20:23], v[174:177], v[206:209], v[20:23]
	v_mfma_f32_16x16x32_bf16 v[16:19], v[182:185], v[206:209], v[16:19]
	v_mfma_f32_16x16x32_bf16 v[4:7], v[174:177], v[218:221], v[4:7]
	v_mfma_f32_16x16x32_bf16 v[0:3], v[182:185], v[218:221], v[0:3]
	s_setprio 0
	s_barrier
; #define PG8_STAGE(bufoff, gbase, voff) do { _Pragma("unroll") for (int _i = 0; _i < 2; ++_i) { unsigned keep_; \
;         asm volatile("s_mov_b32 %0, m0\n\ts_mov_b32 m0, %3\n\ts_nop 0\n\tglobal_load_lds_dwordx4 %1, %2\n\ts_mov_b32 m0, %0" : "=&s"(keep_) : "v"((voff)[_i]), "s"((const char*)(gbase)), "s"(ldsb + (unsigned)((bufoff) + _i * 8192)) : "memory"); } } while (0)
; #define PG8_LDA(dst, b, h) do { _Pragma("unroll") for (int m = 0; m < 4; ++m) _Pragma("unroll") for (int k = 0; k < 2; ++k) dst[m][k] = *(const PG8_LAS bf16x8*)(lds + PG8_SA(b, h) + aoff + m * 2048 + k * 1024); } while (0)
; #define PG8_LDB(dst, b, h) do { _Pragma("unroll") for (int n = 0; n < 2; ++n) _Pragma("unroll") for (int k = 0; k < 2; ++k) dst[n][k] = *(const PG8_LAS bf16x8*)(lds + PG8_SB(b, h) + boff + n * 2048 + k * 1024); } while (0)
; #define PG8_WAIT_V(n) asm volatile("s_waitcnt vmcnt(" #n ")" ::: "memory")
; #define PG8_WAIT_L(n) asm volatile("s_waitcnt lgkmcnt(" #n ")" ::: "memory")
; #define PG8_BAR __builtin_amdgcn_s_barrier()
; #define PG8_SCHED __builtin_amdgcn_sched_barrier(0)
; template <class Epi, class Sched, bool ALIGN_EPI, bool FP8 = false>
; __device__ __forceinline__ void gemm_phase(PG8_LAS unsigned char* lds, const Gemm g, const Sched& S, const Epi& E, const int wid, const int lane) {
;     ...
;             PG8_LDB(B0, 1, 0); PG8_LDB(B1, 1, 1); PG8_SCHED; PG8_LDA(At, 1, 0); PG8_STAGE(PG8_SA(0, 1), a2 + hstepA, vc1);
;             PG8_WAIT_V(8); PG8_WAIT_L(0); PG8_BAR; PG8_MMA(0, 0, At, B0); PG8_MMA(0, 1, At, B1); PG8_BAR; PG8_SCHED;
;             PG8_LDA(At, 1, 1); PG8_STAGE(PG8_SB(1, 0), b3, voffB); PG8_STAGE(PG8_SB(1, 1), b3 + hstep, voffB); PG8_STAGE(PG8_SA(1, 0), a3, vc0);
;             PG8_WAIT_V(8); PG8_WAIT_L(0); PG8_BAR; PG8_MMA(1, 0, At, B0); PG8_MMA(1, 1, At, B1); PG8_BAR; PG8_SCHED;
	ds_read_b128 v[128:131], v166
	ds_read_b128 v[152:155], v166 offset:1024
	ds_read_b128 v[156:159], v166 offset:2048
	ds_read_b128 v[160:163], v166 offset:3072
	ds_read_b128 v[170:173], v167
	ds_read_b128 v[174:177], v167 offset:1024
	ds_read_b128 v[178:181], v167 offset:2048
	ds_read_b128 v[182:185], v167 offset:3072
	ds_read_b128 v[186:189], v165 offset:32768
	ds_read_b128 v[190:193], v165 offset:33792
	ds_read_b128 v[194:197], v165 offset:34816
	ds_read_b128 v[198:201], v165 offset:35840
	ds_read_b128 v[202:205], v165 offset:36864
	ds_read_b128 v[206:209], v165 offset:37888
	ds_read_b128 v[210:213], v165 offset:38912
	ds_read_b128 v[218:221], v165 offset:39936
	s_add_u32 s30, s30, s6
	s_addc_u32 s31, s31, s7
	s_mov_b32 m0, s44
	s_nop 0
	global_load_lds_dwordx4 v132, s[30:31]
	s_mov_b32 m0, s45
	s_nop 0
	global_load_lds_dwordx4 v136, s[30:31]
	s_waitcnt vmcnt(8)
	s_waitcnt lgkmcnt(0)
	s_barrier
	s_setprio 1
	s_waitcnt lgkmcnt(7)
	v_mfma_f32_16x16x32_bf16 v[124:127], v[128:131], v[186:189], v[124:127]
	v_mfma_f32_16x16x32_bf16 v[120:123], v[156:159], v[186:189], v[120:123]
	s_waitcnt lgkmcnt(5)
	v_mfma_f32_16x16x32_bf16 v[108:111], v[128:131], v[194:197], v[108:111]
	v_mfma_f32_16x16x32_bf16 v[104:107], v[156:159], v[194:197], v[104:107]
	s_waitcnt lgkmcnt(3)
	v_mfma_f32_16x16x32_bf16 v[92:95], v[128:131], v[202:205], v[92:95]
	v_mfma_f32_16x16x32_bf16 v[88:91], v[156:159], v[202:205], v[88:91]
	s_waitcnt lgkmcnt(1)
	v_mfma_f32_16x16x32_bf16 v[76:79], v[128:131], v[210:213], v[76:79]
	v_mfma_f32_16x16x32_bf16 v[72:75], v[156:159], v[210:213], v[72:75]
	v_mfma_f32_16x16x32_bf16 v[124:127], v[152:155], v[190:193], v[124:127]
	v_mfma_f32_16x16x32_bf16 v[120:123], v[160:163], v[190:193], v[120:123]
	v_mfma_f32_16x16x32_bf16 v[108:111], v[152:155], v[198:201], v[108:111]
	v_mfma_f32_16x16x32_bf16 v[104:107], v[160:163], v[198:201], v[104:107]
	v_mfma_f32_16x16x32_bf16 v[92:95], v[152:155], v[206:209], v[92:95]
	v_mfma_f32_16x16x32_bf16 v[88:91], v[160:163], v[206:209], v[88:91]
	s_waitcnt lgkmcnt(0)
	v_mfma_f32_16x16x32_bf16 v[76:79], v[152:155], v[218:221], v[76:79]
	v_mfma_f32_16x16x32_bf16 v[72:75], v[160:163], v[218:221], v[72:75]
	s_setprio 0
	s_setprio 1
	v_mfma_f32_16x16x32_bf16 v[116:119], v[170:173], v[186:189], v[116:119]
	v_mfma_f32_16x16x32_bf16 v[112:115], v[178:181], v[186:189], v[112:115]
	v_mfma_f32_16x16x32_bf16 v[100:103], v[170:173], v[194:197], v[100:103]
	v_mfma_f32_16x16x32_bf16 v[96:99], v[178:181], v[194:197], v[96:99]
	v_mfma_f32_16x16x32_bf16 v[84:87], v[170:173], v[202:205], v[84:87]
	v_mfma_f32_16x16x32_bf16 v[80:83], v[178:181], v[202:205], v[80:83]
	v_mfma_f32_16x16x32_bf16 v[68:71], v[170:173], v[210:213], v[68:71]
	v_mfma_f32_16x16x32_bf16 v[64:67], v[178:181], v[210:213], v[64:67]
	v_mfma_f32_16x16x32_bf16 v[116:119], v[174:177], v[190:193], v[116:119]
	v_mfma_f32_16x16x32_bf16 v[112:115], v[182:185], v[190:193], v[112:115]
	v_mfma_f32_16x16x32_bf16 v[100:103], v[174:177], v[198:201], v[100:103]
	v_mfma_f32_16x16x32_bf16 v[96:99], v[182:185], v[198:201], v[96:99]
	v_mfma_f32_16x16x32_bf16 v[84:87], v[174:177], v[206:209], v[84:87]
	v_mfma_f32_16x16x32_bf16 v[80:83], v[182:185], v[206:209], v[80:83]
	v_mfma_f32_16x16x32_bf16 v[68:71], v[174:177], v[218:221], v[68:71]
	v_mfma_f32_16x16x32_bf16 v[64:67], v[182:185], v[218:221], v[64:67]
	s_setprio 0
	s_barrier
	ds_read_b128 v[186:189], v165 offset:49152
	ds_read_b128 v[190:193], v165 offset:50176
	ds_read_b128 v[194:197], v165 offset:51200
	ds_read_b128 v[198:201], v165 offset:52224
	ds_read_b128 v[202:205], v165 offset:53248
	ds_read_b128 v[206:209], v165 offset:54272
	ds_read_b128 v[210:213], v165 offset:55296
	ds_read_b128 v[218:221], v165 offset:56320
	s_add_u32 s28, s28, 0x80
	s_addc_u32 s29, s29, 0
	s_mov_b32 m0, s49
	s_nop 0
	global_load_lds_dwordx4 v134, s[28:29]
	s_mov_b32 m0, s50
	s_nop 0
	global_load_lds_dwordx4 v138, s[28:29]
	s_add_u32 s28, s28, s6
	s_addc_u32 s29, s29, s7
	s_mov_b32 m0, s53
	s_nop 0
	global_load_lds_dwordx4 v134, s[28:29]
	s_mov_b32 m0, s54
	s_nop 0
	global_load_lds_dwordx4 v138, s[28:29]
	s_mov_b32 m0, s51
	s_nop 0
	global_load_lds_dwordx4 v132, s[26:27]
	s_mov_b32 m0, s52
	s_nop 0
	global_load_lds_dwordx4 v136, s[26:27]
	s_waitcnt vmcnt(8)
	s_waitcnt lgkmcnt(0)
	s_barrier
	s_setprio 1
	s_waitcnt lgkmcnt(7)
	v_mfma_f32_16x16x32_bf16 v[60:63], v[128:131], v[186:189], v[60:63]
	v_mfma_f32_16x16x32_bf16 v[56:59], v[156:159], v[186:189], v[56:59]
	s_waitcnt lgkmcnt(5)
	v_mfma_f32_16x16x32_bf16 v[44:47], v[128:131], v[194:197], v[44:47]
	v_mfma_f32_16x16x32_bf16 v[40:43], v[156:159], v[194:197], v[40:43]
	s_waitcnt lgkmcnt(3)
	v_mfma_f32_16x16x32_bf16 v[28:31], v[128:131], v[202:205], v[28:31]
	v_mfma_f32_16x16x32_bf16 v[24:27], v[156:159], v[202:205], v[24:27]
	s_waitcnt lgkmcnt(1)
	v_mfma_f32_16x16x32_bf16 v[12:15], v[128:131], v[210:213], v[12:15]
	v_mfma_f32_16x16x32_bf16 v[8:11], v[156:159], v[210:213], v[8:11]
	v_mfma_f32_16x16x32_bf16 v[60:63], v[152:155], v[190:193], v[60:63]
	v_mfma_f32_16x16x32_bf16 v[56:59], v[160:163], v[190:193], v[56:59]
	v_mfma_f32_16x16x32_bf16 v[44:47], v[152:155], v[198:201], v[44:47]
	v_mfma_f32_16x16x32_bf16 v[40:43], v[160:163], v[198:201], v[40:43]
	v_mfma_f32_16x16x32_bf16 v[28:31], v[152:155], v[206:209], v[28:31]
	v_mfma_f32_16x16x32_bf16 v[24:27], v[160:163], v[206:209], v[24:27]
	s_waitcnt lgkmcnt(0)
	v_mfma_f32_16x16x32_bf16 v[12:15], v[152:155], v[218:221], v[12:15]
	v_mfma_f32_16x16x32_bf16 v[8:11], v[160:163], v[218:221], v[8:11]
	s_setprio 0
	s_setprio 1
	v_mfma_f32_16x16x32_bf16 v[52:55], v[170:173], v[186:189], v[52:55]
	v_mfma_f32_16x16x32_bf16 v[48:51], v[178:181], v[186:189], v[48:51]
	v_mfma_f32_16x16x32_bf16 v[36:39], v[170:173], v[194:197], v[36:39]
	v_mfma_f32_16x16x32_bf16 v[32:35], v[178:181], v[194:197], v[32:35]
	v_mfma_f32_16x16x32_bf16 v[20:23], v[170:173], v[202:205], v[20:23]
	v_mfma_f32_16x16x32_bf16 v[16:19], v[178:181], v[202:205], v[16:19]
	v_mfma_f32_16x16x32_bf16 v[4:7], v[170:173], v[210:213], v[4:7]
	v_mfma_f32_16x16x32_bf16 v[0:3], v[178:181], v[210:213], v[0:3]
	v_mfma_f32_16x16x32_bf16 v[52:55], v[174:177], v[190:193], v[52:55]
	v_mfma_f32_16x16x32_bf16 v[48:51], v[182:185], v[190:193], v[48:51]
	v_mfma_f32_16x16x32_bf16 v[36:39], v[174:177], v[198:201], v[36:39]
	v_mfma_f32_16x16x32_bf16 v[32:35], v[182:185], v[198:201], v[32:35]
	v_mfma_f32_16x16x32_bf16 v[20:23], v[174:177], v[206:209], v[20:23]
	v_mfma_f32_16x16x32_bf16 v[16:19], v[182:185], v[206:209], v[16:19]
	v_mfma_f32_16x16x32_bf16 v[4:7], v[174:177], v[218:221], v[4:7]
	v_mfma_f32_16x16x32_bf16 v[0:3], v[182:185], v[218:221], v[0:3]
	s_setprio 0
	s_barrier
	s_add_u32 s60, s60, 0x100
	s_addc_u32 s61, s61, 0
	s_add_u32 s62, s62, 0x100
	s_addc_u32 s63, s63, 0
	s_add_u32 s4, s4, 0x100
	s_addc_u32 s5, s5, 0
	s_cmp_ge_i32 s33, s46
	s_mov_b32 s26, s33
	s_cbranch_scc0 .LBB0_224

; #define LAS __attribute__((address_space(3)))
; #define ATT_DEQ(ctrp, out) do { __syncthreads(); if (F.tid == 0) uslot[0] = __hip_atomic_fetch_add((ctrp), 1u, RLX_AGENT); __syncthreads(); (out) = (int)uslot[0] * 8 + qid; } while (0)
; template <int l>
; __device__ __forceinline__ void layer_phases(Frame& F, const XcdBarrier& bar, const int lo, const int hi) {
;     ...
;             const bf16* proj = (const bf16*)(ws + WS_PROJ); unsigned char* obuf = ws + WS_OBUF;
;             const float* gn = inptr<const float>(F, I_HNG) + (size_t)l * D;
;             LAS unsigned char* kvbuf = F.lds + RING_OFF; LAS float* ncum = (LAS float*)(F.lds + RING_OFF + 49152); att::lptr wl = F.lds + RING_OFF + 57344 + F.wave * 9216; LAS float* wsf = (LAS float*)(F.lds + WSF_OFF + F.wave * 256);
;             volatile LAS unsigned* uslot = (volatile LAS unsigned*)(F.lds + MISC_OFF + 64);
;             const int qid = blockIdx.x & 7;
;     ...
;             bf16* dstO = (bf16*)(ws + WS_DST_O); float* dstM = (float*)(ws + WS_DST_M);
;             if (rep == 0) { gu32* ctr = F.ctl + CW_AQ + ((l * 4 + 3) * 8 + qid) * 64;
;               for (;;) { int gi; ATT_DEQ(ctr, gi); if (gi >= 768) break;
;                   const int sl_ = gi >> 3, qb = sl_ / 12, bh = 12 * (gi & 7) + sl_ % 12;
;                   att::dil_a_unit(proj, dstO, dstM, F.ctl + CW_DA + ((l * 96 + bh) * 4 + (qb >> 1)) * 16, bh / 12, bh % 12, qb, wl, wsf, F.tid, F.wave); } }
.LBB0_352:
	s_cmp_gt_i32 s92, 3
	s_cselect_b64 s[0:1], -1, 0
	s_cmp_lt_i32 s93, 4
	s_cselect_b64 s[4:5], -1, 0
	s_or_b64 s[0:1], s[0:1], s[4:5]
	s_and_b64 vcc, exec, s[0:1]
	s_mul_i32 s0, s80, 0x2400
	v_writelane_b32 v248, s0, 9
	v_writelane_b32 v248, s78, 10
	v_writelane_b32 v248, s79, 11
	s_cbranch_vccnz .LBB0_525
	s_add_u32 s3, s56, 0x45c00000
	s_addc_u32 s83, s57, 0
	s_and_b32 s23, s2, 7
	s_add_u32 s64, s56, 0x6f400000
	s_addc_u32 s65, s57, 0
	s_add_i32 s0, 0, 0x21438
	v_mov_b32_e32 v132, v216
	v_mov_b32_e32 v0, s0
	v_readlane_b32 s0, v248, 0
	ds_read_b64 v[0:1], v0
	v_lshlrev_b32_e32 v2, 1, v132
	v_add_u32_e32 v124, s0, v132
	s_mul_i32 s0, s80, 0x2400
	v_and_b32_e32 v5, 4, v132
	s_add_i32 s22, s0, 0
	v_lshlrev_b32_e32 v6, 4, v124
	v_and_b32_e32 v127, 32, v2
	v_not_b32_e32 v2, 63
	v_cmp_eq_u32_e32 vcc, 0, v5
	v_bfe_u32 v144, v132, 2, 1
	v_bfe_u32 v125, v132, 5, 1
	v_cndmask_b32_e64 v141, v2, 64, vcc
	v_lshl_add_u32 v133, v144, 11, s22
	v_and_b32_e32 v2, 48, v6
	v_and_b32_e32 v128, 31, v132
	v_add_u32_e32 v155, v133, v2
	v_bitop3_b32 v2, v125, v132, 31 bitop3:0x78
	v_lshlrev_b32_e32 v157, 4, v2
	v_bitop3_b32 v2, v125, v128, 2 bitop3:0x36
	v_lshlrev_b32_e32 v159, 4, v2
	v_bitop3_b32 v2, v125, v128, 4 bitop3:0x36
	v_lshlrev_b32_e32 v161, 4, v2
	v_bitop3_b32 v2, v125, v128, 6 bitop3:0x36
	v_bfe_u32 v167, v132, 3, 3
	v_lshlrev_b32_e32 v163, 4, v2
	v_bitop3_b32 v2, v167, v132, 7 bitop3:0x78
	v_and_b32_e32 v143, 7, v132
	v_lshlrev_b32_e32 v168, 4, v2
	v_xor_b32_e32 v2, v167, v144
	v_lshlrev_b32_e32 v169, 6, v2
	v_bitop3_b32 v2, v167, v143, 8 bitop3:0x36
	v_lshlrev_b32_e32 v170, 4, v2
	v_bitop3_b32 v2, v167, v144, 8 bitop3:0x36
	v_lshlrev_b32_e32 v171, 6, v2
	v_bitop3_b32 v2, v167, v143, 16 bitop3:0x36
	s_lshl_b32 s0, s80, 8
	v_lshlrev_b32_e32 v172, 4, v2
	v_bitop3_b32 v2, v167, v144, 16 bitop3:0x36
	s_add_i32 s86, s0, 0
	v_lshlrev_b32_e32 v173, 6, v2
	v_bitop3_b32 v2, v167, v143, 24 bitop3:0x36
	s_lshl_b32 s24, s23, 6
	s_sub_i32 s84, 0x300, s23
	s_waitcnt lgkmcnt(0)
	v_readfirstlane_b32 s10, v0
	s_add_i32 s86, s86, 0x20000
	s_lshl_b32 s0, s23, 8
	v_and_b32_e32 v0, 63, v132
	v_lshlrev_b32_e32 v3, 3, v132
	v_lshlrev_b32_e32 v112, 4, v132
	v_and_b32_e32 v139, 0x70, v6
	s_movk_i32 s4, 0x380
	v_lshlrev_b32_e32 v174, 4, v2
	v_bitop3_b32 v2, v167, v144, 24 bitop3:0x36
	s_add_u32 s91, s56, s0
	v_lshlrev_b32_e32 v129, 2, v125
	v_bfe_u32 v126, v132, 2, 2
	v_and_or_b32 v114, v112, s4, v139
	v_and_b32_e32 v148, 24, v3
	v_cmp_gt_u32_e64 s[4:5], 32, v0
	v_lshlrev_b32_e32 v0, 2, v128
	v_lshlrev_b32_e32 v175, 6, v2
	v_mul_u32_u24_e32 v2, 0x440, v125
	s_addc_u32 s92, s57, 0
	v_or_b32_e32 v4, v129, v126
	v_add3_u32 v134, s22, v127, v148
	v_add_u32_e32 v165, s86, v0
	v_add3_u32 v179, s22, v2, v0
	v_lshlrev_b32_e32 v0, 5, v132
	s_add_u32 s8, s91, 0xd800
	v_lshl_add_u32 v164, v4, 6, v134
	v_and_b32_e32 v4, 32, v0
	v_readfirstlane_b32 s11, v1
	s_addc_u32 s9, s92, 0
	v_mov_b32_e32 v1, 0
	v_mov_b32_e32 v5, s22
	v_bfe_u32 v140, v132, 1, 5
	v_lshlrev_b32_e32 v0, 1, v4
	s_movk_i32 s6, 0x110
	v_or_b32_e32 v149, 2, v125
	v_or_b32_e32 v150, 4, v125
	v_or_b32_e32 v151, 6, v125
	s_add_u32 s87, s56, 0x14000
	v_lshl_add_u64 v[2:3], s[56:57], 0, v[0:1]
	s_mov_b64 s[12:13], 0x6dc00000
	v_mad_u32_u24 v176, v140, s6, v5
	s_mov_b32 s7, 0
	s_mul_i32 s85, s23, 12
	v_cmp_eq_u32_e64 s[0:1], 0, v124
	v_lshlrev_b32_e32 v138, 3, v125
	v_mov_b32_e32 v115, v1
	v_lshl_add_u32 v154, v143, 9, s22
	v_lshl_add_u32 v156, v125, 9, s22
	v_lshl_add_u32 v158, v149, 9, s22
	v_lshl_add_u32 v160, v150, 9, s22
	v_lshl_add_u32 v162, v151, 9, s22
	v_lshlrev_b32_e32 v166, 4, v125
	s_addc_u32 s88, s57, 0
	v_lshl_add_u64 v[130:131], v[2:3], 0, s[12:13]
	v_lshl_add_u32 v177, v4, 2, v176
	s_add_i32 s25, 0, 0x21540
	s_mov_b64 s[12:13], 0x7800000
	s_mov_b32 s26, 0x7800000
	s_movk_i32 s27, 0x81
	s_movk_i32 s28, 0xff7e
	s_movk_i32 s29, 0x7fff
	s_mov_b32 s30, 0xffff0000
	v_mov_b32_e32 v113, 0xff800000
	s_and_saveexec_b64 s[98:99], s[0:1]
	v_mov_b32_e32 v239, 0
	v_mov_b32_e32 v240, 1
	global_atomic_add v238, v239, v240, s[8:9] sc0
	s_mov_b64 exec, s[98:99]
	s_branch .LBB0_357

; #define ATT_DEQ(ctrp, out) do { __syncthreads(); if (F.tid == 0) uslot[0] = __hip_atomic_fetch_add((ctrp), 1u, RLX_AGENT); __syncthreads(); (out) = (int)uslot[0] * 8 + qid; } while (0)
; template <int l>
; __device__ __forceinline__ void layer_phases(Frame& F, const XcdBarrier& bar, const int lo, const int hi) {
;     ...
;             bf16* dstO = (bf16*)(ws + WS_DST_O); float* dstM = (float*)(ws + WS_DST_M);
;             if (rep == 0) { gu32* ctr = F.ctl + CW_AQ + ((l * 4 + 3) * 8 + qid) * 64;
;               for (;;) { int gi; ATT_DEQ(ctr, gi); if (gi >= 768) break;
.LBB0_357:
	s_barrier
	s_and_saveexec_b64 s[14:15], s[0:1]
	s_cbranch_execz .LBB0_361
	s_waitcnt vmcnt(0)
	v_mov_b32_e32 v2, s25
	ds_write_b32 v2, v238
	v_mov_b32_e32 v240, 1
	v_mov_b32_e32 v239, 0
	s_waitcnt lgkmcnt(0)
	global_atomic_add v238, v239, v240, s[8:9] sc0

; #define ATT_DEQ(ctrp, out) do { __syncthreads(); if (F.tid == 0) uslot[0] = __hip_atomic_fetch_add((ctrp), 1u, RLX_AGENT); __syncthreads(); (out) = (int)uslot[0] * 8 + qid; } while (0)
; template <int l>
; __device__ __forceinline__ void layer_phases(Frame& F, const XcdBarrier& bar, const int lo, const int hi) {
;     ...
;             if (ATT_ONLY < 0 || ATT_ONLY == 0) { gu32* ctr = F.ctl + CW_AQ + ((l * 4 + 0) * 8 + qid) * 64 + rep * 32;
;               for (;;) { int gi; ATT_DEQ(ctr, gi); if (gi >= 512) break;
;                   const int sl_ = gi >> 3, qb = 7 - sl_ / 8, bh = 8 * (gi & 7) + (sl_ & 7);
;                   att::sb_wave_unit(proj, gn, obuf, bh >> 3, bh & 7, 8 * qb + F.wave, wl, wsf, F.lane); } }
.LBB0_376:
	v_and_b32_e32 v1, 64, v216
	v_xor_b32_e32 v0, 1, v216
	v_add_u32_e32 v1, 64, v1
	v_cmp_lt_i32_e32 vcc, v0, v1
	s_lshl_b32 s6, s23, 22
	s_sub_i32 s20, 0x200, s23
	v_cndmask_b32_e32 v0, v216, v0, vcc
	v_lshlrev_b32_e32 v178, 2, v0
	s_add_u32 s89, s56, 0x51c00000
	v_ashrrev_i32_e32 v0, 5, v132
	s_addc_u32 s90, s57, 0
	s_lshl_b32 s12, s23, 20
	s_waitcnt vmcnt(1)
	v_lshlrev_b32_e32 v106, 2, v0
	s_add_u32 s21, s89, s6
	v_or_b32_e32 v1, v106, v126
	s_addc_u32 s23, s90, 0
	s_lshl_b32 s6, s24, 2
	v_lshl_add_u32 v107, v1, 6, v134
	v_ashrrev_i32_e32 v1, 3, v132
	s_add_u32 s6, s56, s6
	v_xor_b32_e32 v10, v1, v143
	v_xor_b32_e32 v11, v144, v1
	v_add_u32_e32 v12, 64, v132
	v_add_u32_e32 v14, 0x80, v132
	v_add_u32_e32 v16, 0xc0, v132
	v_and_b32_e32 v18, 0xffffffc, v1
	s_movk_i32 s16, 0x110
	v_or_b32_e32 v1, 3, v1
	s_addc_u32 s7, s57, 0
	v_lshlrev_b32_e32 v96, 3, v0
	v_lshl_add_u32 v3, v0, 9, s22
	v_xor_b32_e32 v4, v0, v128
	v_add_u32_e32 v5, 2, v0
	v_add_u32_e32 v7, 4, v0
	v_add_u32_e32 v0, 6, v0
	v_ashrrev_i32_e32 v12, 3, v12
	v_ashrrev_i32_e32 v14, 3, v14
	v_ashrrev_i32_e32 v16, 3, v16
	v_mul_lo_u32 v18, v18, s16
	v_lshlrev_b32_e32 v105, 2, v128
	v_mul_lo_u32 v1, v1, s16
	s_waitcnt vmcnt(0)
	v_ashrrev_i32_e32 v110, 1, v132
	s_add_u32 s14, s6, 0xc000
	v_mov_b32_e32 v113, 0
	v_and_b32_e32 v104, 48, v112
	v_lshl_add_u32 v6, v5, 9, s22
	v_xor_b32_e32 v5, v5, v128
	v_lshl_add_u32 v8, v7, 9, s22
	v_xor_b32_e32 v7, v7, v128
	v_lshl_add_u32 v9, v0, 9, s22
	v_xor_b32_e32 v0, v0, v128
	v_xor_b32_e32 v13, v12, v143
	v_xor_b32_e32 v12, v12, v144
	v_xor_b32_e32 v15, v14, v143
	v_xor_b32_e32 v14, v14, v144
	v_xor_b32_e32 v17, v16, v143
	v_xor_b32_e32 v16, v16, v144
	v_add3_u32 v108, s22, v18, v105
	v_add3_u32 v109, s22, v1, v105
	v_and_b32_e32 v1, 1, v132
	v_mul_lo_u32 v18, v110, s16
	s_addc_u32 s15, s7, 0
	v_add_u32_e32 v2, v133, v104
	v_lshlrev_b32_e32 v4, 4, v4
	v_lshlrev_b32_e32 v5, 4, v5
	v_lshlrev_b32_e32 v7, 4, v7
	v_lshlrev_b32_e32 v0, 4, v0
	v_cmp_gt_u32_e64 s[6:7], 32, v132
	v_lshlrev_b32_e32 v10, 4, v10
	v_lshlrev_b32_e32 v11, 6, v11
	v_lshlrev_b32_e32 v13, 4, v13
	v_lshlrev_b32_e32 v12, 6, v12
	v_lshlrev_b32_e32 v15, 4, v15
	v_lshlrev_b32_e32 v14, 6, v14
	v_lshlrev_b32_e32 v17, 4, v17
	v_lshlrev_b32_e32 v16, 6, v16
	v_add_u32_e32 v18, s22, v18
	v_lshlrev_b32_e32 v132, 7, v1
	v_mov_b32_e32 v133, v113
	s_lshl_b32 s25, s80, 5
	s_mov_b32 s13, 0
	s_add_i32 s24, s80, 56
	v_ashrrev_i32_e32 v97, 31, v96
	v_cmp_lt_i32_e64 s[8:9], v106, v128
	v_lshl_add_u32 v111, v110, 2, s86
	v_lshlrev_b32_e32 v134, 5, v1
	v_mov_b32_e32 v135, v113
	v_lshl_add_u64 v[136:137], s[10:11], 0, v[132:133]
	s_addk_i32 s25, 0x6c0
	s_add_i32 s26, 0, 0x21540
	s_lshl_b32 s27, s12, 1
	s_mov_b32 s28, 0xda24260
	v_mov_b32_e32 v114, 1.0
	v_add_u32_e32 v115, v18, v132
	v_mov_b32_e32 v116, 0x358637bd
	s_mov_b32 s29, 0xf800000
	v_mov_b32_e32 v117, 0x260
	v_add_u32_e32 v118, v154, v10
	v_add_u32_e32 v119, v2, v11
	v_add_u32_e32 v120, v154, v13
	v_add_u32_e32 v121, v2, v12
	v_add_u32_e32 v122, v154, v15
	v_add_u32_e32 v123, v2, v14
	v_add_u32_e32 v133, v154, v17
	v_add_u32_e32 v142, v2, v16
	v_add_u32_e32 v145, v3, v4
	v_add_u32_e32 v146, v6, v5
	v_add_u32_e32 v147, v8, v7
	v_add_u32_e32 v152, v9, v0
	s_and_saveexec_b64 s[98:99], s[0:1]
	v_mov_b32_e32 v239, 0
	v_mov_b32_e32 v240, 1
	global_atomic_add v238, v239, v240, s[14:15] sc0
	s_mov_b64 exec, s[98:99]
	s_branch .LBB0_379

; #define ATT_DEQ(ctrp, out) do { __syncthreads(); if (F.tid == 0) uslot[0] = __hip_atomic_fetch_add((ctrp), 1u, RLX_AGENT); __syncthreads(); (out) = (int)uslot[0] * 8 + qid; } while (0)
; template <int l>
; __device__ __forceinline__ void layer_phases(Frame& F, const XcdBarrier& bar, const int lo, const int hi) {
;     ...
;             if (ATT_ONLY < 0 || ATT_ONLY == 0) { gu32* ctr = F.ctl + CW_AQ + ((l * 4 + 0) * 8 + qid) * 64 + rep * 32;
;               for (;;) { int gi; ATT_DEQ(ctr, gi); if (gi >= 512) break;
;                   const int sl_ = gi >> 3, qb = 7 - sl_ / 8, bh = 8 * (gi & 7) + (sl_ & 7);
.LBB0_379:
	s_barrier
	s_and_saveexec_b64 s[10:11], s[0:1]
	s_cbranch_execz .LBB0_383
	s_waitcnt vmcnt(0)
	v_mov_b32_e32 v1, s26
	ds_write_b32 v1, v238
	v_mov_b32_e32 v240, 1
	v_mov_b32_e32 v239, 0
	s_waitcnt lgkmcnt(0)
	global_atomic_add v238, v239, v240, s[14:15] sc0

; #define ATT_DEQ(ctrp, out) do { __syncthreads(); if (F.tid == 0) uslot[0] = __hip_atomic_fetch_add((ctrp), 1u, RLX_AGENT); __syncthreads(); (out) = (int)uslot[0] * 8 + qid; } while (0)
; template <int l>
; __device__ __forceinline__ void layer_phases(Frame& F, const XcdBarrier& bar, const int lo, const int hi) {
;     ...
;             if (ATT_ONLY < 0 || ATT_ONLY == 1) { gu32* ctr = F.ctl + CW_AQ + ((l * 4 + 1) * 8 + qid) * 64 + rep * 32;
;               for (;;) { int gi; ATT_DEQ(ctr, gi); if (gi >= 768) break;
;                   const int sl_ = gi >> 3, qb = 7 - sl_ / 12, bh = 12 * (gi & 7) + sl_ % 12;
;                   att::causal_wg_unit<1>(proj, (const float*)(ws + WS_CUM) + (size_t)bh * SEQ, gn, obuf, bh / 12, bh % 12, qb, kvbuf, ncum, wl, wsf, F.tid, F.wave); } }
.LBB0_396:
	v_ashrrev_i32_e32 v0, 3, v124
	v_lshlrev_b32_e32 v1, 4, v143
	v_and_b32_e32 v6, 4, v167
	v_lshl_or_b32 v142, v0, 7, v1
	v_lshlrev_b32_e32 v1, 10, v143
	v_xor_b32_e32 v2, v0, v143
	v_mul_u32_u24_e32 v6, 0x110, v6
	v_lshl_add_u32 v181, v2, 4, v1
	v_lshlrev_b32_e32 v2, 12, v144
	v_xor_b32_e32 v0, v144, v0
	v_lshlrev_b32_e32 v144, 2, v124
	v_add3_u32 v133, s22, v6, v105
	v_or_b32_e32 v6, 3, v167
	v_ashrrev_i32_e32 v145, 31, v144
	v_mul_u32_u24_e32 v6, 0x110, v6
	v_lshlrev_b32_e32 v3, 6, v0
	v_lshl_add_u64 v[0:1], v[144:145], 2, s[56:57]
	v_add3_u32 v145, s22, v6, v105
	v_lshlrev_b32_e32 v6, 8, v125
	v_or_b32_e32 v4, v104, v2
	s_mov_b64 s[6:7], 0x700000
	v_add_u32_e32 v7, v141, v6
	v_lshlrev_b32_e32 v8, 6, v126
	v_add_u32_e32 v2, v2, v3
	s_add_u32 s66, s91, 0xc800
	v_lshl_add_u64 v[146:147], v[0:1], 0, s[6:7]
	v_mov_b32_e32 v97, 0
	v_add_u32_e32 v0, v4, v3
	v_lshl_add_u32 v1, v149, 10, 0
	v_lshl_add_u32 v4, v150, 10, 0
	v_lshl_add_u32 v5, v151, 10, 0
	v_add3_u32 v7, v7, v8, v127
	v_or3_b32 v6, v6, v8, v127
	v_or_b32_e32 v2, v2, v104
	s_addc_u32 s67, s92, 0
	s_mov_b32 s41, 0
	v_lshl_add_u32 v182, v124, 4, 0
	v_mov_b32_e32 v143, v97
	v_add_u32_e32 v183, 0, v105
	v_lshl_add_u32 v184, v125, 10, 0
	v_lshl_add_u32 v180, v140, 2, s86
	v_add_u32_e32 v185, 0x3e00, v7
	v_add_u32_e32 v186, 0, v148
	v_add_u32_e32 v187, 0x3c00, v7
	v_add_u32_e32 v188, 0x3a00, v7
	v_add_u32_e32 v189, 0x3800, v7
	v_add_u32_e32 v190, 0x3600, v7
	v_add_u32_e32 v191, 0x3400, v7
	v_add_u32_e32 v192, 0x3200, v7
	v_add_u32_e32 v193, 0x3000, v7
	v_or_b32_e32 v194, 0x2e00, v6
	v_or_b32_e32 v195, 0x2c00, v6
	v_or_b32_e32 v196, 0x2a00, v6
	v_or_b32_e32 v197, 0x2800, v6
	v_or_b32_e32 v198, 0x2600, v6
	v_or_b32_e32 v199, 0x2400, v6
	v_or_b32_e32 v200, 0x2200, v6
	v_or_b32_e32 v201, 0x2000, v6
	v_or_b32_e32 v202, 0xc100, v105
	v_add_u32_e32 v203, 0xa000, v2
	v_add_u32_e32 v204, 0x8000, v181
	s_add_i32 s93, 0, 0x21540
	s_mov_b64 s[68:69], 0x3000000
	s_movk_i32 s94, 0x7fff
	s_mov_b32 s95, 0xffff0000
	s_mov_b64 s[70:71], 0x4800000
	s_mov_b64 s[72:73], 0x6000000
	v_add_u32_e32 v205, 0, v0
	v_add_u32_e32 v206, v1, v159
	v_add_u32_e32 v207, v4, v161
	v_add_u32_e32 v208, v5, v163
	s_mov_b32 s96, 0xff800000
	v_mov_b32_e32 v209, 0x358637bd
	s_mov_b32 s97, 0xf800000
	v_mov_b32_e32 v210, 0x260
	v_mov_b32_e32 v211, 1
	v_mov_b32_e32 v212, 0xff800000
	s_and_saveexec_b64 s[98:99], s[0:1]
	v_mov_b32_e32 v239, 0
	v_mov_b32_e32 v240, 1
	global_atomic_add v238, v239, v240, s[66:67] sc0
	s_mov_b64 exec, s[98:99]
	s_branch .LBB0_399

; #define ATT_DEQ(ctrp, out) do { __syncthreads(); if (F.tid == 0) uslot[0] = __hip_atomic_fetch_add((ctrp), 1u, RLX_AGENT); __syncthreads(); (out) = (int)uslot[0] * 8 + qid; } while (0)
; template <int l>
; __device__ __forceinline__ void layer_phases(Frame& F, const XcdBarrier& bar, const int lo, const int hi) {
;     ...
;             if (ATT_ONLY < 0 || ATT_ONLY == 1) { gu32* ctr = F.ctl + CW_AQ + ((l * 4 + 1) * 8 + qid) * 64 + rep * 32;
;               for (;;) { int gi; ATT_DEQ(ctr, gi); if (gi >= 768) break;
;                   const int sl_ = gi >> 3, qb = 7 - sl_ / 12, bh = 12 * (gi & 7) + sl_ % 12;
.LBB0_399:
	s_barrier
	s_and_saveexec_b64 s[6:7], s[0:1]
	s_cbranch_execz .LBB0_403
	s_waitcnt vmcnt(0)
	v_mov_b32_e32 v1, s93
	ds_write_b32 v1, v238
	v_mov_b32_e32 v240, 1
	v_mov_b32_e32 v239, 0
	s_waitcnt lgkmcnt(0)
	global_atomic_add v238, v239, v240, s[66:67] sc0

; #define PG8_STAGE(bufoff, gbase, voff) do { _Pragma("unroll") for (int _i = 0; _i < 2; ++_i) { unsigned keep_; \
;         asm volatile("s_mov_b32 %0, m0\n\ts_mov_b32 m0, %3\n\ts_nop 0\n\tglobal_load_lds_dwordx4 %1, %2\n\ts_mov_b32 m0, %0" : "=&s"(keep_) : "v"((voff)[_i]), "s"((const char*)(gbase)), "s"(ldsb + (unsigned)((bufoff) + _i * 8192)) : "memory"); } } while (0)
; #define PG8_WAIT_V(n) asm volatile("s_waitcnt vmcnt(" #n ")" ::: "memory")
; #define PG8_BAR __builtin_amdgcn_s_barrier()
; template <class Epi, class Sched, bool ALIGN_EPI, bool FP8 = false>
; __device__ __forceinline__ void gemm_phase(PG8_LAS unsigned char* lds, const Gemm g, const Sched& S, const Epi& E, const int wid, const int lane) {
;     ...
;     for (int i = 0; i < 2; ++i) { int R, C; stage_rc(tid * 16 + i * 8192, R, C); const int Rb = Epi::PERM ? ((R & ~31) + perm32(R & 31)) : R;
;         rA[i] = R; cA2[i] = (unsigned)C * 2u; voffA[i] = (unsigned)(R * KB + C * 2); voffB[i] = (unsigned)(Rb * KB + C * 2); }
;     ...
;     const char* cA = GA ? (const char*)g.A : (const char*)g.A + (size_t)cur.pm * tstep; const char* cB = (const char*)g.Bt + (size_t)cur.pn * tstep;
;     PG8_STAGE(PG8_SB(0, 0), cB, voffB); PG8_STAGE(PG8_SB(0, 1), cB + hstep, voffB); PG8_STAGE(PG8_SA(0, 0), cA, vc0); PG8_STAGE(PG8_SA(0, 1), cA + hstepA, vc1);
;     if (wr == 1) PG8_BAR;
;     PG8_WAIT_V(2); PG8_BAR;
;     PG8_STAGE(PG8_SB(1, 0), cB + kstep, voffB); PG8_STAGE(PG8_SA(1, 0), cA + kstep, vc0); PG8_STAGE(PG8_SB(1, 1), cB + hstep + kstep, voffB);
;     PG8_WAIT_V(6); PG8_BAR;
.LBB0_525:
	s_cmp_gt_i32 s92, 4
	s_cselect_b64 s[0:1], -1, 0
	s_cmp_lt_i32 s93, 5
	s_cselect_b64 s[4:5], -1, 0
	s_or_b64 s[0:1], s[0:1], s[4:5]
	s_and_b64 vcc, exec, s[0:1]
	s_cbranch_vccnz .LBB0_605
	s_lshl_b32 s4, s80, 10
	s_cmpk_gt_i32 s2, 0x1ff
	v_mov_b32_e32 v172, v216
	s_movk_i32 s0, 0x800
	s_cbranch_scc1 .LBB0_551
	v_lshl_add_u32 v1, v172, 4, s4
	v_ashrrev_i32_e32 v0, 31, v1
	v_lshrrev_b32_e32 v0, 22, v0
	v_add_u32_e32 v0, v1, v0
	v_ashrrev_i32_e32 v0, 10, v0
	v_mul_i32_i24_e32 v2, 0x400, v0
	v_sub_u32_e32 v2, v1, v2
	v_lshrrev_b32_e32 v3, 4, v2
	v_bitop3_b32 v2, v3, v2, 32 bitop3:0x6c
	v_ashrrev_i32_e32 v4, 31, v2
	v_lshrrev_b32_e32 v4, 26, v4
	v_lshlrev_b32_e32 v3, 3, v0
	v_add_u32_e32 v4, v2, v4
	v_and_b32_e32 v3, -16, v3
	v_ashrrev_i32_e32 v5, 6, v4
	v_and_b32_e32 v4, 0xc0, v4
	v_add_u32_e32 v3, v5, v3
	v_sub_u32_e32 v2, v2, v4
	v_mov_b32_e32 v4, 1
	v_lshlrev_b32_e32 v0, 5, v0
	v_ashrrev_i16_sdwa v2, v4, sext(v2) dst_sel:DWORD dst_unused:UNUSED_PAD src0_sel:DWORD src1_sel:BYTE_0
	v_lshlrev_b32_e32 v6, 1, v3
	v_lshrrev_b32_e32 v7, 2, v3
	v_and_b32_e32 v5, 3, v5
	s_movk_i32 s1, 0xffe0
	v_and_b32_e32 v0, 32, v0
	v_bfe_i32 v2, v2, 0, 16
	v_and_b32_e32 v6, 24, v6
	v_and_b32_e32 v7, 4, v7
	v_and_or_b32 v5, v3, s1, v5
	v_or3_b32 v5, v5, v7, v6
	v_add_lshl_u32 v0, v0, v2, 1
	v_mad_u64_u32 v[160:161], s[6:7], v3, s0, v[0:1]
	v_mad_u64_u32 v[162:163], s[6:7], v5, s0, v[0:1]
	v_add_u32_e32 v0, 0x2000, v1
	v_ashrrev_i32_e32 v1, 31, v0
	v_lshrrev_b32_e32 v1, 22, v1
	v_add_u32_e32 v1, v0, v1
	v_ashrrev_i32_e32 v1, 10, v1
	v_mul_i32_i24_e32 v2, 0x400, v1
	v_sub_u32_e32 v0, v0, v2
	v_lshrrev_b32_e32 v2, 4, v0
	v_bitop3_b32 v0, v2, v0, 32 bitop3:0x6c
	v_ashrrev_i32_e32 v3, 31, v0
	v_lshrrev_b32_e32 v3, 26, v3
	v_add_u32_e32 v3, v0, v3
	v_ashrrev_i32_e32 v5, 6, v3
	v_and_b32_e32 v3, 0xffc0, v3
	s_add_u32 s3, s56, 0x51c00000
	v_sub_u32_e32 v0, v0, v3
	s_addc_u32 s38, s57, 0
	v_lshlrev_b32_e32 v2, 3, v1
	v_lshrrev_b16_e32 v3, 7, v0
	s_add_u32 s39, s56, 0x2800000
	v_and_b32_e32 v2, -16, v2
	v_and_b32_e32 v3, 1, v3
	s_addc_u32 s40, s57, 0
	v_add_u32_e32 v2, v5, v2
	v_add_u16_e32 v0, v0, v3
	s_ashr_i32 s43, s2, 31
	v_lshlrev_b32_e32 v1, 5, v1
	v_ashrrev_i16_sdwa v0, v4, sext(v0) dst_sel:DWORD dst_unused:UNUSED_PAD src0_sel:DWORD src1_sel:BYTE_0
	v_lshlrev_b32_e32 v3, 1, v2
	v_lshrrev_b32_e32 v4, 2, v2
	v_and_b32_e32 v5, 3, v5
	s_add_i32 s42, s4, 0
	s_lshr_b32 s4, s43, 29
	v_and_b32_e32 v1, 32, v1
	v_bfe_i32 v0, v0, 0, 16
	v_and_b32_e32 v3, 24, v3
	v_and_b32_e32 v4, 4, v4
	v_and_or_b32 v5, v2, s1, v5
	s_add_i32 s4, s2, s4
	v_or3_b32 v3, v5, v4, v3
	v_add_lshl_u32 v0, v1, v0, 1
	s_and_b32 s5, s4, -8
	v_mad_u64_u32 v[164:165], s[6:7], v2, s0, v[0:1]
	v_mad_u64_u32 v[166:167], s[6:7], v3, s0, v[0:1]
	s_ashr_i32 s1, s0, 31
	s_sub_i32 s5, s2, s5
	s_lshr_b32 s14, s90, 8
	s_lshl_b64 s[6:7], s[0:1], 7
	s_lshl_b64 s[8:9], s[0:1], 8
	s_lshl_b32 s11, s5, 6
	s_ashr_i32 s4, s4, 3
	s_mul_i32 s10, s5, 0x41
	s_cmp_lt_i32 s5, 0
	s_cselect_b32 s5, s10, s11
	s_add_i32 s4, s5, s4
	s_ashr_i32 s5, s4, 31
	s_lshr_b32 s5, s5, 26
	s_add_i32 s5, s4, s5
	s_ashr_i32 s10, s5, 6
	s_andn2_b32 s5, s5, 63
	s_sub_i32 s4, s4, s5
	s_bfe_i32 s5, s4, 0x80000
	s_bfe_u32 s5, s5, 0x3000c
	s_add_i32 s5, s4, s5
	s_bfe_i32 s11, s5, 0x80000
	s_and_b32 s5, s5, 0xf8
	s_sub_i32 s4, s4, s5
	s_lshl_b32 s10, s10, 3
	s_sext_i32_i8 s4, s4
	s_add_i32 s83, s10, s4
	s_ashr_i32 s4, s83, 31
	s_mul_i32 s4, s8, s4
	s_mul_hi_u32 s5, s8, s83
	s_sext_i32_i16 s13, s11
	s_add_i32 s10, s5, s4
	s_lshr_b64 s[4:5], s[0:1], 24
	s_lshr_b32 s12, s13, 3
	s_mul_i32 s5, s4, s83
	s_add_i32 s15, s10, s5
	s_bfe_i64 s[10:11], s[12:13], 0x100000
	s_ashr_i32 s5, s13, 3
	s_mul_hi_u32 s10, s8, s5
	s_mul_i32 s11, s8, s11
	s_add_i32 s10, s10, s11
	s_mul_i32 s4, s4, s5
	s_add_i32 s10, s10, s4
	s_mul_i32 s4, s8, s5
	s_add_u32 s28, s39, s4
	s_addc_u32 s29, s40, s10
	s_add_i32 s44, s42, 0x10000
	s_mov_b32 m0, s44
	s_nop 0
	global_load_lds_dwordx4 v162, s[28:29]
	s_add_i32 s45, s42, 0x12000
	s_mov_b32 m0, s45
	s_nop 0
	global_load_lds_dwordx4 v166, s[28:29]
	s_add_u32 s4, s28, s6
	s_mul_i32 s16, s8, s83
	s_addc_u32 s5, s29, s7
	s_add_i32 s46, s42, 0x14000
	s_mov_b32 m0, s46
	s_nop 0
	global_load_lds_dwordx4 v162, s[4:5]
	s_add_i32 s47, s42, 0x16000
	s_mov_b32 m0, s47
	s_nop 0
	global_load_lds_dwordx4 v166, s[4:5]
	s_add_u32 s30, s3, s16
	s_addc_u32 s31, s38, s15
	s_mov_b32 m0, s42
	s_nop 0
	global_load_lds_dwordx4 v160, s[30:31]
	s_add_i32 s48, s42, 0x2000
	s_mov_b32 m0, s48
	s_nop 0
	global_load_lds_dwordx4 v164, s[30:31]
	s_add_u32 s16, s30, s6
	s_addc_u32 s17, s31, s7
	s_add_i32 s49, s42, 0x4000
	s_mov_b32 m0, s49
	s_nop 0
	global_load_lds_dwordx4 v160, s[16:17]
	s_add_i32 s50, s42, 0x6000
	s_mov_b32 m0, s50
	s_nop 0
	global_load_lds_dwordx4 v164, s[16:17]
	s_cmp_eq_u32 s14, 1
	s_mov_b32 s41, 0
	s_cselect_b64 s[10:11], -1, 0
	s_cmp_lg_u32 s14, 1
	s_cbranch_scc1 .LBB0_529
	s_barrier
; #define PG8_STAGE(bufoff, gbase, voff) do { _Pragma("unroll") for (int _i = 0; _i < 2; ++_i) { unsigned keep_; \
;         asm volatile("s_mov_b32 %0, m0\n\ts_mov_b32 m0, %3\n\ts_nop 0\n\tglobal_load_lds_dwordx4 %1, %2\n\ts_mov_b32 m0, %0" : "=&s"(keep_) : "v"((voff)[_i]), "s"((const char*)(gbase)), "s"(ldsb + (unsigned)((bufoff) + _i * 8192)) : "memory"); } } while (0)
; #define PG8_WAIT_V(n) asm volatile("s_waitcnt vmcnt(" #n ")" ::: "memory")
; #define PG8_BAR __builtin_amdgcn_s_barrier()
; template <class Epi, class Sched, bool ALIGN_EPI, bool FP8 = false>
; __device__ __forceinline__ void gemm_phase(PG8_LAS unsigned char* lds, const Gemm g, const Sched& S, const Epi& E, const int wid, const int lane) {
;     ...
;     const int aoff = lds_byte(wr * 64 + fr, fq * 8), boff = lds_byte(wc * 32 + fr, fq * 8);
;     ...
;     if (wr == 1) PG8_BAR;
;     PG8_WAIT_V(2); PG8_BAR;
;     PG8_STAGE(PG8_SB(1, 0), cB + kstep, voffB); PG8_STAGE(PG8_SA(1, 0), cA + kstep, vc0); PG8_STAGE(PG8_SB(1, 1), cB + hstep + kstep, voffB);
;     PG8_WAIT_V(6); PG8_BAR;
.LBB0_529:
	s_sext_i32_i8 s84, s12
	s_add_u32 s12, s56, 0x55c00000
	s_addc_u32 s13, s57, 0
	s_lshr_b32 s1, s1, 25
	s_add_i32 s1, s0, s1
	s_ashr_i32 s51, s1, 7
	v_ashrrev_i32_e32 v2, 6, v172
	s_lshl_b32 s1, s14, 13
	v_lshl_add_u32 v4, v2, 10, s1
	s_lshl_b32 s1, s80, 5
	v_and_b32_e32 v0, 15, v172
	s_and_b32 s1, s1, 0x60
	v_lshl_or_b32 v161, s14, 6, v0
	s_lshr_b32 s14, s1, 3
	v_add_lshl_u32 v2, v2, s14, 10
	s_add_u32 s14, s28, 0x80
	s_waitcnt vmcnt(2)
	s_barrier
	s_addc_u32 s15, s29, 0
	s_add_i32 s52, s42, 0x18000
	s_mov_b32 m0, s52
	s_nop 0
	global_load_lds_dwordx4 v162, s[14:15]
	s_add_i32 s53, s42, 0x1a000
	s_mov_b32 m0, s53
	s_nop 0
	global_load_lds_dwordx4 v166, s[14:15]
	s_add_u32 s14, s30, 0x80
	s_addc_u32 s15, s31, 0
	s_add_i32 s54, s42, 0x8000
	s_mov_b32 m0, s54
	s_nop 0
	global_load_lds_dwordx4 v160, s[14:15]
	s_add_i32 s55, s42, 0xa000
	v_and_b32_e32 v3, 48, v172
	s_mov_b32 m0, s55
	s_nop 0
	global_load_lds_dwordx4 v164, s[14:15]
	s_add_u32 s4, s4, 0x80
	v_lshl_or_b32 v0, v0, 6, v3
	v_lshlrev_b32_e32 v3, 2, v172
	s_addc_u32 s5, s5, 0
	s_add_i32 s64, s42, 0x1c000
	s_mov_b32 m0, s64
	s_nop 0
	global_load_lds_dwordx4 v162, s[4:5]
	s_add_i32 s65, s42, 0x1e000
	v_and_b32_e32 v3, 32, v3
	s_mov_b32 m0, s65
	s_nop 0
	global_load_lds_dwordx4 v166, s[4:5]
	s_cmpk_gt_i32 s0, 0x7f
	v_ashrrev_i32_e32 v1, 1, v172
	v_bitop3_b32 v4, v0, v4, v3 bitop3:0xde
	v_bitop3_b32 v0, v0, v2, v3 bitop3:0xde
	s_waitcnt vmcnt(6)
	s_cselect_b64 s[14:15], -1, 0
	s_add_i32 s66, s51, -2
	s_add_i32 s67, s42, 0xc000
	v_and_b32_e32 v1, -8, v1
	s_cmpk_lt_u32 s90, 0x100
	v_add_u32_e32 v0, 0, v0
	s_cselect_b64 s[16:17], -1, 0
	v_add_u32_e32 v163, s1, v1
	s_add_i32 s68, s42, 0xe000
	s_ashr_i32 s69, s76, 31
	v_mov_b64_e32 v[168:169], 0x200
	v_mov_b64_e32 v[170:171], 0x1ff
	v_add_u32_e32 v165, 0x10000, v0
	v_add_u32_e32 v167, 0x14000, v0
	v_add_u32_e32 v173, 0, v4
	v_mov_b32_e32 v174, 0x79
	v_mov_b32_e32 v175, 0x7b
	v_add_u32_e32 v176, 0x18000, v0
	v_add_u32_e32 v177, 0x1c000, v0
	s_mov_b64 s[18:19], 0x80000
	s_mov_b32 s70, 0x80000
	s_mov_b64 s[20:21], 0x90000
	s_mov_b32 s71, 0x90000
	s_mov_b64 s[22:23], 0xa0000
	s_mov_b32 s72, 0xa0000
	s_mov_b64 s[24:25], 0xb0000
	s_mov_b32 s73, 0xb0000
	s_barrier
	s_branch .LBB0_532

; #define PG8_STAGE(bufoff, gbase, voff) do { _Pragma("unroll") for (int _i = 0; _i < 2; ++_i) { unsigned keep_; \
;         asm volatile("s_mov_b32 %0, m0\n\ts_mov_b32 m0, %3\n\ts_nop 0\n\tglobal_load_lds_dwordx4 %1, %2\n\ts_mov_b32 m0, %0" : "=&s"(keep_) : "v"((voff)[_i]), "s"((const char*)(gbase)), "s"(ldsb + (unsigned)((bufoff) + _i * 8192)) : "memory"); } } while (0)
; #define PG8_LDA(dst, b, h) do { _Pragma("unroll") for (int m = 0; m < 4; ++m) _Pragma("unroll") for (int k = 0; k < 2; ++k) dst[m][k] = *(const PG8_LAS bf16x8*)(lds + PG8_SA(b, h) + aoff + m * 2048 + k * 1024); } while (0)
; #define PG8_LDB(dst, b, h) do { _Pragma("unroll") for (int n = 0; n < 2; ++n) _Pragma("unroll") for (int k = 0; k < 2; ++k) dst[n][k] = *(const PG8_LAS bf16x8*)(lds + PG8_SB(b, h) + boff + n * 2048 + k * 1024); } while (0)
; #define PG8_WAIT_V(n) asm volatile("s_waitcnt vmcnt(" #n ")" ::: "memory")
; #define PG8_WAIT_L(n) asm volatile("s_waitcnt lgkmcnt(" #n ")" ::: "memory")
; #define PG8_BAR __builtin_amdgcn_s_barrier()
; #define PG8_SCHED __builtin_amdgcn_sched_barrier(0)
; template <class Epi, class Sched, bool ALIGN_EPI, bool FP8 = false>
; __device__ __forceinline__ void gemm_phase(PG8_LAS unsigned char* lds, const Gemm g, const Sched& S, const Epi& E, const int wid, const int lane) {
;     ...
;             PG8_LDB(B0, 0, 0); PG8_LDB(B1, 0, 1); PG8_SCHED; PG8_LDA(At, 0, 0); PG8_STAGE(PG8_SA(1, 1), a1 + hstepA, vc1);
;             if (GA && last && has_next) { const u32x4 q = *gslot; vc0[0] = q.x; vc0[1] = q.y; vc1[0] = q.z; vc1[1] = q.w; }
;             PG8_WAIT_V(8); PG8_WAIT_L(0); PG8_BAR; PG8_MMA(0, 0, At, B0); PG8_MMA(0, 1, At, B1); PG8_BAR; PG8_SCHED;
;             PG8_LDA(At, 0, 1); PG8_STAGE(PG8_SB(0, 0), b2, voffB); PG8_STAGE(PG8_SB(0, 1), b2 + hstep, voffB); PG8_STAGE(PG8_SA(0, 0), a2, vc0);
;             PG8_WAIT_V(8); PG8_WAIT_L(0); PG8_BAR; PG8_MMA(1, 0, At, B0); PG8_MMA(1, 1, At, B1); PG8_BAR; PG8_SCHED;
.LBB0_544:
	ds_read_b128 v[24:27], v165
	ds_read_b128 v[28:31], v165 offset:1024
	ds_read_b128 v[16:19], v165 offset:2048
	ds_read_b128 v[20:23], v165 offset:3072
	ds_read_b128 v[8:11], v167
	ds_read_b128 v[12:15], v167 offset:1024
	ds_read_b128 v[0:3], v167 offset:2048
	ds_read_b128 v[4:7], v167 offset:3072
	s_add_i32 s33, s30, 2
	s_cmp_eq_u32 s66, s30
	s_cselect_b32 s36, s4, s82
	s_cselect_b32 s37, s5, s85
	s_cselect_b32 s34, s26, s86
	s_cselect_b32 s35, s27, s87
	s_add_u32 s30, s36, 0x80
	s_addc_u32 s31, s37, 0
	ds_read_b128 v[178:181], v173
	ds_read_b128 v[182:185], v173 offset:1024
	ds_read_b128 v[186:189], v173 offset:2048
	ds_read_b128 v[190:193], v173 offset:3072
	ds_read_b128 v[194:197], v173 offset:4096
	ds_read_b128 v[198:201], v173 offset:5120
	ds_read_b128 v[202:205], v173 offset:6144
	ds_read_b128 v[206:209], v173 offset:7168
	s_mov_b32 m0, s67
	s_nop 0
	global_load_lds_dwordx4 v160, s[28:29]
	s_mov_b32 m0, s68
	s_nop 0
	global_load_lds_dwordx4 v164, s[28:29]
	s_waitcnt vmcnt(8)
	s_waitcnt lgkmcnt(0)
	s_barrier
	s_setprio 1
	s_waitcnt lgkmcnt(6)
	v_mfma_scale_f32_16x16x128_f8f6f4 v[156:159], v[24:31], v[178:185], v[156:159], v174, v175 op_sel_hi:[0,0,0]
	v_mfma_scale_f32_16x16x128_f8f6f4 v[152:155], v[16:23], v[178:185], v[152:155], v174, v175 op_sel_hi:[0,0,0]
	s_waitcnt lgkmcnt(4)
	v_mfma_scale_f32_16x16x128_f8f6f4 v[140:143], v[24:31], v[186:193], v[140:143], v174, v175 op_sel_hi:[0,0,0]
	v_mfma_scale_f32_16x16x128_f8f6f4 v[136:139], v[16:23], v[186:193], v[136:139], v174, v175 op_sel_hi:[0,0,0]
	s_waitcnt lgkmcnt(2)
	v_mfma_scale_f32_16x16x128_f8f6f4 v[124:127], v[24:31], v[194:201], v[124:127], v174, v175 op_sel_hi:[0,0,0]
	v_mfma_scale_f32_16x16x128_f8f6f4 v[120:123], v[16:23], v[194:201], v[120:123], v174, v175 op_sel_hi:[0,0,0]
	s_waitcnt lgkmcnt(0)
	v_mfma_scale_f32_16x16x128_f8f6f4 v[108:111], v[24:31], v[202:209], v[108:111], v174, v175 op_sel_hi:[0,0,0]
	v_mfma_scale_f32_16x16x128_f8f6f4 v[104:107], v[16:23], v[202:209], v[104:107], v174, v175 op_sel_hi:[0,0,0]
	s_setprio 0
	s_setprio 1
	v_mfma_scale_f32_16x16x128_f8f6f4 v[148:151], v[8:15], v[178:185], v[148:151], v174, v175 op_sel_hi:[0,0,0]
	v_mfma_scale_f32_16x16x128_f8f6f4 v[144:147], v[0:7], v[178:185], v[144:147], v174, v175 op_sel_hi:[0,0,0]
	v_mfma_scale_f32_16x16x128_f8f6f4 v[132:135], v[8:15], v[186:193], v[132:135], v174, v175 op_sel_hi:[0,0,0]
	v_mfma_scale_f32_16x16x128_f8f6f4 v[128:131], v[0:7], v[186:193], v[128:131], v174, v175 op_sel_hi:[0,0,0]
	v_mfma_scale_f32_16x16x128_f8f6f4 v[116:119], v[8:15], v[194:201], v[116:119], v174, v175 op_sel_hi:[0,0,0]
	v_mfma_scale_f32_16x16x128_f8f6f4 v[112:115], v[0:7], v[194:201], v[112:115], v174, v175 op_sel_hi:[0,0,0]
	v_mfma_scale_f32_16x16x128_f8f6f4 v[100:103], v[8:15], v[202:209], v[100:103], v174, v175 op_sel_hi:[0,0,0]
	v_mfma_scale_f32_16x16x128_f8f6f4 v[96:99], v[0:7], v[202:209], v[96:99], v174, v175 op_sel_hi:[0,0,0]
	s_setprio 0
	s_barrier
	ds_read_b128 v[178:181], v173 offset:16384
	ds_read_b128 v[182:185], v173 offset:17408
	ds_read_b128 v[186:189], v173 offset:18432
	ds_read_b128 v[190:193], v173 offset:19456
	ds_read_b128 v[194:197], v173 offset:20480
	ds_read_b128 v[198:201], v173 offset:21504
	ds_read_b128 v[202:205], v173 offset:22528
	ds_read_b128 v[206:209], v173 offset:23552
	s_mov_b32 m0, s44
	s_nop 0
	global_load_lds_dwordx4 v162, s[34:35]
	s_mov_b32 m0, s45
	s_nop 0
	global_load_lds_dwordx4 v166, s[34:35]
	s_add_u32 s58, s34, s6
	s_addc_u32 s59, s35, s7
	s_mov_b32 m0, s46
	s_nop 0
	global_load_lds_dwordx4 v162, s[58:59]
	s_mov_b32 m0, s47
	s_nop 0
	global_load_lds_dwordx4 v166, s[58:59]
	s_mov_b32 m0, s42
	s_nop 0
	global_load_lds_dwordx4 v160, s[36:37]
	s_mov_b32 m0, s48
	s_nop 0
	global_load_lds_dwordx4 v164, s[36:37]
	s_waitcnt vmcnt(8)
	s_waitcnt lgkmcnt(0)
	s_barrier
	s_setprio 1
	s_waitcnt lgkmcnt(6)
	v_mfma_scale_f32_16x16x128_f8f6f4 v[92:95], v[24:31], v[178:185], v[92:95], v174, v175 op_sel_hi:[0,0,0]
	v_mfma_scale_f32_16x16x128_f8f6f4 v[88:91], v[16:23], v[178:185], v[88:91], v174, v175 op_sel_hi:[0,0,0]
	s_waitcnt lgkmcnt(4)
	v_mfma_scale_f32_16x16x128_f8f6f4 v[76:79], v[24:31], v[186:193], v[76:79], v174, v175 op_sel_hi:[0,0,0]
	v_mfma_scale_f32_16x16x128_f8f6f4 v[72:75], v[16:23], v[186:193], v[72:75], v174, v175 op_sel_hi:[0,0,0]
	s_waitcnt lgkmcnt(2)
	v_mfma_scale_f32_16x16x128_f8f6f4 v[60:63], v[24:31], v[194:201], v[60:63], v174, v175 op_sel_hi:[0,0,0]
	v_mfma_scale_f32_16x16x128_f8f6f4 v[56:59], v[16:23], v[194:201], v[56:59], v174, v175 op_sel_hi:[0,0,0]
	s_waitcnt lgkmcnt(0)
	v_mfma_scale_f32_16x16x128_f8f6f4 v[44:47], v[24:31], v[202:209], v[44:47], v174, v175 op_sel_hi:[0,0,0]
	v_mfma_scale_f32_16x16x128_f8f6f4 v[40:43], v[16:23], v[202:209], v[40:43], v174, v175 op_sel_hi:[0,0,0]
	s_setprio 0
	s_setprio 1
	v_mfma_scale_f32_16x16x128_f8f6f4 v[84:87], v[8:15], v[178:185], v[84:87], v174, v175 op_sel_hi:[0,0,0]
	v_mfma_scale_f32_16x16x128_f8f6f4 v[80:83], v[0:7], v[178:185], v[80:83], v174, v175 op_sel_hi:[0,0,0]
	v_mfma_scale_f32_16x16x128_f8f6f4 v[68:71], v[8:15], v[186:193], v[68:71], v174, v175 op_sel_hi:[0,0,0]
	v_mfma_scale_f32_16x16x128_f8f6f4 v[64:67], v[0:7], v[186:193], v[64:67], v174, v175 op_sel_hi:[0,0,0]
	v_mfma_scale_f32_16x16x128_f8f6f4 v[52:55], v[8:15], v[194:201], v[52:55], v174, v175 op_sel_hi:[0,0,0]
	v_mfma_scale_f32_16x16x128_f8f6f4 v[48:51], v[0:7], v[194:201], v[48:51], v174, v175 op_sel_hi:[0,0,0]
	v_mfma_scale_f32_16x16x128_f8f6f4 v[36:39], v[8:15], v[202:209], v[36:39], v174, v175 op_sel_hi:[0,0,0]
	v_mfma_scale_f32_16x16x128_f8f6f4 v[32:35], v[0:7], v[202:209], v[32:35], v174, v175 op_sel_hi:[0,0,0]
	s_setprio 0
	s_barrier
; #define PG8_STAGE(bufoff, gbase, voff) do { _Pragma("unroll") for (int _i = 0; _i < 2; ++_i) { unsigned keep_; \
;         asm volatile("s_mov_b32 %0, m0\n\ts_mov_b32 m0, %3\n\ts_nop 0\n\tglobal_load_lds_dwordx4 %1, %2\n\ts_mov_b32 m0, %0" : "=&s"(keep_) : "v"((voff)[_i]), "s"((const char*)(gbase)), "s"(ldsb + (unsigned)((bufoff) + _i * 8192)) : "memory"); } } while (0)
; #define PG8_LDA(dst, b, h) do { _Pragma("unroll") for (int m = 0; m < 4; ++m) _Pragma("unroll") for (int k = 0; k < 2; ++k) dst[m][k] = *(const PG8_LAS bf16x8*)(lds + PG8_SA(b, h) + aoff + m * 2048 + k * 1024); } while (0)
; #define PG8_LDB(dst, b, h) do { _Pragma("unroll") for (int n = 0; n < 2; ++n) _Pragma("unroll") for (int k = 0; k < 2; ++k) dst[n][k] = *(const PG8_LAS bf16x8*)(lds + PG8_SB(b, h) + boff + n * 2048 + k * 1024); } while (0)
; #define PG8_WAIT_V(n) asm volatile("s_waitcnt vmcnt(" #n ")" ::: "memory")
; #define PG8_WAIT_L(n) asm volatile("s_waitcnt lgkmcnt(" #n ")" ::: "memory")
; #define PG8_BAR __builtin_amdgcn_s_barrier()
; #define PG8_SCHED __builtin_amdgcn_sched_barrier(0)
; template <class Epi, class Sched, bool ALIGN_EPI, bool FP8 = false>
; __device__ __forceinline__ void gemm_phase(PG8_LAS unsigned char* lds, const Gemm g, const Sched& S, const Epi& E, const int wid, const int lane) {
;     ...
;             PG8_LDB(B0, 1, 0); PG8_LDB(B1, 1, 1); PG8_SCHED; PG8_LDA(At, 1, 0); PG8_STAGE(PG8_SA(0, 1), a2 + hstepA, vc1);
;             PG8_WAIT_V(8); PG8_WAIT_L(0); PG8_BAR; PG8_MMA(0, 0, At, B0); PG8_MMA(0, 1, At, B1); PG8_BAR; PG8_SCHED;
;             PG8_LDA(At, 1, 1); PG8_STAGE(PG8_SB(1, 0), b3, voffB); PG8_STAGE(PG8_SB(1, 1), b3 + hstep, voffB); PG8_STAGE(PG8_SA(1, 0), a3, vc0);
;             PG8_WAIT_V(8); PG8_WAIT_L(0); PG8_BAR; PG8_MMA(1, 0, At, B0); PG8_MMA(1, 1, At, B1); PG8_BAR; PG8_SCHED;
	ds_read_b128 v[0:3], v176
	ds_read_b128 v[4:7], v176 offset:1024
	ds_read_b128 v[8:11], v176 offset:2048
	ds_read_b128 v[12:15], v176 offset:3072
	ds_read_b128 v[16:19], v177
	ds_read_b128 v[20:23], v177 offset:1024
	ds_read_b128 v[24:27], v177 offset:2048
	ds_read_b128 v[28:31], v177 offset:3072
	ds_read_b128 v[178:181], v173 offset:32768
	ds_read_b128 v[182:185], v173 offset:33792
	ds_read_b128 v[186:189], v173 offset:34816
	ds_read_b128 v[190:193], v173 offset:35840
	ds_read_b128 v[194:197], v173 offset:36864
	ds_read_b128 v[198:201], v173 offset:37888
	ds_read_b128 v[202:205], v173 offset:38912
	ds_read_b128 v[206:209], v173 offset:39936
	s_add_u32 s36, s36, s6
	s_addc_u32 s37, s37, s7
	s_mov_b32 m0, s49
	s_nop 0
	global_load_lds_dwordx4 v160, s[36:37]
	s_mov_b32 m0, s50
	s_nop 0
	global_load_lds_dwordx4 v164, s[36:37]
	s_waitcnt vmcnt(8)
	s_waitcnt lgkmcnt(0)
	s_barrier
	s_setprio 1
	s_waitcnt lgkmcnt(6)
	v_mfma_scale_f32_16x16x128_f8f6f4 v[156:159], v[0:7], v[178:185], v[156:159], v174, v175 op_sel_hi:[0,0,0]
	v_mfma_scale_f32_16x16x128_f8f6f4 v[152:155], v[8:15], v[178:185], v[152:155], v174, v175 op_sel_hi:[0,0,0]
	s_waitcnt lgkmcnt(4)
	v_mfma_scale_f32_16x16x128_f8f6f4 v[140:143], v[0:7], v[186:193], v[140:143], v174, v175 op_sel_hi:[0,0,0]
	v_mfma_scale_f32_16x16x128_f8f6f4 v[136:139], v[8:15], v[186:193], v[136:139], v174, v175 op_sel_hi:[0,0,0]
	s_waitcnt lgkmcnt(2)
	v_mfma_scale_f32_16x16x128_f8f6f4 v[124:127], v[0:7], v[194:201], v[124:127], v174, v175 op_sel_hi:[0,0,0]
	v_mfma_scale_f32_16x16x128_f8f6f4 v[120:123], v[8:15], v[194:201], v[120:123], v174, v175 op_sel_hi:[0,0,0]
	s_waitcnt lgkmcnt(0)
	v_mfma_scale_f32_16x16x128_f8f6f4 v[108:111], v[0:7], v[202:209], v[108:111], v174, v175 op_sel_hi:[0,0,0]
	v_mfma_scale_f32_16x16x128_f8f6f4 v[104:107], v[8:15], v[202:209], v[104:107], v174, v175 op_sel_hi:[0,0,0]
	s_setprio 0
	s_setprio 1
	v_mfma_scale_f32_16x16x128_f8f6f4 v[148:151], v[16:23], v[178:185], v[148:151], v174, v175 op_sel_hi:[0,0,0]
	v_mfma_scale_f32_16x16x128_f8f6f4 v[144:147], v[24:31], v[178:185], v[144:147], v174, v175 op_sel_hi:[0,0,0]
	v_mfma_scale_f32_16x16x128_f8f6f4 v[132:135], v[16:23], v[186:193], v[132:135], v174, v175 op_sel_hi:[0,0,0]
	v_mfma_scale_f32_16x16x128_f8f6f4 v[128:131], v[24:31], v[186:193], v[128:131], v174, v175 op_sel_hi:[0,0,0]
	v_mfma_scale_f32_16x16x128_f8f6f4 v[116:119], v[16:23], v[194:201], v[116:119], v174, v175 op_sel_hi:[0,0,0]
	v_mfma_scale_f32_16x16x128_f8f6f4 v[112:115], v[24:31], v[194:201], v[112:115], v174, v175 op_sel_hi:[0,0,0]
	v_mfma_scale_f32_16x16x128_f8f6f4 v[100:103], v[16:23], v[202:209], v[100:103], v174, v175 op_sel_hi:[0,0,0]
	v_mfma_scale_f32_16x16x128_f8f6f4 v[96:99], v[24:31], v[202:209], v[96:99], v174, v175 op_sel_hi:[0,0,0]
	s_setprio 0
	s_barrier
	ds_read_b128 v[178:181], v173 offset:49152
	ds_read_b128 v[182:185], v173 offset:50176
	ds_read_b128 v[186:189], v173 offset:51200
	ds_read_b128 v[190:193], v173 offset:52224
	ds_read_b128 v[194:197], v173 offset:53248
	ds_read_b128 v[198:201], v173 offset:54272
	ds_read_b128 v[202:205], v173 offset:55296
	ds_read_b128 v[206:209], v173 offset:56320
	s_add_u32 s34, s34, 0x80
	s_addc_u32 s35, s35, 0
	s_mov_b32 m0, s52
	s_nop 0
	global_load_lds_dwordx4 v162, s[34:35]
	s_mov_b32 m0, s53
	s_nop 0
	global_load_lds_dwordx4 v166, s[34:35]
	s_add_u32 s34, s34, s6
	s_addc_u32 s35, s35, s7
	s_mov_b32 m0, s64
	s_nop 0
	global_load_lds_dwordx4 v162, s[34:35]
	s_mov_b32 m0, s65
	s_nop 0
	global_load_lds_dwordx4 v166, s[34:35]
	s_mov_b32 m0, s54
	s_nop 0
	global_load_lds_dwordx4 v160, s[30:31]
	s_mov_b32 m0, s55
	s_nop 0
	global_load_lds_dwordx4 v164, s[30:31]
	s_waitcnt vmcnt(8)
	s_waitcnt lgkmcnt(0)
	s_barrier
	s_setprio 1
	s_waitcnt lgkmcnt(6)
	v_mfma_scale_f32_16x16x128_f8f6f4 v[92:95], v[0:7], v[178:185], v[92:95], v174, v175 op_sel_hi:[0,0,0]
	v_mfma_scale_f32_16x16x128_f8f6f4 v[88:91], v[8:15], v[178:185], v[88:91], v174, v175 op_sel_hi:[0,0,0]
	s_waitcnt lgkmcnt(4)
	v_mfma_scale_f32_16x16x128_f8f6f4 v[76:79], v[0:7], v[186:193], v[76:79], v174, v175 op_sel_hi:[0,0,0]
	v_mfma_scale_f32_16x16x128_f8f6f4 v[72:75], v[8:15], v[186:193], v[72:75], v174, v175 op_sel_hi:[0,0,0]
	s_waitcnt lgkmcnt(2)
	v_mfma_scale_f32_16x16x128_f8f6f4 v[60:63], v[0:7], v[194:201], v[60:63], v174, v175 op_sel_hi:[0,0,0]
	v_mfma_scale_f32_16x16x128_f8f6f4 v[56:59], v[8:15], v[194:201], v[56:59], v174, v175 op_sel_hi:[0,0,0]
	s_waitcnt lgkmcnt(0)
	v_mfma_scale_f32_16x16x128_f8f6f4 v[44:47], v[0:7], v[202:209], v[44:47], v174, v175 op_sel_hi:[0,0,0]
	v_mfma_scale_f32_16x16x128_f8f6f4 v[40:43], v[8:15], v[202:209], v[40:43], v174, v175 op_sel_hi:[0,0,0]
	s_setprio 0
	s_setprio 1
	v_mfma_scale_f32_16x16x128_f8f6f4 v[84:87], v[16:23], v[178:185], v[84:87], v174, v175 op_sel_hi:[0,0,0]
	v_mfma_scale_f32_16x16x128_f8f6f4 v[80:83], v[24:31], v[178:185], v[80:83], v174, v175 op_sel_hi:[0,0,0]
	v_mfma_scale_f32_16x16x128_f8f6f4 v[68:71], v[16:23], v[186:193], v[68:71], v174, v175 op_sel_hi:[0,0,0]
	v_mfma_scale_f32_16x16x128_f8f6f4 v[64:67], v[24:31], v[186:193], v[64:67], v174, v175 op_sel_hi:[0,0,0]
	v_mfma_scale_f32_16x16x128_f8f6f4 v[52:55], v[16:23], v[194:201], v[52:55], v174, v175 op_sel_hi:[0,0,0]
	v_mfma_scale_f32_16x16x128_f8f6f4 v[48:51], v[24:31], v[194:201], v[48:51], v174, v175 op_sel_hi:[0,0,0]
	v_mfma_scale_f32_16x16x128_f8f6f4 v[36:39], v[16:23], v[202:209], v[36:39], v174, v175 op_sel_hi:[0,0,0]
	v_mfma_scale_f32_16x16x128_f8f6f4 v[32:35], v[24:31], v[202:209], v[32:35], v174, v175 op_sel_hi:[0,0,0]
	s_setprio 0
	s_barrier
	s_add_u32 s82, s82, 0x100
	s_addc_u32 s85, s85, 0
	s_add_u32 s86, s86, 0x100
	s_addc_u32 s87, s87, 0
	s_add_u32 s28, s28, 0x100
	s_addc_u32 s29, s29, 0
	s_cmp_ge_i32 s33, s51
	s_mov_b32 s30, s33
	s_cbranch_scc0 .LBB0_544

; #define PG8_STAGE(bufoff, gbase, voff) do { _Pragma("unroll") for (int _i = 0; _i < 2; ++_i) { unsigned keep_; \
;         asm volatile("s_mov_b32 %0, m0\n\ts_mov_b32 m0, %3\n\ts_nop 0\n\tglobal_load_lds_dwordx4 %1, %2\n\ts_mov_b32 m0, %0" : "=&s"(keep_) : "v"((voff)[_i]), "s"((const char*)(gbase)), "s"(ldsb + (unsigned)((bufoff) + _i * 8192)) : "memory"); } } while (0)
; #define PG8_WAIT_V(n) asm volatile("s_waitcnt vmcnt(" #n ")" ::: "memory")
; #define PG8_BAR __builtin_amdgcn_s_barrier()
; template <class Epi, class Sched, bool ALIGN_EPI, bool FP8 = false>
; __device__ __forceinline__ void gemm_phase(PG8_LAS unsigned char* lds, const Gemm g, const Sched& S, const Epi& E, const int wid, const int lane) {
;     ...
;         if (GA) { vc0[i] = S.tok_off(cur, rA[i]) + cA2[i]; vc1[i] = S.tok_off(cur, HALF + rA[i]) + cA2[i]; }
;         else { vc0[i] = voffA[i]; vc1[i] = voffA[i]; } }
;     if (GA) asm volatile("" : "+v"(vc0[0]), "+v"(vc0[1]), "+v"(vc1[0]), "+v"(vc1[1]));
;     const char* cA = GA ? (const char*)g.A : (const char*)g.A + (size_t)cur.pm * tstep; const char* cB = (const char*)g.Bt + (size_t)cur.pn * tstep;
;     PG8_STAGE(PG8_SB(0, 0), cB, voffB); PG8_STAGE(PG8_SB(0, 1), cB + hstep, voffB); PG8_STAGE(PG8_SA(0, 0), cA, vc0); PG8_STAGE(PG8_SA(0, 1), cA + hstepA, vc1);
;     if (wr == 1) PG8_BAR;
;     PG8_WAIT_V(2); PG8_BAR;
;     PG8_STAGE(PG8_SB(1, 0), cB + kstep, voffB); PG8_STAGE(PG8_SA(1, 0), cA + kstep, vc0); PG8_STAGE(PG8_SB(1, 1), cB + hstep + kstep, voffB);
;     PG8_WAIT_V(6); PG8_BAR;
.LBB0_711:
	v_lshlrev_b32_e32 v3, 6, v1
	v_lshlrev_b32_e32 v2, 5, v5
	v_sub_u32_e32 v3, v15, v3
	v_mov_b32_e32 v5, 1
	v_ashrrev_i16_sdwa v3, v5, sext(v3) dst_sel:DWORD dst_unused:UNUSED_PAD src0_sel:DWORD src1_sel:BYTE_0
	v_and_b32_e32 v2, 32, v2
	v_bfe_i32 v3, v3, 0, 16
	v_add_lshl_u32 v196, v2, v3, 1
	v_lshlrev_b32_e32 v3, 6, v13
	v_sub_u32_e32 v3, v12, v3
	v_lshlrev_b32_e32 v2, 5, v11
	v_ashrrev_i16_sdwa v3, v5, sext(v3) dst_sel:DWORD dst_unused:UNUSED_PAD src0_sel:DWORD src1_sel:BYTE_0
	v_and_b32_e32 v2, 32, v2
	v_bfe_i32 v3, v3, 0, 16
	v_add_lshl_u32 v198, v2, v3, 1
	v_lshl_add_u32 v64, v0, 11, v198
	v_lshlrev_b32_e32 v0, 1, v199
	v_lshrrev_b32_e32 v2, 2, v199
	v_and_b32_e32 v3, 3, v13
	s_movk_i32 s5, 0xffe0
	v_and_b32_e32 v0, 24, v0
	v_and_b32_e32 v2, 4, v2
	v_and_or_b32 v3, v199, s5, v3
	v_or3_b32 v0, v3, v2, v0
	v_mad_u64_u32 v[200:201], s[0:1], s8, v0, v[198:199]
	v_lshlrev_b32_e32 v0, 1, v204
	v_lshrrev_b32_e32 v2, 2, v204
	v_and_b32_e32 v1, 3, v1
	v_and_b32_e32 v0, 24, v0
	v_and_b32_e32 v2, 4, v2
	v_and_or_b32 v1, v204, s5, v1
	v_or3_b32 v0, v1, v2, v0
	v_mad_u64_u32 v[202:203], s[0:1], s8, v0, v[196:197]
	s_ashr_i32 s9, s8, 31
	s_lshl_b32 s0, s80, 10
	s_lshr_b32 s4, s90, 8
	s_lshl_b64 s[16:17], s[8:9], 7
	s_lshl_b64 s[18:19], s[8:9], 8
	s_add_i32 s47, s0, 0
	s_add_u32 s20, s56, 0x41c00000
	s_addc_u32 s21, s57, 0
	s_add_u32 s48, s56, 0x3000000
	s_addc_u32 s49, s57, 0
	s_ashr_i32 s0, s89, 31
	s_mul_i32 s0, s18, s0
	s_mul_hi_u32 s1, s18, s89
	s_add_i32 s5, s1, s0
	s_lshr_b64 s[0:1], s[8:9], 24
	s_mul_i32 s0, s0, s89
	s_add_i32 s5, s5, s0
	s_mul_i32 s0, s18, s89
	v_lshl_add_u32 v65, v8, 11, v196
	v_lshl_add_u32 v66, v4, 11, v198
	v_lshl_add_u32 v67, v6, 11, v196
	s_add_u32 s34, s48, s0
	s_addc_u32 s35, s49, s5
	s_add_i32 s51, s47, 0x10000
	s_mov_b32 m0, s51
	s_nop 0
	global_load_lds_dwordx4 v200, s[34:35]
	s_add_i32 s53, s47, 0x12000
	s_mov_b32 m0, s53
	s_nop 0
	global_load_lds_dwordx4 v202, s[34:35]
	s_add_u32 s0, s34, s16
	s_addc_u32 s1, s35, s17
	s_add_i32 s55, s47, 0x14000
	s_mov_b32 m0, s55
	s_nop 0
	global_load_lds_dwordx4 v200, s[0:1]
	s_add_i32 s64, s47, 0x16000
	s_mov_b32 m0, s64
	s_nop 0
	global_load_lds_dwordx4 v202, s[0:1]
	s_add_i32 s65, s47, 0x2000
	s_mov_b32 m0, s47
	s_nop 0
	global_load_lds_dwordx4 v64, s[20:21]
	s_add_i32 s66, s47, 0x4000
	s_mov_b32 m0, s65
	s_nop 0
	global_load_lds_dwordx4 v65, s[20:21]
	s_add_i32 s67, s47, 0x6000
	s_mov_b32 m0, s66
	s_nop 0
	global_load_lds_dwordx4 v66, s[20:21]
	s_cmp_eq_u32 s4, 1
	s_mov_b32 m0, s67
	s_nop 0
	global_load_lds_dwordx4 v67, s[20:21]
	s_mov_b32 s46, 0
	s_mov_b32 s50, 0x10000
	s_mov_b32 s52, 0x12000
	s_mov_b32 s54, 0x14000
	s_cselect_b64 s[22:23], -1, 0
	s_cmp_lg_u32 s4, 1
	s_cbranch_scc1 .LBB0_713
	s_barrier
.LBB0_713:
	v_and_b32_e32 v0, 15, v10
	s_add_i32 s5, 0, 0x21800
	v_lshl_or_b32 v203, s4, 6, v0
	v_ashrrev_i32_e32 v2, 6, v10
	s_lshl_b32 s4, s4, 13
	v_lshl_add_u32 v201, v197, 4, s5
	s_lshr_b32 s5, s9, 25
	v_lshl_add_u32 v4, v2, 10, s4
	s_lshl_b32 s4, s80, 5
	s_add_i32 s5, s8, s5
	s_and_b32 s9, s4, 0x60
	s_ashr_i32 s68, s5, 7
	s_lshr_b32 s4, s9, 3
	s_add_u32 s24, s56, 0x45c00000
	s_addc_u32 s25, s57, 0
	v_add_lshl_u32 v2, v2, s4, 10
	s_add_u32 s4, s56, 0x41c00080
	s_addc_u32 s5, s57, 0
	s_add_u32 s26, s34, 0x80
	s_waitcnt vmcnt(2)
	s_barrier
	s_addc_u32 s27, s35, 0
	s_add_i32 s69, s47, 0x18000
	s_mov_b32 m0, s69
	s_nop 0
	global_load_lds_dwordx4 v200, s[26:27]
	s_add_i32 s70, s47, 0x1a000
	s_add_i32 s71, s47, 0x8000
	s_add_i32 s72, s47, 0xa000
	s_mov_b32 m0, s70
	s_nop 0
	global_load_lds_dwordx4 v202, s[26:27]
	s_add_u32 s0, s0, 0x80
	s_mov_b32 m0, s71
	s_nop 0
	global_load_lds_dwordx4 v64, s[4:5]
	s_addc_u32 s1, s1, 0
	s_add_i32 s73, s47, 0x1c000
	s_add_i32 s74, s47, 0x1e000
	v_and_b32_e32 v3, 48, v10
	s_mov_b32 m0, s72
	s_nop 0
	global_load_lds_dwordx4 v65, s[4:5]
	s_cmpk_gt_i32 s8, 0x7f
	v_lshl_or_b32 v0, v0, 6, v3
	v_lshlrev_b32_e32 v3, 2, v10
	s_mov_b32 m0, s73
	s_nop 0
	global_load_lds_dwordx4 v200, s[0:1]
	s_cselect_b64 s[26:27], -1, 0
	s_add_i32 s75, s68, -2
	s_add_i32 s83, s47, 0xc000
	v_ashrrev_i32_e32 v1, 1, v10
	v_and_b32_e32 v3, 32, v3
	s_mov_b32 m0, s74
	s_nop 0
	global_load_lds_dwordx4 v202, s[0:1]
	s_cmpk_lt_u32 s90, 0x100
	v_and_b32_e32 v1, -8, v1
	v_bitop3_b32 v4, v0, v4, v3 bitop3:0xde
	v_bitop3_b32 v0, v0, v2, v3 bitop3:0xde
	s_waitcnt vmcnt(6)
	s_cselect_b64 s[28:29], -1, 0
	s_ashr_i32 s0, s76, 3
	v_add_u32_e32 v205, s9, v1
	s_mul_i32 s85, s0, s3
	v_cndmask_b32_e64 v1, 0, 1, s[6:7]
	v_add_u32_e32 v206, 0, v0
	s_add_i32 s84, s47, 0xe000
	s_add_i32 s85, s85, s44
	v_cmp_ne_u32_e64 s[0:1], 1, v1
	v_add_u32_e32 v207, 0x10000, v206
	v_add_u32_e32 v208, 0x14000, v206
	v_add_u32_e32 v209, 0, v4
	v_mov_b32_e32 v210, 0x79
	v_mov_b32_e32 v211, 0x7f
	s_barrier
	s_branch .LBB0_716

; #define PG8_STAGE(bufoff, gbase, voff) do { _Pragma("unroll") for (int _i = 0; _i < 2; ++_i) { unsigned keep_; \
;         asm volatile("s_mov_b32 %0, m0\n\ts_mov_b32 m0, %3\n\ts_nop 0\n\tglobal_load_lds_dwordx4 %1, %2\n\ts_mov_b32 m0, %0" : "=&s"(keep_) : "v"((voff)[_i]), "s"((const char*)(gbase)), "s"(ldsb + (unsigned)((bufoff) + _i * 8192)) : "memory"); } } while (0)
; #define PG8_LDA(dst, b, h) do { _Pragma("unroll") for (int m = 0; m < 4; ++m) _Pragma("unroll") for (int k = 0; k < 2; ++k) dst[m][k] = *(const PG8_LAS bf16x8*)(lds + PG8_SA(b, h) + aoff + m * 2048 + k * 1024); } while (0)
; #define PG8_LDB(dst, b, h) do { _Pragma("unroll") for (int n = 0; n < 2; ++n) _Pragma("unroll") for (int k = 0; k < 2; ++k) dst[n][k] = *(const PG8_LAS bf16x8*)(lds + PG8_SB(b, h) + boff + n * 2048 + k * 1024); } while (0)
; #define PG8_WAIT_V(n) asm volatile("s_waitcnt vmcnt(" #n ")" ::: "memory")
; #define PG8_WAIT_L(n) asm volatile("s_waitcnt lgkmcnt(" #n ")" ::: "memory")
; #define PG8_BAR __builtin_amdgcn_s_barrier()
; #define PG8_SCHED __builtin_amdgcn_sched_barrier(0)
; template <class Epi, class Sched, bool ALIGN_EPI, bool FP8 = false>
; __device__ __forceinline__ void gemm_phase(PG8_LAS unsigned char* lds, const Gemm g, const Sched& S, const Epi& E, const int wid, const int lane) {
;     ...
;             const char* a2 = last ? nA : cA + (size_t)(t + 2) * kstep; const char* b2 = last ? nB : cB + (size_t)(t + 2) * kstep;
;             const char* a3 = a2 + kstep; const char* b3 = b2 + kstep;
;             PG8_LDB(B0, 0, 0); PG8_LDB(B1, 0, 1); PG8_SCHED; PG8_LDA(At, 0, 0); PG8_STAGE(PG8_SA(1, 1), a1 + hstepA, vc1);
;             if (GA && last && has_next) { const u32x4 q = *gslot; vc0[0] = q.x; vc0[1] = q.y; vc1[0] = q.z; vc1[1] = q.w; }
;             PG8_WAIT_V(8); PG8_WAIT_L(0); PG8_BAR; PG8_MMA(0, 0, At, B0); PG8_MMA(0, 1, At, B1); PG8_BAR; PG8_SCHED;
;             PG8_LDA(At, 0, 1); PG8_STAGE(PG8_SB(0, 0), b2, voffB); PG8_STAGE(PG8_SB(0, 1), b2 + hstep, voffB); PG8_STAGE(PG8_SA(0, 0), a2, vc0);
;             PG8_WAIT_V(8); PG8_WAIT_L(0); PG8_BAR; PG8_MMA(1, 0, At, B0); PG8_MMA(1, 1, At, B1); PG8_BAR; PG8_SCHED;
;             PG8_LDB(B0, 1, 0); PG8_LDB(B1, 1, 1); PG8_SCHED; PG8_LDA(At, 1, 0); PG8_STAGE(PG8_SA(0, 1), a2 + hstepA, vc1);
;             PG8_WAIT_V(8); PG8_WAIT_L(0); PG8_BAR; PG8_MMA(0, 0, At, B0); PG8_MMA(0, 1, At, B1); PG8_BAR; PG8_SCHED;
.LBB0_727:
	s_add_i32 s82, s82, 2
	s_and_b64 s[8:9], s[38:39], exec
	s_cselect_b32 s9, 0, s6
	s_cselect_b32 s8, 0, s7
	s_add_u32 s40, s20, s9
	s_addc_u32 s41, s21, s8
	s_add_u32 s33, s34, s6
	s_addc_u32 s42, s35, s7
	s_add_u32 s8, s40, 0x80
	s_addc_u32 s9, s41, 0
	s_waitcnt vmcnt(8)
	s_and_b64 s[38:39], s[38:39], exec
	s_waitcnt lgkmcnt(0)
	s_cselect_b32 s43, s31, s42
	s_cselect_b32 s42, s30, s33
	s_add_u32 s38, s42, 0x80
	s_addc_u32 s39, s43, 0
	s_barrier
	s_setprio 1
	s_waitcnt lgkmcnt(6)
	v_mfma_scale_f32_16x16x128_f8f6f4 v[192:195], v[24:31], v[56:63], v[192:195], v210, v211 op_sel_hi:[0,0,0]
	v_mfma_scale_f32_16x16x128_f8f6f4 v[184:187], v[16:23], v[56:63], v[184:187], v210, v211 op_sel_hi:[0,0,0]
	s_waitcnt lgkmcnt(4)
	v_mfma_scale_f32_16x16x128_f8f6f4 v[176:179], v[24:31], v[48:55], v[176:179], v210, v211 op_sel_hi:[0,0,0]
	v_mfma_scale_f32_16x16x128_f8f6f4 v[168:171], v[16:23], v[48:55], v[168:171], v210, v211 op_sel_hi:[0,0,0]
	s_waitcnt lgkmcnt(2)
	v_mfma_scale_f32_16x16x128_f8f6f4 v[160:163], v[24:31], v[40:47], v[160:163], v210, v211 op_sel_hi:[0,0,0]
	v_mfma_scale_f32_16x16x128_f8f6f4 v[152:155], v[16:23], v[40:47], v[152:155], v210, v211 op_sel_hi:[0,0,0]
	s_waitcnt lgkmcnt(0)
	v_mfma_scale_f32_16x16x128_f8f6f4 v[144:147], v[24:31], v[32:39], v[144:147], v210, v211 op_sel_hi:[0,0,0]
	v_mfma_scale_f32_16x16x128_f8f6f4 v[136:139], v[16:23], v[32:39], v[136:139], v210, v211 op_sel_hi:[0,0,0]
	s_setprio 0
	s_setprio 1
	v_mfma_scale_f32_16x16x128_f8f6f4 v[188:191], v[8:15], v[56:63], v[188:191], v210, v211 op_sel_hi:[0,0,0]
	v_mfma_scale_f32_16x16x128_f8f6f4 v[180:183], v[0:7], v[56:63], v[180:183], v210, v211 op_sel_hi:[0,0,0]
	v_mfma_scale_f32_16x16x128_f8f6f4 v[172:175], v[8:15], v[48:55], v[172:175], v210, v211 op_sel_hi:[0,0,0]
	v_mfma_scale_f32_16x16x128_f8f6f4 v[164:167], v[0:7], v[48:55], v[164:167], v210, v211 op_sel_hi:[0,0,0]
	v_mfma_scale_f32_16x16x128_f8f6f4 v[156:159], v[8:15], v[40:47], v[156:159], v210, v211 op_sel_hi:[0,0,0]
	v_mfma_scale_f32_16x16x128_f8f6f4 v[148:151], v[0:7], v[40:47], v[148:151], v210, v211 op_sel_hi:[0,0,0]
	v_mfma_scale_f32_16x16x128_f8f6f4 v[140:143], v[8:15], v[32:39], v[140:143], v210, v211 op_sel_hi:[0,0,0]
	v_mfma_scale_f32_16x16x128_f8f6f4 v[132:135], v[0:7], v[32:39], v[132:135], v210, v211 op_sel_hi:[0,0,0]
	s_setprio 0
	s_barrier
	ds_read_b128 v[32:35], v209 offset:16384
	ds_read_b128 v[36:39], v209 offset:17408
	ds_read_b128 v[40:43], v209 offset:18432
	ds_read_b128 v[44:47], v209 offset:19456
	ds_read_b128 v[48:51], v209 offset:20480
	ds_read_b128 v[52:55], v209 offset:21504
	ds_read_b128 v[56:59], v209 offset:22528
	ds_read_b128 v[60:63], v209 offset:23552
	s_mov_b32 m0, s51
	s_nop 0
	global_load_lds_dwordx4 v200, s[42:43]
	s_mov_b32 m0, s53
	s_nop 0
	global_load_lds_dwordx4 v202, s[42:43]
	s_add_u32 s42, s42, s16
	s_addc_u32 s43, s43, s17
	s_mov_b32 m0, s55
	s_nop 0
	global_load_lds_dwordx4 v200, s[42:43]
	s_mov_b32 m0, s64
	s_nop 0
	global_load_lds_dwordx4 v202, s[42:43]
	s_mov_b32 m0, s47
	s_nop 0
	global_load_lds_dwordx4 v64, s[40:41]
	s_mov_b32 m0, s65
	s_nop 0
	global_load_lds_dwordx4 v65, s[40:41]
	s_waitcnt vmcnt(8)
	s_waitcnt lgkmcnt(0)
	s_barrier
	s_setprio 1
	s_waitcnt lgkmcnt(6)
	v_mfma_scale_f32_16x16x128_f8f6f4 v[128:131], v[24:31], v[32:39], v[128:131], v210, v211 op_sel_hi:[0,0,0]
	v_mfma_scale_f32_16x16x128_f8f6f4 v[120:123], v[16:23], v[32:39], v[120:123], v210, v211 op_sel_hi:[0,0,0]
	s_waitcnt lgkmcnt(4)
	v_mfma_scale_f32_16x16x128_f8f6f4 v[112:115], v[24:31], v[40:47], v[112:115], v210, v211 op_sel_hi:[0,0,0]
	v_mfma_scale_f32_16x16x128_f8f6f4 v[104:107], v[16:23], v[40:47], v[104:107], v210, v211 op_sel_hi:[0,0,0]
	s_waitcnt lgkmcnt(2)
	v_mfma_scale_f32_16x16x128_f8f6f4 v[96:99], v[24:31], v[48:55], v[96:99], v210, v211 op_sel_hi:[0,0,0]
	v_mfma_scale_f32_16x16x128_f8f6f4 v[88:91], v[16:23], v[48:55], v[88:91], v210, v211 op_sel_hi:[0,0,0]
	s_waitcnt lgkmcnt(0)
	v_mfma_scale_f32_16x16x128_f8f6f4 v[80:83], v[24:31], v[56:63], v[80:83], v210, v211 op_sel_hi:[0,0,0]
	v_mfma_scale_f32_16x16x128_f8f6f4 v[72:75], v[16:23], v[56:63], v[72:75], v210, v211 op_sel_hi:[0,0,0]
	s_setprio 0
	s_setprio 1
	v_mfma_scale_f32_16x16x128_f8f6f4 v[124:127], v[8:15], v[32:39], v[124:127], v210, v211 op_sel_hi:[0,0,0]
	v_mfma_scale_f32_16x16x128_f8f6f4 v[116:119], v[0:7], v[32:39], v[116:119], v210, v211 op_sel_hi:[0,0,0]
	v_mfma_scale_f32_16x16x128_f8f6f4 v[108:111], v[8:15], v[40:47], v[108:111], v210, v211 op_sel_hi:[0,0,0]
	v_mfma_scale_f32_16x16x128_f8f6f4 v[100:103], v[0:7], v[40:47], v[100:103], v210, v211 op_sel_hi:[0,0,0]
	v_mfma_scale_f32_16x16x128_f8f6f4 v[92:95], v[8:15], v[48:55], v[92:95], v210, v211 op_sel_hi:[0,0,0]
	v_mfma_scale_f32_16x16x128_f8f6f4 v[84:87], v[0:7], v[48:55], v[84:87], v210, v211 op_sel_hi:[0,0,0]
	v_mfma_scale_f32_16x16x128_f8f6f4 v[76:79], v[8:15], v[56:63], v[76:79], v210, v211 op_sel_hi:[0,0,0]
	v_mfma_scale_f32_16x16x128_f8f6f4 v[68:71], v[0:7], v[56:63], v[68:71], v210, v211 op_sel_hi:[0,0,0]
	s_setprio 0
	s_barrier
	v_add_u32_e32 v12, 0x18000, v206
	v_add_u32_e32 v28, 0x1c000, v206
	ds_read_b128 v[0:3], v12
	ds_read_b128 v[4:7], v12 offset:1024
	ds_read_b128 v[8:11], v12 offset:2048
	ds_read_b128 v[12:15], v12 offset:3072
	ds_read_b128 v[16:19], v28
	ds_read_b128 v[20:23], v28 offset:1024
	ds_read_b128 v[24:27], v28 offset:2048
	ds_read_b128 v[28:31], v28 offset:3072
	ds_read_b128 v[32:35], v209 offset:32768
	ds_read_b128 v[36:39], v209 offset:33792
	ds_read_b128 v[40:43], v209 offset:34816
	ds_read_b128 v[44:47], v209 offset:35840
	ds_read_b128 v[48:51], v209 offset:36864
	ds_read_b128 v[52:55], v209 offset:37888
	ds_read_b128 v[56:59], v209 offset:38912
	ds_read_b128 v[60:63], v209 offset:39936
	s_mov_b32 m0, s66
	s_nop 0
	global_load_lds_dwordx4 v66, s[40:41]
	s_mov_b32 m0, s67
	s_nop 0
	global_load_lds_dwordx4 v67, s[40:41]
	s_waitcnt vmcnt(8)
	s_waitcnt lgkmcnt(0)
	s_barrier
; #define PG8_STAGE(bufoff, gbase, voff) do { _Pragma("unroll") for (int _i = 0; _i < 2; ++_i) { unsigned keep_; \
;         asm volatile("s_mov_b32 %0, m0\n\ts_mov_b32 m0, %3\n\ts_nop 0\n\tglobal_load_lds_dwordx4 %1, %2\n\ts_mov_b32 m0, %0" : "=&s"(keep_) : "v"((voff)[_i]), "s"((const char*)(gbase)), "s"(ldsb + (unsigned)((bufoff) + _i * 8192)) : "memory"); } } while (0)
; #define PG8_LDA(dst, b, h) do { _Pragma("unroll") for (int m = 0; m < 4; ++m) _Pragma("unroll") for (int k = 0; k < 2; ++k) dst[m][k] = *(const PG8_LAS bf16x8*)(lds + PG8_SA(b, h) + aoff + m * 2048 + k * 1024); } while (0)
; #define PG8_LDB(dst, b, h) do { _Pragma("unroll") for (int n = 0; n < 2; ++n) _Pragma("unroll") for (int k = 0; k < 2; ++k) dst[n][k] = *(const PG8_LAS bf16x8*)(lds + PG8_SB(b, h) + boff + n * 2048 + k * 1024); } while (0)
; #define PG8_WAIT_V(n) asm volatile("s_waitcnt vmcnt(" #n ")" ::: "memory")
; #define PG8_WAIT_L(n) asm volatile("s_waitcnt lgkmcnt(" #n ")" ::: "memory")
; #define PG8_BAR __builtin_amdgcn_s_barrier()
; template <class Epi, class Sched, bool ALIGN_EPI, bool FP8 = false>
; __device__ __forceinline__ void gemm_phase(PG8_LAS unsigned char* lds, const Gemm g, const Sched& S, const Epi& E, const int wid, const int lane) {
;     ...
;             PG8_LDB(B0, 0, 0); PG8_LDB(B1, 0, 1); PG8_SCHED; PG8_LDA(At, 0, 0); PG8_STAGE(PG8_SA(1, 1), a1 + hstepA, vc1);
;             if (GA && last && has_next) { const u32x4 q = *gslot; vc0[0] = q.x; vc0[1] = q.y; vc1[0] = q.z; vc1[1] = q.w; }
;             PG8_WAIT_V(8); PG8_WAIT_L(0); PG8_BAR; PG8_MMA(0, 0, At, B0); PG8_MMA(0, 1, At, B1); PG8_BAR; PG8_SCHED;
;             PG8_LDA(At, 0, 1); PG8_STAGE(PG8_SB(0, 0), b2, voffB); PG8_STAGE(PG8_SB(0, 1), b2 + hstep, voffB); PG8_STAGE(PG8_SA(0, 0), a2, vc0);
;             PG8_WAIT_V(8); PG8_WAIT_L(0); PG8_BAR; PG8_MMA(1, 0, At, B0); PG8_MMA(1, 1, At, B1); PG8_BAR; PG8_SCHED;
;             PG8_LDB(B0, 1, 0); PG8_LDB(B1, 1, 1); PG8_SCHED; PG8_LDA(At, 1, 0); PG8_STAGE(PG8_SA(0, 1), a2 + hstepA, vc1);
;             PG8_WAIT_V(8); PG8_WAIT_L(0); PG8_BAR; PG8_MMA(0, 0, At, B0); PG8_MMA(0, 1, At, B1); PG8_BAR; PG8_SCHED;
;             PG8_LDA(At, 1, 1); PG8_STAGE(PG8_SB(1, 0), b3, voffB); PG8_STAGE(PG8_SB(1, 1), b3 + hstep, voffB); PG8_STAGE(PG8_SA(1, 0), a3, vc0);
;             PG8_WAIT_V(8); PG8_WAIT_L(0); PG8_BAR; PG8_MMA(1, 0, At, B0); PG8_MMA(1, 1, At, B1); PG8_BAR; PG8_SCHED;
	s_setprio 1
	s_waitcnt lgkmcnt(6)
	v_mfma_scale_f32_16x16x128_f8f6f4 v[192:195], v[0:7], v[32:39], v[192:195], v210, v211 op_sel_hi:[0,0,0]
	v_mfma_scale_f32_16x16x128_f8f6f4 v[184:187], v[8:15], v[32:39], v[184:187], v210, v211 op_sel_hi:[0,0,0]
	s_waitcnt lgkmcnt(4)
	v_mfma_scale_f32_16x16x128_f8f6f4 v[176:179], v[0:7], v[40:47], v[176:179], v210, v211 op_sel_hi:[0,0,0]
	v_mfma_scale_f32_16x16x128_f8f6f4 v[168:171], v[8:15], v[40:47], v[168:171], v210, v211 op_sel_hi:[0,0,0]
	s_waitcnt lgkmcnt(2)
	v_mfma_scale_f32_16x16x128_f8f6f4 v[160:163], v[0:7], v[48:55], v[160:163], v210, v211 op_sel_hi:[0,0,0]
	v_mfma_scale_f32_16x16x128_f8f6f4 v[152:155], v[8:15], v[48:55], v[152:155], v210, v211 op_sel_hi:[0,0,0]
	s_waitcnt lgkmcnt(0)
	v_mfma_scale_f32_16x16x128_f8f6f4 v[144:147], v[0:7], v[56:63], v[144:147], v210, v211 op_sel_hi:[0,0,0]
	v_mfma_scale_f32_16x16x128_f8f6f4 v[136:139], v[8:15], v[56:63], v[136:139], v210, v211 op_sel_hi:[0,0,0]
	s_setprio 0
	s_setprio 1
	v_mfma_scale_f32_16x16x128_f8f6f4 v[188:191], v[16:23], v[32:39], v[188:191], v210, v211 op_sel_hi:[0,0,0]
	v_mfma_scale_f32_16x16x128_f8f6f4 v[180:183], v[24:31], v[32:39], v[180:183], v210, v211 op_sel_hi:[0,0,0]
	v_mfma_scale_f32_16x16x128_f8f6f4 v[172:175], v[16:23], v[40:47], v[172:175], v210, v211 op_sel_hi:[0,0,0]
	v_mfma_scale_f32_16x16x128_f8f6f4 v[164:167], v[24:31], v[40:47], v[164:167], v210, v211 op_sel_hi:[0,0,0]
	v_mfma_scale_f32_16x16x128_f8f6f4 v[156:159], v[16:23], v[48:55], v[156:159], v210, v211 op_sel_hi:[0,0,0]
	v_mfma_scale_f32_16x16x128_f8f6f4 v[148:151], v[24:31], v[48:55], v[148:151], v210, v211 op_sel_hi:[0,0,0]
	v_mfma_scale_f32_16x16x128_f8f6f4 v[140:143], v[16:23], v[56:63], v[140:143], v210, v211 op_sel_hi:[0,0,0]
	v_mfma_scale_f32_16x16x128_f8f6f4 v[132:135], v[24:31], v[56:63], v[132:135], v210, v211 op_sel_hi:[0,0,0]
	s_setprio 0
	s_barrier
	ds_read_b128 v[32:35], v209 offset:49152
	ds_read_b128 v[36:39], v209 offset:50176
	ds_read_b128 v[40:43], v209 offset:51200
	ds_read_b128 v[44:47], v209 offset:52224
	ds_read_b128 v[48:51], v209 offset:53248
	ds_read_b128 v[52:55], v209 offset:54272
	ds_read_b128 v[56:59], v209 offset:55296
	ds_read_b128 v[60:63], v209 offset:56320
	s_mov_b32 m0, s69
	s_nop 0
	global_load_lds_dwordx4 v200, s[38:39]
	s_mov_b32 m0, s70
	s_nop 0
	global_load_lds_dwordx4 v202, s[38:39]
	s_add_u32 s38, s38, s16
	s_addc_u32 s39, s39, s17
	s_mov_b32 m0, s73
	s_nop 0
	global_load_lds_dwordx4 v200, s[38:39]
	s_mov_b32 m0, s74
	s_nop 0
	global_load_lds_dwordx4 v202, s[38:39]
	s_mov_b32 m0, s71
	s_nop 0
	global_load_lds_dwordx4 v64, s[8:9]
	s_mov_b32 m0, s72
	s_nop 0
	global_load_lds_dwordx4 v65, s[8:9]
	s_waitcnt vmcnt(8)
	s_waitcnt lgkmcnt(0)
	s_barrier
	s_setprio 1
	s_waitcnt lgkmcnt(6)
	v_mfma_scale_f32_16x16x128_f8f6f4 v[128:131], v[0:7], v[32:39], v[128:131], v210, v211 op_sel_hi:[0,0,0]
	v_mfma_scale_f32_16x16x128_f8f6f4 v[120:123], v[8:15], v[32:39], v[120:123], v210, v211 op_sel_hi:[0,0,0]
	s_waitcnt lgkmcnt(4)
	v_mfma_scale_f32_16x16x128_f8f6f4 v[112:115], v[0:7], v[40:47], v[112:115], v210, v211 op_sel_hi:[0,0,0]
	v_mfma_scale_f32_16x16x128_f8f6f4 v[104:107], v[8:15], v[40:47], v[104:107], v210, v211 op_sel_hi:[0,0,0]
	s_waitcnt lgkmcnt(2)
	v_mfma_scale_f32_16x16x128_f8f6f4 v[96:99], v[0:7], v[48:55], v[96:99], v210, v211 op_sel_hi:[0,0,0]
	v_mfma_scale_f32_16x16x128_f8f6f4 v[88:91], v[8:15], v[48:55], v[88:91], v210, v211 op_sel_hi:[0,0,0]
	s_waitcnt lgkmcnt(0)
	v_mfma_scale_f32_16x16x128_f8f6f4 v[80:83], v[0:7], v[56:63], v[80:83], v210, v211 op_sel_hi:[0,0,0]
	v_mfma_scale_f32_16x16x128_f8f6f4 v[72:75], v[8:15], v[56:63], v[72:75], v210, v211 op_sel_hi:[0,0,0]
	s_setprio 0
	s_setprio 1
	v_mfma_scale_f32_16x16x128_f8f6f4 v[124:127], v[16:23], v[32:39], v[124:127], v210, v211 op_sel_hi:[0,0,0]
	v_mfma_scale_f32_16x16x128_f8f6f4 v[116:119], v[24:31], v[32:39], v[116:119], v210, v211 op_sel_hi:[0,0,0]
	v_mfma_scale_f32_16x16x128_f8f6f4 v[108:111], v[16:23], v[40:47], v[108:111], v210, v211 op_sel_hi:[0,0,0]
	v_mfma_scale_f32_16x16x128_f8f6f4 v[100:103], v[24:31], v[40:47], v[100:103], v210, v211 op_sel_hi:[0,0,0]
	v_mfma_scale_f32_16x16x128_f8f6f4 v[92:95], v[16:23], v[48:55], v[92:95], v210, v211 op_sel_hi:[0,0,0]
	v_mfma_scale_f32_16x16x128_f8f6f4 v[84:87], v[24:31], v[48:55], v[84:87], v210, v211 op_sel_hi:[0,0,0]
	v_mfma_scale_f32_16x16x128_f8f6f4 v[76:79], v[16:23], v[56:63], v[76:79], v210, v211 op_sel_hi:[0,0,0]
	v_mfma_scale_f32_16x16x128_f8f6f4 v[68:71], v[24:31], v[56:63], v[68:71], v210, v211 op_sel_hi:[0,0,0]
	s_setprio 0
	s_barrier
	s_add_u32 s6, s6, 0x100
	s_addc_u32 s7, s7, 0
	s_cmp_ge_i32 s82, s68
	s_cbranch_scc1 .LBB0_749
.LBB0_728:
	ds_read_b128 v[24:27], v207
	ds_read_b128 v[28:31], v207 offset:1024
	ds_read_b128 v[16:19], v207 offset:2048
	ds_read_b128 v[20:23], v207 offset:3072
	ds_read_b128 v[8:11], v208
	ds_read_b128 v[12:15], v208 offset:1024
	ds_read_b128 v[0:3], v208 offset:2048
	ds_read_b128 v[4:7], v208 offset:3072
	s_cmp_eq_u32 s75, s82
	s_cselect_b64 s[38:39], -1, 0
	s_add_u32 s8, s20, s6
	s_addc_u32 s9, s21, s7
	s_add_u32 s8, s8, 0xffffff80
	s_addc_u32 s9, s9, -1
	ds_read_b128 v[56:59], v209
	ds_read_b128 v[60:63], v209 offset:1024
	ds_read_b128 v[48:51], v209 offset:2048
	ds_read_b128 v[52:55], v209 offset:3072
	ds_read_b128 v[40:43], v209 offset:4096
	ds_read_b128 v[44:47], v209 offset:5120
	ds_read_b128 v[32:35], v209 offset:6144
	ds_read_b128 v[36:39], v209 offset:7168
	s_mov_b32 m0, s83
	s_nop 0
	global_load_lds_dwordx4 v66, s[8:9]
	s_and_b64 s[40:41], s[36:37], s[38:39]
	s_mov_b32 m0, s84
	s_nop 0
	global_load_lds_dwordx4 v67, s[8:9]
	s_andn2_b64 vcc, exec, s[40:41]
	s_cbranch_vccnz .LBB0_727
	ds_read_b128 v[64:67], v201
	s_branch .LBB0_727

; #define PG8_STAGE(bufoff, gbase, voff) do { _Pragma("unroll") for (int _i = 0; _i < 2; ++_i) { unsigned keep_; \
;         asm volatile("s_mov_b32 %0, m0\n\ts_mov_b32 m0, %3\n\ts_nop 0\n\tglobal_load_lds_dwordx4 %1, %2\n\ts_mov_b32 m0, %0" : "=&s"(keep_) : "v"((voff)[_i]), "s"((const char*)(gbase)), "s"(ldsb + (unsigned)((bufoff) + _i * 8192)) : "memory"); } } while (0)
; #define PG8_WAIT_V(n) asm volatile("s_waitcnt vmcnt(" #n ")" ::: "memory")
; #define PG8_BAR __builtin_amdgcn_s_barrier()
; template <class Epi, class Sched, bool ALIGN_EPI, bool FP8 = false>
; __device__ __forceinline__ void gemm_phase(PG8_LAS unsigned char* lds, const Gemm g, const Sched& S, const Epi& E, const int wid, const int lane) {
;     ...
;     for (int i = 0; i < 2; ++i) { int R, C; stage_rc(tid * 16 + i * 8192, R, C); const int Rb = Epi::PERM ? ((R & ~31) + perm32(R & 31)) : R;
;         rA[i] = R; cA2[i] = (unsigned)C * 2u; voffA[i] = (unsigned)(R * KB + C * 2); voffB[i] = (unsigned)(Rb * KB + C * 2); }
;     ...
;     const char* cA = GA ? (const char*)g.A : (const char*)g.A + (size_t)cur.pm * tstep; const char* cB = (const char*)g.Bt + (size_t)cur.pn * tstep;
;     PG8_STAGE(PG8_SB(0, 0), cB, voffB); PG8_STAGE(PG8_SB(0, 1), cB + hstep, voffB); PG8_STAGE(PG8_SA(0, 0), cA, vc0); PG8_STAGE(PG8_SA(0, 1), cA + hstepA, vc1);
;     if (wr == 1) PG8_BAR;
;     PG8_WAIT_V(2); PG8_BAR;
;     PG8_STAGE(PG8_SB(1, 0), cB + kstep, voffB); PG8_STAGE(PG8_SA(1, 0), cA + kstep, vc0); PG8_STAGE(PG8_SB(1, 1), cB + hstep + kstep, voffB);
;     PG8_WAIT_V(6); PG8_BAR;
.LBB0_834:
	v_lshlrev_b32_e32 v0, 4, v2
	v_add_u32_e32 v1, s16, v0
	v_ashrrev_i32_e32 v3, 31, v1
	v_lshrrev_b32_e32 v3, 22, v3
	v_add_u32_e32 v3, v1, v3
	v_ashrrev_i32_e32 v3, 10, v3
	v_mul_i32_i24_e32 v4, 0x400, v3
	v_sub_u32_e32 v4, v1, v4
	v_lshrrev_b32_e32 v5, 4, v4
	v_bitop3_b32 v4, v5, v4, 32 bitop3:0x6c
	v_ashrrev_i32_e32 v6, 31, v4
	v_lshrrev_b32_e32 v6, 26, v6
	v_add_u32_e32 v6, v4, v6
	v_ashrrev_i32_e32 v7, 6, v6
	v_and_b32_e32 v6, 0xc0, v6
	v_sub_u32_e32 v4, v4, v6
	v_mov_b32_e32 v6, 1
	v_lshlrev_b32_e32 v5, 3, v3
	v_lshlrev_b32_e32 v3, 5, v3
	v_ashrrev_i16_sdwa v4, v6, sext(v4) dst_sel:DWORD dst_unused:UNUSED_PAD src0_sel:DWORD src1_sel:BYTE_0
	v_and_b32_e32 v5, -16, v5
	v_and_b32_e32 v3, 32, v3
	v_bfe_i32 v4, v4, 0, 16
	v_add_u32_e32 v1, 0x2000, v1
	v_add_u32_e32 v5, v7, v5
	v_add_lshl_u32 v4, v3, v4, 1
	v_ashrrev_i32_e32 v3, 31, v1
	v_lshlrev_b32_e32 v8, 1, v5
	v_lshrrev_b32_e32 v9, 2, v5
	v_and_b32_e32 v7, 3, v7
	s_movk_i32 s5, 0xffe0
	v_lshrrev_b32_e32 v3, 22, v3
	v_and_b32_e32 v8, 24, v8
	v_and_b32_e32 v9, 4, v9
	v_and_or_b32 v7, v5, s5, v7
	v_add_u32_e32 v3, v1, v3
	v_or3_b32 v7, v7, v9, v8
	v_ashrrev_i32_e32 v3, 10, v3
	v_mad_u64_u32 v[160:161], s[6:7], s4, v5, v[4:5]
	v_mad_u64_u32 v[162:163], s[6:7], s4, v7, v[4:5]
	v_mul_i32_i24_e32 v4, 0x400, v3
	v_sub_u32_e32 v1, v1, v4
	v_lshrrev_b32_e32 v4, 4, v1
	v_bitop3_b32 v1, v4, v1, 32 bitop3:0x6c
	v_ashrrev_i32_e32 v5, 31, v1
	v_lshrrev_b32_e32 v5, 26, v5
	v_lshlrev_b32_e32 v4, 3, v3
	v_add_u32_e32 v5, v1, v5
	v_and_b32_e32 v4, -16, v4
	v_ashrrev_i32_e32 v7, 6, v5
	v_add_u32_e32 v8, v7, v4
	v_and_b32_e32 v4, 0xffc0, v5
	v_sub_u32_e32 v1, v1, v4
	v_lshrrev_b16_e32 v4, 7, v1
	v_and_b32_e32 v4, 1, v4
	v_add_u16_e32 v1, v1, v4
	v_ashrrev_i16_sdwa v1, v6, sext(v1) dst_sel:DWORD dst_unused:UNUSED_PAD src0_sel:DWORD src1_sel:BYTE_0
	v_and_b32_e32 v6, 3, v7
	v_and_or_b32 v6, v8, s5, v6
	s_ashr_i32 s5, s4, 31
	v_lshlrev_b32_e32 v3, 5, v3
	v_lshlrev_b32_e32 v4, 1, v8
	v_lshrrev_b32_e32 v5, 2, v8
	s_lshr_b32 s18, s90, 8
	s_lshl_b64 s[12:13], s[4:5], 7
	s_lshl_b64 s[14:15], s[4:5], 8
	s_add_i32 s40, s16, 0
	v_and_b32_e32 v3, 32, v3
	v_bfe_i32 v1, v1, 0, 16
	v_and_b32_e32 v4, 24, v4
	v_and_b32_e32 v5, 4, v5
	s_add_u32 s41, s56, 0x45c00000
	v_or3_b32 v5, v6, v5, v4
	v_add_lshl_u32 v4, v3, v1, 1
	s_addc_u32 s42, s57, 0
	v_mad_u64_u32 v[164:165], s[6:7], s4, v8, v[4:5]
	v_mad_u64_u32 v[166:167], s[6:7], s4, v5, v[4:5]
	s_add_u32 s43, s56, 0x13400000
	s_addc_u32 s44, s57, 0
	s_ashr_i32 s6, s74, 31
	s_mul_i32 s6, s14, s6
	s_mul_hi_u32 s7, s14, s74
	s_add_i32 s8, s7, s6
	s_lshr_b64 s[6:7], s[4:5], 24
	s_mul_i32 s7, s6, s74
	s_add_i32 s9, s8, s7
	s_ashr_i32 s7, s73, 31
	s_mul_i32 s7, s14, s7
	s_mul_hi_u32 s16, s14, s73
	s_add_i32 s7, s16, s7
	s_mul_i32 s6, s6, s73
	s_add_i32 s7, s7, s6
	s_mul_i32 s6, s14, s73
	s_add_u32 s6, s43, s6
	s_addc_u32 s7, s44, s7
	s_add_i32 s45, s40, 0x10000
	s_mov_b32 m0, s45
	s_nop 0
	global_load_lds_dwordx4 v162, s[6:7]
	s_add_i32 s46, s40, 0x12000
	s_mov_b32 m0, s46
	s_nop 0
	global_load_lds_dwordx4 v166, s[6:7]
	s_add_u32 s22, s6, s12
	s_mul_i32 s8, s14, s74
	s_addc_u32 s23, s7, s13
	s_add_i32 s47, s40, 0x14000
	s_mov_b32 m0, s47
	s_nop 0
	global_load_lds_dwordx4 v162, s[22:23]
	s_add_i32 s48, s40, 0x16000
	s_mov_b32 m0, s48
	s_nop 0
	global_load_lds_dwordx4 v166, s[22:23]
	s_add_u32 s8, s41, s8
	s_addc_u32 s9, s42, s9
	s_mov_b32 m0, s40
	s_nop 0
	global_load_lds_dwordx4 v160, s[8:9]
	s_add_i32 s49, s40, 0x2000
	s_mov_b32 m0, s49
	s_nop 0
	global_load_lds_dwordx4 v164, s[8:9]
	s_add_u32 s20, s8, s12
	s_addc_u32 s21, s9, s13
	s_add_i32 s50, s40, 0x4000
	s_mov_b32 m0, s50
	s_nop 0
	global_load_lds_dwordx4 v160, s[20:21]
	s_add_i32 s51, s40, 0x6000
	s_mov_b32 m0, s51
	s_nop 0
	global_load_lds_dwordx4 v164, s[20:21]
	s_cmp_eq_u32 s18, 1
	s_mov_b32 s39, 0
	s_cselect_b64 s[16:17], -1, 0
	s_cmp_lg_u32 s18, 1
	s_cbranch_scc1 .LBB0_836
	s_barrier
.LBB0_836:
	s_lshr_b32 s5, s5, 25
	s_add_i32 s5, s4, s5
	s_bfe_u32 s26, s90, 0x20006
	v_and_b32_e32 v1, 15, v2
	s_ashr_i32 s52, s5, 7
	v_and_b32_e32 v0, 0xfffffc00, v0
	v_lshl_or_b32 v161, s18, 6, v1
	v_lshl_add_u32 v4, s18, 13, v0
	s_add_u32 s18, s56, 0x4dc00000
	s_addc_u32 s19, s57, 0
	s_add_u32 s20, s56, 0x6f600000
	s_addc_u32 s21, s57, 0
	s_add_u32 s24, s6, 0x80
	s_waitcnt vmcnt(2)
	s_barrier
	s_addc_u32 s25, s7, 0
	s_add_i32 s53, s40, 0x18000
	s_mov_b32 m0, s53
	s_nop 0
	global_load_lds_dwordx4 v162, s[24:25]
	s_add_i32 s54, s40, 0x1a000
	s_mov_b32 m0, s54
	s_nop 0
	global_load_lds_dwordx4 v166, s[24:25]
	s_add_u32 s24, s8, 0x80
	s_addc_u32 s25, s9, 0
	s_add_i32 s55, s40, 0x8000
	s_add_i32 s64, s40, 0xa000
	s_mov_b32 m0, s55
	s_nop 0
	global_load_lds_dwordx4 v160, s[24:25]
	s_add_u32 s22, s22, 0x80
	s_mov_b32 m0, s64
	s_nop 0
	global_load_lds_dwordx4 v164, s[24:25]
	s_addc_u32 s23, s23, 0
	s_add_i32 s65, s40, 0x1c000
	s_add_i32 s66, s40, 0x1e000
	v_and_b32_e32 v3, 48, v2
	s_mov_b32 m0, s65
	s_nop 0
	global_load_lds_dwordx4 v162, s[22:23]
	s_cmpk_gt_i32 s4, 0x7f
	v_lshl_or_b32 v1, v1, 6, v3
	v_lshlrev_b32_e32 v3, 2, v2
	s_mov_b32 m0, s66
	s_nop 0
	global_load_lds_dwordx4 v166, s[22:23]
	s_cselect_b64 s[22:23], -1, 0
	s_add_i32 s67, s52, -2
	s_add_i32 s68, s40, 0xc000
	v_and_b32_e32 v3, 32, v3
	v_lshl_add_u32 v0, s26, 12, v0
	s_cmpk_lt_u32 s90, 0x100
	v_bitop3_b32 v4, v1, v4, v3 bitop3:0xde
	v_bitop3_b32 v0, v1, v0, v3 bitop3:0xde
	s_waitcnt vmcnt(6)
	s_cselect_b64 s[24:25], -1, 0
	v_and_b32_e32 v1, -16, v2
	s_ashr_i32 s4, s76, 3
	v_lshl_add_u32 v163, s26, 6, v1
	s_mul_i32 s70, s4, s3
	v_cndmask_b32_e64 v1, 0, 1, s[0:1]
	v_add_u32_e32 v0, 0, v0
	s_add_i32 s69, s40, 0xe000
	s_add_i32 s70, s70, s27
	v_cmp_ne_u32_e64 s[0:1], 1, v1
	v_add_u32_e32 v165, 0x10000, v0
	v_add_u32_e32 v167, 0x14000, v0
	v_add_u32_e32 v169, 0, v4
	v_mov_b32_e32 v170, 0x79
	v_mov_b32_e32 v171, 0x7b
	v_add_u32_e32 v172, 0x18000, v0
	v_add_u32_e32 v173, 0x1c000, v0
	s_mov_b32 s26, 0x41800000
	s_barrier
	s_branch .LBB0_839

; #define PG8_STAGE(bufoff, gbase, voff) do { _Pragma("unroll") for (int _i = 0; _i < 2; ++_i) { unsigned keep_; \
;         asm volatile("s_mov_b32 %0, m0\n\ts_mov_b32 m0, %3\n\ts_nop 0\n\tglobal_load_lds_dwordx4 %1, %2\n\ts_mov_b32 m0, %0" : "=&s"(keep_) : "v"((voff)[_i]), "s"((const char*)(gbase)), "s"(ldsb + (unsigned)((bufoff) + _i * 8192)) : "memory"); } } while (0)
; #define PG8_LDA(dst, b, h) do { _Pragma("unroll") for (int m = 0; m < 4; ++m) _Pragma("unroll") for (int k = 0; k < 2; ++k) dst[m][k] = *(const PG8_LAS bf16x8*)(lds + PG8_SA(b, h) + aoff + m * 2048 + k * 1024); } while (0)
; #define PG8_LDB(dst, b, h) do { _Pragma("unroll") for (int n = 0; n < 2; ++n) _Pragma("unroll") for (int k = 0; k < 2; ++k) dst[n][k] = *(const PG8_LAS bf16x8*)(lds + PG8_SB(b, h) + boff + n * 2048 + k * 1024); } while (0)
; #define PG8_WAIT_V(n) asm volatile("s_waitcnt vmcnt(" #n ")" ::: "memory")
; #define PG8_WAIT_L(n) asm volatile("s_waitcnt lgkmcnt(" #n ")" ::: "memory")
; #define PG8_BAR __builtin_amdgcn_s_barrier()
; #define PG8_SCHED __builtin_amdgcn_sched_barrier(0)
; template <class Epi, class Sched, bool ALIGN_EPI, bool FP8 = false>
; __device__ __forceinline__ void gemm_phase(PG8_LAS unsigned char* lds, const Gemm g, const Sched& S, const Epi& E, const int wid, const int lane) {
;     ...
;         for (int t = 0; t < nt; t += 2) {
;             const bool last = (t == nt - 2);
;             const char* a1 = cA + (size_t)(t + 1) * kstep;
;             const char* a2 = last ? nA : cA + (size_t)(t + 2) * kstep; const char* b2 = last ? nB : cB + (size_t)(t + 2) * kstep;
;             const char* a3 = a2 + kstep; const char* b3 = b2 + kstep;
;             PG8_LDB(B0, 0, 0); PG8_LDB(B1, 0, 1); PG8_SCHED; PG8_LDA(At, 0, 0); PG8_STAGE(PG8_SA(1, 1), a1 + hstepA, vc1);
;             if (GA && last && has_next) { const u32x4 q = *gslot; vc0[0] = q.x; vc0[1] = q.y; vc1[0] = q.z; vc1[1] = q.w; }
;             PG8_WAIT_V(8); PG8_WAIT_L(0); PG8_BAR; PG8_MMA(0, 0, At, B0); PG8_MMA(0, 1, At, B1); PG8_BAR; PG8_SCHED;
;             PG8_LDA(At, 0, 1); PG8_STAGE(PG8_SB(0, 0), b2, voffB); PG8_STAGE(PG8_SB(0, 1), b2 + hstep, voffB); PG8_STAGE(PG8_SA(0, 0), a2, vc0);
;             PG8_WAIT_V(8); PG8_WAIT_L(0); PG8_BAR; PG8_MMA(1, 0, At, B0); PG8_MMA(1, 1, At, B1); PG8_BAR; PG8_SCHED;
.LBB0_852:
	ds_read_b128 v[24:27], v165
	ds_read_b128 v[28:31], v165 offset:1024
	ds_read_b128 v[16:19], v165 offset:2048
	ds_read_b128 v[20:23], v165 offset:3072
	ds_read_b128 v[8:11], v167
	ds_read_b128 v[12:15], v167 offset:1024
	ds_read_b128 v[0:3], v167 offset:2048
	ds_read_b128 v[4:7], v167 offset:3072
	s_add_i32 s33, s8, 2
	s_cmp_eq_u32 s67, s8
	s_cselect_b32 s36, s28, s75
	s_cselect_b32 s37, s29, s82
	s_cselect_b32 s34, s30, s83
	s_cselect_b32 s35, s31, s84
	s_add_u32 s8, s36, 0x80
	s_addc_u32 s9, s37, 0
	ds_read_b128 v[174:177], v169
	ds_read_b128 v[178:181], v169 offset:1024
	ds_read_b128 v[182:185], v169 offset:2048
	ds_read_b128 v[186:189], v169 offset:3072
	ds_read_b128 v[190:193], v169 offset:4096
	ds_read_b128 v[194:197], v169 offset:5120
	ds_read_b128 v[198:201], v169 offset:6144
	ds_read_b128 v[202:205], v169 offset:7168
	s_mov_b32 m0, s68
	s_nop 0
	global_load_lds_dwordx4 v160, s[6:7]
	s_mov_b32 m0, s69
	s_nop 0
	global_load_lds_dwordx4 v164, s[6:7]
	s_waitcnt vmcnt(8)
	s_waitcnt lgkmcnt(0)
	s_barrier
	s_setprio 1
	s_waitcnt lgkmcnt(6)
	v_mfma_scale_f32_16x16x128_f8f6f4 v[156:159], v[24:31], v[174:181], v[156:159], v170, v171 op_sel_hi:[0,0,0]
	v_mfma_scale_f32_16x16x128_f8f6f4 v[152:155], v[16:23], v[174:181], v[152:155], v170, v171 op_sel_hi:[0,0,0]
	s_waitcnt lgkmcnt(4)
	v_mfma_scale_f32_16x16x128_f8f6f4 v[140:143], v[24:31], v[182:189], v[140:143], v170, v171 op_sel_hi:[0,0,0]
	v_mfma_scale_f32_16x16x128_f8f6f4 v[136:139], v[16:23], v[182:189], v[136:139], v170, v171 op_sel_hi:[0,0,0]
	s_waitcnt lgkmcnt(2)
	v_mfma_scale_f32_16x16x128_f8f6f4 v[124:127], v[24:31], v[190:197], v[124:127], v170, v171 op_sel_hi:[0,0,0]
	v_mfma_scale_f32_16x16x128_f8f6f4 v[120:123], v[16:23], v[190:197], v[120:123], v170, v171 op_sel_hi:[0,0,0]
	s_waitcnt lgkmcnt(0)
	v_mfma_scale_f32_16x16x128_f8f6f4 v[108:111], v[24:31], v[198:205], v[108:111], v170, v171 op_sel_hi:[0,0,0]
	v_mfma_scale_f32_16x16x128_f8f6f4 v[104:107], v[16:23], v[198:205], v[104:107], v170, v171 op_sel_hi:[0,0,0]
	s_setprio 0
	s_setprio 1
	v_mfma_scale_f32_16x16x128_f8f6f4 v[148:151], v[8:15], v[174:181], v[148:151], v170, v171 op_sel_hi:[0,0,0]
	v_mfma_scale_f32_16x16x128_f8f6f4 v[144:147], v[0:7], v[174:181], v[144:147], v170, v171 op_sel_hi:[0,0,0]
	v_mfma_scale_f32_16x16x128_f8f6f4 v[132:135], v[8:15], v[182:189], v[132:135], v170, v171 op_sel_hi:[0,0,0]
	v_mfma_scale_f32_16x16x128_f8f6f4 v[128:131], v[0:7], v[182:189], v[128:131], v170, v171 op_sel_hi:[0,0,0]
	v_mfma_scale_f32_16x16x128_f8f6f4 v[116:119], v[8:15], v[190:197], v[116:119], v170, v171 op_sel_hi:[0,0,0]
	v_mfma_scale_f32_16x16x128_f8f6f4 v[112:115], v[0:7], v[190:197], v[112:115], v170, v171 op_sel_hi:[0,0,0]
	v_mfma_scale_f32_16x16x128_f8f6f4 v[100:103], v[8:15], v[198:205], v[100:103], v170, v171 op_sel_hi:[0,0,0]
	v_mfma_scale_f32_16x16x128_f8f6f4 v[96:99], v[0:7], v[198:205], v[96:99], v170, v171 op_sel_hi:[0,0,0]
	s_setprio 0
	s_barrier
	ds_read_b128 v[174:177], v169 offset:16384
	ds_read_b128 v[178:181], v169 offset:17408
	ds_read_b128 v[182:185], v169 offset:18432
	ds_read_b128 v[186:189], v169 offset:19456
	ds_read_b128 v[190:193], v169 offset:20480
	ds_read_b128 v[194:197], v169 offset:21504
	ds_read_b128 v[198:201], v169 offset:22528
	ds_read_b128 v[202:205], v169 offset:23552
	s_mov_b32 m0, s45
	s_nop 0
	global_load_lds_dwordx4 v162, s[34:35]
	s_mov_b32 m0, s46
	s_nop 0
	global_load_lds_dwordx4 v166, s[34:35]
	s_add_u32 s58, s34, s12
	s_addc_u32 s59, s35, s13
	s_mov_b32 m0, s47
	s_nop 0
	global_load_lds_dwordx4 v162, s[58:59]
	s_mov_b32 m0, s48
	s_nop 0
	global_load_lds_dwordx4 v166, s[58:59]
	s_mov_b32 m0, s40
	s_nop 0
	global_load_lds_dwordx4 v160, s[36:37]
	s_mov_b32 m0, s49
	s_nop 0
	global_load_lds_dwordx4 v164, s[36:37]
	s_waitcnt vmcnt(8)
	s_waitcnt lgkmcnt(0)
	s_barrier
	s_setprio 1
	s_waitcnt lgkmcnt(6)
	v_mfma_scale_f32_16x16x128_f8f6f4 v[92:95], v[24:31], v[174:181], v[92:95], v170, v171 op_sel_hi:[0,0,0]
	v_mfma_scale_f32_16x16x128_f8f6f4 v[88:91], v[16:23], v[174:181], v[88:91], v170, v171 op_sel_hi:[0,0,0]
	s_waitcnt lgkmcnt(4)
	v_mfma_scale_f32_16x16x128_f8f6f4 v[76:79], v[24:31], v[182:189], v[76:79], v170, v171 op_sel_hi:[0,0,0]
	v_mfma_scale_f32_16x16x128_f8f6f4 v[72:75], v[16:23], v[182:189], v[72:75], v170, v171 op_sel_hi:[0,0,0]
	s_waitcnt lgkmcnt(2)
	v_mfma_scale_f32_16x16x128_f8f6f4 v[60:63], v[24:31], v[190:197], v[60:63], v170, v171 op_sel_hi:[0,0,0]
	v_mfma_scale_f32_16x16x128_f8f6f4 v[56:59], v[16:23], v[190:197], v[56:59], v170, v171 op_sel_hi:[0,0,0]
	s_waitcnt lgkmcnt(0)
	v_mfma_scale_f32_16x16x128_f8f6f4 v[44:47], v[24:31], v[198:205], v[44:47], v170, v171 op_sel_hi:[0,0,0]
	v_mfma_scale_f32_16x16x128_f8f6f4 v[40:43], v[16:23], v[198:205], v[40:43], v170, v171 op_sel_hi:[0,0,0]
	s_setprio 0
	s_setprio 1
	v_mfma_scale_f32_16x16x128_f8f6f4 v[84:87], v[8:15], v[174:181], v[84:87], v170, v171 op_sel_hi:[0,0,0]
	v_mfma_scale_f32_16x16x128_f8f6f4 v[80:83], v[0:7], v[174:181], v[80:83], v170, v171 op_sel_hi:[0,0,0]
	v_mfma_scale_f32_16x16x128_f8f6f4 v[68:71], v[8:15], v[182:189], v[68:71], v170, v171 op_sel_hi:[0,0,0]
	v_mfma_scale_f32_16x16x128_f8f6f4 v[64:67], v[0:7], v[182:189], v[64:67], v170, v171 op_sel_hi:[0,0,0]
	v_mfma_scale_f32_16x16x128_f8f6f4 v[52:55], v[8:15], v[190:197], v[52:55], v170, v171 op_sel_hi:[0,0,0]
	v_mfma_scale_f32_16x16x128_f8f6f4 v[48:51], v[0:7], v[190:197], v[48:51], v170, v171 op_sel_hi:[0,0,0]
	v_mfma_scale_f32_16x16x128_f8f6f4 v[36:39], v[8:15], v[198:205], v[36:39], v170, v171 op_sel_hi:[0,0,0]
	v_mfma_scale_f32_16x16x128_f8f6f4 v[32:35], v[0:7], v[198:205], v[32:35], v170, v171 op_sel_hi:[0,0,0]
	s_setprio 0
	s_barrier
; #define PG8_STAGE(bufoff, gbase, voff) do { _Pragma("unroll") for (int _i = 0; _i < 2; ++_i) { unsigned keep_; \
;         asm volatile("s_mov_b32 %0, m0\n\ts_mov_b32 m0, %3\n\ts_nop 0\n\tglobal_load_lds_dwordx4 %1, %2\n\ts_mov_b32 m0, %0" : "=&s"(keep_) : "v"((voff)[_i]), "s"((const char*)(gbase)), "s"(ldsb + (unsigned)((bufoff) + _i * 8192)) : "memory"); } } while (0)
; #define PG8_LDA(dst, b, h) do { _Pragma("unroll") for (int m = 0; m < 4; ++m) _Pragma("unroll") for (int k = 0; k < 2; ++k) dst[m][k] = *(const PG8_LAS bf16x8*)(lds + PG8_SA(b, h) + aoff + m * 2048 + k * 1024); } while (0)
; #define PG8_LDB(dst, b, h) do { _Pragma("unroll") for (int n = 0; n < 2; ++n) _Pragma("unroll") for (int k = 0; k < 2; ++k) dst[n][k] = *(const PG8_LAS bf16x8*)(lds + PG8_SB(b, h) + boff + n * 2048 + k * 1024); } while (0)
; #define PG8_WAIT_V(n) asm volatile("s_waitcnt vmcnt(" #n ")" ::: "memory")
; #define PG8_WAIT_L(n) asm volatile("s_waitcnt lgkmcnt(" #n ")" ::: "memory")
; #define PG8_BAR __builtin_amdgcn_s_barrier()
; #define PG8_SCHED __builtin_amdgcn_sched_barrier(0)
; template <class Epi, class Sched, bool ALIGN_EPI, bool FP8 = false>
; __device__ __forceinline__ void gemm_phase(PG8_LAS unsigned char* lds, const Gemm g, const Sched& S, const Epi& E, const int wid, const int lane) {
;     ...
;         for (int t = 0; t < nt; t += 2) {
;             const bool last = (t == nt - 2);
;             const char* a1 = cA + (size_t)(t + 1) * kstep;
;             const char* a2 = last ? nA : cA + (size_t)(t + 2) * kstep; const char* b2 = last ? nB : cB + (size_t)(t + 2) * kstep;
;             const char* a3 = a2 + kstep; const char* b3 = b2 + kstep;
;     ...
;             PG8_LDB(B0, 1, 0); PG8_LDB(B1, 1, 1); PG8_SCHED; PG8_LDA(At, 1, 0); PG8_STAGE(PG8_SA(0, 1), a2 + hstepA, vc1);
;             PG8_WAIT_V(8); PG8_WAIT_L(0); PG8_BAR; PG8_MMA(0, 0, At, B0); PG8_MMA(0, 1, At, B1); PG8_BAR; PG8_SCHED;
;             PG8_LDA(At, 1, 1); PG8_STAGE(PG8_SB(1, 0), b3, voffB); PG8_STAGE(PG8_SB(1, 1), b3 + hstep, voffB); PG8_STAGE(PG8_SA(1, 0), a3, vc0);
;             PG8_WAIT_V(8); PG8_WAIT_L(0); PG8_BAR; PG8_MMA(1, 0, At, B0); PG8_MMA(1, 1, At, B1); PG8_BAR; PG8_SCHED;
	ds_read_b128 v[0:3], v172
	ds_read_b128 v[4:7], v172 offset:1024
	ds_read_b128 v[8:11], v172 offset:2048
	ds_read_b128 v[12:15], v172 offset:3072
	ds_read_b128 v[16:19], v173
	ds_read_b128 v[20:23], v173 offset:1024
	ds_read_b128 v[24:27], v173 offset:2048
	ds_read_b128 v[28:31], v173 offset:3072
	ds_read_b128 v[174:177], v169 offset:32768
	ds_read_b128 v[178:181], v169 offset:33792
	ds_read_b128 v[182:185], v169 offset:34816
	ds_read_b128 v[186:189], v169 offset:35840
	ds_read_b128 v[190:193], v169 offset:36864
	ds_read_b128 v[194:197], v169 offset:37888
	ds_read_b128 v[198:201], v169 offset:38912
	ds_read_b128 v[202:205], v169 offset:39936
	s_add_u32 s36, s36, s12
	s_addc_u32 s37, s37, s13
	s_mov_b32 m0, s50
	s_nop 0
	global_load_lds_dwordx4 v160, s[36:37]
	s_mov_b32 m0, s51
	s_nop 0
	global_load_lds_dwordx4 v164, s[36:37]
	s_waitcnt vmcnt(8)
	s_waitcnt lgkmcnt(0)
	s_barrier
	s_setprio 1
	s_waitcnt lgkmcnt(6)
	v_mfma_scale_f32_16x16x128_f8f6f4 v[156:159], v[0:7], v[174:181], v[156:159], v170, v171 op_sel_hi:[0,0,0]
	v_mfma_scale_f32_16x16x128_f8f6f4 v[152:155], v[8:15], v[174:181], v[152:155], v170, v171 op_sel_hi:[0,0,0]
	s_waitcnt lgkmcnt(4)
	v_mfma_scale_f32_16x16x128_f8f6f4 v[140:143], v[0:7], v[182:189], v[140:143], v170, v171 op_sel_hi:[0,0,0]
	v_mfma_scale_f32_16x16x128_f8f6f4 v[136:139], v[8:15], v[182:189], v[136:139], v170, v171 op_sel_hi:[0,0,0]
	s_waitcnt lgkmcnt(2)
	v_mfma_scale_f32_16x16x128_f8f6f4 v[124:127], v[0:7], v[190:197], v[124:127], v170, v171 op_sel_hi:[0,0,0]
	v_mfma_scale_f32_16x16x128_f8f6f4 v[120:123], v[8:15], v[190:197], v[120:123], v170, v171 op_sel_hi:[0,0,0]
	s_waitcnt lgkmcnt(0)
	v_mfma_scale_f32_16x16x128_f8f6f4 v[108:111], v[0:7], v[198:205], v[108:111], v170, v171 op_sel_hi:[0,0,0]
	v_mfma_scale_f32_16x16x128_f8f6f4 v[104:107], v[8:15], v[198:205], v[104:107], v170, v171 op_sel_hi:[0,0,0]
	s_setprio 0
	s_setprio 1
	v_mfma_scale_f32_16x16x128_f8f6f4 v[148:151], v[16:23], v[174:181], v[148:151], v170, v171 op_sel_hi:[0,0,0]
	v_mfma_scale_f32_16x16x128_f8f6f4 v[144:147], v[24:31], v[174:181], v[144:147], v170, v171 op_sel_hi:[0,0,0]
	v_mfma_scale_f32_16x16x128_f8f6f4 v[132:135], v[16:23], v[182:189], v[132:135], v170, v171 op_sel_hi:[0,0,0]
	v_mfma_scale_f32_16x16x128_f8f6f4 v[128:131], v[24:31], v[182:189], v[128:131], v170, v171 op_sel_hi:[0,0,0]
	v_mfma_scale_f32_16x16x128_f8f6f4 v[116:119], v[16:23], v[190:197], v[116:119], v170, v171 op_sel_hi:[0,0,0]
	v_mfma_scale_f32_16x16x128_f8f6f4 v[112:115], v[24:31], v[190:197], v[112:115], v170, v171 op_sel_hi:[0,0,0]
	v_mfma_scale_f32_16x16x128_f8f6f4 v[100:103], v[16:23], v[198:205], v[100:103], v170, v171 op_sel_hi:[0,0,0]
	v_mfma_scale_f32_16x16x128_f8f6f4 v[96:99], v[24:31], v[198:205], v[96:99], v170, v171 op_sel_hi:[0,0,0]
	s_setprio 0
	s_barrier
	ds_read_b128 v[174:177], v169 offset:49152
	ds_read_b128 v[178:181], v169 offset:50176
	ds_read_b128 v[182:185], v169 offset:51200
	ds_read_b128 v[186:189], v169 offset:52224
	ds_read_b128 v[190:193], v169 offset:53248
	ds_read_b128 v[194:197], v169 offset:54272
	ds_read_b128 v[198:201], v169 offset:55296
	ds_read_b128 v[202:205], v169 offset:56320
	s_add_u32 s34, s34, 0x80
	s_addc_u32 s35, s35, 0
	s_mov_b32 m0, s53
	s_nop 0
	global_load_lds_dwordx4 v162, s[34:35]
	s_mov_b32 m0, s54
	s_nop 0
	global_load_lds_dwordx4 v166, s[34:35]
	s_add_u32 s34, s34, s12
	s_addc_u32 s35, s35, s13
	s_mov_b32 m0, s65
	s_nop 0
	global_load_lds_dwordx4 v162, s[34:35]
	s_mov_b32 m0, s66
	s_nop 0
	global_load_lds_dwordx4 v166, s[34:35]
	s_mov_b32 m0, s55
	s_nop 0
	global_load_lds_dwordx4 v160, s[8:9]
	s_mov_b32 m0, s64
	s_nop 0
	global_load_lds_dwordx4 v164, s[8:9]
	s_waitcnt vmcnt(8)
	s_waitcnt lgkmcnt(0)
	s_barrier
	s_setprio 1
	s_waitcnt lgkmcnt(6)
	v_mfma_scale_f32_16x16x128_f8f6f4 v[92:95], v[0:7], v[174:181], v[92:95], v170, v171 op_sel_hi:[0,0,0]
	v_mfma_scale_f32_16x16x128_f8f6f4 v[88:91], v[8:15], v[174:181], v[88:91], v170, v171 op_sel_hi:[0,0,0]
	s_waitcnt lgkmcnt(4)
	v_mfma_scale_f32_16x16x128_f8f6f4 v[76:79], v[0:7], v[182:189], v[76:79], v170, v171 op_sel_hi:[0,0,0]
	v_mfma_scale_f32_16x16x128_f8f6f4 v[72:75], v[8:15], v[182:189], v[72:75], v170, v171 op_sel_hi:[0,0,0]
	s_waitcnt lgkmcnt(2)
	v_mfma_scale_f32_16x16x128_f8f6f4 v[60:63], v[0:7], v[190:197], v[60:63], v170, v171 op_sel_hi:[0,0,0]
	v_mfma_scale_f32_16x16x128_f8f6f4 v[56:59], v[8:15], v[190:197], v[56:59], v170, v171 op_sel_hi:[0,0,0]
	s_waitcnt lgkmcnt(0)
	v_mfma_scale_f32_16x16x128_f8f6f4 v[44:47], v[0:7], v[198:205], v[44:47], v170, v171 op_sel_hi:[0,0,0]
	v_mfma_scale_f32_16x16x128_f8f6f4 v[40:43], v[8:15], v[198:205], v[40:43], v170, v171 op_sel_hi:[0,0,0]
	s_setprio 0
	s_setprio 1
	v_mfma_scale_f32_16x16x128_f8f6f4 v[84:87], v[16:23], v[174:181], v[84:87], v170, v171 op_sel_hi:[0,0,0]
	v_mfma_scale_f32_16x16x128_f8f6f4 v[80:83], v[24:31], v[174:181], v[80:83], v170, v171 op_sel_hi:[0,0,0]
	v_mfma_scale_f32_16x16x128_f8f6f4 v[68:71], v[16:23], v[182:189], v[68:71], v170, v171 op_sel_hi:[0,0,0]
	v_mfma_scale_f32_16x16x128_f8f6f4 v[64:67], v[24:31], v[182:189], v[64:67], v170, v171 op_sel_hi:[0,0,0]
	v_mfma_scale_f32_16x16x128_f8f6f4 v[52:55], v[16:23], v[190:197], v[52:55], v170, v171 op_sel_hi:[0,0,0]
	v_mfma_scale_f32_16x16x128_f8f6f4 v[48:51], v[24:31], v[190:197], v[48:51], v170, v171 op_sel_hi:[0,0,0]
	v_mfma_scale_f32_16x16x128_f8f6f4 v[36:39], v[16:23], v[198:205], v[36:39], v170, v171 op_sel_hi:[0,0,0]
	v_mfma_scale_f32_16x16x128_f8f6f4 v[32:35], v[24:31], v[198:205], v[32:35], v170, v171 op_sel_hi:[0,0,0]
	s_setprio 0
	s_barrier
	s_add_u32 s75, s75, 0x100
	s_addc_u32 s82, s82, 0
	s_add_u32 s83, s83, 0x100
	s_addc_u32 s84, s84, 0
	s_add_u32 s6, s6, 0x100
	s_addc_u32 s7, s7, 0
	s_cmp_ge_i32 s33, s52
	s_mov_b32 s8, s33
	s_cbranch_scc0 .LBB0_852

; #define GAS __attribute__((address_space(1)))
; __device__ __forceinline__ void refresh(Frame& F) { int l = (int)__builtin_amdgcn_mbcnt_hi(~0u, __builtin_amdgcn_mbcnt_lo(~0u, 0u)); asm volatile("" : "+v"(l)); F.lane = l; F.tid = F.wave * 64 + l; }
; template <int l>
; __device__ __forceinline__ void layer_phases(Frame& F, const XcdBarrier& bar, const int lo, const int hi) {
;     ...
;         if (IN(pb + 6)) for (int rep = 0; rep < NREP(8); ++rep) {
;             refresh(F);
;             const unsigned char* yb = ws + WS_YBUF; const bf16* x1 = (const bf16*)(ws + WS_X1); bf16* x2b = (bf16*)(ws + WS_X2B);
;             const int* tinfo = (const int*)(ws + WS_TINFO); const float* gates = (const float*)(ws + WS_GATE);
;             const float* g2 = inptr<const float>(F, I_LN2G) + (size_t)l * D; const float* b2 = inptr<const float>(F, I_LN2B) + (size_t)l * D; float* Fout = inptr<float>(F, I_OUT);
;             auto row_of = [&](const int m_) { return (F.G == 256) ? (2048 * ((m_ >> 3) & 7) + 8 * ((m_ & 2047) >> 6) + (m_ & 7) + 256 * (m_ >> 11)) : m_; };
;             auto load_row = [&](const int m, v4u (&xr)[4], v4u (&yr)[14], float& gtv) {
;                 int ln = F.lane; asm volatile("" : "+v"(ln));
;                 gtv = 0.f; if (ln < 6) gtv = gates[(size_t)m * 6 + ln];
; #pragma unroll
;                 for (int jh = 0; jh < 2; ++jh) { xr[2 * jh] = __builtin_nontemporal_load((const GAS v4u*)(x1 + (size_t)m * D + 16 * ln + 1024 * jh)); xr[2 * jh + 1] = __builtin_nontemporal_load((const GAS v4u*)(x1 + (size_t)m * D + 16 * ln + 1024 * jh + 8)); }
; #pragma unroll
;                 for (int jh = 0; jh < 2; ++jh)
; #pragma unroll
;                     for (int q = 0; q < 7; ++q) yr[7 * jh + q] = __builtin_nontemporal_load((const GAS v4u*)(yb + ((size_t)m * 7 + q) * D + 16 * ln + 1024 * jh));
;                 asm volatile("" ::: "memory");
;             };
.LBB0_964:
	s_cmp_gt_i32 s92, 8
	s_cselect_b64 s[0:1], -1, 0
	s_cmp_lt_i32 s93, 9
	s_cselect_b64 s[4:5], -1, 0
	s_or_b64 s[0:1], s[0:1], s[4:5]
	s_and_b64 vcc, exec, s[0:1]
	s_cbranch_vccnz .LBB0_1042
	s_add_i32 s0, 0, 0x21498
	v_mov_b32_e32 v206, v216
	v_mov_b32_e32 v0, s0
	ds_read2_b64 v[0:3], v0 offset1:1
	s_cmpk_gt_i32 s79, 0x3fff
	s_waitcnt lgkmcnt(0)
	v_readfirstlane_b32 s7, v1
	v_readfirstlane_b32 s6, v0
	v_readfirstlane_b32 s9, v3
	v_readfirstlane_b32 s8, v2
	s_nop 0
	s_lshl_b32 s98, s80, 10
	v_lshl_add_u32 v238, v216, 4, s98
	s_add_u32 s100, s56, 0x10a000
	s_addc_u32 s101, s57, 0
	global_load_dwordx4 v[100:103], v238, s[100:101]
	s_add_u32 s100, s100, 0xc000
	s_addc_u32 s101, s101, 0
	global_load_dwordx4 v[104:107], v238, s[100:101]
	s_add_u32 s100, s100, 0xc000
	s_addc_u32 s101, s101, 0
	global_load_dwordx4 v[108:111], v238, s[100:101]
	s_add_u32 s100, s100, 0xc000
	s_addc_u32 s101, s101, 0
	global_load_dwordx4 v[112:115], v238, s[100:101]
	s_add_u32 s100, s100, 0xc000
	s_addc_u32 s101, s101, 0
	global_load_dwordx4 v[116:119], v238, s[100:101]
	s_add_u32 s100, s100, 0xc000
	s_addc_u32 s101, s101, 0
	global_load_dwordx4 v[120:123], v238, s[100:101]
	s_add_u32 s100, s100, 0xc000
	s_addc_u32 s101, s101, 0
	global_load_dwordx4 v[124:127], v238, s[100:101]
	s_add_u32 s100, s100, 0xc000
	s_addc_u32 s101, s101, 0
	global_load_dwordx4 v[128:131], v238, s[100:101]
	global_load_dwordx4 v[132:135], v238, s[6:7]
	global_load_dwordx4 v[136:139], v238, s[8:9]
	v_add_u32_e32 v239, 0x10000, v238
	s_waitcnt vmcnt(9)
	ds_write_b128 v238, v[100:103] offset:0
	s_waitcnt vmcnt(8)
	ds_write_b128 v238, v[104:107] offset:8192
	s_waitcnt vmcnt(7)
	ds_write_b128 v238, v[108:111] offset:16384
	s_waitcnt vmcnt(6)
	ds_write_b128 v238, v[112:115] offset:24576
	s_waitcnt vmcnt(5)
	ds_write_b128 v238, v[116:119] offset:32768
	s_waitcnt vmcnt(4)
	ds_write_b128 v238, v[120:123] offset:40960
	s_waitcnt vmcnt(3)
	ds_write_b128 v238, v[124:127] offset:49152
	s_waitcnt vmcnt(2)
	ds_write_b128 v238, v[128:131] offset:57344
	s_waitcnt vmcnt(1)
	ds_write_b128 v239, v[132:135]
	s_waitcnt vmcnt(0)
	ds_write_b128 v239, v[136:139] offset:8192
	s_sub_u32 s98, 0x10000, s6
	s_sub_u32 s99, 0x12000, s8
	s_waitcnt lgkmcnt(0)
	s_barrier
	s_cmpk_gt_i32 s79, 0x3fff
	s_cbranch_scc1 .LBB0_988
	s_add_u32 s3, s56, 0x900000
	s_addc_u32 s25, s57, 0
	s_ashr_i32 s0, s79, 3
	s_lshr_b32 s1, s79, 3
	s_and_b32 s0, s0, 0xffffff00
	s_and_b32 s1, s1, 0xf8
	s_lshl_b32 s41, s79, 8
	s_bfe_u32 s27, s90, 0x30006
	s_or_b32 s0, s0, s1
	s_and_b32 s1, s41, 0x3800
	s_or_b32 s1, s1, s27
	s_add_i32 s4, s1, s0
	s_cmpk_eq_i32 s76, 0x100
	s_cselect_b64 s[10:11], -1, 0
	s_and_b64 s[0:1], s[10:11], exec
	s_cselect_b32 s0, s4, s79
	v_mov_b32_e32 v0, v206
	s_ashr_i32 s1, s0, 31
	v_cmp_gt_i32_e32 vcc, 6, v0
	v_mov_b32_e32 v207, 0
	v_mov_b32_e32 v208, 0
	s_and_saveexec_b64 s[4:5], vcc
	s_cbranch_execz .LBB0_968
	s_mul_i32 s12, s0, 24
	s_mul_hi_i32 s13, s0, 24
	s_add_u32 s12, s3, s12
	v_ashrrev_i32_e32 v1, 31, v0
	s_addc_u32 s13, s25, s13
	v_lshl_add_u64 v[2:3], v[0:1], 2, s[12:13]
	global_load_dword v208, v[2:3], off

; #define GAS __attribute__((address_space(1)))
; __device__ __forceinline__ f32x4 bf4(unsigned a, unsigned b) { return (f32x4){bflo(a), bfhi(a), bflo(b), bfhi(b)}; }
; template <int l>
; __device__ __forceinline__ void layer_phases(Frame& F, const XcdBarrier& bar, const int lo, const int hi) {
;     ...
;             auto process_row = [&](const int m, v4u (&xr)[4], v4u (&yr)[14], const float gtv) {
;                 int ln = F.lane; asm volatile("" : "+v"(ln));
;                 const float* mrow = (const float*)(ws + WS_MOD) + ((size_t)l * 8 + (m >> 11)) * 12288;
;                 float gt[7];
; #pragma unroll
;                 for (int k = 0; k < 6; ++k) gt[k] = __uint_as_float((unsigned)__builtin_amdgcn_readlane((int)__float_as_uint(gtv), k));
;                 gt[6] = 1.0f;
;                 f32x4 v[8]; float s = 0.f;
; #pragma unroll
;                 for (int jh = 0; jh < 2; ++jh) { const v4u xa = xr[2 * jh], xb = xr[2 * jh + 1];
;                     v[4 * jh] = bf4(xa.x, xa.y); v[4 * jh + 1] = bf4(xa.z, xa.w); v[4 * jh + 2] = bf4(xb.x, xb.y); v[4 * jh + 3] = bf4(xb.z, xb.w); }
; #pragma unroll
;                 for (int jh = 0; jh < 2; ++jh) {
; #pragma unroll
;                     for (int i = 0; i < 4; ++i) { const int j = 4 * jh + i, k = 16 * ln + 1024 * jh + 4 * i; f32x4 f = (f32x4){0.f, 0.f, 0.f, 0.f};
; #pragma unroll
;                         for (int q = 0; q < 7; ++q) { const unsigned w = yr[7 * jh + q][i]; const float gq = gt[q];
;                             const auto lo2 = __builtin_amdgcn_cvt_pk_f32_fp8((int)w, false), hi2 = __builtin_amdgcn_cvt_pk_f32_fp8((int)w, true);
;                             f.x += gq * lo2[0]; f.y += gq * lo2[1]; f.z += gq * hi2[0]; f.w += gq * hi2[1]; }
;                         v[j] = v[j] * ALPHA + *(const GAS f32x4*)(mrow + 10240 + k) * (f * (1.0f / (float)(1 << YSHIFT)));
;                         s += (v[j].x + v[j].y) + (v[j].z + v[j].w); }
.LBB0_969:
	v_cvt_pk_f32_fp8_sdwa v[146:147], v100 src0_sel:WORD_1
	v_mov_b32_e32 v144, v206
	v_cvt_pk_f32_fp8_sdwa v[150:151], v104 src0_sel:WORD_1
	v_cvt_pk_f32_fp8_sdwa v[158:159], v96 src0_sel:WORD_1
	v_readlane_b32 s42, v207, 0
	v_lshlrev_b32_e32 v156, 4, v144
	v_cvt_pk_f32_fp8_e32 v[144:145], v100
	v_cvt_pk_f32_fp8_sdwa v[192:193], v112 src0_sel:WORD_1
	v_readlane_b32 s40, v207, 1
	v_cvt_pk_f32_fp8_e32 v[148:149], v104
	v_cvt_pk_f32_fp8_sdwa v[196:197], v88 src0_sel:WORD_1
	v_pk_fma_f32 v[146:147], s[42:43], v[146:147], 0 op_sel_hi:[0,1,0]
	v_readlane_b32 s38, v207, 2
	v_cvt_pk_f32_fp8_e32 v[152:153], v96
	v_cvt_pk_f32_fp8_sdwa v[200:201], v92 src0_sel:WORD_1
	v_pk_fma_f32 v[146:147], s[40:41], v[150:151], v[146:147] op_sel_hi:[0,1,1]
	s_ashr_i32 s0, s30, 11
	s_lshl_b32 s100, s0, 13
	v_readlane_b32 s36, v207, 3
	v_cvt_pk_f32_fp8_e32 v[190:191], v112
	v_cvt_pk_f32_fp8_sdwa v[204:205], v108 src0_sel:WORD_1
	v_pk_fma_f32 v[146:147], s[38:39], v[158:159], v[146:147] op_sel_hi:[0,1,1]
	s_mul_i32 s31, s0, 0xc000
	v_readlane_b32 s34, v207, 4
	v_cvt_pk_f32_fp8_e32 v[194:195], v88
	v_pk_fma_f32 v[144:145], s[42:43], v[144:145], 0 op_sel_hi:[0,1,0]
	v_pk_fma_f32 v[146:147], s[36:37], v[192:193], v[146:147] op_sel_hi:[0,1,1]
	s_mul_hi_i32 s1, s0, 0xc000
	v_readlane_b32 s0, v207, 5
	s_add_u32 s44, s56, s31
	v_cvt_pk_f32_fp8_e32 v[198:199], v92
	v_pk_fma_f32 v[144:145], s[40:41], v[148:149], v[144:145] op_sel_hi:[0,1,1]
	v_pk_fma_f32 v[146:147], s[34:35], v[196:197], v[146:147] op_sel_hi:[0,1,1]
	v_ashrrev_i32_e32 v157, 31, v156
	s_addc_u32 s45, s57, s1
	s_sub_u32 s100, s100, s44
	s_sub_u32 s100, s100, 0x10a000
	v_cvt_pk_f32_fp8_e32 v[202:203], v108
	v_pk_fma_f32 v[144:145], s[38:39], v[152:153], v[144:145] op_sel_hi:[0,1,1]
	v_pk_fma_f32 v[146:147], s[0:1], v[200:201], v[146:147] op_sel_hi:[0,1,1]
	v_lshlrev_b64 v[158:159], 2, v[156:157]
	v_pk_fma_f32 v[144:145], s[36:37], v[190:191], v[144:145] op_sel_hi:[0,1,1]
	v_pk_add_f32 v[190:191], v[146:147], v[204:205]
	v_lshl_add_u64 v[204:205], s[44:45], 0, v[158:159]
	v_pk_fma_f32 v[144:145], s[34:35], v[194:195], v[144:145] op_sel_hi:[0,1,1]
	v_add_co_u32_e32 v152, vcc, s67, v204
	v_pk_fma_f32 v[144:145], s[0:1], v[198:199], v[144:145] op_sel_hi:[0,1,1]
	v_lshl_add_u64 v[198:199], v[204:205], 0, s[22:23]
	v_addc_co_u32_e32 v153, vcc, 0, v205, vcc
	v_pk_add_f32 v[192:193], v[144:145], v[202:203]
	v_add_u32_e32 v247, s100, v152
	v_add_u32_e32 v247, 0xfffff000, v247
	ds_read_b128 v[194:197], v247
	v_add_u32_e32 v247, s100, v198
	ds_read_b128 v[144:147], v247 offset:48
	v_add_u32_e32 v247, s100, v198
	ds_read_b128 v[148:151], v247 offset:32
	s_nop 0
	v_add_u32_e32 v247, s100, v198
	ds_read_b128 v[198:201], v247 offset:16
	v_pk_mul_f32 v[192:193], v[192:193], s[24:25] op_sel_hi:[1,0]
	v_pk_mul_f32 v[190:191], v[190:191], s[24:25] op_sel_hi:[1,0]
	v_lshlrev_b32_e32 v186, 16, v68
	v_and_b32_e32 v187, 0xffff0000, v68
	v_lshlrev_b32_e32 v188, 16, v69
	v_and_b32_e32 v189, 0xffff0000, v69
	v_cvt_pk_f32_fp8_e32 v[202:203], v97
	v_cvt_pk_f32_fp8_sdwa v[218:219], v97 src0_sel:WORD_1
	v_cvt_pk_f32_fp8_e32 v[220:221], v113
	v_cvt_pk_f32_fp8_sdwa v[222:223], v113 src0_sel:WORD_1
	v_cvt_pk_f32_fp8_e32 v[224:225], v89
	v_cvt_pk_f32_fp8_sdwa v[226:227], v89 src0_sel:WORD_1
	v_cvt_pk_f32_fp8_e32 v[228:229], v93
	v_cvt_pk_f32_fp8_sdwa v[230:231], v93 src0_sel:WORD_1
	v_cvt_pk_f32_fp8_e32 v[232:233], v109
	v_cvt_pk_f32_fp8_sdwa v[234:235], v109 src0_sel:WORD_1
	v_lshlrev_b32_e32 v178, 16, v70
	v_and_b32_e32 v179, 0xffff0000, v70
	v_lshlrev_b32_e32 v176, 16, v71
	v_and_b32_e32 v177, 0xffff0000, v71
	v_lshlrev_b32_e32 v182, 16, v72
	v_and_b32_e32 v183, 0xffff0000, v72
	v_lshlrev_b32_e32 v180, 16, v73
	v_and_b32_e32 v181, 0xffff0000, v73
	v_lshlrev_b32_e32 v154, 16, v74
	v_and_b32_e32 v155, 0xffff0000, v74
	v_lshlrev_b32_e32 v184, 16, v75
	v_and_b32_e32 v185, 0xffff0000, v75
	v_lshl_add_u64 v[204:205], v[204:205], 0, s[28:29]
	v_lshlrev_b32_e32 v172, 16, v80
	v_and_b32_e32 v173, 0xffff0000, v80
	v_lshlrev_b32_e32 v174, 16, v81
	v_and_b32_e32 v175, 0xffff0000, v81
	v_lshlrev_b32_e32 v168, 16, v82
	v_and_b32_e32 v169, 0xffff0000, v82
	v_lshlrev_b32_e32 v170, 16, v83
	v_and_b32_e32 v171, 0xffff0000, v83
	v_lshlrev_b32_e32 v164, 16, v84
	v_and_b32_e32 v165, 0xffff0000, v84
	v_lshlrev_b32_e32 v166, 16, v85
	v_and_b32_e32 v167, 0xffff0000, v85
	v_lshlrev_b32_e32 v160, 16, v86
	v_and_b32_e32 v161, 0xffff0000, v86
	v_lshlrev_b32_e32 v162, 16, v87
	v_and_b32_e32 v163, 0xffff0000, v87
	s_ashr_i32 s31, s30, 31
	s_waitcnt lgkmcnt(0)
	v_pk_mul_f32 v[190:191], v[196:197], v[190:191]
	v_pk_mul_f32 v[192:193], v[194:195], v[192:193]
	v_pk_fma_f32 v[188:189], v[188:189], s[26:27], v[190:191] op_sel_hi:[1,0,1]
	v_pk_fma_f32 v[190:191], v[186:187], s[26:27], v[192:193] op_sel_hi:[1,0,1]
	v_cvt_pk_f32_fp8_e32 v[186:187], v101
	v_cvt_pk_f32_fp8_sdwa v[192:193], v101 src0_sel:WORD_1
	v_cvt_pk_f32_fp8_e32 v[194:195], v105
	v_cvt_pk_f32_fp8_sdwa v[196:197], v105 src0_sel:WORD_1
	v_pk_fma_f32 v[186:187], s[42:43], v[186:187], 0 op_sel_hi:[0,1,0]
	v_pk_fma_f32 v[192:193], s[42:43], v[192:193], 0 op_sel_hi:[0,1,0]
	v_pk_fma_f32 v[186:187], s[40:41], v[194:195], v[186:187] op_sel_hi:[0,1,1]
	v_pk_fma_f32 v[192:193], s[40:41], v[196:197], v[192:193] op_sel_hi:[0,1,1]
	v_pk_fma_f32 v[186:187], s[38:39], v[202:203], v[186:187] op_sel_hi:[0,1,1]
	v_pk_fma_f32 v[192:193], s[38:39], v[218:219], v[192:193] op_sel_hi:[0,1,1]
	v_pk_fma_f32 v[186:187], s[36:37], v[220:221], v[186:187] op_sel_hi:[0,1,1]
	v_pk_fma_f32 v[192:193], s[36:37], v[222:223], v[192:193] op_sel_hi:[0,1,1]
	v_pk_fma_f32 v[186:187], s[34:35], v[224:225], v[186:187] op_sel_hi:[0,1,1]
	v_pk_fma_f32 v[192:193], s[34:35], v[226:227], v[192:193] op_sel_hi:[0,1,1]
	v_pk_fma_f32 v[186:187], s[0:1], v[228:229], v[186:187] op_sel_hi:[0,1,1]
	v_pk_fma_f32 v[192:193], s[0:1], v[230:231], v[192:193] op_sel_hi:[0,1,1]
	v_pk_add_f32 v[186:187], v[186:187], v[232:233]
	v_pk_add_f32 v[192:193], v[192:193], v[234:235]
	v_pk_mul_f32 v[186:187], v[186:187], s[24:25] op_sel_hi:[1,0]
	v_pk_mul_f32 v[192:193], v[192:193], s[24:25] op_sel_hi:[1,0]
	s_waitcnt lgkmcnt(0)
; #define GAS __attribute__((address_space(1)))
; template <int l>
; __device__ __forceinline__ void layer_phases(Frame& F, const XcdBarrier& bar, const int lo, const int hi) {
;     ...
;                 for (int jh = 0; jh < 2; ++jh) {
; #pragma unroll
;                     for (int i = 0; i < 4; ++i) { const int j = 4 * jh + i, k = 16 * ln + 1024 * jh + 4 * i; f32x4 f = (f32x4){0.f, 0.f, 0.f, 0.f};
; #pragma unroll
;                         for (int q = 0; q < 7; ++q) { const unsigned w = yr[7 * jh + q][i]; const float gq = gt[q];
;                             const auto lo2 = __builtin_amdgcn_cvt_pk_f32_fp8((int)w, false), hi2 = __builtin_amdgcn_cvt_pk_f32_fp8((int)w, true);
;                             f.x += gq * lo2[0]; f.y += gq * lo2[1]; f.z += gq * hi2[0]; f.w += gq * hi2[1]; }
;                         v[j] = v[j] * ALPHA + *(const GAS f32x4*)(mrow + 10240 + k) * (f * (1.0f / (float)(1 << YSHIFT)));
;                         s += (v[j].x + v[j].y) + (v[j].z + v[j].w); }
	v_pk_mul_f32 v[186:187], v[198:199], v[186:187]
	v_pk_mul_f32 v[192:193], v[200:201], v[192:193]
	v_pk_fma_f32 v[178:179], v[178:179], s[26:27], v[186:187] op_sel_hi:[1,0,1]
	v_pk_fma_f32 v[176:177], v[176:177], s[26:27], v[192:193] op_sel_hi:[1,0,1]
	v_mov_b32_e32 v186, v190
	v_mov_b32_e32 v187, v178
	v_mov_b32_e32 v192, v191
	v_mov_b32_e32 v193, v179
	v_pk_add_f32 v[186:187], v[186:187], v[192:193]
	v_mov_b32_e32 v192, v188
	v_mov_b32_e32 v193, v176
	v_mov_b32_e32 v194, v189
	v_mov_b32_e32 v195, v177
	v_pk_add_f32 v[192:193], v[192:193], v[194:195]
	v_cvt_pk_f32_fp8_sdwa v[194:195], v102 src0_sel:WORD_1
	v_pk_add_f32 v[186:187], v[186:187], v[192:193]
	v_cvt_pk_f32_fp8_e32 v[196:197], v106
	v_add_f32_e32 v186, 0, v186
	v_add_f32_e32 v192, v186, v187
	v_cvt_pk_f32_fp8_e32 v[186:187], v102
	v_cvt_pk_f32_fp8_sdwa v[198:199], v106 src0_sel:WORD_1
	v_cvt_pk_f32_fp8_e32 v[200:201], v98
	v_cvt_pk_f32_fp8_sdwa v[202:203], v98 src0_sel:WORD_1
	v_cvt_pk_f32_fp8_e32 v[218:219], v114
	v_cvt_pk_f32_fp8_sdwa v[220:221], v114 src0_sel:WORD_1
	v_cvt_pk_f32_fp8_e32 v[222:223], v90
	v_cvt_pk_f32_fp8_sdwa v[224:225], v90 src0_sel:WORD_1
	v_pk_fma_f32 v[194:195], s[42:43], v[194:195], 0 op_sel_hi:[0,1,0]
	v_pk_fma_f32 v[186:187], s[42:43], v[186:187], 0 op_sel_hi:[0,1,0]
	v_cvt_pk_f32_fp8_e32 v[226:227], v94
	v_cvt_pk_f32_fp8_sdwa v[228:229], v94 src0_sel:WORD_1
	v_pk_fma_f32 v[186:187], s[40:41], v[196:197], v[186:187] op_sel_hi:[0,1,1]
	v_pk_fma_f32 v[194:195], s[40:41], v[198:199], v[194:195] op_sel_hi:[0,1,1]
	v_cvt_pk_f32_fp8_e32 v[230:231], v110
	v_cvt_pk_f32_fp8_sdwa v[232:233], v110 src0_sel:WORD_1
	v_pk_fma_f32 v[194:195], s[38:39], v[202:203], v[194:195] op_sel_hi:[0,1,1]
	v_pk_fma_f32 v[186:187], s[38:39], v[200:201], v[186:187] op_sel_hi:[0,1,1]
	v_pk_fma_f32 v[186:187], s[36:37], v[218:219], v[186:187] op_sel_hi:[0,1,1]
	v_pk_fma_f32 v[194:195], s[36:37], v[220:221], v[194:195] op_sel_hi:[0,1,1]
	v_pk_fma_f32 v[194:195], s[34:35], v[224:225], v[194:195] op_sel_hi:[0,1,1]
	v_pk_fma_f32 v[186:187], s[34:35], v[222:223], v[186:187] op_sel_hi:[0,1,1]
	v_pk_fma_f32 v[186:187], s[0:1], v[226:227], v[186:187] op_sel_hi:[0,1,1]
	v_pk_fma_f32 v[194:195], s[0:1], v[228:229], v[194:195] op_sel_hi:[0,1,1]
	v_pk_add_f32 v[194:195], v[194:195], v[232:233]
	v_pk_add_f32 v[186:187], v[186:187], v[230:231]
	v_pk_mul_f32 v[194:195], v[194:195], s[24:25] op_sel_hi:[1,0]
	v_pk_mul_f32 v[186:187], v[186:187], s[24:25] op_sel_hi:[1,0]
	v_pk_mul_f32 v[150:151], v[150:151], v[194:195]
	v_pk_mul_f32 v[148:149], v[148:149], v[186:187]
	v_pk_fma_f32 v[180:181], v[180:181], s[26:27], v[150:151] op_sel_hi:[1,0,1]
	v_pk_fma_f32 v[182:183], v[182:183], s[26:27], v[148:149] op_sel_hi:[1,0,1]
	v_mov_b32_e32 v151, v181
	v_pk_mov_b32 v[148:149], v[182:183], v[180:181] op_sel:[1,0]
	v_mov_b32_e32 v150, v182
	v_pk_add_f32 v[148:149], v[148:149], v[150:151]
	v_cvt_pk_f32_fp8_sdwa v[150:151], v103 src0_sel:WORD_1
	v_pk_add_f32 v[194:195], v[148:149], v[148:149] op_sel:[0,1] op_sel_hi:[1,0]
	v_cvt_pk_f32_fp8_e32 v[148:149], v103
	v_cvt_pk_f32_fp8_e32 v[186:187], v107
	v_cvt_pk_f32_fp8_sdwa v[196:197], v107 src0_sel:WORD_1
	v_cvt_pk_f32_fp8_e32 v[198:199], v99
	v_cvt_pk_f32_fp8_sdwa v[200:201], v99 src0_sel:WORD_1
	v_cvt_pk_f32_fp8_e32 v[202:203], v115
	v_cvt_pk_f32_fp8_sdwa v[218:219], v115 src0_sel:WORD_1
	v_cvt_pk_f32_fp8_e32 v[220:221], v91
	v_cvt_pk_f32_fp8_sdwa v[222:223], v91 src0_sel:WORD_1
	v_pk_fma_f32 v[150:151], s[42:43], v[150:151], 0 op_sel_hi:[0,1,0]
	v_pk_fma_f32 v[148:149], s[42:43], v[148:149], 0 op_sel_hi:[0,1,0]
	v_cvt_pk_f32_fp8_e32 v[224:225], v95
	v_cvt_pk_f32_fp8_sdwa v[226:227], v95 src0_sel:WORD_1
	v_pk_fma_f32 v[148:149], s[40:41], v[186:187], v[148:149] op_sel_hi:[0,1,1]
	v_pk_fma_f32 v[150:151], s[40:41], v[196:197], v[150:151] op_sel_hi:[0,1,1]
	v_cvt_pk_f32_fp8_e32 v[228:229], v111
	v_cvt_pk_f32_fp8_sdwa v[230:231], v111 src0_sel:WORD_1
	v_pk_fma_f32 v[150:151], s[38:39], v[200:201], v[150:151] op_sel_hi:[0,1,1]
	v_pk_fma_f32 v[148:149], s[38:39], v[198:199], v[148:149] op_sel_hi:[0,1,1]
	v_pk_fma_f32 v[148:149], s[36:37], v[202:203], v[148:149] op_sel_hi:[0,1,1]
	v_pk_fma_f32 v[150:151], s[36:37], v[218:219], v[150:151] op_sel_hi:[0,1,1]
	v_pk_fma_f32 v[150:151], s[34:35], v[222:223], v[150:151] op_sel_hi:[0,1,1]
	v_pk_fma_f32 v[148:149], s[34:35], v[220:221], v[148:149] op_sel_hi:[0,1,1]
	v_pk_fma_f32 v[148:149], s[0:1], v[224:225], v[148:149] op_sel_hi:[0,1,1]
	v_pk_fma_f32 v[150:151], s[0:1], v[226:227], v[150:151] op_sel_hi:[0,1,1]
	v_pk_add_f32 v[150:151], v[150:151], v[230:231]
	v_pk_add_f32 v[148:149], v[148:149], v[228:229]
	v_pk_mul_f32 v[150:151], v[150:151], s[24:25] op_sel_hi:[1,0]
	v_pk_mul_f32 v[148:149], v[148:149], s[24:25] op_sel_hi:[1,0]
	v_pk_mul_f32 v[146:147], v[146:147], v[150:151]
	v_pk_mul_f32 v[144:145], v[144:145], v[148:149]
	v_pk_fma_f32 v[184:185], v[184:185], s[26:27], v[146:147] op_sel_hi:[1,0,1]
	v_pk_fma_f32 v[186:187], v[154:155], s[26:27], v[144:145] op_sel_hi:[1,0,1]
	v_cvt_pk_f32_fp8_e32 v[144:145], v116
	v_cvt_pk_f32_fp8_sdwa v[146:147], v116 src0_sel:WORD_1
	v_cvt_pk_f32_fp8_e32 v[148:149], v120
	v_cvt_pk_f32_fp8_sdwa v[150:151], v120 src0_sel:WORD_1
	v_cvt_pk_f32_fp8_e32 v[154:155], v124
	v_cvt_pk_f32_fp8_sdwa v[200:201], v124 src0_sel:WORD_1
	v_cvt_pk_f32_fp8_e32 v[202:203], v128
	v_cvt_pk_f32_fp8_sdwa v[218:219], v128 src0_sel:WORD_1
	v_cvt_pk_f32_fp8_e32 v[220:221], v132
	v_cvt_pk_f32_fp8_sdwa v[222:223], v132 src0_sel:WORD_1
	v_pk_fma_f32 v[146:147], s[42:43], v[146:147], 0 op_sel_hi:[0,1,0]
	v_pk_fma_f32 v[144:145], s[42:43], v[144:145], 0 op_sel_hi:[0,1,0]
	v_cvt_pk_f32_fp8_e32 v[224:225], v136
; #define GAS __attribute__((address_space(1)))
; template <int l>
; __device__ __forceinline__ void layer_phases(Frame& F, const XcdBarrier& bar, const int lo, const int hi) {
;     ...
;                     for (int i = 0; i < 4; ++i) { const int j = 4 * jh + i, k = 16 * ln + 1024 * jh + 4 * i; f32x4 f = (f32x4){0.f, 0.f, 0.f, 0.f};
; #pragma unroll
;                         for (int q = 0; q < 7; ++q) { const unsigned w = yr[7 * jh + q][i]; const float gq = gt[q];
;                             const auto lo2 = __builtin_amdgcn_cvt_pk_f32_fp8((int)w, false), hi2 = __builtin_amdgcn_cvt_pk_f32_fp8((int)w, true);
;                             f.x += gq * lo2[0]; f.y += gq * lo2[1]; f.z += gq * hi2[0]; f.w += gq * hi2[1]; }
;                         v[j] = v[j] * ALPHA + *(const GAS f32x4*)(mrow + 10240 + k) * (f * (1.0f / (float)(1 << YSHIFT)));
;                         s += (v[j].x + v[j].y) + (v[j].z + v[j].w); }
	v_cvt_pk_f32_fp8_sdwa v[226:227], v136 src0_sel:WORD_1
	v_pk_fma_f32 v[144:145], s[40:41], v[148:149], v[144:145] op_sel_hi:[0,1,1]
	v_pk_fma_f32 v[146:147], s[40:41], v[150:151], v[146:147] op_sel_hi:[0,1,1]
	v_cvt_pk_f32_fp8_e32 v[228:229], v140
	v_cvt_pk_f32_fp8_sdwa v[230:231], v140 src0_sel:WORD_1
	v_pk_fma_f32 v[146:147], s[38:39], v[200:201], v[146:147] op_sel_hi:[0,1,1]
	v_pk_fma_f32 v[144:145], s[38:39], v[154:155], v[144:145] op_sel_hi:[0,1,1]
	v_pk_fma_f32 v[144:145], s[36:37], v[202:203], v[144:145] op_sel_hi:[0,1,1]
	v_pk_fma_f32 v[146:147], s[36:37], v[218:219], v[146:147] op_sel_hi:[0,1,1]
	v_pk_fma_f32 v[146:147], s[34:35], v[222:223], v[146:147] op_sel_hi:[0,1,1]
	v_pk_fma_f32 v[144:145], s[34:35], v[220:221], v[144:145] op_sel_hi:[0,1,1]
	v_pk_fma_f32 v[144:145], s[0:1], v[224:225], v[144:145] op_sel_hi:[0,1,1]
	v_pk_fma_f32 v[146:147], s[0:1], v[226:227], v[146:147] op_sel_hi:[0,1,1]
	v_pk_add_f32 v[200:201], v[146:147], v[230:231]
	v_pk_add_f32 v[202:203], v[144:145], v[228:229]
	v_add_u32_e32 v247, s100, v152
	ds_read_b128 v[152:155], v247
	s_nop 0
	v_add_u32_e32 v247, s100, v204
	ds_read_b128 v[144:147], v247 offset:48
	v_add_u32_e32 v247, s100, v204
	ds_read_b128 v[148:151], v247 offset:32
	v_add_u32_e32 v247, s100, v204
	ds_read_b128 v[218:221], v247 offset:16
	v_pk_mul_f32 v[202:203], v[202:203], s[24:25] op_sel_hi:[1,0]
	v_pk_mul_f32 v[200:201], v[200:201], s[24:25] op_sel_hi:[1,0]
	v_add_f32_e32 v196, v186, v187
	v_add_f32_e32 v198, v184, v185
	v_cvt_pk_f32_fp8_sdwa v[204:205], v129 src0_sel:WORD_1
	v_cvt_pk_f32_fp8_e32 v[222:223], v133
	v_cvt_pk_f32_fp8_sdwa v[224:225], v133 src0_sel:WORD_1
	v_cvt_pk_f32_fp8_e32 v[226:227], v137
	v_cvt_pk_f32_fp8_sdwa v[228:229], v137 src0_sel:WORD_1
	v_cvt_pk_f32_fp8_e32 v[230:231], v141
	v_cvt_pk_f32_fp8_sdwa v[232:233], v141 src0_sel:WORD_1
	s_waitcnt lgkmcnt(0)
	v_pk_mul_f32 v[154:155], v[154:155], v[200:201]
	v_pk_mul_f32 v[152:153], v[152:153], v[202:203]
	v_pk_fma_f32 v[174:175], v[174:175], s[26:27], v[154:155] op_sel_hi:[1,0,1]
	v_pk_fma_f32 v[172:173], v[172:173], s[26:27], v[152:153] op_sel_hi:[1,0,1]
	v_mov_b32_e32 v197, v174
	v_mov_b32_e32 v193, v172
	v_mov_b32_e32 v195, v173
	v_mov_b32_e32 v199, v175
	v_pk_add_f32 v[152:153], v[192:193], v[194:195]
	v_pk_add_f32 v[154:155], v[196:197], v[198:199]
	v_cvt_pk_f32_fp8_e32 v[194:195], v121
	v_pk_add_f32 v[152:153], v[152:153], v[154:155]
	v_cvt_pk_f32_fp8_sdwa v[154:155], v117 src0_sel:WORD_1
	v_pk_add_f32 v[192:193], v[152:153], v[152:153] op_sel:[0,1] op_sel_hi:[1,0]
	v_cvt_pk_f32_fp8_e32 v[152:153], v117
	v_cvt_pk_f32_fp8_sdwa v[196:197], v121 src0_sel:WORD_1
	v_cvt_pk_f32_fp8_e32 v[198:199], v125
	v_cvt_pk_f32_fp8_sdwa v[200:201], v125 src0_sel:WORD_1
	v_cvt_pk_f32_fp8_e32 v[202:203], v129
	v_pk_fma_f32 v[154:155], s[42:43], v[154:155], 0 op_sel_hi:[0,1,0]
	v_pk_fma_f32 v[152:153], s[42:43], v[152:153], 0 op_sel_hi:[0,1,0]
	v_pk_fma_f32 v[152:153], s[40:41], v[194:195], v[152:153] op_sel_hi:[0,1,1]
	v_pk_fma_f32 v[154:155], s[40:41], v[196:197], v[154:155] op_sel_hi:[0,1,1]
	v_pk_fma_f32 v[154:155], s[38:39], v[200:201], v[154:155] op_sel_hi:[0,1,1]
	v_pk_fma_f32 v[152:153], s[38:39], v[198:199], v[152:153] op_sel_hi:[0,1,1]
	v_pk_fma_f32 v[152:153], s[36:37], v[202:203], v[152:153] op_sel_hi:[0,1,1]
	v_pk_fma_f32 v[154:155], s[36:37], v[204:205], v[154:155] op_sel_hi:[0,1,1]
	v_pk_fma_f32 v[154:155], s[34:35], v[224:225], v[154:155] op_sel_hi:[0,1,1]
	v_pk_fma_f32 v[152:153], s[34:35], v[222:223], v[152:153] op_sel_hi:[0,1,1]
	v_pk_fma_f32 v[152:153], s[0:1], v[226:227], v[152:153] op_sel_hi:[0,1,1]
	v_pk_fma_f32 v[154:155], s[0:1], v[228:229], v[154:155] op_sel_hi:[0,1,1]
	v_pk_add_f32 v[154:155], v[154:155], v[232:233]
	v_pk_add_f32 v[152:153], v[152:153], v[230:231]
	v_pk_mul_f32 v[154:155], v[154:155], s[24:25] op_sel_hi:[1,0]
	v_pk_mul_f32 v[152:153], v[152:153], s[24:25] op_sel_hi:[1,0]
	s_waitcnt lgkmcnt(0)
	v_pk_mul_f32 v[154:155], v[220:221], v[154:155]
	v_pk_mul_f32 v[194:195], v[218:219], v[152:153]
	v_pk_fma_f32 v[152:153], v[170:171], s[26:27], v[154:155] op_sel_hi:[1,0,1]
	v_pk_fma_f32 v[154:155], v[168:169], s[26:27], v[194:195] op_sel_hi:[1,0,1]
	v_mov_b32_e32 v171, v153
	v_pk_mov_b32 v[168:169], v[154:155], v[152:153] op_sel:[1,0]
	v_mov_b32_e32 v170, v154
	v_pk_add_f32 v[168:169], v[168:169], v[170:171]
	v_cvt_pk_f32_fp8_e32 v[170:171], v118
	v_cvt_pk_f32_fp8_sdwa v[194:195], v118 src0_sel:WORD_1
	v_cvt_pk_f32_fp8_e32 v[196:197], v122
	v_cvt_pk_f32_fp8_sdwa v[198:199], v122 src0_sel:WORD_1
	v_cvt_pk_f32_fp8_e32 v[200:201], v126
	v_cvt_pk_f32_fp8_sdwa v[202:203], v126 src0_sel:WORD_1
	v_cvt_pk_f32_fp8_e32 v[204:205], v130
	v_cvt_pk_f32_fp8_sdwa v[218:219], v130 src0_sel:WORD_1
	v_cvt_pk_f32_fp8_e32 v[220:221], v134
	v_cvt_pk_f32_fp8_sdwa v[222:223], v134 src0_sel:WORD_1
	v_pk_fma_f32 v[194:195], s[42:43], v[194:195], 0 op_sel_hi:[0,1,0]
	v_pk_fma_f32 v[170:171], s[42:43], v[170:171], 0 op_sel_hi:[0,1,0]
	v_cvt_pk_f32_fp8_e32 v[224:225], v138
	v_cvt_pk_f32_fp8_sdwa v[226:227], v138 src0_sel:WORD_1
	v_pk_fma_f32 v[170:171], s[40:41], v[196:197], v[170:171] op_sel_hi:[0,1,1]
	v_pk_fma_f32 v[194:195], s[40:41], v[198:199], v[194:195] op_sel_hi:[0,1,1]
	v_cvt_pk_f32_fp8_e32 v[228:229], v142
	v_cvt_pk_f32_fp8_sdwa v[230:231], v142 src0_sel:WORD_1
	v_pk_fma_f32 v[194:195], s[38:39], v[202:203], v[194:195] op_sel_hi:[0,1,1]
	v_pk_fma_f32 v[170:171], s[38:39], v[200:201], v[170:171] op_sel_hi:[0,1,1]
	v_pk_fma_f32 v[170:171], s[36:37], v[204:205], v[170:171] op_sel_hi:[0,1,1]
	v_pk_fma_f32 v[194:195], s[36:37], v[218:219], v[194:195] op_sel_hi:[0,1,1]
	v_pk_fma_f32 v[194:195], s[34:35], v[222:223], v[194:195] op_sel_hi:[0,1,1]
; #define GAS __attribute__((address_space(1)))
; template <int l>
; __device__ __forceinline__ void layer_phases(Frame& F, const XcdBarrier& bar, const int lo, const int hi) {
;     ...
;                         v[j] = v[j] * ALPHA + *(const GAS f32x4*)(mrow + 10240 + k) * (f * (1.0f / (float)(1 << YSHIFT)));
;                         s += (v[j].x + v[j].y) + (v[j].z + v[j].w); }
;                 }
;                 const float mean = wave_sum(s) * (1.f / D); float s2 = 0.f;
; #pragma unroll
;                 for (int j = 0; j < 8; ++j) { v[j] = v[j] - mean; s2 += (v[j].x * v[j].x + v[j].y * v[j].y) + (v[j].z * v[j].z + v[j].w * v[j].w); }
;                 const float rstd = 1.f / sqrtf(wave_sum(s2) * (1.f / D) + LN_EPS);
	v_pk_fma_f32 v[170:171], s[34:35], v[220:221], v[170:171] op_sel_hi:[0,1,1]
	v_pk_fma_f32 v[170:171], s[0:1], v[224:225], v[170:171] op_sel_hi:[0,1,1]
	v_pk_fma_f32 v[194:195], s[0:1], v[226:227], v[194:195] op_sel_hi:[0,1,1]
	v_pk_add_f32 v[194:195], v[194:195], v[230:231]
	v_pk_add_f32 v[170:171], v[170:171], v[228:229]
	v_pk_mul_f32 v[194:195], v[194:195], s[24:25] op_sel_hi:[1,0]
	v_pk_mul_f32 v[170:171], v[170:171], s[24:25] op_sel_hi:[1,0]
	v_pk_mul_f32 v[150:151], v[150:151], v[194:195]
	v_pk_mul_f32 v[170:171], v[148:149], v[170:171]
	v_pk_fma_f32 v[148:149], v[166:167], s[26:27], v[150:151] op_sel_hi:[1,0,1]
	v_pk_fma_f32 v[150:151], v[164:165], s[26:27], v[170:171] op_sel_hi:[1,0,1]
	v_cvt_pk_f32_fp8_e32 v[170:171], v119
	v_cvt_pk_f32_fp8_sdwa v[194:195], v119 src0_sel:WORD_1
	v_cvt_pk_f32_fp8_e32 v[196:197], v123
	v_cvt_pk_f32_fp8_sdwa v[198:199], v123 src0_sel:WORD_1
	v_cvt_pk_f32_fp8_e32 v[200:201], v127
	v_cvt_pk_f32_fp8_sdwa v[202:203], v127 src0_sel:WORD_1
	v_cvt_pk_f32_fp8_e32 v[204:205], v131
	v_cvt_pk_f32_fp8_sdwa v[218:219], v131 src0_sel:WORD_1
	v_cvt_pk_f32_fp8_e32 v[220:221], v135
	v_cvt_pk_f32_fp8_sdwa v[222:223], v135 src0_sel:WORD_1
	v_pk_fma_f32 v[194:195], s[42:43], v[194:195], 0 op_sel_hi:[0,1,0]
	v_pk_fma_f32 v[170:171], s[42:43], v[170:171], 0 op_sel_hi:[0,1,0]
	v_cvt_pk_f32_fp8_e32 v[224:225], v139
	v_cvt_pk_f32_fp8_sdwa v[226:227], v139 src0_sel:WORD_1
	v_pk_fma_f32 v[170:171], s[40:41], v[196:197], v[170:171] op_sel_hi:[0,1,1]
	v_pk_fma_f32 v[194:195], s[40:41], v[198:199], v[194:195] op_sel_hi:[0,1,1]
	v_cvt_pk_f32_fp8_e32 v[228:229], v143
	v_cvt_pk_f32_fp8_sdwa v[230:231], v143 src0_sel:WORD_1
	v_pk_fma_f32 v[194:195], s[38:39], v[202:203], v[194:195] op_sel_hi:[0,1,1]
	v_pk_fma_f32 v[170:171], s[38:39], v[200:201], v[170:171] op_sel_hi:[0,1,1]
	v_pk_fma_f32 v[170:171], s[36:37], v[204:205], v[170:171] op_sel_hi:[0,1,1]
	v_pk_fma_f32 v[194:195], s[36:37], v[218:219], v[194:195] op_sel_hi:[0,1,1]
	v_pk_fma_f32 v[194:195], s[34:35], v[222:223], v[194:195] op_sel_hi:[0,1,1]
	v_pk_fma_f32 v[170:171], s[34:35], v[220:221], v[170:171] op_sel_hi:[0,1,1]
	v_pk_fma_f32 v[170:171], s[0:1], v[224:225], v[170:171] op_sel_hi:[0,1,1]
	v_pk_fma_f32 v[194:195], s[0:1], v[226:227], v[194:195] op_sel_hi:[0,1,1]
	v_pk_add_f32 v[194:195], v[194:195], v[230:231]
	v_pk_add_f32 v[170:171], v[170:171], v[228:229]
	v_pk_mul_f32 v[194:195], v[194:195], s[24:25] op_sel_hi:[1,0]
	v_pk_mul_f32 v[170:171], v[170:171], s[24:25] op_sel_hi:[1,0]
	v_pk_mul_f32 v[146:147], v[146:147], v[194:195]
	v_pk_mul_f32 v[170:171], v[144:145], v[170:171]
	v_pk_add_f32 v[168:169], v[168:169], v[168:169] op_sel:[0,1] op_sel_hi:[1,0]
	v_pk_fma_f32 v[144:145], v[162:163], s[26:27], v[146:147] op_sel_hi:[1,0,1]
	v_pk_fma_f32 v[146:147], v[160:161], s[26:27], v[170:171] op_sel_hi:[1,0,1]
	v_add_f32_e32 v164, v150, v151
	v_add_f32_e32 v166, v148, v149
	v_mov_b32_e32 v193, v146
	v_mov_b32_e32 v169, v147
	v_mov_b32_e32 v165, v144
	v_mov_b32_e32 v167, v145
	v_pk_add_f32 v[160:161], v[192:193], v[168:169]
	v_pk_add_f32 v[162:163], v[164:165], v[166:167]
	v_lshl_add_u64 v[204:205], s[6:7], 0, v[158:159]
	v_pk_add_f32 v[160:161], v[160:161], v[162:163]
	v_lshl_add_u64 v[230:231], s[8:9], 0, v[158:159]
	v_add_f32_e32 v160, v160, v161
	ds_bpermute_b32 v161, v209, v160
	s_waitcnt lgkmcnt(0)
	v_add_f32_e32 v160, v160, v161
	ds_bpermute_b32 v161, v210, v160
	s_waitcnt lgkmcnt(0)
	v_add_f32_e32 v160, v160, v161
	ds_bpermute_b32 v161, v211, v160
	s_waitcnt lgkmcnt(0)
	v_add_f32_e32 v160, v160, v161
	ds_bpermute_b32 v161, v212, v160
	s_waitcnt lgkmcnt(0)
	v_add_f32_e32 v160, v160, v161
	ds_bpermute_b32 v161, v213, v160
	s_waitcnt lgkmcnt(0)
	v_add_f32_e32 v160, v160, v161
	ds_bpermute_b32 v161, v214, v160
	s_waitcnt lgkmcnt(0)
	v_add_f32_e32 v168, v160, v161
	v_fmamk_f32 v191, v168, 0xba000000, v191
	v_fmamk_f32 v179, v168, 0xba000000, v179
	v_fmamk_f32 v189, v168, 0xba000000, v189
	v_fmac_f32_e32 v190, 0xba000000, v168
	v_fmamk_f32 v177, v168, 0xba000000, v177
	v_fmac_f32_e32 v178, 0xba000000, v168
	v_mov_b32_e32 v162, v191
	v_mov_b32_e32 v163, v179
	v_fmac_f32_e32 v188, 0xba000000, v168
	v_fmac_f32_e32 v176, 0xba000000, v168
	v_mov_b32_e32 v160, v190
	v_mov_b32_e32 v161, v178
	v_pk_mul_f32 v[162:163], v[162:163], v[162:163]
	v_mov_b32_e32 v164, v189
	v_mov_b32_e32 v165, v177
	v_pk_fma_f32 v[160:161], v[160:161], v[160:161], v[162:163]
	v_mov_b32_e32 v162, v188
	v_mov_b32_e32 v163, v176
	v_pk_mul_f32 v[164:165], v[164:165], v[164:165]
	v_fmamk_f32 v183, v168, 0xba000000, v183
	v_pk_fma_f32 v[162:163], v[162:163], v[162:163], v[164:165]
	v_fmac_f32_e32 v182, 0xba000000, v168
	v_pk_add_f32 v[160:161], v[160:161], v[162:163]
	v_fmamk_f32 v181, v168, 0xba000000, v181
	v_fmac_f32_e32 v180, 0xba000000, v168
	v_pk_add_f32 v[160:161], v[160:161], v[160:161] op_sel_hi:[0,1]
	v_pk_mul_f32 v[162:163], v[180:181], v[180:181]
	v_pk_mul_f32 v[164:165], v[182:183], v[182:183]
	v_fmac_f32_e32 v186, 0xba000000, v168
	v_pk_mov_b32 v[166:167], v[164:165], v[162:163] op_sel:[1,0]
	v_mov_b32_e32 v165, v163
	v_fmamk_f32 v187, v168, 0xba000000, v187
	v_fmac_f32_e32 v184, 0xba000000, v168
	v_mul_f32_e32 v160, v186, v186
	v_pk_add_f32 v[162:163], v[166:167], v[164:165]
	v_fmamk_f32 v185, v168, 0xba000000, v185
	v_pk_fma_f32 v[164:165], v[186:187], v[186:187], v[160:161] op_sel_hi:[1,1,0]
	v_mul_f32_e32 v160, v184, v184
	v_pk_add_f32 v[162:163], v[162:163], v[162:163] op_sel_hi:[0,1]
	v_pk_fma_f32 v[166:167], v[184:185], v[184:185], v[160:161] op_sel_hi:[1,1,0]
	v_fmamk_f32 v175, v168, 0xba000000, v175
	v_fmac_f32_e32 v174, 0xba000000, v168
	v_fmamk_f32 v173, v168, 0xba000000, v173
; #define GAS __attribute__((address_space(1)))
; template <int l>
; __device__ __forceinline__ void layer_phases(Frame& F, const XcdBarrier& bar, const int lo, const int hi) {
;     ...
;                 const float mean = wave_sum(s) * (1.f / D); float s2 = 0.f;
; #pragma unroll
;                 for (int j = 0; j < 8; ++j) { v[j] = v[j] - mean; s2 += (v[j].x * v[j].x + v[j].y * v[j].y) + (v[j].z * v[j].z + v[j].w * v[j].w); }
;                 const float rstd = 1.f / sqrtf(wave_sum(s2) * (1.f / D) + LN_EPS);
;                 float* orow = Fout + (size_t)m * D;
; #pragma unroll
;                 for (int j = 0; j < 8; ++j) { const int k = 16 * ln + 1024 * (j >> 2) + 4 * (j & 3);
;                     v[j] = v[j] * rstd * *(const GAS f32x4*)(g2 + k) + *(const GAS f32x4*)(b2 + k);
	v_fmac_f32_e32 v172, 0xba000000, v168
	v_mul_f32_e32 v164, v172, v172
	v_mul_f32_e32 v166, v173, v173
	v_mul_f32_e32 v162, v174, v174
	v_mul_f32_e32 v160, v175, v175
	v_pk_add_f32 v[164:165], v[164:165], v[166:167]
	v_pk_add_f32 v[160:161], v[162:163], v[160:161]
	v_fmamk_f32 v155, v168, 0xba000000, v155
	v_pk_add_f32 v[160:161], v[164:165], v[160:161]
	v_fmac_f32_e32 v154, 0xba000000, v168
	v_fmamk_f32 v153, v168, 0xba000000, v153
	v_fmac_f32_e32 v152, 0xba000000, v168
	v_pk_add_f32 v[160:161], v[160:161], v[160:161] op_sel_hi:[0,1]
	v_pk_mul_f32 v[162:163], v[152:153], v[152:153]
	v_pk_mul_f32 v[164:165], v[154:155], v[154:155]
	v_fmac_f32_e32 v150, 0xba000000, v168
	v_pk_mov_b32 v[166:167], v[164:165], v[162:163] op_sel:[1,0]
	v_mov_b32_e32 v165, v163
	v_fmamk_f32 v151, v168, 0xba000000, v151
	v_fmac_f32_e32 v148, 0xba000000, v168
	v_mul_f32_e32 v160, v150, v150
	v_pk_add_f32 v[162:163], v[166:167], v[164:165]
	v_fmamk_f32 v149, v168, 0xba000000, v149
	v_pk_fma_f32 v[164:165], v[150:151], v[150:151], v[160:161] op_sel_hi:[1,1,0]
	v_mul_f32_e32 v160, v148, v148
	v_pk_add_f32 v[162:163], v[162:163], v[162:163] op_sel_hi:[0,1]
	v_pk_fma_f32 v[166:167], v[148:149], v[148:149], v[160:161] op_sel_hi:[1,1,0]
	v_fmamk_f32 v145, v168, 0xba000000, v145
	v_fmac_f32_e32 v144, 0xba000000, v168
	v_fmamk_f32 v147, v168, 0xba000000, v147
	v_fmac_f32_e32 v146, 0xba000000, v168
	v_mul_f32_e32 v164, v146, v146
	v_mul_f32_e32 v166, v147, v147
	v_mul_f32_e32 v162, v144, v144
	v_mul_f32_e32 v160, v145, v145
	v_pk_add_f32 v[164:165], v[164:165], v[166:167]
	v_pk_add_f32 v[160:161], v[162:163], v[160:161]
	s_nop 0
	v_pk_add_f32 v[160:161], v[164:165], v[160:161]
	s_nop 0
	v_add_f32_e32 v160, v160, v161
	ds_bpermute_b32 v161, v209, v160
	s_waitcnt lgkmcnt(0)
	v_add_f32_e32 v160, v160, v161
	ds_bpermute_b32 v161, v210, v160
	s_waitcnt lgkmcnt(0)
	v_add_f32_e32 v160, v160, v161
	ds_bpermute_b32 v161, v211, v160
	s_waitcnt lgkmcnt(0)
	v_add_f32_e32 v160, v160, v161
	ds_bpermute_b32 v161, v212, v160
	s_waitcnt lgkmcnt(0)
	v_add_f32_e32 v160, v160, v161
	ds_bpermute_b32 v161, v213, v160
	s_waitcnt lgkmcnt(0)
	v_add_f32_e32 v160, v160, v161
	ds_bpermute_b32 v161, v214, v160
	s_waitcnt lgkmcnt(0)
	v_add_f32_e32 v160, v160, v161
	v_fmamk_f32 v160, v160, 0x3a000000, v215
	v_cmp_gt_f32_e32 vcc, s68, v160
	v_mul_f32_e32 v161, 0x4f800000, v160
	s_nop 0
	v_cndmask_b32_e32 v160, v160, v161, vcc
	v_sqrt_f32_e32 v161, v160
	s_nop 0
	v_add_u32_e32 v162, -1, v161
	v_fma_f32 v163, -v162, v161, v160
	v_cmp_ge_f32_e64 s[0:1], 0, v163
	v_add_u32_e32 v163, 1, v161
	s_nop 0
	v_cndmask_b32_e64 v162, v161, v162, s[0:1]
	v_fma_f32 v161, -v163, v161, v160
	v_cmp_lt_f32_e64 s[0:1], 0, v161
	s_nop 1
	v_cndmask_b32_e64 v161, v162, v163, s[0:1]
	v_mul_f32_e32 v162, 0x37800000, v161
	v_cndmask_b32_e32 v161, v161, v162, vcc
	v_cmp_class_f32_e32 vcc, v160, v217
	s_nop 1
	v_cndmask_b32_e32 v160, v161, v160, vcc
	v_div_scale_f32 v161, s[0:1], v160, v160, 1.0
	v_rcp_f32_e32 v162, v161
	s_lshl_b64 s[0:1], s[30:31], 12
	s_add_u32 s0, s52, s0
	s_addc_u32 s1, s53, s1
	v_fma_f32 v163, -v161, v162, 1.0
	v_fmac_f32_e32 v162, v163, v162
	v_div_scale_f32 v163, vcc, 1.0, v160, 1.0
	v_mul_f32_e32 v164, v163, v162
	v_fma_f32 v165, -v161, v164, v163
	v_fmac_f32_e32 v164, v165, v162
	v_fma_f32 v161, -v161, v164, v163
	v_div_fmas_f32 v161, v161, v162, v164
	v_add_u32_e32 v247, s98, v204
	ds_read_b128 v[192:195], v247 offset:48
	v_add_u32_e32 v247, s98, v204
	ds_read_b128 v[162:165], v247 offset:32
	v_add_u32_e32 v247, s98, v204
	ds_read_b128 v[166:169], v247 offset:16
	v_add_u32_e32 v247, s98, v204
	ds_read_b128 v[196:199], v247
	v_add_u32_e32 v247, s99, v230
	ds_read_b128 v[200:203], v247 offset:48
	v_add_u32_e32 v247, s99, v230
	ds_read_b128 v[218:221], v247 offset:32
	v_add_u32_e32 v247, s99, v230
	ds_read_b128 v[222:225], v247 offset:16
	v_add_u32_e32 v247, s99, v230
	ds_read_b128 v[226:229], v247
	v_div_fixup_f32 v160, v161, v160, 1.0
	v_pk_mul_f32 v[170:171], v[190:191], v[160:161] op_sel_hi:[1,0]
	v_pk_mul_f32 v[158:159], v[178:179], v[160:161] op_sel_hi:[1,0]
	v_pk_mul_f32 v[188:189], v[188:189], v[160:161] op_sel_hi:[1,0]
	v_pk_mul_f32 v[144:145], v[144:145], v[160:161] op_sel_hi:[1,0]
	v_pk_mul_f32 v[146:147], v[146:147], v[160:161] op_sel_hi:[1,0]
	v_pk_mul_f32 v[148:149], v[148:149], v[160:161] op_sel_hi:[1,0]
	v_pk_mul_f32 v[150:151], v[150:151], v[160:161] op_sel_hi:[1,0]
	s_waitcnt lgkmcnt(0)
	v_pk_fma_f32 v[190:191], v[196:197], v[170:171], v[226:227]
	v_pk_mul_f32 v[170:171], v[176:177], v[160:161] op_sel_hi:[1,0]
	v_pk_fma_f32 v[188:189], v[198:199], v[188:189], v[228:229]
	v_pk_fma_f32 v[168:169], v[168:169], v[170:171], v[224:225]
	v_pk_fma_f32 v[170:171], v[166:167], v[158:159], v[222:223]
	v_pk_mul_f32 v[158:159], v[182:183], v[160:161] op_sel_hi:[1,0]
	v_pk_mul_f32 v[182:183], v[172:173], v[160:161] op_sel_hi:[1,0]
	v_pk_mul_f32 v[172:173], v[174:175], v[160:161] op_sel_hi:[1,0]
	v_add_co_u32_e32 v174, vcc, s55, v204
	v_pk_mul_f32 v[166:167], v[180:181], v[160:161] op_sel_hi:[1,0]
	s_nop 0
	v_addc_co_u32_e32 v175, vcc, 0, v205, vcc
	v_add_co_u32_e32 v178, vcc, s55, v230
	v_add_u32_e32 v247, s98, v174
	ds_read_b128 v[174:177], v247
	s_nop 0
	v_addc_co_u32_e32 v179, vcc, 0, v231, vcc
	v_add_u32_e32 v247, s99, v178
	ds_read_b128 v[178:181], v247
	v_pk_fma_f32 v[164:165], v[164:165], v[166:167], v[220:221]
	v_pk_fma_f32 v[166:167], v[162:163], v[158:159], v[218:219]
	v_pk_mul_f32 v[158:159], v[184:185], v[160:161] op_sel_hi:[1,0]
	v_pk_mul_f32 v[162:163], v[186:187], v[160:161] op_sel_hi:[1,0]
	v_pk_fma_f32 v[158:159], v[194:195], v[158:159], v[202:203]
	v_pk_fma_f32 v[162:163], v[192:193], v[162:163], v[200:201]
	v_pk_mul_f32 v[200:201], v[154:155], v[160:161] op_sel_hi:[1,0]
	v_pk_mul_f32 v[202:203], v[152:153], v[160:161] op_sel_hi:[1,0]
	s_waitcnt lgkmcnt(0)
; #define GAS __attribute__((address_space(1)))
; __device__ __forceinline__ unsigned pk2(float lo, float hi) { return f2bf(lo) | (f2bf(hi) << 16); }
; template <int l>
; __device__ __forceinline__ void layer_phases(Frame& F, const XcdBarrier& bar, const int lo, const int hi) {
;     ...
;                 const float rstd = 1.f / sqrtf(wave_sum(s2) * (1.f / D) + LN_EPS);
;                 float* orow = Fout + (size_t)m * D;
; #pragma unroll
;                 for (int j = 0; j < 8; ++j) { const int k = 16 * ln + 1024 * (j >> 2) + 4 * (j & 3);
;                     v[j] = v[j] * rstd * *(const GAS f32x4*)(g2 + k) + *(const GAS f32x4*)(b2 + k);
;                     if (l == 1) { *(GAS f32x4*)(orow + k) = v[j]; if (j & 1) asm volatile("" ::: "memory"); } }
;                 if (l == 0) {
; #pragma unroll
;                     for (int jh = 0; jh < 2; ++jh) { v4u wa, wb; wa.x = pk2(v[4 * jh].x, v[4 * jh].y); wa.y = pk2(v[4 * jh].z, v[4 * jh].w); wa.z = pk2(v[4 * jh + 1].x, v[4 * jh + 1].y); wa.w = pk2(v[4 * jh + 1].z, v[4 * jh + 1].w);
;                         wb.x = pk2(v[4 * jh + 2].x, v[4 * jh + 2].y); wb.y = pk2(v[4 * jh + 2].z, v[4 * jh + 2].w); wb.z = pk2(v[4 * jh + 3].x, v[4 * jh + 3].y); wb.w = pk2(v[4 * jh + 3].z, v[4 * jh + 3].w);
;                         *(GAS v4u*)(x2b + (size_t)m * D + 16 * ln + 1024 * jh) = wa; *(GAS v4u*)(x2b + (size_t)m * D + 16 * ln + 1024 * jh + 8) = wb; } }
	v_pk_fma_f32 v[172:173], v[176:177], v[172:173], v[180:181]
	v_add_u32_e32 v176, 0x404, v156
	v_ashrrev_i32_e32 v177, 31, v176
	v_lshlrev_b64 v[184:185], 2, v[176:177]
	v_lshl_add_u64 v[180:181], s[6:7], 0, v[184:185]
	v_lshl_add_u64 v[196:197], s[8:9], 0, v[184:185]
	v_pk_fma_f32 v[174:175], v[174:175], v[182:183], v[178:179]
	v_add_u32_e32 v247, s98, v180
	ds_read_b128 v[152:155], v247 offset:32
	v_add_u32_e32 v247, s98, v180
	ds_read_b128 v[176:179], v247 offset:16
	s_nop 0
	v_add_u32_e32 v247, s98, v180
	ds_read_b128 v[180:183], v247
	s_nop 0
	v_add_u32_e32 v247, s99, v196
	ds_read_b128 v[184:187], v247 offset:32
	v_add_u32_e32 v247, s99, v196
	ds_read_b128 v[192:195], v247 offset:16
	s_nop 0
	v_add_u32_e32 v247, s99, v196
	ds_read_b128 v[196:199], v247
	v_lshl_add_u64 v[156:157], v[156:157], 1, s[0:1]
	s_waitcnt lgkmcnt(0)
	v_pk_fma_f32 v[154:155], v[154:155], v[144:145], v[186:187]
	v_bfe_u32 v144, v190, 16, 1
	v_add3_u32 v144, v190, v144, s69
	v_bfe_u32 v145, v191, 16, 1
	v_lshrrev_b32_e32 v144, 16, v144
	v_add3_u32 v145, v191, v145, s69
	v_and_or_b32 v144, v145, s66, v144
	v_bfe_u32 v145, v188, 16, 1
	v_pk_fma_f32 v[152:153], v[152:153], v[146:147], v[184:185]
	v_add3_u32 v145, v188, v145, s69
	v_bfe_u32 v146, v189, 16, 1
	v_lshrrev_b32_e32 v145, 16, v145
	v_add3_u32 v146, v189, v146, s69
	v_and_or_b32 v145, v146, s66, v145
	v_bfe_u32 v146, v170, 16, 1
	v_add3_u32 v146, v170, v146, s69
	v_bfe_u32 v147, v171, 16, 1
	v_lshrrev_b32_e32 v146, 16, v146
	v_add3_u32 v147, v171, v147, s69
	v_and_or_b32 v146, v147, s66, v146
	v_bfe_u32 v147, v168, 16, 1
	s_waitcnt lgkmcnt(0)
	v_pk_fma_f32 v[178:179], v[178:179], v[148:149], v[194:195]
	v_add3_u32 v147, v168, v147, s69
	v_bfe_u32 v148, v169, 16, 1
	v_lshrrev_b32_e32 v147, 16, v147
	v_add3_u32 v148, v169, v148, s69
	v_and_or_b32 v147, v148, s66, v147
	v_bfe_u32 v148, v166, 16, 1
	v_add3_u32 v148, v166, v148, s69
	v_bfe_u32 v149, v167, 16, 1
	v_lshrrev_b32_e32 v148, 16, v148
	v_add3_u32 v149, v167, v149, s69
	v_and_or_b32 v148, v149, s66, v148
	v_bfe_u32 v149, v164, 16, 1
	v_pk_fma_f32 v[176:177], v[176:177], v[150:151], v[192:193]
	v_add3_u32 v149, v164, v149, s69
	v_bfe_u32 v150, v165, 16, 1
	v_lshrrev_b32_e32 v149, 16, v149
	v_add3_u32 v150, v165, v150, s69
	v_and_or_b32 v149, v150, s66, v149
	v_bfe_u32 v150, v162, 16, 1
	v_add3_u32 v150, v162, v150, s69
	v_bfe_u32 v151, v163, 16, 1
	v_lshrrev_b32_e32 v150, 16, v150
	v_add3_u32 v151, v163, v151, s69
	v_and_or_b32 v150, v151, s66, v150
	v_bfe_u32 v151, v158, 16, 1
	v_add3_u32 v151, v158, v151, s69
	v_bfe_u32 v158, v159, 16, 1
	v_lshrrev_b32_e32 v151, 16, v151
	v_add3_u32 v158, v159, v158, s69
	v_and_or_b32 v151, v158, s66, v151
	global_store_dwordx4 v[156:157], v[144:147], off
	global_store_dwordx4 v[156:157], v[148:151], off offset:16
	s_waitcnt lgkmcnt(0)
	v_pk_fma_f32 v[180:181], v[180:181], v[200:201], v[196:197]
	v_bfe_u32 v144, v174, 16, 1
	v_add3_u32 v144, v174, v144, s69
	v_bfe_u32 v145, v175, 16, 1
	v_lshrrev_b32_e32 v144, 16, v144
	v_add3_u32 v145, v175, v145, s69
	v_and_or_b32 v144, v145, s66, v144
	v_bfe_u32 v145, v172, 16, 1
	v_add3_u32 v145, v172, v145, s69
	v_bfe_u32 v146, v173, 16, 1
	v_lshrrev_b32_e32 v145, 16, v145
	v_add3_u32 v146, v173, v146, s69
	v_and_or_b32 v145, v146, s66, v145
	v_bfe_u32 v146, v180, 16, 1
	v_add3_u32 v146, v180, v146, s69
	v_bfe_u32 v147, v181, 16, 1
	v_pk_fma_f32 v[182:183], v[182:183], v[202:203], v[198:199]
	v_lshrrev_b32_e32 v146, 16, v146
	v_add3_u32 v147, v181, v147, s69
	v_and_or_b32 v146, v147, s66, v146
	v_bfe_u32 v147, v182, 16, 1
	v_add3_u32 v147, v182, v147, s69
	v_bfe_u32 v148, v183, 16, 1
	v_lshrrev_b32_e32 v147, 16, v147
	v_add3_u32 v148, v183, v148, s69
	v_and_or_b32 v147, v148, s66, v147
	v_bfe_u32 v148, v176, 16, 1
	v_add3_u32 v148, v176, v148, s69
	v_bfe_u32 v149, v177, 16, 1
	v_lshrrev_b32_e32 v148, 16, v148
	v_add3_u32 v149, v177, v149, s69
	v_and_or_b32 v148, v149, s66, v148
	v_bfe_u32 v149, v178, 16, 1
	v_add3_u32 v149, v178, v149, s69
	v_bfe_u32 v150, v179, 16, 1
	v_lshrrev_b32_e32 v149, 16, v149
	v_add3_u32 v150, v179, v150, s69
	v_and_or_b32 v149, v150, s66, v149
	v_bfe_u32 v150, v152, 16, 1
	v_add3_u32 v150, v152, v150, s69
	v_bfe_u32 v151, v153, 16, 1
	v_lshrrev_b32_e32 v150, 16, v150
	v_add3_u32 v151, v153, v151, s69
	v_and_or_b32 v150, v151, s66, v150
	v_bfe_u32 v151, v154, 16, 1
	v_add3_u32 v151, v154, v151, s69
	v_bfe_u32 v152, v155, 16, 1
	v_lshrrev_b32_e32 v151, 16, v151
	v_add3_u32 v152, v155, v152, s69
	v_and_or_b32 v151, v152, s66, v151
	global_store_dwordx4 v[156:157], v[144:147], off offset:2048
	global_store_dwordx4 v[156:157], v[148:151], off offset:2064

; #define GAS __attribute__((address_space(1)))
; template <int l>
; __device__ __forceinline__ void layer_phases(Frame& F, const XcdBarrier& bar, const int lo, const int hi) {
;     ...
;             auto load_row = [&](const int m, v4u (&xr)[4], v4u (&yr)[14], float& gtv) {
;                 int ln = F.lane; asm volatile("" : "+v"(ln));
;                 gtv = 0.f; if (ln < 6) gtv = gates[(size_t)m * 6 + ln];
; #pragma unroll
;                 for (int jh = 0; jh < 2; ++jh) { xr[2 * jh] = __builtin_nontemporal_load((const GAS v4u*)(x1 + (size_t)m * D + 16 * ln + 1024 * jh)); xr[2 * jh + 1] = __builtin_nontemporal_load((const GAS v4u*)(x1 + (size_t)m * D + 16 * ln + 1024 * jh + 8)); }
; #pragma unroll
;                 for (int jh = 0; jh < 2; ++jh)
; #pragma unroll
;                     for (int q = 0; q < 7; ++q) yr[7 * jh + q] = __builtin_nontemporal_load((const GAS v4u*)(yb + ((size_t)m * 7 + q) * D + 16 * ln + 1024 * jh));
;                 asm volatile("" ::: "memory");
.LBB0_976:
	s_or_b64 exec, exec, s[36:37]
	s_lshl_b64 s[36:37], s[4:5], 12
	s_add_u32 s36, s50, s36
	s_addc_u32 s37, s51, s37
	s_mul_hi_i32 s5, s4, 0x3800
	s_mulk_i32 s4, 0x3800
	v_lshlrev_b32_e32 v88, 4, v68
	s_add_u32 s4, s43, s4
	v_ashrrev_i32_e32 v89, 31, v88
	s_addc_u32 s5, s47, s5
	v_lshl_add_u64 v[112:113], s[4:5], 0, v[88:89]
	v_add_co_u32_e32 v114, vcc, s55, v112
	v_lshl_add_u64 v[80:81], v[88:89], 1, s[36:37]
	s_nop 0
	v_addc_co_u32_e32 v115, vcc, 0, v113, vcc
	v_add_co_u32_e32 v96, vcc, s64, v112
	v_lshl_add_u64 v[124:125], v[112:113], 0, s[12:13]
	s_nop 0
	v_addc_co_u32_e32 v97, vcc, 0, v113, vcc
	v_add_co_u32_e32 v100, vcc, 0x3000, v112
	v_lshl_add_u64 v[128:129], v[112:113], 0, s[14:15]
	v_lshl_add_u64 v[132:133], v[112:113], 0, s[16:17]
	v_lshl_add_u64 v[136:137], v[112:113], 0, s[18:19]
	v_lshl_add_u64 v[140:141], v[112:113], 0, s[20:21]
	v_addc_co_u32_e32 v101, vcc, 0, v113, vcc
	global_load_dwordx4 v[72:75], v[80:81], off offset:16 nt
	global_load_dwordx4 v[68:71], v[80:81], off nt
	global_load_dwordx4 v[84:87], v[80:81], off offset:2064 nt
	s_nop 0
	global_load_dwordx4 v[80:83], v[80:81], off offset:2048 nt
	s_nop 0
	global_load_dwordx4 v[88:91], v[96:97], off nt
	global_load_dwordx4 v[92:95], v[96:97], off offset:2048 nt
	s_nop 0
	global_load_dwordx4 v[96:99], v[96:97], off offset:-4096 nt
	s_nop 0
	global_load_dwordx4 v[108:111], v[100:101], off nt
	s_nop 0
	global_load_dwordx4 v[100:103], v[112:113], off nt
	global_load_dwordx4 v[116:119], v[112:113], off offset:1024 nt
	global_load_dwordx4 v[104:107], v[112:113], off offset:2048 nt
	global_load_dwordx4 v[120:123], v[112:113], off offset:3072 nt
	s_nop 0
	global_load_dwordx4 v[112:115], v[114:115], off offset:2048 nt
	s_nop 0
	global_load_dwordx4 v[124:127], v[124:125], off offset:1024 nt
	s_nop 0
	global_load_dwordx4 v[128:131], v[128:129], off offset:1024 nt
	s_nop 0
	global_load_dwordx4 v[132:135], v[132:133], off offset:1024 nt
	s_nop 0
	global_load_dwordx4 v[136:139], v[136:137], off offset:1024 nt
	s_nop 0
	global_load_dwordx4 v[140:143], v[140:141], off offset:1024 nt
	s_waitcnt vmcnt(19)

; #define GAS __attribute__((address_space(1)))
; __device__ __forceinline__ f32x4 bf4(unsigned a, unsigned b) { return (f32x4){bflo(a), bfhi(a), bflo(b), bfhi(b)}; }
; template <int l>
; __device__ __forceinline__ void layer_phases(Frame& F, const XcdBarrier& bar, const int lo, const int hi) {
;     ...
;             auto process_row = [&](const int m, v4u (&xr)[4], v4u (&yr)[14], const float gtv) {
;                 int ln = F.lane; asm volatile("" : "+v"(ln));
;                 const float* mrow = (const float*)(ws + WS_MOD) + ((size_t)l * 8 + (m >> 11)) * 12288;
;                 float gt[7];
; #pragma unroll
;                 for (int k = 0; k < 6; ++k) gt[k] = __uint_as_float((unsigned)__builtin_amdgcn_readlane((int)__float_as_uint(gtv), k));
;                 gt[6] = 1.0f;
;                 f32x4 v[8]; float s = 0.f;
; #pragma unroll
;                 for (int jh = 0; jh < 2; ++jh) { const v4u xa = xr[2 * jh], xb = xr[2 * jh + 1];
;                     v[4 * jh] = bf4(xa.x, xa.y); v[4 * jh + 1] = bf4(xa.z, xa.w); v[4 * jh + 2] = bf4(xb.x, xb.y); v[4 * jh + 3] = bf4(xb.z, xb.w); }
; #pragma unroll
;                 for (int jh = 0; jh < 2; ++jh) {
; #pragma unroll
;                     for (int i = 0; i < 4; ++i) { const int j = 4 * jh + i, k = 16 * ln + 1024 * jh + 4 * i; f32x4 f = (f32x4){0.f, 0.f, 0.f, 0.f};
; #pragma unroll
;                         for (int q = 0; q < 7; ++q) { const unsigned w = yr[7 * jh + q][i]; const float gq = gt[q];
;                             const auto lo2 = __builtin_amdgcn_cvt_pk_f32_fp8((int)w, false), hi2 = __builtin_amdgcn_cvt_pk_f32_fp8((int)w, true);
;                             f.x += gq * lo2[0]; f.y += gq * lo2[1]; f.z += gq * hi2[0]; f.w += gq * hi2[1]; }
;                         v[j] = v[j] * ALPHA + *(const GAS f32x4*)(mrow + 10240 + k) * (f * (1.0f / (float)(1 << YSHIFT)));
;                         s += (v[j].x + v[j].y) + (v[j].z + v[j].w); }
.LBB0_979:
	s_waitcnt lgkmcnt(0)
	v_cvt_pk_f32_fp8_sdwa v[146:147], v32 src0_sel:WORD_1
	v_mov_b32_e32 v144, v206
	s_waitcnt lgkmcnt(0)
	v_cvt_pk_f32_fp8_sdwa v[150:151], v40 src0_sel:WORD_1
	v_cvt_pk_f32_fp8_sdwa v[158:159], v24 src0_sel:WORD_1
	v_readlane_b32 s46, v208, 0
	v_lshlrev_b32_e32 v156, 4, v144
	v_cvt_pk_f32_fp8_e32 v[144:145], v32
	s_waitcnt lgkmcnt(0)
	v_cvt_pk_f32_fp8_sdwa v[192:193], v48 src0_sel:WORD_1
	v_readlane_b32 s44, v208, 1
	v_cvt_pk_f32_fp8_e32 v[148:149], v40
	v_cvt_pk_f32_fp8_sdwa v[196:197], v16 src0_sel:WORD_1
	v_pk_fma_f32 v[146:147], s[46:47], v[146:147], 0 op_sel_hi:[0,1,0]
	v_readlane_b32 s42, v208, 2
	v_cvt_pk_f32_fp8_e32 v[152:153], v24
	v_cvt_pk_f32_fp8_sdwa v[200:201], v20 src0_sel:WORD_1
	v_pk_fma_f32 v[146:147], s[44:45], v[150:151], v[146:147] op_sel_hi:[0,1,1]
	s_ashr_i32 s4, s36, 11
	s_lshl_b32 s100, s4, 13
	v_readlane_b32 s40, v208, 3
	v_cvt_pk_f32_fp8_e32 v[190:191], v48
	v_cvt_pk_f32_fp8_sdwa v[204:205], v28 src0_sel:WORD_1
	v_pk_fma_f32 v[146:147], s[42:43], v[158:159], v[146:147] op_sel_hi:[0,1,1]
	s_mul_i32 s33, s4, 0xc000
	v_readlane_b32 s38, v208, 4
	v_cvt_pk_f32_fp8_e32 v[194:195], v16
	v_pk_fma_f32 v[144:145], s[46:47], v[144:145], 0 op_sel_hi:[0,1,0]
	v_pk_fma_f32 v[146:147], s[40:41], v[192:193], v[146:147] op_sel_hi:[0,1,1]
	s_mul_hi_i32 s5, s4, 0xc000
	v_readlane_b32 s4, v208, 5
	s_add_u32 s48, s56, s33
	v_cvt_pk_f32_fp8_e32 v[198:199], v20
	v_pk_fma_f32 v[144:145], s[44:45], v[148:149], v[144:145] op_sel_hi:[0,1,1]
	v_pk_fma_f32 v[146:147], s[38:39], v[196:197], v[146:147] op_sel_hi:[0,1,1]
	v_ashrrev_i32_e32 v157, 31, v156
	s_addc_u32 s49, s57, s5
	s_sub_u32 s100, s100, s48
	s_sub_u32 s100, s100, 0x10a000
	v_cvt_pk_f32_fp8_e32 v[202:203], v28
	v_pk_fma_f32 v[144:145], s[42:43], v[152:153], v[144:145] op_sel_hi:[0,1,1]
	v_pk_fma_f32 v[146:147], s[4:5], v[200:201], v[146:147] op_sel_hi:[0,1,1]
	v_lshlrev_b64 v[158:159], 2, v[156:157]
	v_pk_fma_f32 v[144:145], s[40:41], v[190:191], v[144:145] op_sel_hi:[0,1,1]
	v_pk_add_f32 v[190:191], v[146:147], v[204:205]
	v_lshl_add_u64 v[204:205], s[48:49], 0, v[158:159]
	v_pk_fma_f32 v[144:145], s[38:39], v[194:195], v[144:145] op_sel_hi:[0,1,1]
	v_add_co_u32_e32 v152, vcc, s67, v204
	v_pk_fma_f32 v[144:145], s[4:5], v[198:199], v[144:145] op_sel_hi:[0,1,1]
	v_lshl_add_u64 v[198:199], v[204:205], 0, s[22:23]
	v_addc_co_u32_e32 v153, vcc, 0, v205, vcc
	v_pk_add_f32 v[192:193], v[144:145], v[202:203]
	v_add_u32_e32 v247, s100, v152
	v_add_u32_e32 v247, 0xfffff000, v247
	ds_read_b128 v[194:197], v247
	v_add_u32_e32 v247, s100, v198
	ds_read_b128 v[144:147], v247 offset:48
	v_add_u32_e32 v247, s100, v198
	ds_read_b128 v[148:151], v247 offset:32
	s_nop 0
	v_add_u32_e32 v247, s100, v198
	ds_read_b128 v[198:201], v247 offset:16
	v_pk_mul_f32 v[192:193], v[192:193], s[24:25] op_sel_hi:[1,0]
	v_pk_mul_f32 v[190:191], v[190:191], s[24:25] op_sel_hi:[1,0]
	v_lshlrev_b32_e32 v186, 16, v4
	v_and_b32_e32 v187, 0xffff0000, v4
	v_lshlrev_b32_e32 v188, 16, v5
	v_and_b32_e32 v189, 0xffff0000, v5
	v_cvt_pk_f32_fp8_e32 v[202:203], v25
	v_cvt_pk_f32_fp8_sdwa v[218:219], v25 src0_sel:WORD_1
	v_cvt_pk_f32_fp8_e32 v[220:221], v49
	v_cvt_pk_f32_fp8_sdwa v[222:223], v49 src0_sel:WORD_1
	v_cvt_pk_f32_fp8_e32 v[224:225], v17
	v_cvt_pk_f32_fp8_sdwa v[226:227], v17 src0_sel:WORD_1
	v_cvt_pk_f32_fp8_e32 v[228:229], v21
	v_cvt_pk_f32_fp8_sdwa v[230:231], v21 src0_sel:WORD_1
	v_cvt_pk_f32_fp8_e32 v[232:233], v29
	v_cvt_pk_f32_fp8_sdwa v[234:235], v29 src0_sel:WORD_1
	v_lshlrev_b32_e32 v178, 16, v6
	v_and_b32_e32 v179, 0xffff0000, v6
	v_lshlrev_b32_e32 v176, 16, v7
	v_and_b32_e32 v177, 0xffff0000, v7
	v_lshlrev_b32_e32 v182, 16, v0
	v_and_b32_e32 v183, 0xffff0000, v0
	v_lshlrev_b32_e32 v180, 16, v1
	v_and_b32_e32 v181, 0xffff0000, v1
	v_lshlrev_b32_e32 v154, 16, v2
	v_and_b32_e32 v155, 0xffff0000, v2
	v_lshlrev_b32_e32 v184, 16, v3
	v_and_b32_e32 v185, 0xffff0000, v3
	v_lshl_add_u64 v[204:205], v[204:205], 0, s[28:29]
	v_lshlrev_b32_e32 v172, 16, v12
	v_and_b32_e32 v173, 0xffff0000, v12
	v_lshlrev_b32_e32 v174, 16, v13
	v_and_b32_e32 v175, 0xffff0000, v13
	v_lshlrev_b32_e32 v168, 16, v14
	v_and_b32_e32 v169, 0xffff0000, v14
	v_lshlrev_b32_e32 v170, 16, v15
	v_and_b32_e32 v171, 0xffff0000, v15
	v_lshlrev_b32_e32 v164, 16, v8
	v_and_b32_e32 v165, 0xffff0000, v8
	v_lshlrev_b32_e32 v166, 16, v9
	v_and_b32_e32 v167, 0xffff0000, v9
	v_lshlrev_b32_e32 v160, 16, v10
	v_and_b32_e32 v161, 0xffff0000, v10
	v_lshlrev_b32_e32 v162, 16, v11
	v_and_b32_e32 v163, 0xffff0000, v11
	s_ashr_i32 s37, s36, 31
	s_waitcnt lgkmcnt(0)
	v_pk_mul_f32 v[190:191], v[196:197], v[190:191]
	v_pk_mul_f32 v[192:193], v[194:195], v[192:193]
	v_pk_fma_f32 v[188:189], v[188:189], s[26:27], v[190:191] op_sel_hi:[1,0,1]
	v_pk_fma_f32 v[190:191], v[186:187], s[26:27], v[192:193] op_sel_hi:[1,0,1]
	v_cvt_pk_f32_fp8_e32 v[186:187], v33
	v_cvt_pk_f32_fp8_sdwa v[192:193], v33 src0_sel:WORD_1
	v_cvt_pk_f32_fp8_e32 v[194:195], v41
	v_cvt_pk_f32_fp8_sdwa v[196:197], v41 src0_sel:WORD_1
	v_pk_fma_f32 v[186:187], s[46:47], v[186:187], 0 op_sel_hi:[0,1,0]
	v_pk_fma_f32 v[192:193], s[46:47], v[192:193], 0 op_sel_hi:[0,1,0]
	v_pk_fma_f32 v[186:187], s[44:45], v[194:195], v[186:187] op_sel_hi:[0,1,1]
	v_pk_fma_f32 v[192:193], s[44:45], v[196:197], v[192:193] op_sel_hi:[0,1,1]
	v_pk_fma_f32 v[186:187], s[42:43], v[202:203], v[186:187] op_sel_hi:[0,1,1]
	v_pk_fma_f32 v[192:193], s[42:43], v[218:219], v[192:193] op_sel_hi:[0,1,1]
	v_pk_fma_f32 v[186:187], s[40:41], v[220:221], v[186:187] op_sel_hi:[0,1,1]
	v_pk_fma_f32 v[192:193], s[40:41], v[222:223], v[192:193] op_sel_hi:[0,1,1]
	v_pk_fma_f32 v[186:187], s[38:39], v[224:225], v[186:187] op_sel_hi:[0,1,1]
	v_pk_fma_f32 v[192:193], s[38:39], v[226:227], v[192:193] op_sel_hi:[0,1,1]
	v_pk_fma_f32 v[186:187], s[4:5], v[228:229], v[186:187] op_sel_hi:[0,1,1]
	v_pk_fma_f32 v[192:193], s[4:5], v[230:231], v[192:193] op_sel_hi:[0,1,1]
	v_pk_add_f32 v[186:187], v[186:187], v[232:233]
	v_pk_add_f32 v[192:193], v[192:193], v[234:235]
	v_pk_mul_f32 v[186:187], v[186:187], s[24:25] op_sel_hi:[1,0]
	v_pk_mul_f32 v[192:193], v[192:193], s[24:25] op_sel_hi:[1,0]
	s_waitcnt lgkmcnt(0)
; #define GAS __attribute__((address_space(1)))
; template <int l>
; __device__ __forceinline__ void layer_phases(Frame& F, const XcdBarrier& bar, const int lo, const int hi) {
;     ...
;                 for (int jh = 0; jh < 2; ++jh) {
; #pragma unroll
;                     for (int i = 0; i < 4; ++i) { const int j = 4 * jh + i, k = 16 * ln + 1024 * jh + 4 * i; f32x4 f = (f32x4){0.f, 0.f, 0.f, 0.f};
; #pragma unroll
;                         for (int q = 0; q < 7; ++q) { const unsigned w = yr[7 * jh + q][i]; const float gq = gt[q];
;                             const auto lo2 = __builtin_amdgcn_cvt_pk_f32_fp8((int)w, false), hi2 = __builtin_amdgcn_cvt_pk_f32_fp8((int)w, true);
;                             f.x += gq * lo2[0]; f.y += gq * lo2[1]; f.z += gq * hi2[0]; f.w += gq * hi2[1]; }
;                         v[j] = v[j] * ALPHA + *(const GAS f32x4*)(mrow + 10240 + k) * (f * (1.0f / (float)(1 << YSHIFT)));
;                         s += (v[j].x + v[j].y) + (v[j].z + v[j].w); }
	v_pk_mul_f32 v[186:187], v[198:199], v[186:187]
	v_pk_mul_f32 v[192:193], v[200:201], v[192:193]
	v_pk_fma_f32 v[178:179], v[178:179], s[26:27], v[186:187] op_sel_hi:[1,0,1]
	v_pk_fma_f32 v[176:177], v[176:177], s[26:27], v[192:193] op_sel_hi:[1,0,1]
	v_mov_b32_e32 v186, v190
	v_mov_b32_e32 v187, v178
	v_mov_b32_e32 v192, v191
	v_mov_b32_e32 v193, v179
	v_pk_add_f32 v[186:187], v[186:187], v[192:193]
	v_mov_b32_e32 v192, v188
	v_mov_b32_e32 v193, v176
	v_mov_b32_e32 v194, v189
	v_mov_b32_e32 v195, v177
	v_pk_add_f32 v[192:193], v[192:193], v[194:195]
	v_cvt_pk_f32_fp8_sdwa v[194:195], v34 src0_sel:WORD_1
	v_pk_add_f32 v[186:187], v[186:187], v[192:193]
	v_cvt_pk_f32_fp8_e32 v[196:197], v42
	v_add_f32_e32 v186, 0, v186
	v_add_f32_e32 v192, v186, v187
	v_cvt_pk_f32_fp8_e32 v[186:187], v34
	v_cvt_pk_f32_fp8_sdwa v[198:199], v42 src0_sel:WORD_1
	v_cvt_pk_f32_fp8_e32 v[200:201], v26
	v_cvt_pk_f32_fp8_sdwa v[202:203], v26 src0_sel:WORD_1
	v_cvt_pk_f32_fp8_e32 v[218:219], v50
	v_cvt_pk_f32_fp8_sdwa v[220:221], v50 src0_sel:WORD_1
	v_cvt_pk_f32_fp8_e32 v[222:223], v18
	v_cvt_pk_f32_fp8_sdwa v[224:225], v18 src0_sel:WORD_1
	v_pk_fma_f32 v[194:195], s[46:47], v[194:195], 0 op_sel_hi:[0,1,0]
	v_pk_fma_f32 v[186:187], s[46:47], v[186:187], 0 op_sel_hi:[0,1,0]
	v_cvt_pk_f32_fp8_e32 v[226:227], v22
	v_cvt_pk_f32_fp8_sdwa v[228:229], v22 src0_sel:WORD_1
	v_pk_fma_f32 v[186:187], s[44:45], v[196:197], v[186:187] op_sel_hi:[0,1,1]
	v_pk_fma_f32 v[194:195], s[44:45], v[198:199], v[194:195] op_sel_hi:[0,1,1]
	v_cvt_pk_f32_fp8_e32 v[230:231], v30
	v_cvt_pk_f32_fp8_sdwa v[232:233], v30 src0_sel:WORD_1
	v_pk_fma_f32 v[194:195], s[42:43], v[202:203], v[194:195] op_sel_hi:[0,1,1]
	v_pk_fma_f32 v[186:187], s[42:43], v[200:201], v[186:187] op_sel_hi:[0,1,1]
	v_pk_fma_f32 v[186:187], s[40:41], v[218:219], v[186:187] op_sel_hi:[0,1,1]
	v_pk_fma_f32 v[194:195], s[40:41], v[220:221], v[194:195] op_sel_hi:[0,1,1]
	v_pk_fma_f32 v[194:195], s[38:39], v[224:225], v[194:195] op_sel_hi:[0,1,1]
	v_pk_fma_f32 v[186:187], s[38:39], v[222:223], v[186:187] op_sel_hi:[0,1,1]
	v_pk_fma_f32 v[186:187], s[4:5], v[226:227], v[186:187] op_sel_hi:[0,1,1]
	v_pk_fma_f32 v[194:195], s[4:5], v[228:229], v[194:195] op_sel_hi:[0,1,1]
	v_pk_add_f32 v[194:195], v[194:195], v[232:233]
	v_pk_add_f32 v[186:187], v[186:187], v[230:231]
	v_pk_mul_f32 v[194:195], v[194:195], s[24:25] op_sel_hi:[1,0]
	v_pk_mul_f32 v[186:187], v[186:187], s[24:25] op_sel_hi:[1,0]
	v_pk_mul_f32 v[150:151], v[150:151], v[194:195]
	v_pk_mul_f32 v[148:149], v[148:149], v[186:187]
	v_pk_fma_f32 v[180:181], v[180:181], s[26:27], v[150:151] op_sel_hi:[1,0,1]
	v_pk_fma_f32 v[182:183], v[182:183], s[26:27], v[148:149] op_sel_hi:[1,0,1]
	v_mov_b32_e32 v151, v181
	v_pk_mov_b32 v[148:149], v[182:183], v[180:181] op_sel:[1,0]
	v_mov_b32_e32 v150, v182
	v_pk_add_f32 v[148:149], v[148:149], v[150:151]
	v_cvt_pk_f32_fp8_sdwa v[150:151], v35 src0_sel:WORD_1
	v_pk_add_f32 v[194:195], v[148:149], v[148:149] op_sel:[0,1] op_sel_hi:[1,0]
	v_cvt_pk_f32_fp8_e32 v[148:149], v35
	v_cvt_pk_f32_fp8_e32 v[186:187], v43
	v_cvt_pk_f32_fp8_sdwa v[196:197], v43 src0_sel:WORD_1
	v_cvt_pk_f32_fp8_e32 v[198:199], v27
	v_cvt_pk_f32_fp8_sdwa v[200:201], v27 src0_sel:WORD_1
	v_cvt_pk_f32_fp8_e32 v[202:203], v51
	v_cvt_pk_f32_fp8_sdwa v[218:219], v51 src0_sel:WORD_1
	v_cvt_pk_f32_fp8_e32 v[220:221], v19
	v_cvt_pk_f32_fp8_sdwa v[222:223], v19 src0_sel:WORD_1
	v_pk_fma_f32 v[150:151], s[46:47], v[150:151], 0 op_sel_hi:[0,1,0]
	v_pk_fma_f32 v[148:149], s[46:47], v[148:149], 0 op_sel_hi:[0,1,0]
	v_cvt_pk_f32_fp8_e32 v[224:225], v23
	v_cvt_pk_f32_fp8_sdwa v[226:227], v23 src0_sel:WORD_1
	v_pk_fma_f32 v[148:149], s[44:45], v[186:187], v[148:149] op_sel_hi:[0,1,1]
	v_pk_fma_f32 v[150:151], s[44:45], v[196:197], v[150:151] op_sel_hi:[0,1,1]
	v_cvt_pk_f32_fp8_e32 v[228:229], v31
	v_cvt_pk_f32_fp8_sdwa v[230:231], v31 src0_sel:WORD_1
	v_pk_fma_f32 v[150:151], s[42:43], v[200:201], v[150:151] op_sel_hi:[0,1,1]
	v_pk_fma_f32 v[148:149], s[42:43], v[198:199], v[148:149] op_sel_hi:[0,1,1]
	v_pk_fma_f32 v[148:149], s[40:41], v[202:203], v[148:149] op_sel_hi:[0,1,1]
	v_pk_fma_f32 v[150:151], s[40:41], v[218:219], v[150:151] op_sel_hi:[0,1,1]
	v_pk_fma_f32 v[150:151], s[38:39], v[222:223], v[150:151] op_sel_hi:[0,1,1]
	v_pk_fma_f32 v[148:149], s[38:39], v[220:221], v[148:149] op_sel_hi:[0,1,1]
	v_pk_fma_f32 v[148:149], s[4:5], v[224:225], v[148:149] op_sel_hi:[0,1,1]
	v_pk_fma_f32 v[150:151], s[4:5], v[226:227], v[150:151] op_sel_hi:[0,1,1]
	v_pk_add_f32 v[150:151], v[150:151], v[230:231]
	v_pk_add_f32 v[148:149], v[148:149], v[228:229]
	v_pk_mul_f32 v[150:151], v[150:151], s[24:25] op_sel_hi:[1,0]
	v_pk_mul_f32 v[148:149], v[148:149], s[24:25] op_sel_hi:[1,0]
	v_pk_mul_f32 v[146:147], v[146:147], v[150:151]
	v_pk_mul_f32 v[144:145], v[144:145], v[148:149]
	v_pk_fma_f32 v[184:185], v[184:185], s[26:27], v[146:147] op_sel_hi:[1,0,1]
	v_pk_fma_f32 v[186:187], v[154:155], s[26:27], v[144:145] op_sel_hi:[1,0,1]
	v_cvt_pk_f32_fp8_e32 v[144:145], v36
	v_cvt_pk_f32_fp8_sdwa v[146:147], v36 src0_sel:WORD_1
	v_cvt_pk_f32_fp8_e32 v[148:149], v44
	v_cvt_pk_f32_fp8_sdwa v[150:151], v44 src0_sel:WORD_1
	v_cvt_pk_f32_fp8_e32 v[154:155], v52
	v_cvt_pk_f32_fp8_sdwa v[200:201], v52 src0_sel:WORD_1
	v_cvt_pk_f32_fp8_e32 v[202:203], v56
	v_cvt_pk_f32_fp8_sdwa v[218:219], v56 src0_sel:WORD_1
	v_cvt_pk_f32_fp8_e32 v[220:221], v60
	v_cvt_pk_f32_fp8_sdwa v[222:223], v60 src0_sel:WORD_1
	v_pk_fma_f32 v[146:147], s[46:47], v[146:147], 0 op_sel_hi:[0,1,0]
	v_pk_fma_f32 v[144:145], s[46:47], v[144:145], 0 op_sel_hi:[0,1,0]
	v_cvt_pk_f32_fp8_e32 v[224:225], v64
	v_cvt_pk_f32_fp8_sdwa v[226:227], v64 src0_sel:WORD_1
; #define GAS __attribute__((address_space(1)))
; template <int l>
; __device__ __forceinline__ void layer_phases(Frame& F, const XcdBarrier& bar, const int lo, const int hi) {
;     ...
;                     for (int i = 0; i < 4; ++i) { const int j = 4 * jh + i, k = 16 * ln + 1024 * jh + 4 * i; f32x4 f = (f32x4){0.f, 0.f, 0.f, 0.f};
; #pragma unroll
;                         for (int q = 0; q < 7; ++q) { const unsigned w = yr[7 * jh + q][i]; const float gq = gt[q];
;                             const auto lo2 = __builtin_amdgcn_cvt_pk_f32_fp8((int)w, false), hi2 = __builtin_amdgcn_cvt_pk_f32_fp8((int)w, true);
;                             f.x += gq * lo2[0]; f.y += gq * lo2[1]; f.z += gq * hi2[0]; f.w += gq * hi2[1]; }
;                         v[j] = v[j] * ALPHA + *(const GAS f32x4*)(mrow + 10240 + k) * (f * (1.0f / (float)(1 << YSHIFT)));
;                         s += (v[j].x + v[j].y) + (v[j].z + v[j].w); }
	v_pk_fma_f32 v[144:145], s[44:45], v[148:149], v[144:145] op_sel_hi:[0,1,1]
	v_pk_fma_f32 v[146:147], s[44:45], v[150:151], v[146:147] op_sel_hi:[0,1,1]
	v_cvt_pk_f32_fp8_e32 v[228:229], v76
	v_cvt_pk_f32_fp8_sdwa v[230:231], v76 src0_sel:WORD_1
	v_pk_fma_f32 v[146:147], s[42:43], v[200:201], v[146:147] op_sel_hi:[0,1,1]
	v_pk_fma_f32 v[144:145], s[42:43], v[154:155], v[144:145] op_sel_hi:[0,1,1]
	v_pk_fma_f32 v[144:145], s[40:41], v[202:203], v[144:145] op_sel_hi:[0,1,1]
	v_pk_fma_f32 v[146:147], s[40:41], v[218:219], v[146:147] op_sel_hi:[0,1,1]
	v_pk_fma_f32 v[146:147], s[38:39], v[222:223], v[146:147] op_sel_hi:[0,1,1]
	v_pk_fma_f32 v[144:145], s[38:39], v[220:221], v[144:145] op_sel_hi:[0,1,1]
	v_pk_fma_f32 v[144:145], s[4:5], v[224:225], v[144:145] op_sel_hi:[0,1,1]
	v_pk_fma_f32 v[146:147], s[4:5], v[226:227], v[146:147] op_sel_hi:[0,1,1]
	v_pk_add_f32 v[200:201], v[146:147], v[230:231]
	v_pk_add_f32 v[202:203], v[144:145], v[228:229]
	v_add_u32_e32 v247, s100, v152
	ds_read_b128 v[152:155], v247
	s_nop 0
	v_add_u32_e32 v247, s100, v204
	ds_read_b128 v[144:147], v247 offset:48
	v_add_u32_e32 v247, s100, v204
	ds_read_b128 v[148:151], v247 offset:32
	v_add_u32_e32 v247, s100, v204
	ds_read_b128 v[218:221], v247 offset:16
	v_pk_mul_f32 v[202:203], v[202:203], s[24:25] op_sel_hi:[1,0]
	v_pk_mul_f32 v[200:201], v[200:201], s[24:25] op_sel_hi:[1,0]
	v_add_f32_e32 v196, v186, v187
	v_add_f32_e32 v198, v184, v185
	v_cvt_pk_f32_fp8_sdwa v[204:205], v57 src0_sel:WORD_1
	v_cvt_pk_f32_fp8_e32 v[222:223], v61
	v_cvt_pk_f32_fp8_sdwa v[224:225], v61 src0_sel:WORD_1
	v_cvt_pk_f32_fp8_e32 v[226:227], v65
	v_cvt_pk_f32_fp8_sdwa v[228:229], v65 src0_sel:WORD_1
	v_cvt_pk_f32_fp8_e32 v[230:231], v77
	v_cvt_pk_f32_fp8_sdwa v[232:233], v77 src0_sel:WORD_1
	s_waitcnt lgkmcnt(0)
	v_pk_mul_f32 v[154:155], v[154:155], v[200:201]
	v_pk_mul_f32 v[152:153], v[152:153], v[202:203]
	v_pk_fma_f32 v[174:175], v[174:175], s[26:27], v[154:155] op_sel_hi:[1,0,1]
	v_pk_fma_f32 v[172:173], v[172:173], s[26:27], v[152:153] op_sel_hi:[1,0,1]
	v_mov_b32_e32 v197, v174
	v_mov_b32_e32 v193, v172
	v_mov_b32_e32 v195, v173
	v_mov_b32_e32 v199, v175
	v_pk_add_f32 v[152:153], v[192:193], v[194:195]
	v_pk_add_f32 v[154:155], v[196:197], v[198:199]
	v_cvt_pk_f32_fp8_e32 v[194:195], v45
	v_pk_add_f32 v[152:153], v[152:153], v[154:155]
	v_cvt_pk_f32_fp8_sdwa v[154:155], v37 src0_sel:WORD_1
	v_pk_add_f32 v[192:193], v[152:153], v[152:153] op_sel:[0,1] op_sel_hi:[1,0]
	v_cvt_pk_f32_fp8_e32 v[152:153], v37
	v_cvt_pk_f32_fp8_sdwa v[196:197], v45 src0_sel:WORD_1
	v_cvt_pk_f32_fp8_e32 v[198:199], v53
	v_cvt_pk_f32_fp8_sdwa v[200:201], v53 src0_sel:WORD_1
	v_cvt_pk_f32_fp8_e32 v[202:203], v57
	v_pk_fma_f32 v[154:155], s[46:47], v[154:155], 0 op_sel_hi:[0,1,0]
	v_pk_fma_f32 v[152:153], s[46:47], v[152:153], 0 op_sel_hi:[0,1,0]
	v_pk_fma_f32 v[152:153], s[44:45], v[194:195], v[152:153] op_sel_hi:[0,1,1]
	v_pk_fma_f32 v[154:155], s[44:45], v[196:197], v[154:155] op_sel_hi:[0,1,1]
	v_pk_fma_f32 v[154:155], s[42:43], v[200:201], v[154:155] op_sel_hi:[0,1,1]
	v_pk_fma_f32 v[152:153], s[42:43], v[198:199], v[152:153] op_sel_hi:[0,1,1]
	v_pk_fma_f32 v[152:153], s[40:41], v[202:203], v[152:153] op_sel_hi:[0,1,1]
	v_pk_fma_f32 v[154:155], s[40:41], v[204:205], v[154:155] op_sel_hi:[0,1,1]
	v_pk_fma_f32 v[154:155], s[38:39], v[224:225], v[154:155] op_sel_hi:[0,1,1]
	v_pk_fma_f32 v[152:153], s[38:39], v[222:223], v[152:153] op_sel_hi:[0,1,1]
	v_pk_fma_f32 v[152:153], s[4:5], v[226:227], v[152:153] op_sel_hi:[0,1,1]
	v_pk_fma_f32 v[154:155], s[4:5], v[228:229], v[154:155] op_sel_hi:[0,1,1]
	v_pk_add_f32 v[154:155], v[154:155], v[232:233]
	v_pk_add_f32 v[152:153], v[152:153], v[230:231]
	v_pk_mul_f32 v[154:155], v[154:155], s[24:25] op_sel_hi:[1,0]
	v_pk_mul_f32 v[152:153], v[152:153], s[24:25] op_sel_hi:[1,0]
	s_waitcnt lgkmcnt(0)
	v_pk_mul_f32 v[154:155], v[220:221], v[154:155]
	v_pk_mul_f32 v[194:195], v[218:219], v[152:153]
	v_pk_fma_f32 v[152:153], v[170:171], s[26:27], v[154:155] op_sel_hi:[1,0,1]
	v_pk_fma_f32 v[154:155], v[168:169], s[26:27], v[194:195] op_sel_hi:[1,0,1]
	v_mov_b32_e32 v171, v153
	v_pk_mov_b32 v[168:169], v[154:155], v[152:153] op_sel:[1,0]
	v_mov_b32_e32 v170, v154
	v_pk_add_f32 v[168:169], v[168:169], v[170:171]
	v_cvt_pk_f32_fp8_e32 v[170:171], v38
	v_cvt_pk_f32_fp8_sdwa v[194:195], v38 src0_sel:WORD_1
	v_cvt_pk_f32_fp8_e32 v[196:197], v46
	v_cvt_pk_f32_fp8_sdwa v[198:199], v46 src0_sel:WORD_1
	v_cvt_pk_f32_fp8_e32 v[200:201], v54
	v_cvt_pk_f32_fp8_sdwa v[202:203], v54 src0_sel:WORD_1
	v_cvt_pk_f32_fp8_e32 v[204:205], v58
	v_cvt_pk_f32_fp8_sdwa v[218:219], v58 src0_sel:WORD_1
	v_cvt_pk_f32_fp8_e32 v[220:221], v62
	v_cvt_pk_f32_fp8_sdwa v[222:223], v62 src0_sel:WORD_1
	v_pk_fma_f32 v[194:195], s[46:47], v[194:195], 0 op_sel_hi:[0,1,0]
	v_pk_fma_f32 v[170:171], s[46:47], v[170:171], 0 op_sel_hi:[0,1,0]
	v_cvt_pk_f32_fp8_e32 v[224:225], v66
	v_cvt_pk_f32_fp8_sdwa v[226:227], v66 src0_sel:WORD_1
	v_pk_fma_f32 v[170:171], s[44:45], v[196:197], v[170:171] op_sel_hi:[0,1,1]
	v_pk_fma_f32 v[194:195], s[44:45], v[198:199], v[194:195] op_sel_hi:[0,1,1]
	v_cvt_pk_f32_fp8_e32 v[228:229], v78
	v_cvt_pk_f32_fp8_sdwa v[230:231], v78 src0_sel:WORD_1
	v_pk_fma_f32 v[194:195], s[42:43], v[202:203], v[194:195] op_sel_hi:[0,1,1]
	v_pk_fma_f32 v[170:171], s[42:43], v[200:201], v[170:171] op_sel_hi:[0,1,1]
	v_pk_fma_f32 v[170:171], s[40:41], v[204:205], v[170:171] op_sel_hi:[0,1,1]
	v_pk_fma_f32 v[194:195], s[40:41], v[218:219], v[194:195] op_sel_hi:[0,1,1]
	v_pk_fma_f32 v[194:195], s[38:39], v[222:223], v[194:195] op_sel_hi:[0,1,1]
	v_pk_fma_f32 v[170:171], s[38:39], v[220:221], v[170:171] op_sel_hi:[0,1,1]
; #define GAS __attribute__((address_space(1)))
; template <int l>
; __device__ __forceinline__ void layer_phases(Frame& F, const XcdBarrier& bar, const int lo, const int hi) {
;     ...
;                         v[j] = v[j] * ALPHA + *(const GAS f32x4*)(mrow + 10240 + k) * (f * (1.0f / (float)(1 << YSHIFT)));
;                         s += (v[j].x + v[j].y) + (v[j].z + v[j].w); }
;                 }
;                 const float mean = wave_sum(s) * (1.f / D); float s2 = 0.f;
; #pragma unroll
;                 for (int j = 0; j < 8; ++j) { v[j] = v[j] - mean; s2 += (v[j].x * v[j].x + v[j].y * v[j].y) + (v[j].z * v[j].z + v[j].w * v[j].w); }
;                 const float rstd = 1.f / sqrtf(wave_sum(s2) * (1.f / D) + LN_EPS);
	v_pk_fma_f32 v[170:171], s[4:5], v[224:225], v[170:171] op_sel_hi:[0,1,1]
	v_pk_fma_f32 v[194:195], s[4:5], v[226:227], v[194:195] op_sel_hi:[0,1,1]
	v_pk_add_f32 v[194:195], v[194:195], v[230:231]
	v_pk_add_f32 v[170:171], v[170:171], v[228:229]
	v_pk_mul_f32 v[194:195], v[194:195], s[24:25] op_sel_hi:[1,0]
	v_pk_mul_f32 v[170:171], v[170:171], s[24:25] op_sel_hi:[1,0]
	v_pk_mul_f32 v[150:151], v[150:151], v[194:195]
	v_pk_mul_f32 v[170:171], v[148:149], v[170:171]
	v_pk_fma_f32 v[148:149], v[166:167], s[26:27], v[150:151] op_sel_hi:[1,0,1]
	v_pk_fma_f32 v[150:151], v[164:165], s[26:27], v[170:171] op_sel_hi:[1,0,1]
	v_cvt_pk_f32_fp8_e32 v[170:171], v39
	v_cvt_pk_f32_fp8_sdwa v[194:195], v39 src0_sel:WORD_1
	v_cvt_pk_f32_fp8_e32 v[196:197], v47
	v_cvt_pk_f32_fp8_sdwa v[198:199], v47 src0_sel:WORD_1
	v_cvt_pk_f32_fp8_e32 v[200:201], v55
	v_cvt_pk_f32_fp8_sdwa v[202:203], v55 src0_sel:WORD_1
	v_cvt_pk_f32_fp8_e32 v[204:205], v59
	v_cvt_pk_f32_fp8_sdwa v[218:219], v59 src0_sel:WORD_1
	v_cvt_pk_f32_fp8_e32 v[220:221], v63
	v_cvt_pk_f32_fp8_sdwa v[222:223], v63 src0_sel:WORD_1
	v_pk_fma_f32 v[194:195], s[46:47], v[194:195], 0 op_sel_hi:[0,1,0]
	v_pk_fma_f32 v[170:171], s[46:47], v[170:171], 0 op_sel_hi:[0,1,0]
	v_cvt_pk_f32_fp8_e32 v[224:225], v67
	v_cvt_pk_f32_fp8_sdwa v[226:227], v67 src0_sel:WORD_1
	v_pk_fma_f32 v[170:171], s[44:45], v[196:197], v[170:171] op_sel_hi:[0,1,1]
	v_pk_fma_f32 v[194:195], s[44:45], v[198:199], v[194:195] op_sel_hi:[0,1,1]
	v_cvt_pk_f32_fp8_e32 v[228:229], v79
	v_cvt_pk_f32_fp8_sdwa v[230:231], v79 src0_sel:WORD_1
	v_pk_fma_f32 v[194:195], s[42:43], v[202:203], v[194:195] op_sel_hi:[0,1,1]
	v_pk_fma_f32 v[170:171], s[42:43], v[200:201], v[170:171] op_sel_hi:[0,1,1]
	v_pk_fma_f32 v[170:171], s[40:41], v[204:205], v[170:171] op_sel_hi:[0,1,1]
	v_pk_fma_f32 v[194:195], s[40:41], v[218:219], v[194:195] op_sel_hi:[0,1,1]
	v_pk_fma_f32 v[194:195], s[38:39], v[222:223], v[194:195] op_sel_hi:[0,1,1]
	v_pk_fma_f32 v[170:171], s[38:39], v[220:221], v[170:171] op_sel_hi:[0,1,1]
	v_pk_fma_f32 v[170:171], s[4:5], v[224:225], v[170:171] op_sel_hi:[0,1,1]
	v_pk_fma_f32 v[194:195], s[4:5], v[226:227], v[194:195] op_sel_hi:[0,1,1]
	v_pk_add_f32 v[194:195], v[194:195], v[230:231]
	v_pk_add_f32 v[170:171], v[170:171], v[228:229]
	v_pk_mul_f32 v[194:195], v[194:195], s[24:25] op_sel_hi:[1,0]
	v_pk_mul_f32 v[170:171], v[170:171], s[24:25] op_sel_hi:[1,0]
	v_pk_mul_f32 v[146:147], v[146:147], v[194:195]
	v_pk_mul_f32 v[170:171], v[144:145], v[170:171]
	v_pk_add_f32 v[168:169], v[168:169], v[168:169] op_sel:[0,1] op_sel_hi:[1,0]
	v_pk_fma_f32 v[144:145], v[162:163], s[26:27], v[146:147] op_sel_hi:[1,0,1]
	v_pk_fma_f32 v[146:147], v[160:161], s[26:27], v[170:171] op_sel_hi:[1,0,1]
	v_add_f32_e32 v164, v150, v151
	v_add_f32_e32 v166, v148, v149
	v_mov_b32_e32 v193, v146
	v_mov_b32_e32 v169, v147
	v_mov_b32_e32 v165, v144
	v_mov_b32_e32 v167, v145
	v_pk_add_f32 v[160:161], v[192:193], v[168:169]
	v_pk_add_f32 v[162:163], v[164:165], v[166:167]
	v_lshl_add_u64 v[204:205], s[6:7], 0, v[158:159]
	v_pk_add_f32 v[160:161], v[160:161], v[162:163]
	v_lshl_add_u64 v[230:231], s[8:9], 0, v[158:159]
	v_add_f32_e32 v160, v160, v161
	ds_bpermute_b32 v161, v209, v160
	s_waitcnt lgkmcnt(0)
	v_add_f32_e32 v160, v160, v161
	ds_bpermute_b32 v161, v210, v160
	s_waitcnt lgkmcnt(0)
	v_add_f32_e32 v160, v160, v161
	ds_bpermute_b32 v161, v211, v160
	s_waitcnt lgkmcnt(0)
	v_add_f32_e32 v160, v160, v161
	ds_bpermute_b32 v161, v212, v160
	s_waitcnt lgkmcnt(0)
	v_add_f32_e32 v160, v160, v161
	ds_bpermute_b32 v161, v213, v160
	s_waitcnt lgkmcnt(0)
	v_add_f32_e32 v160, v160, v161
	ds_bpermute_b32 v161, v214, v160
	s_waitcnt lgkmcnt(0)
	v_add_f32_e32 v168, v160, v161
	v_fmamk_f32 v191, v168, 0xba000000, v191
	v_fmamk_f32 v179, v168, 0xba000000, v179
	v_fmamk_f32 v189, v168, 0xba000000, v189
	v_fmac_f32_e32 v190, 0xba000000, v168
	v_fmamk_f32 v177, v168, 0xba000000, v177
	v_fmac_f32_e32 v178, 0xba000000, v168
	v_mov_b32_e32 v162, v191
	v_mov_b32_e32 v163, v179
	v_fmac_f32_e32 v188, 0xba000000, v168
	v_fmac_f32_e32 v176, 0xba000000, v168
	v_mov_b32_e32 v160, v190
	v_mov_b32_e32 v161, v178
	v_pk_mul_f32 v[162:163], v[162:163], v[162:163]
	v_mov_b32_e32 v164, v189
	v_mov_b32_e32 v165, v177
	v_pk_fma_f32 v[160:161], v[160:161], v[160:161], v[162:163]
	v_mov_b32_e32 v162, v188
	v_mov_b32_e32 v163, v176
	v_pk_mul_f32 v[164:165], v[164:165], v[164:165]
	v_fmamk_f32 v183, v168, 0xba000000, v183
	v_pk_fma_f32 v[162:163], v[162:163], v[162:163], v[164:165]
	v_fmac_f32_e32 v182, 0xba000000, v168
	v_pk_add_f32 v[160:161], v[160:161], v[162:163]
	v_fmamk_f32 v181, v168, 0xba000000, v181
	v_fmac_f32_e32 v180, 0xba000000, v168
	v_pk_add_f32 v[160:161], v[160:161], v[160:161] op_sel_hi:[0,1]
	v_pk_mul_f32 v[162:163], v[180:181], v[180:181]
	v_pk_mul_f32 v[164:165], v[182:183], v[182:183]
	v_fmac_f32_e32 v186, 0xba000000, v168
	v_pk_mov_b32 v[166:167], v[164:165], v[162:163] op_sel:[1,0]
	v_mov_b32_e32 v165, v163
	v_fmamk_f32 v187, v168, 0xba000000, v187
	v_fmac_f32_e32 v184, 0xba000000, v168
	v_mul_f32_e32 v160, v186, v186
	v_pk_add_f32 v[162:163], v[166:167], v[164:165]
	v_fmamk_f32 v185, v168, 0xba000000, v185
	v_pk_fma_f32 v[164:165], v[186:187], v[186:187], v[160:161] op_sel_hi:[1,1,0]
	v_mul_f32_e32 v160, v184, v184
	v_pk_add_f32 v[162:163], v[162:163], v[162:163] op_sel_hi:[0,1]
	v_pk_fma_f32 v[166:167], v[184:185], v[184:185], v[160:161] op_sel_hi:[1,1,0]
	v_fmamk_f32 v175, v168, 0xba000000, v175
	v_fmac_f32_e32 v174, 0xba000000, v168
	v_fmamk_f32 v173, v168, 0xba000000, v173
	v_fmac_f32_e32 v172, 0xba000000, v168
	v_mul_f32_e32 v164, v172, v172
	v_mul_f32_e32 v166, v173, v173
; #define GAS __attribute__((address_space(1)))
; template <int l>
; __device__ __forceinline__ void layer_phases(Frame& F, const XcdBarrier& bar, const int lo, const int hi) {
;     ...
;                 const float mean = wave_sum(s) * (1.f / D); float s2 = 0.f;
; #pragma unroll
;                 for (int j = 0; j < 8; ++j) { v[j] = v[j] - mean; s2 += (v[j].x * v[j].x + v[j].y * v[j].y) + (v[j].z * v[j].z + v[j].w * v[j].w); }
;                 const float rstd = 1.f / sqrtf(wave_sum(s2) * (1.f / D) + LN_EPS);
;                 float* orow = Fout + (size_t)m * D;
; #pragma unroll
;                 for (int j = 0; j < 8; ++j) { const int k = 16 * ln + 1024 * (j >> 2) + 4 * (j & 3);
;                     v[j] = v[j] * rstd * *(const GAS f32x4*)(g2 + k) + *(const GAS f32x4*)(b2 + k);
	v_mul_f32_e32 v162, v174, v174
	v_mul_f32_e32 v160, v175, v175
	v_pk_add_f32 v[164:165], v[164:165], v[166:167]
	v_pk_add_f32 v[160:161], v[162:163], v[160:161]
	v_fmamk_f32 v155, v168, 0xba000000, v155
	v_pk_add_f32 v[160:161], v[164:165], v[160:161]
	v_fmac_f32_e32 v154, 0xba000000, v168
	v_fmamk_f32 v153, v168, 0xba000000, v153
	v_fmac_f32_e32 v152, 0xba000000, v168
	v_pk_add_f32 v[160:161], v[160:161], v[160:161] op_sel_hi:[0,1]
	v_pk_mul_f32 v[162:163], v[152:153], v[152:153]
	v_pk_mul_f32 v[164:165], v[154:155], v[154:155]
	v_fmac_f32_e32 v150, 0xba000000, v168
	v_pk_mov_b32 v[166:167], v[164:165], v[162:163] op_sel:[1,0]
	v_mov_b32_e32 v165, v163
	v_fmamk_f32 v151, v168, 0xba000000, v151
	v_fmac_f32_e32 v148, 0xba000000, v168
	v_mul_f32_e32 v160, v150, v150
	v_pk_add_f32 v[162:163], v[166:167], v[164:165]
	v_fmamk_f32 v149, v168, 0xba000000, v149
	v_pk_fma_f32 v[164:165], v[150:151], v[150:151], v[160:161] op_sel_hi:[1,1,0]
	v_mul_f32_e32 v160, v148, v148
	v_pk_add_f32 v[162:163], v[162:163], v[162:163] op_sel_hi:[0,1]
	v_pk_fma_f32 v[166:167], v[148:149], v[148:149], v[160:161] op_sel_hi:[1,1,0]
	v_fmamk_f32 v145, v168, 0xba000000, v145
	v_fmac_f32_e32 v144, 0xba000000, v168
	v_fmamk_f32 v147, v168, 0xba000000, v147
	v_fmac_f32_e32 v146, 0xba000000, v168
	v_mul_f32_e32 v164, v146, v146
	v_mul_f32_e32 v166, v147, v147
	v_mul_f32_e32 v162, v144, v144
	v_mul_f32_e32 v160, v145, v145
	v_pk_add_f32 v[164:165], v[164:165], v[166:167]
	v_pk_add_f32 v[160:161], v[162:163], v[160:161]
	s_nop 0
	v_pk_add_f32 v[160:161], v[164:165], v[160:161]
	s_nop 0
	v_add_f32_e32 v160, v160, v161
	ds_bpermute_b32 v161, v209, v160
	s_waitcnt lgkmcnt(0)
	v_add_f32_e32 v160, v160, v161
	ds_bpermute_b32 v161, v210, v160
	s_waitcnt lgkmcnt(0)
	v_add_f32_e32 v160, v160, v161
	ds_bpermute_b32 v161, v211, v160
	s_waitcnt lgkmcnt(0)
	v_add_f32_e32 v160, v160, v161
	ds_bpermute_b32 v161, v212, v160
	s_waitcnt lgkmcnt(0)
	v_add_f32_e32 v160, v160, v161
	ds_bpermute_b32 v161, v213, v160
	s_waitcnt lgkmcnt(0)
	v_add_f32_e32 v160, v160, v161
	ds_bpermute_b32 v161, v214, v160
	s_waitcnt lgkmcnt(0)
	v_add_f32_e32 v160, v160, v161
	v_fmamk_f32 v160, v160, 0x3a000000, v215
	v_cmp_gt_f32_e32 vcc, s68, v160
	v_mul_f32_e32 v161, 0x4f800000, v160
	s_nop 0
	v_cndmask_b32_e32 v160, v160, v161, vcc
	v_sqrt_f32_e32 v161, v160
	s_nop 0
	v_add_u32_e32 v162, -1, v161
	v_fma_f32 v163, -v162, v161, v160
	v_cmp_ge_f32_e64 s[4:5], 0, v163
	v_add_u32_e32 v163, 1, v161
	s_nop 0
	v_cndmask_b32_e64 v162, v161, v162, s[4:5]
	v_fma_f32 v161, -v163, v161, v160
	v_cmp_lt_f32_e64 s[4:5], 0, v161
	s_nop 1
	v_cndmask_b32_e64 v161, v162, v163, s[4:5]
	v_mul_f32_e32 v162, 0x37800000, v161
	v_cndmask_b32_e32 v161, v161, v162, vcc
	v_cmp_class_f32_e32 vcc, v160, v217
	s_nop 1
	v_cndmask_b32_e32 v160, v161, v160, vcc
	v_div_scale_f32 v161, s[4:5], v160, v160, 1.0
	v_rcp_f32_e32 v162, v161
	s_lshl_b64 s[4:5], s[36:37], 12
	s_add_u32 s4, s52, s4
	s_addc_u32 s5, s53, s5
	v_fma_f32 v163, -v161, v162, 1.0
	v_fmac_f32_e32 v162, v163, v162
	v_div_scale_f32 v163, vcc, 1.0, v160, 1.0
	v_mul_f32_e32 v164, v163, v162
	v_fma_f32 v165, -v161, v164, v163
	v_fmac_f32_e32 v164, v165, v162
	v_fma_f32 v161, -v161, v164, v163
	v_div_fmas_f32 v161, v161, v162, v164
	v_add_u32_e32 v247, s98, v204
	ds_read_b128 v[192:195], v247 offset:48
	v_add_u32_e32 v247, s98, v204
	ds_read_b128 v[162:165], v247 offset:32
	v_add_u32_e32 v247, s98, v204
	ds_read_b128 v[166:169], v247 offset:16
	v_add_u32_e32 v247, s98, v204
	ds_read_b128 v[196:199], v247
	v_add_u32_e32 v247, s99, v230
	ds_read_b128 v[200:203], v247 offset:48
	v_add_u32_e32 v247, s99, v230
	ds_read_b128 v[218:221], v247 offset:32
	v_add_u32_e32 v247, s99, v230
	ds_read_b128 v[222:225], v247 offset:16
	v_add_u32_e32 v247, s99, v230
	ds_read_b128 v[226:229], v247
	v_div_fixup_f32 v160, v161, v160, 1.0
	v_pk_mul_f32 v[170:171], v[190:191], v[160:161] op_sel_hi:[1,0]
	v_pk_mul_f32 v[158:159], v[178:179], v[160:161] op_sel_hi:[1,0]
	v_pk_mul_f32 v[188:189], v[188:189], v[160:161] op_sel_hi:[1,0]
	v_pk_mul_f32 v[144:145], v[144:145], v[160:161] op_sel_hi:[1,0]
	v_pk_mul_f32 v[146:147], v[146:147], v[160:161] op_sel_hi:[1,0]
	v_pk_mul_f32 v[148:149], v[148:149], v[160:161] op_sel_hi:[1,0]
	v_pk_mul_f32 v[150:151], v[150:151], v[160:161] op_sel_hi:[1,0]
	s_add_i32 s46, s31, s54
	s_cmpk_gt_i32 s46, 0x3fff
	s_waitcnt lgkmcnt(0)
	v_pk_fma_f32 v[190:191], v[196:197], v[170:171], v[226:227]
	v_pk_mul_f32 v[170:171], v[176:177], v[160:161] op_sel_hi:[1,0]
	v_pk_fma_f32 v[188:189], v[198:199], v[188:189], v[228:229]
	v_pk_fma_f32 v[168:169], v[168:169], v[170:171], v[224:225]
	v_pk_fma_f32 v[170:171], v[166:167], v[158:159], v[222:223]
	v_pk_mul_f32 v[158:159], v[182:183], v[160:161] op_sel_hi:[1,0]
	v_pk_mul_f32 v[182:183], v[172:173], v[160:161] op_sel_hi:[1,0]
	v_pk_mul_f32 v[172:173], v[174:175], v[160:161] op_sel_hi:[1,0]
	v_add_co_u32_e32 v174, vcc, s55, v204
	v_pk_mul_f32 v[166:167], v[180:181], v[160:161] op_sel_hi:[1,0]
	s_nop 0
	v_addc_co_u32_e32 v175, vcc, 0, v205, vcc
	v_add_co_u32_e32 v178, vcc, s55, v230
	v_add_u32_e32 v247, s98, v174
	ds_read_b128 v[174:177], v247
	s_nop 0
	v_addc_co_u32_e32 v179, vcc, 0, v231, vcc
	v_add_u32_e32 v247, s99, v178
	ds_read_b128 v[178:181], v247
	v_pk_fma_f32 v[164:165], v[164:165], v[166:167], v[220:221]
	v_pk_fma_f32 v[166:167], v[162:163], v[158:159], v[218:219]
	v_pk_mul_f32 v[158:159], v[184:185], v[160:161] op_sel_hi:[1,0]
	v_pk_mul_f32 v[162:163], v[186:187], v[160:161] op_sel_hi:[1,0]
	v_pk_fma_f32 v[158:159], v[194:195], v[158:159], v[202:203]
	v_pk_fma_f32 v[162:163], v[192:193], v[162:163], v[200:201]
	v_pk_mul_f32 v[200:201], v[154:155], v[160:161] op_sel_hi:[1,0]
	v_pk_mul_f32 v[202:203], v[152:153], v[160:161] op_sel_hi:[1,0]
	s_waitcnt lgkmcnt(0)
; #define GAS __attribute__((address_space(1)))
; __device__ __forceinline__ unsigned pk2(float lo, float hi) { return f2bf(lo) | (f2bf(hi) << 16); }
; template <int l>
; __device__ __forceinline__ void layer_phases(Frame& F, const XcdBarrier& bar, const int lo, const int hi) {
;     ...
;                 for (int j = 0; j < 8; ++j) { const int k = 16 * ln + 1024 * (j >> 2) + 4 * (j & 3);
;                     v[j] = v[j] * rstd * *(const GAS f32x4*)(g2 + k) + *(const GAS f32x4*)(b2 + k);
;                     if (l == 1) { *(GAS f32x4*)(orow + k) = v[j]; if (j & 1) asm volatile("" ::: "memory"); } }
;                 if (l == 0) {
; #pragma unroll
;                     for (int jh = 0; jh < 2; ++jh) { v4u wa, wb; wa.x = pk2(v[4 * jh].x, v[4 * jh].y); wa.y = pk2(v[4 * jh].z, v[4 * jh].w); wa.z = pk2(v[4 * jh + 1].x, v[4 * jh + 1].y); wa.w = pk2(v[4 * jh + 1].z, v[4 * jh + 1].w);
;                         wb.x = pk2(v[4 * jh + 2].x, v[4 * jh + 2].y); wb.y = pk2(v[4 * jh + 2].z, v[4 * jh + 2].w); wb.z = pk2(v[4 * jh + 3].x, v[4 * jh + 3].y); wb.w = pk2(v[4 * jh + 3].z, v[4 * jh + 3].w);
;                         *(GAS v4u*)(x2b + (size_t)m * D + 16 * ln + 1024 * jh) = wa; *(GAS v4u*)(x2b + (size_t)m * D + 16 * ln + 1024 * jh + 8) = wb; } }
;                 asm volatile("" ::: "memory");
;             };
;             {
;                 v4u xA[4], yA[14], xB[4], yB[14]; float gA = 0.f, gB = 0.f;
;                 if (gw < T) load_row(row_of(gw), xA, yA, gA);
; #pragma clang loop unroll(disable)
;                 for (int m_ = gw; m_ < T; m_ += 2 * NGW) {
;                     const bool hasB = m_ + NGW < T;
;                     if (hasB) load_row(row_of(m_ + NGW), xB, yB, gB);
;                     process_row(row_of(m_), xA, yA, gA);
;                     if (m_ + 2 * NGW < T) load_row(row_of(m_ + 2 * NGW), xA, yA, gA);
;                     if (hasB) process_row(row_of(m_ + NGW), xB, yB, gB);
;                 }
	v_pk_fma_f32 v[172:173], v[176:177], v[172:173], v[180:181]
	v_add_u32_e32 v176, 0x404, v156
	v_ashrrev_i32_e32 v177, 31, v176
	v_lshlrev_b64 v[184:185], 2, v[176:177]
	v_lshl_add_u64 v[180:181], s[6:7], 0, v[184:185]
	v_lshl_add_u64 v[196:197], s[8:9], 0, v[184:185]
	v_pk_fma_f32 v[174:175], v[174:175], v[182:183], v[178:179]
	v_add_u32_e32 v247, s98, v180
	ds_read_b128 v[152:155], v247 offset:32
	v_add_u32_e32 v247, s98, v180
	ds_read_b128 v[176:179], v247 offset:16
	s_nop 0
	v_add_u32_e32 v247, s98, v180
	ds_read_b128 v[180:183], v247
	s_nop 0
	v_add_u32_e32 v247, s99, v196
	ds_read_b128 v[184:187], v247 offset:32
	v_add_u32_e32 v247, s99, v196
	ds_read_b128 v[192:195], v247 offset:16
	s_nop 0
	v_add_u32_e32 v247, s99, v196
	ds_read_b128 v[196:199], v247
	v_lshl_add_u64 v[156:157], v[156:157], 1, s[4:5]
	s_cselect_b64 s[4:5], -1, 0
	s_and_b64 vcc, exec, s[4:5]
	s_waitcnt lgkmcnt(0)
	v_pk_fma_f32 v[154:155], v[154:155], v[144:145], v[186:187]
	v_bfe_u32 v144, v190, 16, 1
	v_add3_u32 v144, v190, v144, s69
	v_bfe_u32 v145, v191, 16, 1
	v_lshrrev_b32_e32 v144, 16, v144
	v_add3_u32 v145, v191, v145, s69
	v_and_or_b32 v144, v145, s66, v144
	v_bfe_u32 v145, v188, 16, 1
	v_pk_fma_f32 v[152:153], v[152:153], v[146:147], v[184:185]
	v_add3_u32 v145, v188, v145, s69
	v_bfe_u32 v146, v189, 16, 1
	v_lshrrev_b32_e32 v145, 16, v145
	v_add3_u32 v146, v189, v146, s69
	v_and_or_b32 v145, v146, s66, v145
	v_bfe_u32 v146, v170, 16, 1
	v_add3_u32 v146, v170, v146, s69
	v_bfe_u32 v147, v171, 16, 1
	v_lshrrev_b32_e32 v146, 16, v146
	v_add3_u32 v147, v171, v147, s69
	v_and_or_b32 v146, v147, s66, v146
	v_bfe_u32 v147, v168, 16, 1
	s_waitcnt lgkmcnt(0)
	v_pk_fma_f32 v[178:179], v[178:179], v[148:149], v[194:195]
	v_add3_u32 v147, v168, v147, s69
	v_bfe_u32 v148, v169, 16, 1
	v_lshrrev_b32_e32 v147, 16, v147
	v_add3_u32 v148, v169, v148, s69
	v_and_or_b32 v147, v148, s66, v147
	v_bfe_u32 v148, v166, 16, 1
	v_add3_u32 v148, v166, v148, s69
	v_bfe_u32 v149, v167, 16, 1
	v_lshrrev_b32_e32 v148, 16, v148
	v_add3_u32 v149, v167, v149, s69
	v_and_or_b32 v148, v149, s66, v148
	v_bfe_u32 v149, v164, 16, 1
	v_pk_fma_f32 v[176:177], v[176:177], v[150:151], v[192:193]
	v_add3_u32 v149, v164, v149, s69
	v_bfe_u32 v150, v165, 16, 1
	v_lshrrev_b32_e32 v149, 16, v149
	v_add3_u32 v150, v165, v150, s69
	v_and_or_b32 v149, v150, s66, v149
	v_bfe_u32 v150, v162, 16, 1
	v_add3_u32 v150, v162, v150, s69
	v_bfe_u32 v151, v163, 16, 1
	v_lshrrev_b32_e32 v150, 16, v150
	v_add3_u32 v151, v163, v151, s69
	v_and_or_b32 v150, v151, s66, v150
	v_bfe_u32 v151, v158, 16, 1
	v_add3_u32 v151, v158, v151, s69
	v_bfe_u32 v158, v159, 16, 1
	v_lshrrev_b32_e32 v151, 16, v151
	v_add3_u32 v158, v159, v158, s69
	v_and_or_b32 v151, v158, s66, v151
	global_store_dwordx4 v[156:157], v[144:147], off
	global_store_dwordx4 v[156:157], v[148:151], off offset:16
	s_waitcnt lgkmcnt(0)
	v_pk_fma_f32 v[180:181], v[180:181], v[200:201], v[196:197]
	v_bfe_u32 v144, v174, 16, 1
	v_add3_u32 v144, v174, v144, s69
	v_bfe_u32 v145, v175, 16, 1
	v_lshrrev_b32_e32 v144, 16, v144
	v_add3_u32 v145, v175, v145, s69
	v_and_or_b32 v144, v145, s66, v144
	v_bfe_u32 v145, v172, 16, 1
	v_add3_u32 v145, v172, v145, s69
	v_bfe_u32 v146, v173, 16, 1
	v_lshrrev_b32_e32 v145, 16, v145
	v_add3_u32 v146, v173, v146, s69
	v_and_or_b32 v145, v146, s66, v145
	v_bfe_u32 v146, v180, 16, 1
	v_add3_u32 v146, v180, v146, s69
	v_bfe_u32 v147, v181, 16, 1
	v_pk_fma_f32 v[182:183], v[182:183], v[202:203], v[198:199]
	v_lshrrev_b32_e32 v146, 16, v146
	v_add3_u32 v147, v181, v147, s69
	v_and_or_b32 v146, v147, s66, v146
	v_bfe_u32 v147, v182, 16, 1
	v_add3_u32 v147, v182, v147, s69
	v_bfe_u32 v148, v183, 16, 1
	v_lshrrev_b32_e32 v147, 16, v147
	v_add3_u32 v148, v183, v148, s69
	v_and_or_b32 v147, v148, s66, v147
	v_bfe_u32 v148, v176, 16, 1
	v_add3_u32 v148, v176, v148, s69
	v_bfe_u32 v149, v177, 16, 1
	v_lshrrev_b32_e32 v148, 16, v148
	v_add3_u32 v149, v177, v149, s69
	v_and_or_b32 v148, v149, s66, v148
	v_bfe_u32 v149, v178, 16, 1
	v_add3_u32 v149, v178, v149, s69
	v_bfe_u32 v150, v179, 16, 1
	v_lshrrev_b32_e32 v149, 16, v149
	v_add3_u32 v150, v179, v150, s69
	v_and_or_b32 v149, v150, s66, v149
	v_bfe_u32 v150, v152, 16, 1
	v_add3_u32 v150, v152, v150, s69
	v_bfe_u32 v151, v153, 16, 1
	v_lshrrev_b32_e32 v150, 16, v150
	v_add3_u32 v151, v153, v151, s69
	v_and_or_b32 v150, v151, s66, v150
	v_bfe_u32 v151, v154, 16, 1
	v_add3_u32 v151, v154, v151, s69
	v_bfe_u32 v152, v155, 16, 1
	v_lshrrev_b32_e32 v151, 16, v151
	v_add3_u32 v152, v155, v152, s69
	v_and_or_b32 v151, v152, s66, v151
	global_store_dwordx4 v[156:157], v[144:147], off offset:2048
	global_store_dwordx4 v[156:157], v[148:151], off offset:2064
	s_cbranch_vccnz .LBB0_985
	s_and_b64 vcc, exec, s[0:1]
	s_mov_b32 s36, s46
	s_cbranch_vccnz .LBB0_982
	s_lshr_b32 s36, s31, 3
	s_ashr_i32 s37, s46, 3
	s_and_b32 s33, s41, 0x3800
	s_and_b32 s36, s36, 0xf8
	s_and_b32 s37, s37, 0xffffff00
	s_or_b32 s36, s36, s37
	s_or_b32 s33, s33, s27
	s_add_i32 s36, s33, s36

; #define GAS __attribute__((address_space(1)))
; template <int l>
; __device__ __forceinline__ void layer_phases(Frame& F, const XcdBarrier& bar, const int lo, const int hi) {
;     ...
;             auto load_row = [&](const int m, v4u (&xr)[4], v4u (&yr)[14], float& gtv) {
;                 int ln = F.lane; asm volatile("" : "+v"(ln));
;                 gtv = 0.f; if (ln < 6) gtv = gates[(size_t)m * 6 + ln];
; #pragma unroll
;                 for (int jh = 0; jh < 2; ++jh) { xr[2 * jh] = __builtin_nontemporal_load((const GAS v4u*)(x1 + (size_t)m * D + 16 * ln + 1024 * jh)); xr[2 * jh + 1] = __builtin_nontemporal_load((const GAS v4u*)(x1 + (size_t)m * D + 16 * ln + 1024 * jh + 8)); }
; #pragma unroll
;                 for (int jh = 0; jh < 2; ++jh)
; #pragma unroll
;                     for (int q = 0; q < 7; ++q) yr[7 * jh + q] = __builtin_nontemporal_load((const GAS v4u*)(yb + ((size_t)m * 7 + q) * D + 16 * ln + 1024 * jh));
;                 asm volatile("" ::: "memory");
;             };
;     ...
;                 for (int m_ = gw; m_ < T; m_ += 2 * NGW) {
;                     const bool hasB = m_ + NGW < T;
;                     if (hasB) load_row(row_of(m_ + NGW), xB, yB, gB);
;                     process_row(row_of(m_), xA, yA, gA);
;                     if (m_ + 2 * NGW < T) load_row(row_of(m_ + 2 * NGW), xA, yA, gA);
;                     if (hasB) process_row(row_of(m_ + NGW), xB, yB, gB);
;                 }
.LBB0_984:
	s_or_b64 exec, exec, s[38:39]
	s_lshl_b64 s[38:39], s[36:37], 12
	s_add_u32 s38, s50, s38
	s_addc_u32 s39, s51, s39
	s_mul_hi_i32 s33, s36, 0x3800
	s_mulk_i32 s36, 0x3800
	v_lshlrev_b32_e32 v16, 4, v0
	s_add_u32 s36, s43, s36
	v_ashrrev_i32_e32 v17, 31, v16
	s_addc_u32 s37, s47, s33
	v_lshl_add_u64 v[44:45], s[36:37], 0, v[16:17]
	v_add_co_u32_e32 v48, vcc, s55, v44
	v_lshl_add_u64 v[12:13], v[16:17], 1, s[38:39]
	s_nop 0
	v_addc_co_u32_e32 v49, vcc, 0, v45, vcc
	v_add_co_u32_e32 v24, vcc, s64, v44
	v_lshl_add_u64 v[52:53], v[44:45], 0, s[12:13]
	s_nop 0
	v_addc_co_u32_e32 v25, vcc, 0, v45, vcc
	v_add_co_u32_e32 v28, vcc, 0x3000, v44
	v_lshl_add_u64 v[56:57], v[44:45], 0, s[14:15]
	v_lshl_add_u64 v[60:61], v[44:45], 0, s[16:17]
	v_lshl_add_u64 v[64:65], v[44:45], 0, s[18:19]
	v_lshl_add_u64 v[76:77], v[44:45], 0, s[20:21]
	v_addc_co_u32_e32 v29, vcc, 0, v45, vcc
	global_load_dwordx4 v[0:3], v[12:13], off offset:16 nt
	global_load_dwordx4 v[4:7], v[12:13], off nt
	global_load_dwordx4 v[8:11], v[12:13], off offset:2064 nt
	s_nop 0
	global_load_dwordx4 v[12:15], v[12:13], off offset:2048 nt
	s_nop 0
	global_load_dwordx4 v[16:19], v[24:25], off nt
	global_load_dwordx4 v[20:23], v[24:25], off offset:2048 nt
	s_nop 0
	global_load_dwordx4 v[24:27], v[24:25], off offset:-4096 nt
	s_nop 0
	global_load_dwordx4 v[28:31], v[28:29], off nt
	s_nop 0
	global_load_dwordx4 v[32:35], v[44:45], off nt
	global_load_dwordx4 v[36:39], v[44:45], off offset:1024 nt
	global_load_dwordx4 v[40:43], v[44:45], off offset:2048 nt
	s_nop 0
	global_load_dwordx4 v[44:47], v[44:45], off offset:3072 nt
	s_nop 0
	global_load_dwordx4 v[48:51], v[48:49], off offset:2048 nt
	s_nop 0
	global_load_dwordx4 v[52:55], v[52:53], off offset:1024 nt
	s_nop 0
	global_load_dwordx4 v[56:59], v[56:57], off offset:1024 nt
	s_nop 0
	global_load_dwordx4 v[60:63], v[60:61], off offset:1024 nt
	s_nop 0
	global_load_dwordx4 v[64:67], v[64:65], off offset:1024 nt
	s_nop 0
	global_load_dwordx4 v[76:79], v[76:77], off offset:1024 nt
	s_waitcnt vmcnt(23)
	s_andn2_b64 vcc, exec, s[34:35]
	s_cbranch_vccnz .LBB0_970
	s_branch .LBB0_986
.LBB0_985:
	s_waitcnt vmcnt(4)
	s_andn2_b64 vcc, exec, s[34:35]
	s_cbranch_vccnz .LBB0_970

; template <int l>
; __device__ __forceinline__ void layer_phases(Frame& F, const XcdBarrier& bar, const int lo, const int hi) {
;     ...
;                 for (int m_ = gw; m_ < T; m_ += 2 * NGW) {
;                     const bool hasB = m_ + NGW < T;
;                     if (hasB) load_row(row_of(m_ + NGW), xB, yB, gB);
;                     process_row(row_of(m_), xA, yA, gA);
;                     if (m_ + 2 * NGW < T) load_row(row_of(m_ + 2 * NGW), xA, yA, gA);
;                     if (hasB) process_row(row_of(m_ + NGW), xB, yB, gB);
;                 }
.Lp8a_skipB:
	s_waitcnt vmcnt(0)
	s_branch .LBB0_977

; #define PG8_STAGE(bufoff, gbase, voff) do { _Pragma("unroll") for (int _i = 0; _i < 2; ++_i) { unsigned keep_; \
;         asm volatile("s_mov_b32 %0, m0\n\ts_mov_b32 m0, %3\n\ts_nop 0\n\tglobal_load_lds_dwordx4 %1, %2\n\ts_mov_b32 m0, %0" : "=&s"(keep_) : "v"((voff)[_i]), "s"((const char*)(gbase)), "s"(ldsb + (unsigned)((bufoff) + _i * 8192)) : "memory"); } } while (0)
; #define PG8_BAR __builtin_amdgcn_s_barrier()
; template <class Epi, class Sched, bool ALIGN_EPI, bool FP8 = false>
; __device__ __forceinline__ void gemm_phase(PG8_LAS unsigned char* lds, const Gemm g, const Sched& S, const Epi& E, const int wid, const int lane) {
;     ...
;     for (int i = 0; i < 2; ++i) { int R, C; stage_rc(tid * 16 + i * 8192, R, C); const int Rb = Epi::PERM ? ((R & ~31) + perm32(R & 31)) : R;
;         rA[i] = R; cA2[i] = (unsigned)C * 2u; voffA[i] = (unsigned)(R * KB + C * 2); voffB[i] = (unsigned)(Rb * KB + C * 2); }
;     ...
;     const char* cA = GA ? (const char*)g.A : (const char*)g.A + (size_t)cur.pm * tstep; const char* cB = (const char*)g.Bt + (size_t)cur.pn * tstep;
;     PG8_STAGE(PG8_SB(0, 0), cB, voffB); PG8_STAGE(PG8_SB(0, 1), cB + hstep, voffB); PG8_STAGE(PG8_SA(0, 0), cA, vc0); PG8_STAGE(PG8_SA(0, 1), cA + hstepA, vc1);
;     if (wr == 1) PG8_BAR;
.LBB0_1121:
	v_lshlrev_b32_e32 v0, 4, v7
	v_add_u32_e32 v1, s10, v0
	v_ashrrev_i32_e32 v2, 31, v1
	v_lshrrev_b32_e32 v2, 22, v2
	v_add_u32_e32 v2, v1, v2
	v_ashrrev_i32_e32 v2, 10, v2
	v_mul_i32_i24_e32 v3, 0x400, v2
	v_sub_u32_e32 v3, v1, v3
	v_lshrrev_b32_e32 v4, 4, v3
	v_bitop3_b32 v3, v4, v3, 32 bitop3:0x6c
	v_ashrrev_i32_e32 v5, 31, v3
	v_lshrrev_b32_e32 v5, 26, v5
	v_lshlrev_b32_e32 v4, 3, v2
	v_add_u32_e32 v5, v3, v5
	v_and_b32_e32 v4, -16, v4
	v_ashrrev_i32_e32 v6, 6, v5
	v_and_b32_e32 v5, 0xc0, v5
	v_add_u32_e32 v4, v6, v4
	v_sub_u32_e32 v3, v3, v5
	v_mov_b32_e32 v5, 1
	v_lshlrev_b32_e32 v2, 5, v2
	v_ashrrev_i16_sdwa v3, v5, sext(v3) dst_sel:DWORD dst_unused:UNUSED_PAD src0_sel:DWORD src1_sel:BYTE_0
	s_waitcnt vmcnt(15)
	v_lshlrev_b32_e32 v8, 1, v4
	v_lshrrev_b32_e32 v9, 2, v4
	v_and_b32_e32 v6, 3, v6
	s_movk_i32 s1, 0xffe0
	v_and_b32_e32 v2, 32, v2
	v_bfe_i32 v3, v3, 0, 16
	v_and_b32_e32 v8, 24, v8
	v_and_b32_e32 v9, 4, v9
	v_and_or_b32 v6, v4, s1, v6
	v_or3_b32 v6, v6, v9, v8
	v_add_lshl_u32 v2, v2, v3, 1
	v_add_u32_e32 v1, 0x2000, v1
	v_mad_u64_u32 v[132:133], s[4:5], s0, v4, v[2:3]
	v_mad_u64_u32 v[134:135], s[4:5], s0, v6, v[2:3]
	v_ashrrev_i32_e32 v2, 31, v1
	v_lshrrev_b32_e32 v2, 22, v2
	v_add_u32_e32 v2, v1, v2
	v_ashrrev_i32_e32 v2, 10, v2
	v_mul_i32_i24_e32 v3, 0x400, v2
	v_sub_u32_e32 v1, v1, v3
	v_lshrrev_b32_e32 v3, 4, v1
	v_bitop3_b32 v1, v3, v1, 32 bitop3:0x6c
	v_ashrrev_i32_e32 v4, 31, v1
	v_lshrrev_b32_e32 v4, 26, v4
	v_add_u32_e32 v4, v1, v4
	v_ashrrev_i32_e32 v6, 6, v4
	v_and_b32_e32 v4, 0xffc0, v4
	v_lshlrev_b32_e32 v3, 3, v2
	v_sub_u32_e32 v1, v1, v4
	v_and_b32_e32 v3, -16, v3
	v_lshrrev_b16_e32 v4, 7, v1
	v_add_u32_e32 v3, v6, v3
	v_and_b32_e32 v4, 1, v4
	v_and_b32_e32 v6, 3, v6
	v_add_u16_e32 v1, v1, v4
	v_and_or_b32 v6, v3, s1, v6
	s_ashr_i32 s1, s0, 31
	v_lshlrev_b32_e32 v2, 5, v2
	v_ashrrev_i16_sdwa v1, v5, sext(v1) dst_sel:DWORD dst_unused:UNUSED_PAD src0_sel:DWORD src1_sel:BYTE_0
	v_lshlrev_b32_e32 v4, 1, v3
	v_lshrrev_b32_e32 v5, 2, v3
	s_lshr_b32 s12, s90, 8
	s_lshl_b64 s[6:7], s[0:1], 7
	s_lshl_b64 s[8:9], s[0:1], 8
	s_add_i32 s34, s10, 0
	v_and_b32_e32 v2, 32, v2
	v_bfe_i32 v1, v1, 0, 16
	v_and_b32_e32 v4, 24, v4
	v_and_b32_e32 v5, 4, v5
	s_add_u32 s35, s56, 0x1b600000
	v_or3_b32 v4, v6, v5, v4
	v_add_lshl_u32 v2, v2, v1, 1
	s_addc_u32 s36, s57, 0
	v_mad_u64_u32 v[136:137], s[4:5], s0, v3, v[2:3]
	v_mad_u64_u32 v[138:139], s[4:5], s0, v4, v[2:3]
	s_add_u32 s37, s56, 0x35c00000
	s_addc_u32 s38, s57, 0
	s_ashr_i32 s4, s84, 31
	s_mul_i32 s4, s8, s4
	s_mul_hi_u32 s5, s8, s84
	s_add_i32 s10, s5, s4
	s_lshr_b64 s[4:5], s[0:1], 24
	s_mul_i32 s5, s4, s84
	s_add_i32 s10, s10, s5
	s_ashr_i32 s5, s83, 31
	s_mul_i32 s5, s8, s5
	s_mul_hi_u32 s13, s8, s83
	s_add_i32 s5, s13, s5
	s_mul_i32 s4, s4, s83
	s_add_i32 s5, s5, s4
	s_mul_i32 s4, s8, s83
	s_add_u32 s26, s35, s4
	s_addc_u32 s27, s36, s5
	s_add_i32 s39, s34, 0x10000
	s_mov_b32 m0, s39
	s_nop 0
	global_load_lds_dwordx4 v134, s[26:27]
	s_add_i32 s40, s34, 0x12000
	s_mov_b32 m0, s40
	s_nop 0
	global_load_lds_dwordx4 v138, s[26:27]
	s_add_u32 s4, s26, s6
	s_mul_i32 s11, s8, s84
	s_addc_u32 s5, s27, s7
	s_add_i32 s41, s34, 0x14000
	s_mov_b32 m0, s41
	s_nop 0
	global_load_lds_dwordx4 v134, s[4:5]
	s_add_i32 s42, s34, 0x16000
	s_mov_b32 m0, s42
	s_nop 0
	global_load_lds_dwordx4 v138, s[4:5]
	s_add_u32 s28, s37, s11
	s_addc_u32 s29, s38, s10
	s_mov_b32 m0, s34
	s_nop 0
	global_load_lds_dwordx4 v132, s[28:29]
	s_add_i32 s43, s34, 0x2000
	s_mov_b32 m0, s43
	s_nop 0
	global_load_lds_dwordx4 v136, s[28:29]
	s_add_u32 s14, s28, s6
	s_addc_u32 s15, s29, s7
	s_add_i32 s44, s34, 0x4000
	s_mov_b32 m0, s44
	s_nop 0
	global_load_lds_dwordx4 v132, s[14:15]
	s_add_i32 s45, s34, 0x6000
	s_mov_b32 m0, s45
	s_nop 0
	global_load_lds_dwordx4 v136, s[14:15]
	s_cmp_eq_u32 s12, 1
	s_mov_b32 s3, 0
	s_cselect_b64 s[10:11], -1, 0
	s_cmp_lg_u32 s12, 1
	s_cbranch_scc1 .LBB0_1123
	s_barrier

; #define GAS __attribute__((address_space(1)))
; #define LAS __attribute__((address_space(3)))
; __device__ __forceinline__ void refresh(Frame& F) { int l = (int)__builtin_amdgcn_mbcnt_hi(~0u, __builtin_amdgcn_mbcnt_lo(~0u, 0u)); asm volatile("" : "+v"(l)); F.lane = l; F.tid = F.wave * 64 + l; }
; __device__ __forceinline__ void dil_a_unit(const bf16* proj, bf16* SO, float* SM, gu32* done, int b, int h, int qb, lptr wl, LAS float* wsf, int tid, int wave) {
;     const int lane = tid & 63, r32 = lane & 31, hi = lane >> 5;
;     const bf16* Qp = proj + hm_off(QCOL_DL, 12, b, h); const bf16* Kp = proj + hm_off(KCOL_DL, 12, b, h); const bf16* Vp = proj + hm_off(VCOL_DL, 12, b, h);
;     const int qt = 8 * qb + wave, qtok = 32 * qt + r32;
;     bf16x8 qr[4];
; #pragma unroll
;     for (int d0 = 0; d0 < 4; ++d0) qr[d0] = *(const GAS bf16x8*)(Qp + (size_t)qtok * APITCH + d0 * 16 + hi * 8);
;     f32x16 o[2]; o[0] = f32x16{}; o[1] = f32x16{};
;     float mrun = -1e30f, lrun = 0.f;
;     const int vbo = 4096 + ((lane >> 4) & 1) * 32 + (lane & 3) * 8 + (4 * hi + ((lane & 15) >> 2)) * 64, vsw = ((lane >> 2) & 1) ? -64 : 64;
; template <int l>
; __device__ __forceinline__ void layer_phases(Frame& F, const XcdBarrier& bar, const int lo, const int hi) {
;     ...
;             refresh(F);
;             const bf16* proj = (const bf16*)(ws + WS_PROJ); unsigned char* obuf = ws + WS_OBUF;
;             const float* gn = inptr<const float>(F, I_HNG) + (size_t)l * D;
;             LAS unsigned char* kvbuf = F.lds + RING_OFF; LAS float* ncum = (LAS float*)(F.lds + RING_OFF + 49152); att::lptr wl = F.lds + RING_OFF + 57344 + F.wave * 9216; LAS float* wsf = (LAS float*)(F.lds + WSF_OFF + F.wave * 256);
;             volatile LAS unsigned* uslot = (volatile LAS unsigned*)(F.lds + MISC_OFF + 64);
;             const int qid = blockIdx.x & 7;
;     ...
;             bf16* dstO = (bf16*)(ws + WS_DST_O); float* dstM = (float*)(ws + WS_DST_M);
;             if (rep == 0) { gu32* ctr = F.ctl + CW_AQ + ((l * 4 + 3) * 8 + qid) * 64;
;               for (;;) { int gi; ATT_DEQ(ctr, gi); if (gi >= 768) break;
;                   const int sl_ = gi >> 3, qb = sl_ / 12, bh = 12 * (gi & 7) + sl_ % 12;
;                   att::dil_a_unit(proj, dstO, dstM, F.ctl + CW_DA + ((l * 96 + bh) * 4 + (qb >> 1)) * 16, bh / 12, bh % 12, qb, wl, wsf, F.tid, F.wave); } }
.LBB0_1262:
	s_cmp_gt_i32 s92, 11
	s_cselect_b64 s[0:1], -1, 0
	s_cmp_lt_i32 s93, 12
	s_cselect_b64 s[4:5], -1, 0
	s_or_b64 s[0:1], s[0:1], s[4:5]
	s_and_b64 vcc, exec, s[0:1]
	s_cbranch_vccnz .LBB0_1435
	s_add_u32 s3, s56, 0x45c00000
	s_addc_u32 s83, s57, 0
	s_and_b32 s23, s2, 7
	s_add_u32 s64, s56, 0x6f400000
	s_addc_u32 s65, s57, 0
	s_add_i32 s0, 0, 0x21438
	v_mov_b32_e32 v132, v216
	s_waitcnt vmcnt(17)
	v_mov_b32_e32 v0, s0
	v_readlane_b32 s0, v248, 0
	ds_read_b64 v[0:1], v0
	v_lshlrev_b32_e32 v2, 1, v132
	v_add_u32_e32 v124, s0, v132
	v_readlane_b32 s0, v248, 9
	s_waitcnt vmcnt(16)
	v_and_b32_e32 v5, 4, v132
	s_add_i32 s22, s0, 0
	v_lshlrev_b32_e32 v6, 4, v124
	v_and_b32_e32 v127, 32, v2
	v_not_b32_e32 v2, 63
	v_cmp_eq_u32_e32 vcc, 0, v5
	v_bfe_u32 v144, v132, 2, 1
	v_bfe_u32 v125, v132, 5, 1
	v_cndmask_b32_e64 v141, v2, 64, vcc
	v_lshl_add_u32 v133, v144, 11, s22
	v_and_b32_e32 v2, 48, v6
	v_and_b32_e32 v128, 31, v132
	v_add_u32_e32 v155, v133, v2
	v_bitop3_b32 v2, v125, v132, 31 bitop3:0x78
	v_lshlrev_b32_e32 v157, 4, v2
	v_bitop3_b32 v2, v125, v128, 2 bitop3:0x36
	v_lshlrev_b32_e32 v159, 4, v2
	v_bitop3_b32 v2, v125, v128, 4 bitop3:0x36
	v_lshlrev_b32_e32 v161, 4, v2
	v_bitop3_b32 v2, v125, v128, 6 bitop3:0x36
	v_bfe_u32 v167, v132, 3, 3
	v_lshlrev_b32_e32 v163, 4, v2
	v_bitop3_b32 v2, v167, v132, 7 bitop3:0x78
	v_and_b32_e32 v143, 7, v132
	v_lshlrev_b32_e32 v168, 4, v2
	v_xor_b32_e32 v2, v167, v144
	v_lshlrev_b32_e32 v169, 6, v2
	v_bitop3_b32 v2, v167, v143, 8 bitop3:0x36
	v_lshlrev_b32_e32 v170, 4, v2
	v_bitop3_b32 v2, v167, v144, 8 bitop3:0x36
	v_lshlrev_b32_e32 v171, 6, v2
	v_bitop3_b32 v2, v167, v143, 16 bitop3:0x36
	s_lshl_b32 s0, s80, 8
	v_lshlrev_b32_e32 v172, 4, v2
	v_bitop3_b32 v2, v167, v144, 16 bitop3:0x36
	s_add_i32 s82, s0, 0
	v_lshlrev_b32_e32 v173, 6, v2
	v_bitop3_b32 v2, v167, v143, 24 bitop3:0x36
	s_sub_i32 s84, 0x300, s23
	s_waitcnt lgkmcnt(0)
	v_readfirstlane_b32 s10, v0
	s_add_i32 s82, s82, 0x20000
	s_lshl_b32 s0, s23, 8
	v_and_b32_e32 v0, 63, v132
	v_lshlrev_b32_e32 v3, 3, v132
	v_lshlrev_b32_e32 v112, 4, v132
	v_and_b32_e32 v139, 0x70, v6
	s_movk_i32 s4, 0x380
	v_lshlrev_b32_e32 v174, 4, v2
	v_bitop3_b32 v2, v167, v144, 24 bitop3:0x36
	s_add_u32 s90, s56, s0
	v_lshlrev_b32_e32 v129, 2, v125
	v_bfe_u32 v126, v132, 2, 2
	v_and_or_b32 v114, v112, s4, v139
	v_and_b32_e32 v148, 24, v3
	v_cmp_gt_u32_e64 s[4:5], 32, v0
	v_lshlrev_b32_e32 v0, 2, v128
	v_lshlrev_b32_e32 v175, 6, v2
	v_mul_u32_u24_e32 v2, 0x440, v125
	s_addc_u32 s91, s57, 0
	v_or_b32_e32 v4, v129, v126
	v_add3_u32 v134, s22, v127, v148
	v_add_u32_e32 v165, s82, v0
	v_add3_u32 v179, s22, v2, v0
	v_lshlrev_b32_e32 v0, 5, v132
	s_add_u32 s8, s90, 0xf800
	v_lshl_add_u32 v164, v4, 6, v134
	v_and_b32_e32 v4, 32, v0
	v_readfirstlane_b32 s11, v1
	s_addc_u32 s9, s91, 0
	v_mov_b32_e32 v1, 0
	v_mov_b32_e32 v5, s22
	v_bfe_u32 v140, v132, 1, 5
	v_lshlrev_b32_e32 v0, 1, v4
	s_movk_i32 s6, 0x110
	v_or_b32_e32 v149, 2, v125
	v_or_b32_e32 v150, 4, v125
	v_or_b32_e32 v151, 6, v125
	s_add_u32 s86, s56, 0x14000
	v_lshl_add_u64 v[2:3], s[56:57], 0, v[0:1]
	s_mov_b64 s[12:13], 0x6dc00000
	v_mad_u32_u24 v176, v140, s6, v5
	s_mul_i32 s85, s23, 12
	s_mov_b32 s7, 0
	v_cmp_eq_u32_e64 s[0:1], 0, v124
	v_lshlrev_b32_e32 v138, 3, v125
	v_mov_b32_e32 v115, v1
	v_lshl_add_u32 v154, v143, 9, s22
	v_lshl_add_u32 v156, v125, 9, s22
	v_lshl_add_u32 v158, v149, 9, s22
	v_lshl_add_u32 v160, v150, 9, s22
	v_lshl_add_u32 v162, v151, 9, s22
	v_lshlrev_b32_e32 v166, 4, v125
	s_addc_u32 s87, s57, 0
	v_lshl_add_u64 v[130:131], v[2:3], 0, s[12:13]
	v_lshl_add_u32 v177, v4, 2, v176
	s_add_i32 s24, 0, 0x21540
	s_mov_b64 s[12:13], 0x7800000
	s_mov_b32 s25, 0x7800000
	s_movk_i32 s26, 0x81
	s_movk_i32 s27, 0xff7e
	s_movk_i32 s28, 0x7fff
	s_mov_b32 s29, 0xffff0000
	v_mov_b32_e32 v113, 0xff800000
	s_and_saveexec_b64 s[98:99], s[0:1]
	v_mov_b32_e32 v239, 0
	v_mov_b32_e32 v240, 1
	global_atomic_add v238, v239, v240, s[8:9] sc0
	s_mov_b64 exec, s[98:99]
	s_branch .LBB0_1267

; #define ATT_DEQ(ctrp, out) do { __syncthreads(); if (F.tid == 0) uslot[0] = __hip_atomic_fetch_add((ctrp), 1u, RLX_AGENT); __syncthreads(); (out) = (int)uslot[0] * 8 + qid; } while (0)
; template <int l>
; __device__ __forceinline__ void layer_phases(Frame& F, const XcdBarrier& bar, const int lo, const int hi) {
;     ...
;             bf16* dstO = (bf16*)(ws + WS_DST_O); float* dstM = (float*)(ws + WS_DST_M);
;             if (rep == 0) { gu32* ctr = F.ctl + CW_AQ + ((l * 4 + 3) * 8 + qid) * 64;
;               for (;;) { int gi; ATT_DEQ(ctr, gi); if (gi >= 768) break;
.LBB0_1267:
	s_barrier
	s_and_saveexec_b64 s[14:15], s[0:1]
	s_cbranch_execz .LBB0_1271
	s_waitcnt vmcnt(0)
	v_mov_b32_e32 v2, s24
	ds_write_b32 v2, v238
	v_mov_b32_e32 v240, 1
	v_mov_b32_e32 v239, 0
	s_waitcnt lgkmcnt(0)
	global_atomic_add v238, v239, v240, s[8:9] sc0

; #define GAS __attribute__((address_space(1)))
; #define LAS __attribute__((address_space(3)))
; __device__ __forceinline__ size_t hm_off(int cs, int Hg, int b, int h) { return (size_t)NB * SEQ * cs + ((size_t)(b * Hg + h) * SEQ) * 64; }
; #define ATT_DEQ(ctrp, out) do { __syncthreads(); if (F.tid == 0) uslot[0] = __hip_atomic_fetch_add((ctrp), 1u, RLX_AGENT); __syncthreads(); (out) = (int)uslot[0] * 8 + qid; } while (0)
; __device__ __forceinline__ void sb_wave_unit(const bf16* proj, const float* gn, unsigned char* obuf, int b, int h, int qt, lptr wl, LAS float* wsf, int lane) {
;     const int r32 = lane & 31, hi = lane >> 5;
;     const bf16* Qp = proj + hm_off(QCOL_SB, 8, b, h); const bf16* Kp = proj + hm_off(KCOL_SB, 8, b, h); const bf16* Vp = proj + hm_off(VCOL_SB, 8, b, h);
;     const int qtok = 32 * qt + r32;
;     bf16x8 qr[4];
; #pragma unroll
;     for (int d0 = 0; d0 < 4; ++d0) qr[d0] = *(const GAS bf16x8*)(Qp + (size_t)qtok * APITCH + d0 * 16 + hi * 8);
;     f32x16 o[2]; o[0] = f32x16{}; o[1] = f32x16{};
;     float R = 1.f;
;     const int vbo = 4096 + ((lane >> 4) & 1) * 32 + (lane & 3) * 8 + (4 * hi + ((lane & 15) >> 2)) * 64, vsw = ((lane >> 2) & 1) ? -64 : 64;
;     v4u kreg[4], vreg[4];
;     int tt = qt;
;     DILP_LOAD(0, 0, tt);
; template <int l>
; __device__ __forceinline__ void layer_phases(Frame& F, const XcdBarrier& bar, const int lo, const int hi) {
;     ...
;             if (ATT_ONLY < 0 || ATT_ONLY == 0) { gu32* ctr = F.ctl + CW_AQ + ((l * 4 + 0) * 8 + qid) * 64 + rep * 32;
;               for (;;) { int gi; ATT_DEQ(ctr, gi); if (gi >= 512) break;
;                   const int sl_ = gi >> 3, qb = 7 - sl_ / 8, bh = 8 * (gi & 7) + (sl_ & 7);
;                   att::sb_wave_unit(proj, gn, obuf, bh >> 3, bh & 7, 8 * qb + F.wave, wl, wsf, F.lane); } }
.LBB0_1286:
	v_and_b32_e32 v1, 64, v216
	v_xor_b32_e32 v0, 1, v216
	v_add_u32_e32 v1, 64, v1
	v_cmp_lt_i32_e32 vcc, v0, v1
	s_lshl_b32 s6, s23, 22
	s_sub_i32 s20, 0x200, s23
	v_cndmask_b32_e32 v0, v216, v0, vcc
	v_lshlrev_b32_e32 v178, 2, v0
	v_ashrrev_i32_e32 v0, 5, v132
	s_waitcnt vmcnt(3)
	v_lshlrev_b32_e32 v96, 3, v0
	s_waitcnt vmcnt(1)
	v_lshlrev_b32_e32 v106, 2, v0
	v_lshl_add_u32 v3, v0, 9, s22
	v_xor_b32_e32 v4, v0, v128
	v_add_u32_e32 v5, 2, v0
	v_add_u32_e32 v7, 4, v0
	v_add_u32_e32 v0, 6, v0
	v_lshl_add_u32 v9, v0, 9, s22
	v_xor_b32_e32 v0, v0, v128
	v_or_b32_e32 v1, v106, v126
	v_lshlrev_b32_e32 v10, 4, v0
	v_ashrrev_i32_e32 v0, 3, v132
	v_lshl_add_u32 v107, v1, 6, v134
	v_xor_b32_e32 v1, v0, v143
	v_lshlrev_b32_e32 v11, 4, v1
	v_xor_b32_e32 v1, v144, v0
	v_lshlrev_b32_e32 v12, 6, v1
	v_add_u32_e32 v1, 64, v132
	v_ashrrev_i32_e32 v1, 3, v1
	v_xor_b32_e32 v13, v1, v143
	v_xor_b32_e32 v1, v1, v144
	v_lshlrev_b32_e32 v14, 6, v1
	v_add_u32_e32 v1, 0x80, v132
	v_ashrrev_i32_e32 v1, 3, v1
	v_xor_b32_e32 v15, v1, v143
	v_xor_b32_e32 v1, v1, v144
	v_lshlrev_b32_e32 v16, 6, v1
	v_add_u32_e32 v1, 0xc0, v132
	v_ashrrev_i32_e32 v1, 3, v1
	s_add_u32 s88, s56, 0x51c00000
	v_xor_b32_e32 v17, v1, v143
	v_xor_b32_e32 v1, v1, v144
	s_addc_u32 s89, s57, 0
	s_lshl_b32 s12, s23, 20
	v_lshlrev_b32_e32 v18, 6, v1
	v_and_b32_e32 v1, 0xffffffc, v0
	s_movk_i32 s16, 0x110
	v_or_b32_e32 v0, 3, v0
	s_add_u32 s21, s88, s6
	v_lshlrev_b32_e32 v105, 2, v128
	v_mul_lo_u32 v0, v0, s16
	s_addc_u32 s23, s89, 0
	v_mov_b32_e32 v113, 0
	v_and_b32_e32 v104, 48, v112
	v_mul_lo_u32 v1, v1, s16
	s_waitcnt vmcnt(0)
	v_add3_u32 v109, s22, v0, v105
	v_ashrrev_i32_e32 v110, 1, v132
	v_and_b32_e32 v0, 1, v132
	s_add_u32 s14, s90, 0xe000
	v_add_u32_e32 v2, v133, v104
	v_lshl_add_u32 v6, v5, 9, s22
	v_xor_b32_e32 v5, v5, v128
	v_lshl_add_u32 v8, v7, 9, s22
	v_xor_b32_e32 v7, v7, v128
	v_cmp_gt_u32_e64 s[6:7], 32, v132
	v_add3_u32 v108, s22, v1, v105
	v_mul_lo_u32 v1, v110, s16
	v_lshlrev_b32_e32 v132, 7, v0
	v_mov_b32_e32 v133, v113
	s_addc_u32 s15, s91, 0
	v_lshlrev_b32_e32 v4, 4, v4
	v_lshlrev_b32_e32 v5, 4, v5
	v_lshlrev_b32_e32 v7, 4, v7
	v_lshlrev_b32_e32 v13, 4, v13
	v_lshlrev_b32_e32 v15, 4, v15
	v_lshlrev_b32_e32 v17, 4, v17
	v_add_u32_e32 v19, s22, v1
	v_lshlrev_b32_e32 v134, 5, v0
	v_lshl_add_u64 v[0:1], s[10:11], 0, v[132:133]
	s_mov_b64 s[10:11], 0x2000
	s_lshl_b32 s25, s80, 5
	s_mov_b32 s13, 0
	s_add_i32 s24, s80, 56
	v_ashrrev_i32_e32 v97, 31, v96
	v_cmp_lt_i32_e64 s[8:9], v106, v128
	v_lshl_add_u32 v111, v110, 2, s82
	v_mov_b32_e32 v135, v113
	v_lshl_add_u64 v[136:137], v[0:1], 0, s[10:11]
	s_addk_i32 s25, 0x6c0
	s_add_i32 s26, 0, 0x21540
	s_lshl_b32 s27, s12, 1
	s_mov_b32 s28, 0xda24260
	v_mov_b32_e32 v114, 1.0
	v_add_u32_e32 v115, v19, v132
	v_mov_b32_e32 v116, 0x358637bd
	s_mov_b32 s29, 0xf800000
	v_mov_b32_e32 v117, 0x260
	v_add_u32_e32 v118, v154, v11
	v_add_u32_e32 v119, v2, v12
	v_add_u32_e32 v120, v154, v13
	v_add_u32_e32 v121, v2, v14
	v_add_u32_e32 v122, v154, v15
	v_add_u32_e32 v123, v2, v16
	v_add_u32_e32 v133, v154, v17
	v_add_u32_e32 v142, v2, v18
	v_add_u32_e32 v145, v3, v4
	v_add_u32_e32 v146, v6, v5
	v_add_u32_e32 v147, v8, v7
	v_add_u32_e32 v152, v9, v10
	s_and_saveexec_b64 s[98:99], s[0:1]
	v_mov_b32_e32 v239, 0
	v_mov_b32_e32 v240, 1
	global_atomic_add v238, v239, v240, s[14:15] sc0
	s_mov_b64 exec, s[98:99]
	s_branch .LBB0_1289

; template <int TYPE>
; __device__ __forceinline__ void causal_wg_unit(const bf16* proj, const float* cum2, const float* gn, unsigned char* obuf, int b, int h, int qb, LAS unsigned char* kvbuf, LAS float* ncum, lptr wl, LAS float* wsf, int tid, int wave) {
;     const int lane = tid & 63, r32 = lane & 31, hi = lane >> 5;
;     constexpr int QC = TYPE == 0 ? QCOL_SB : QCOL_FX, KC = TYPE == 0 ? KCOL_SB : KCOL_FX, VC = TYPE == 0 ? VCOL_SB : VCOL_FX;
;     constexpr int HG = TYPE == 0 ? 8 : 12;
;     const bf16* Qp = proj + hm_off(QC, HG, b, h); const bf16* Kp = proj + hm_off(KC, HG, b, h); const bf16* Vp = proj + hm_off(VC, HG, b, h);
;     const int qt = 8 * qb + wave, qtok = 32 * qt + r32;
;     bf16x8 qr[4];
; #pragma unroll
;     for (int d0 = 0; d0 < 4; ++d0) qr[d0] = *(const GAS bf16x8*)(Qp + (size_t)qtok * APITCH + d0 * 16 + hi * 8);
;     const int NT = 4 * qb + 4, my_tlast = qt >> 1;
;     const unsigned lvoff = (unsigned)(((tid >> 3) * APITCH + (tid & 7) * 8) * 2);
;     const int skey = tid >> 3, sch = tid & 7;
;     const int kst = sch * 1024 + ((skey ^ sch) << 4), vst = 8192 + (sch >> 2) * 4096 + ((skey ^ (sch >> 2)) << 6) + (sch & 3) * 16;
;     v4u kreg, vreg;
;     ...
;     if (TYPE == 1) { const int n = 256 * (qb + 1); if (4 * tid < n) { const f32x4 c = *(const GAS f32x4*)(cum2 + 4 * tid); v4u w;
; #pragma unroll
;         for (int e = 0; e < 4; ++e) { const float v = -c[e]; const unsigned hb = f2bf(v); const unsigned lb = f2bf(v - __builtin_bit_cast(float, hb << 16)); w[e] = hb | (lb << 16); }
;         *(LAS v4u*)(ncum + 4 * tid) = w; } }
;     const bf16x8 qone = hi ? (bf16x8){0, 0, 0, 0, 0, 0, 0, 0} : (bf16x8){(short)0x3f80, (short)0x3f80, 0, 0, 0, 0, 0, 0};
;     f32x16 o[2]; o[0] = f32x16{}; o[1] = f32x16{};
;     float mrun = -1e30f, lrun = 0.f, R = 1.f;
; template <int l>
; __device__ __forceinline__ void layer_phases(Frame& F, const XcdBarrier& bar, const int lo, const int hi) {
;     ...
;             if (ATT_ONLY < 0 || ATT_ONLY == 1) { gu32* ctr = F.ctl + CW_AQ + ((l * 4 + 1) * 8 + qid) * 64 + rep * 32;
;               for (;;) { int gi; ATT_DEQ(ctr, gi); if (gi >= 768) break;
;                   const int sl_ = gi >> 3, qb = 7 - sl_ / 12, bh = 12 * (gi & 7) + sl_ % 12;
;                   att::causal_wg_unit<1>(proj, (const float*)(ws + WS_CUM) + (size_t)bh * SEQ, gn, obuf, bh / 12, bh % 12, qb, kvbuf, ncum, wl, wsf, F.tid, F.wave); } }
.LBB0_1306:
	v_ashrrev_i32_e32 v0, 3, v124
	v_lshlrev_b32_e32 v1, 4, v143
	v_and_b32_e32 v6, 4, v167
	v_lshl_or_b32 v142, v0, 7, v1
	v_lshlrev_b32_e32 v1, 10, v143
	v_xor_b32_e32 v2, v0, v143
	v_mul_u32_u24_e32 v6, 0x110, v6
	v_lshl_add_u32 v181, v2, 4, v1
	v_lshlrev_b32_e32 v2, 12, v144
	v_xor_b32_e32 v0, v144, v0
	v_lshlrev_b32_e32 v144, 2, v124
	v_add3_u32 v133, s22, v6, v105
	v_or_b32_e32 v6, 3, v167
	v_ashrrev_i32_e32 v145, 31, v144
	v_mul_u32_u24_e32 v6, 0x110, v6
	v_lshlrev_b32_e32 v3, 6, v0
	v_lshl_add_u64 v[0:1], v[144:145], 2, s[56:57]
	v_add3_u32 v145, s22, v6, v105
	v_lshlrev_b32_e32 v6, 8, v125
	v_or_b32_e32 v4, v104, v2
	s_mov_b64 s[6:7], 0x700000
	v_add_u32_e32 v7, v141, v6
	v_lshlrev_b32_e32 v8, 6, v126
	v_add_u32_e32 v2, v2, v3
	s_add_u32 s66, s90, 0xe800
	v_lshl_add_u64 v[146:147], v[0:1], 0, s[6:7]
	v_mov_b32_e32 v97, 0
	v_add_u32_e32 v0, v4, v3
	v_lshl_add_u32 v1, v149, 10, 0
	v_lshl_add_u32 v4, v150, 10, 0
	v_lshl_add_u32 v5, v151, 10, 0
	v_add3_u32 v7, v7, v8, v127
	v_or3_b32 v6, v6, v8, v127
	v_or_b32_e32 v2, v2, v104
	s_addc_u32 s67, s91, 0
	s_mov_b32 s41, 0
	v_lshl_add_u32 v182, v124, 4, 0
	v_mov_b32_e32 v143, v97
	v_add_u32_e32 v183, 0, v105
	v_lshl_add_u32 v184, v125, 10, 0
	v_lshl_add_u32 v180, v140, 2, s82
	v_add_u32_e32 v185, 0x3e00, v7
	v_add_u32_e32 v186, 0, v148
	v_add_u32_e32 v187, 0x3c00, v7
	v_add_u32_e32 v188, 0x3a00, v7
	v_add_u32_e32 v189, 0x3800, v7
	v_add_u32_e32 v190, 0x3600, v7
	v_add_u32_e32 v191, 0x3400, v7
	v_add_u32_e32 v192, 0x3200, v7
	v_add_u32_e32 v193, 0x3000, v7
	v_or_b32_e32 v194, 0x2e00, v6
	v_or_b32_e32 v195, 0x2c00, v6
	v_or_b32_e32 v196, 0x2a00, v6
	v_or_b32_e32 v197, 0x2800, v6
	v_or_b32_e32 v198, 0x2600, v6
	v_or_b32_e32 v199, 0x2400, v6
	v_or_b32_e32 v200, 0x2200, v6
	v_or_b32_e32 v201, 0x2000, v6
	v_or_b32_e32 v202, 0xc100, v105
	v_add_u32_e32 v203, 0xa000, v2
	v_add_u32_e32 v204, 0x8000, v181
	s_add_i32 s92, 0, 0x21540
	s_mov_b64 s[68:69], 0x3000000
	s_movk_i32 s93, 0x7fff
	s_mov_b32 s94, 0xffff0000
	s_mov_b64 s[70:71], 0x4800000
	s_mov_b64 s[72:73], 0x6000000
	v_add_u32_e32 v205, 0, v0
	v_add_u32_e32 v206, v1, v159
	v_add_u32_e32 v207, v4, v161
	v_add_u32_e32 v208, v5, v163
	s_mov_b32 s95, 0xff800000
	v_mov_b32_e32 v209, 0x358637bd
	s_mov_b32 s96, 0xf800000
	v_mov_b32_e32 v210, 0x260
	v_mov_b32_e32 v211, 1
	v_mov_b32_e32 v212, 0xff800000
	s_and_saveexec_b64 s[98:99], s[0:1]
	v_mov_b32_e32 v239, 0
	v_mov_b32_e32 v240, 1
	global_atomic_add v238, v239, v240, s[66:67] sc0
	s_mov_b64 exec, s[98:99]
	s_branch .LBB0_1309

; #define ATT_DEQ(ctrp, out) do { __syncthreads(); if (F.tid == 0) uslot[0] = __hip_atomic_fetch_add((ctrp), 1u, RLX_AGENT); __syncthreads(); (out) = (int)uslot[0] * 8 + qid; } while (0)
; template <int l>
; __device__ __forceinline__ void layer_phases(Frame& F, const XcdBarrier& bar, const int lo, const int hi) {
;     ...
;             if (ATT_ONLY < 0 || ATT_ONLY == 1) { gu32* ctr = F.ctl + CW_AQ + ((l * 4 + 1) * 8 + qid) * 64 + rep * 32;
;               for (;;) { int gi; ATT_DEQ(ctr, gi); if (gi >= 768) break;
;                   const int sl_ = gi >> 3, qb = 7 - sl_ / 12, bh = 12 * (gi & 7) + sl_ % 12;
;                   att::causal_wg_unit<1>(proj, (const float*)(ws + WS_CUM) + (size_t)bh * SEQ, gn, obuf, bh / 12, bh % 12, qb, kvbuf, ncum, wl, wsf, F.tid, F.wave); } }
.LBB0_1309:
	s_barrier
	s_and_saveexec_b64 s[6:7], s[0:1]
	s_cbranch_execz .LBB0_1313
	s_waitcnt vmcnt(0)
	v_mov_b32_e32 v1, s92
	ds_write_b32 v1, v238
	v_mov_b32_e32 v240, 1
	v_mov_b32_e32 v239, 0
	s_waitcnt lgkmcnt(0)
	global_atomic_add v238, v239, v240, s[66:67] sc0

; #define PG8_LAS __attribute__((address_space(3)))
; #define PG8_BAR __builtin_amdgcn_s_barrier()
;     __device__ bool next(int i, Unit& u) const {
;         const long L = (long)i * G + c; if (L >= nwg) return false;
;         int wgid = (int)L; { const int q = nwg / NXCD, r = nwg % NXCD, xcd = wgid % NXCD, off = wgid / NXCD; wgid = (xcd < r ? xcd * (q + 1) : r * (q + 1) + (xcd - r) * q) + off; }
;         const int nig = WGM * nN, gid = wgid / nig, fm = gid * WGM, gsz = (nM - fm) < WGM ? (nM - fm) : WGM;
;         u.pm = fm + ((wgid % nig) % gsz); u.pn = (wgid % nig) / gsz; return true;
;     }
; __device__ __forceinline__ v8i_t cat8(bf16x8 a, bf16x8 b) { const v4i_t x = __builtin_bit_cast(v4i_t, a), y = __builtin_bit_cast(v4i_t, b); return __builtin_shufflevector(x, y, 0, 1, 2, 3, 4, 5, 6, 7); }
; __device__ __forceinline__ unsigned cvt_pk_bf16(float lo, float hi) { unsigned r; asm volatile("v_cvt_pk_bf16_f32 %0, %1, %2" : "=v"(r) : "v"(lo), "v"(hi)); return r; }
; template <class Epi, class Sched, bool ALIGN_EPI, bool FP8 = false>
; __device__ __forceinline__ void gemm_phase(PG8_LAS unsigned char* lds, const Gemm g, const Sched& S, const Epi& E, const int wid, const int lane) {
;     constexpr bool GA = Sched::GATHER;
;     const int tid = wid * 64 + lane, wr = wid >> 2, wc = wid & 3, fr = lane & 15, fq = lane >> 4;
;     int KB = g.KB; asm volatile("" : "+s"(KB)); const int nt = KB / 128;
;     unsigned voffA[2], voffB[2]; int rA[2]; unsigned cA2[2];
; #pragma unroll
;     for (int i = 0; i < 2; ++i) { int R, C; stage_rc(tid * 16 + i * 8192, R, C); const int Rb = Epi::PERM ? ((R & ~31) + perm32(R & 31)) : R;
;         rA[i] = R; cA2[i] = (unsigned)C * 2u; voffA[i] = (unsigned)(R * KB + C * 2); voffB[i] = (unsigned)(Rb * KB + C * 2); }
;     ...
;     const char* cA = GA ? (const char*)g.A : (const char*)g.A + (size_t)cur.pm * tstep; const char* cB = (const char*)g.Bt + (size_t)cur.pn * tstep;
;     PG8_STAGE(PG8_SB(0, 0), cB, voffB); PG8_STAGE(PG8_SB(0, 1), cB + hstep, voffB); PG8_STAGE(PG8_SA(0, 0), cA, vc0); PG8_STAGE(PG8_SA(0, 1), cA + hstepA, vc1);
;     if (wr == 1) PG8_BAR;
.LBB0_1435:
	s_cmp_gt_i32 s92, 12
	s_cselect_b64 s[0:1], -1, 0
	s_cmp_lt_i32 s93, 13
	s_cselect_b64 s[4:5], -1, 0
	s_or_b64 s[0:1], s[0:1], s[4:5]
	s_and_b64 vcc, exec, s[0:1]
	s_cbranch_vccnz .LBB0_1515
	s_lshl_b32 s4, s80, 10
	s_cmpk_gt_i32 s2, 0x1ff
	v_mov_b32_e32 v172, v216
	s_movk_i32 s0, 0x800
	s_cbranch_scc1 .LBB0_1461
	s_waitcnt vmcnt(17)
	v_lshl_add_u32 v1, v172, 4, s4
	v_ashrrev_i32_e32 v0, 31, v1
	v_lshrrev_b32_e32 v0, 22, v0
	v_add_u32_e32 v0, v1, v0
	v_ashrrev_i32_e32 v0, 10, v0
	v_mul_i32_i24_e32 v2, 0x400, v0
	v_sub_u32_e32 v2, v1, v2
	v_lshrrev_b32_e32 v3, 4, v2
	v_bitop3_b32 v2, v3, v2, 32 bitop3:0x6c
	s_waitcnt vmcnt(16)
	v_ashrrev_i32_e32 v4, 31, v2
	v_lshrrev_b32_e32 v4, 26, v4
	v_lshlrev_b32_e32 v3, 3, v0
	v_add_u32_e32 v4, v2, v4
	v_and_b32_e32 v3, -16, v3
	v_ashrrev_i32_e32 v5, 6, v4
	v_and_b32_e32 v4, 0xc0, v4
	v_add_u32_e32 v3, v5, v3
	v_sub_u32_e32 v2, v2, v4
	v_mov_b32_e32 v4, 1
	v_lshlrev_b32_e32 v0, 5, v0
	v_ashrrev_i16_sdwa v2, v4, sext(v2) dst_sel:DWORD dst_unused:UNUSED_PAD src0_sel:DWORD src1_sel:BYTE_0
	v_lshlrev_b32_e32 v6, 1, v3
	v_lshrrev_b32_e32 v7, 2, v3
	v_and_b32_e32 v5, 3, v5
	s_movk_i32 s1, 0xffe0
	v_and_b32_e32 v0, 32, v0
	v_bfe_i32 v2, v2, 0, 16
	v_and_b32_e32 v6, 24, v6
	v_and_b32_e32 v7, 4, v7
	v_and_or_b32 v5, v3, s1, v5
	v_or3_b32 v5, v5, v7, v6
	v_add_lshl_u32 v0, v0, v2, 1
	v_mad_u64_u32 v[160:161], s[6:7], v3, s0, v[0:1]
	v_mad_u64_u32 v[162:163], s[6:7], v5, s0, v[0:1]
	v_add_u32_e32 v0, 0x2000, v1
	v_ashrrev_i32_e32 v1, 31, v0
	v_lshrrev_b32_e32 v1, 22, v1
	v_add_u32_e32 v1, v0, v1
	v_ashrrev_i32_e32 v1, 10, v1
	v_mul_i32_i24_e32 v2, 0x400, v1
	v_sub_u32_e32 v0, v0, v2
	v_lshrrev_b32_e32 v2, 4, v0
	v_bitop3_b32 v0, v2, v0, 32 bitop3:0x6c
	v_ashrrev_i32_e32 v3, 31, v0
	v_lshrrev_b32_e32 v3, 26, v3
	v_add_u32_e32 v3, v0, v3
	v_ashrrev_i32_e32 v5, 6, v3
	v_and_b32_e32 v3, 0xffc0, v3
	s_add_u32 s3, s56, 0x51c00000
	v_sub_u32_e32 v0, v0, v3
	s_addc_u32 s38, s57, 0
	v_lshlrev_b32_e32 v2, 3, v1
	v_lshrrev_b16_e32 v3, 7, v0
	s_add_u32 s39, s56, 0x1ce00000
	v_and_b32_e32 v2, -16, v2
	v_and_b32_e32 v3, 1, v3
	s_addc_u32 s40, s57, 0
	v_add_u32_e32 v2, v5, v2
	v_add_u16_e32 v0, v0, v3
	s_ashr_i32 s43, s2, 31
	v_lshlrev_b32_e32 v1, 5, v1
	v_ashrrev_i16_sdwa v0, v4, sext(v0) dst_sel:DWORD dst_unused:UNUSED_PAD src0_sel:DWORD src1_sel:BYTE_0
	v_lshlrev_b32_e32 v3, 1, v2
	v_lshrrev_b32_e32 v4, 2, v2
	v_and_b32_e32 v5, 3, v5
	s_add_i32 s42, s4, 0
	s_lshr_b32 s4, s43, 29
	v_and_b32_e32 v1, 32, v1
	v_bfe_i32 v0, v0, 0, 16
	v_and_b32_e32 v3, 24, v3
	v_and_b32_e32 v4, 4, v4
	v_and_or_b32 v5, v2, s1, v5
	s_add_i32 s4, s2, s4
	v_or3_b32 v3, v5, v4, v3
	v_add_lshl_u32 v0, v1, v0, 1
	s_ashr_i32 s5, s4, 3
	s_and_b32 s4, s4, -8
	v_mad_u64_u32 v[164:165], s[6:7], v2, s0, v[0:1]
	v_mad_u64_u32 v[166:167], s[6:7], v3, s0, v[0:1]
	s_ashr_i32 s1, s0, 31
	s_sub_i32 s4, s2, s4
	s_lshr_b32 s14, s90, 8
	s_lshl_b64 s[6:7], s[0:1], 7
	s_lshl_b64 s[8:9], s[0:1], 8
	s_lshl_b32 s11, s4, 6
	s_mul_i32 s10, s4, 0x41
	s_cmp_lt_i32 s4, 0
	s_cselect_b32 s4, s10, s11
	s_add_i32 s4, s4, s5
	s_ashr_i32 s5, s4, 31
	s_lshr_b32 s5, s5, 26
	s_add_i32 s5, s4, s5
	s_ashr_i32 s10, s5, 6
	s_and_b32 s5, s5, 0xffc0
	s_sub_i32 s4, s4, s5
	s_bfe_i32 s5, s4, 0x80000
	s_bfe_u32 s5, s5, 0x3000c
	s_add_i32 s5, s4, s5
	s_bfe_i32 s11, s5, 0x80000
	s_and_b32 s5, s5, 0xf8
	s_sub_i32 s4, s4, s5
	s_lshl_b32 s10, s10, 3
	s_sext_i32_i8 s4, s4
	s_add_i32 s82, s10, s4
	s_ashr_i32 s4, s82, 31
	s_mul_i32 s4, s8, s4
	s_mul_hi_u32 s5, s8, s82
	s_sext_i32_i16 s13, s11
	s_add_i32 s10, s5, s4
	s_lshr_b64 s[4:5], s[0:1], 24
	s_lshr_b32 s12, s13, 3
	s_mul_i32 s5, s4, s82
	s_add_i32 s15, s10, s5
	s_bfe_i64 s[10:11], s[12:13], 0x100000
	s_ashr_i32 s5, s13, 3
	s_mul_hi_u32 s10, s8, s5
	s_mul_i32 s11, s8, s11
	s_add_i32 s10, s10, s11
	s_mul_i32 s4, s4, s5
	s_add_i32 s10, s10, s4
	s_mul_i32 s4, s8, s5
	s_add_u32 s28, s39, s4
	s_addc_u32 s29, s40, s10
	s_add_i32 s44, s42, 0x10000
	s_mov_b32 m0, s44
	s_nop 0
	global_load_lds_dwordx4 v162, s[28:29]
	s_add_i32 s45, s42, 0x12000
	s_mov_b32 m0, s45
	s_nop 0
	global_load_lds_dwordx4 v166, s[28:29]
	s_add_u32 s4, s28, s6
	s_mul_i32 s16, s8, s82
	s_addc_u32 s5, s29, s7
	s_add_i32 s46, s42, 0x14000
	s_mov_b32 m0, s46
	s_nop 0
	global_load_lds_dwordx4 v162, s[4:5]
	s_add_i32 s47, s42, 0x16000
	s_mov_b32 m0, s47
	s_nop 0
	global_load_lds_dwordx4 v166, s[4:5]
	s_add_u32 s30, s3, s16
	s_addc_u32 s31, s38, s15
	s_mov_b32 m0, s42
	s_nop 0
	global_load_lds_dwordx4 v160, s[30:31]
	s_add_i32 s48, s42, 0x2000
	s_mov_b32 m0, s48
	s_nop 0
	global_load_lds_dwordx4 v164, s[30:31]
	s_add_u32 s16, s30, s6
	s_addc_u32 s17, s31, s7
	s_add_i32 s49, s42, 0x4000
	s_mov_b32 m0, s49
	s_nop 0
	global_load_lds_dwordx4 v160, s[16:17]
	s_add_i32 s50, s42, 0x6000
	s_mov_b32 m0, s50
	s_nop 0
	global_load_lds_dwordx4 v164, s[16:17]
	s_cmp_eq_u32 s14, 1
	s_mov_b32 s41, 0
	s_cselect_b64 s[10:11], -1, 0
	s_cmp_lg_u32 s14, 1
	s_cbranch_scc1 .LBB0_1439
	s_barrier
; #define PG8_STAGE(bufoff, gbase, voff) do { _Pragma("unroll") for (int _i = 0; _i < 2; ++_i) { unsigned keep_; \
;         asm volatile("s_mov_b32 %0, m0\n\ts_mov_b32 m0, %3\n\ts_nop 0\n\tglobal_load_lds_dwordx4 %1, %2\n\ts_mov_b32 m0, %0" : "=&s"(keep_) : "v"((voff)[_i]), "s"((const char*)(gbase)), "s"(ldsb + (unsigned)((bufoff) + _i * 8192)) : "memory"); } } while (0)
; #define PG8_WAIT_V(n) asm volatile("s_waitcnt vmcnt(" #n ")" ::: "memory")
; #define PG8_BAR __builtin_amdgcn_s_barrier()
; template <class Epi, class Sched, bool ALIGN_EPI, bool FP8 = false>
; __device__ __forceinline__ void gemm_phase(PG8_LAS unsigned char* lds, const Gemm g, const Sched& S, const Epi& E, const int wid, const int lane) {
;     ...
;     const size_t kstep = (size_t)(BK * 2);
;     const size_t hstep = (size_t)HALF * KB;
;     const size_t hstepA = GA ? (size_t)0 : hstep;
;     const size_t tstep = 2 * hstep;
;     const unsigned ldsw = (unsigned)wid * 1024u;
;     const int aoff = lds_byte(wr * 64 + fr, fq * 8), boff = lds_byte(wc * 32 + fr, fq * 8);
;     ...
;     const unsigned ldsb = (unsigned)__builtin_amdgcn_readfirstlane((int)((unsigned)(__UINTPTR_TYPE__)lds + ldsw));
;     ...
;     PG8_WAIT_V(2); PG8_BAR;
;     PG8_STAGE(PG8_SB(1, 0), cB + kstep, voffB); PG8_STAGE(PG8_SA(1, 0), cA + kstep, vc0); PG8_STAGE(PG8_SB(1, 1), cB + hstep + kstep, voffB);
;     PG8_WAIT_V(6); PG8_BAR;
.LBB0_1439:
	s_sext_i32_i8 s83, s12
	s_add_u32 s12, s56, 0x55c00000
	s_addc_u32 s13, s57, 0
	s_lshr_b32 s1, s1, 25
	s_add_i32 s1, s0, s1
	s_ashr_i32 s51, s1, 7
	v_ashrrev_i32_e32 v2, 6, v172
	s_lshl_b32 s1, s14, 13
	v_lshl_add_u32 v4, v2, 10, s1
	s_lshl_b32 s1, s80, 5
	v_and_b32_e32 v0, 15, v172
	s_and_b32 s1, s1, 0x60
	v_lshl_or_b32 v161, s14, 6, v0
	s_lshr_b32 s14, s1, 3
	v_add_lshl_u32 v2, v2, s14, 10
	s_add_u32 s14, s28, 0x80
	s_waitcnt vmcnt(2)
	s_barrier
	s_addc_u32 s15, s29, 0
	s_add_i32 s52, s42, 0x18000
	s_mov_b32 m0, s52
	s_nop 0
	global_load_lds_dwordx4 v162, s[14:15]
	s_add_i32 s53, s42, 0x1a000
	s_mov_b32 m0, s53
	s_nop 0
	global_load_lds_dwordx4 v166, s[14:15]
	s_add_u32 s14, s30, 0x80
	s_addc_u32 s15, s31, 0
	s_add_i32 s54, s42, 0x8000
	s_mov_b32 m0, s54
	s_nop 0
	global_load_lds_dwordx4 v160, s[14:15]
	s_add_i32 s55, s42, 0xa000
	v_and_b32_e32 v3, 48, v172
	s_mov_b32 m0, s55
	s_nop 0
	global_load_lds_dwordx4 v164, s[14:15]
	s_add_u32 s4, s4, 0x80
	v_lshl_or_b32 v0, v0, 6, v3
	v_lshlrev_b32_e32 v3, 2, v172
	s_addc_u32 s5, s5, 0
	s_add_i32 s64, s42, 0x1c000
	s_mov_b32 m0, s64
	s_nop 0
	global_load_lds_dwordx4 v162, s[4:5]
	s_add_i32 s65, s42, 0x1e000
	v_and_b32_e32 v3, 32, v3
	s_mov_b32 m0, s65
	s_nop 0
	global_load_lds_dwordx4 v166, s[4:5]
	s_cmpk_gt_i32 s0, 0x7f
	v_ashrrev_i32_e32 v1, 1, v172
	v_bitop3_b32 v4, v0, v4, v3 bitop3:0xde
	v_bitop3_b32 v0, v0, v2, v3 bitop3:0xde
	s_waitcnt vmcnt(6)
	s_cselect_b64 s[14:15], -1, 0
	s_add_i32 s66, s51, -2
	s_add_i32 s67, s42, 0xc000
	v_and_b32_e32 v1, -8, v1
	s_cmpk_lt_u32 s90, 0x100
	v_add_u32_e32 v0, 0, v0
	s_cselect_b64 s[16:17], -1, 0
	v_add_u32_e32 v163, s1, v1
	s_add_i32 s68, s42, 0xe000
	s_ashr_i32 s69, s76, 31
	v_mov_b64_e32 v[168:169], 0x200
	v_mov_b64_e32 v[170:171], 0x1ff
	v_add_u32_e32 v165, 0x10000, v0
	v_add_u32_e32 v167, 0x14000, v0
	v_add_u32_e32 v173, 0, v4
	v_mov_b32_e32 v174, 0x79
	v_mov_b32_e32 v175, 0x7b
	v_add_u32_e32 v176, 0x18000, v0
	v_add_u32_e32 v177, 0x1c000, v0
	s_mov_b64 s[18:19], 0x80000
	s_mov_b32 s70, 0x80000
	s_mov_b64 s[20:21], 0x90000
	s_mov_b32 s71, 0x90000
	s_mov_b64 s[22:23], 0xa0000
	s_mov_b32 s72, 0xa0000
	s_mov_b64 s[24:25], 0xb0000
	s_mov_b32 s73, 0xb0000
	s_barrier
	s_waitcnt vmcnt(0)
	s_branch .LBB0_1442

; #define PG8_STAGE(bufoff, gbase, voff) do { _Pragma("unroll") for (int _i = 0; _i < 2; ++_i) { unsigned keep_; \
;         asm volatile("s_mov_b32 %0, m0\n\ts_mov_b32 m0, %3\n\ts_nop 0\n\tglobal_load_lds_dwordx4 %1, %2\n\ts_mov_b32 m0, %0" : "=&s"(keep_) : "v"((voff)[_i]), "s"((const char*)(gbase)), "s"(ldsb + (unsigned)((bufoff) + _i * 8192)) : "memory"); } } while (0)
; #define PG8_LDA(dst, b, h) do { _Pragma("unroll") for (int m = 0; m < 4; ++m) _Pragma("unroll") for (int k = 0; k < 2; ++k) dst[m][k] = *(const PG8_LAS bf16x8*)(lds + PG8_SA(b, h) + aoff + m * 2048 + k * 1024); } while (0)
; #define PG8_LDB(dst, b, h) do { _Pragma("unroll") for (int n = 0; n < 2; ++n) _Pragma("unroll") for (int k = 0; k < 2; ++k) dst[n][k] = *(const PG8_LAS bf16x8*)(lds + PG8_SB(b, h) + boff + n * 2048 + k * 1024); } while (0)
; #define PG8_WAIT_V(n) asm volatile("s_waitcnt vmcnt(" #n ")" ::: "memory")
; #define PG8_WAIT_L(n) asm volatile("s_waitcnt lgkmcnt(" #n ")" ::: "memory")
; #define PG8_BAR __builtin_amdgcn_s_barrier()
; #define PG8_SCHED __builtin_amdgcn_sched_barrier(0)
; template <class Epi, class Sched, bool ALIGN_EPI, bool FP8 = false>
; __device__ __forceinline__ void gemm_phase(PG8_LAS unsigned char* lds, const Gemm g, const Sched& S, const Epi& E, const int wid, const int lane) {
;     ...
;         for (int t = 0; t < nt; t += 2) {
;             const bool last = (t == nt - 2);
;             const char* a1 = cA + (size_t)(t + 1) * kstep;
;             const char* a2 = last ? nA : cA + (size_t)(t + 2) * kstep; const char* b2 = last ? nB : cB + (size_t)(t + 2) * kstep;
;             const char* a3 = a2 + kstep; const char* b3 = b2 + kstep;
;             PG8_LDB(B0, 0, 0); PG8_LDB(B1, 0, 1); PG8_SCHED; PG8_LDA(At, 0, 0); PG8_STAGE(PG8_SA(1, 1), a1 + hstepA, vc1);
;             if (GA && last && has_next) { const u32x4 q = *gslot; vc0[0] = q.x; vc0[1] = q.y; vc1[0] = q.z; vc1[1] = q.w; }
;             PG8_WAIT_V(8); PG8_WAIT_L(0); PG8_BAR; PG8_MMA(0, 0, At, B0); PG8_MMA(0, 1, At, B1); PG8_BAR; PG8_SCHED;
;             PG8_LDA(At, 0, 1); PG8_STAGE(PG8_SB(0, 0), b2, voffB); PG8_STAGE(PG8_SB(0, 1), b2 + hstep, voffB); PG8_STAGE(PG8_SA(0, 0), a2, vc0);
;             PG8_WAIT_V(8); PG8_WAIT_L(0); PG8_BAR; PG8_MMA(1, 0, At, B0); PG8_MMA(1, 1, At, B1); PG8_BAR; PG8_SCHED;
.LBB0_1454:
	ds_read_b128 v[24:27], v165
	ds_read_b128 v[28:31], v165 offset:1024
	ds_read_b128 v[16:19], v165 offset:2048
	ds_read_b128 v[20:23], v165 offset:3072
	ds_read_b128 v[8:11], v167
	ds_read_b128 v[12:15], v167 offset:1024
	ds_read_b128 v[0:3], v167 offset:2048
	ds_read_b128 v[4:7], v167 offset:3072
	s_add_i32 s33, s30, 2
	s_cmp_eq_u32 s66, s30
	s_cselect_b32 s36, s4, s84
	s_cselect_b32 s37, s5, s85
	s_cselect_b32 s34, s26, s86
	s_cselect_b32 s35, s27, s87
	s_add_u32 s30, s36, 0x80
	s_addc_u32 s31, s37, 0
	ds_read_b128 v[178:181], v173
	ds_read_b128 v[182:185], v173 offset:1024
	ds_read_b128 v[186:189], v173 offset:2048
	ds_read_b128 v[190:193], v173 offset:3072
	ds_read_b128 v[194:197], v173 offset:4096
	ds_read_b128 v[198:201], v173 offset:5120
	ds_read_b128 v[202:205], v173 offset:6144
	ds_read_b128 v[206:209], v173 offset:7168
	s_mov_b32 m0, s67
	s_nop 0
	global_load_lds_dwordx4 v160, s[28:29]
	s_mov_b32 m0, s68
	s_nop 0
	global_load_lds_dwordx4 v164, s[28:29]
	s_waitcnt vmcnt(8)
	s_waitcnt lgkmcnt(0)
	s_barrier
	s_setprio 1
	s_waitcnt lgkmcnt(6)
	v_mfma_scale_f32_16x16x128_f8f6f4 v[156:159], v[24:31], v[178:185], v[156:159], v174, v175 op_sel_hi:[0,0,0]
	v_mfma_scale_f32_16x16x128_f8f6f4 v[152:155], v[16:23], v[178:185], v[152:155], v174, v175 op_sel_hi:[0,0,0]
	s_waitcnt lgkmcnt(4)
	v_mfma_scale_f32_16x16x128_f8f6f4 v[140:143], v[24:31], v[186:193], v[140:143], v174, v175 op_sel_hi:[0,0,0]
	v_mfma_scale_f32_16x16x128_f8f6f4 v[136:139], v[16:23], v[186:193], v[136:139], v174, v175 op_sel_hi:[0,0,0]
	s_waitcnt lgkmcnt(2)
	v_mfma_scale_f32_16x16x128_f8f6f4 v[124:127], v[24:31], v[194:201], v[124:127], v174, v175 op_sel_hi:[0,0,0]
	v_mfma_scale_f32_16x16x128_f8f6f4 v[120:123], v[16:23], v[194:201], v[120:123], v174, v175 op_sel_hi:[0,0,0]
	s_waitcnt lgkmcnt(0)
	v_mfma_scale_f32_16x16x128_f8f6f4 v[108:111], v[24:31], v[202:209], v[108:111], v174, v175 op_sel_hi:[0,0,0]
	v_mfma_scale_f32_16x16x128_f8f6f4 v[104:107], v[16:23], v[202:209], v[104:107], v174, v175 op_sel_hi:[0,0,0]
	s_setprio 0
	s_setprio 1
	v_mfma_scale_f32_16x16x128_f8f6f4 v[148:151], v[8:15], v[178:185], v[148:151], v174, v175 op_sel_hi:[0,0,0]
	v_mfma_scale_f32_16x16x128_f8f6f4 v[144:147], v[0:7], v[178:185], v[144:147], v174, v175 op_sel_hi:[0,0,0]
	v_mfma_scale_f32_16x16x128_f8f6f4 v[132:135], v[8:15], v[186:193], v[132:135], v174, v175 op_sel_hi:[0,0,0]
	v_mfma_scale_f32_16x16x128_f8f6f4 v[128:131], v[0:7], v[186:193], v[128:131], v174, v175 op_sel_hi:[0,0,0]
	v_mfma_scale_f32_16x16x128_f8f6f4 v[116:119], v[8:15], v[194:201], v[116:119], v174, v175 op_sel_hi:[0,0,0]
	v_mfma_scale_f32_16x16x128_f8f6f4 v[112:115], v[0:7], v[194:201], v[112:115], v174, v175 op_sel_hi:[0,0,0]
	v_mfma_scale_f32_16x16x128_f8f6f4 v[100:103], v[8:15], v[202:209], v[100:103], v174, v175 op_sel_hi:[0,0,0]
	v_mfma_scale_f32_16x16x128_f8f6f4 v[96:99], v[0:7], v[202:209], v[96:99], v174, v175 op_sel_hi:[0,0,0]
	s_setprio 0
	s_barrier
	ds_read_b128 v[178:181], v173 offset:16384
	ds_read_b128 v[182:185], v173 offset:17408
	ds_read_b128 v[186:189], v173 offset:18432
	ds_read_b128 v[190:193], v173 offset:19456
	ds_read_b128 v[194:197], v173 offset:20480
	ds_read_b128 v[198:201], v173 offset:21504
	ds_read_b128 v[202:205], v173 offset:22528
	ds_read_b128 v[206:209], v173 offset:23552
	s_mov_b32 m0, s44
	s_nop 0
	global_load_lds_dwordx4 v162, s[34:35]
	s_mov_b32 m0, s45
	s_nop 0
	global_load_lds_dwordx4 v166, s[34:35]
	s_add_u32 s58, s34, s6
	s_addc_u32 s59, s35, s7
	s_mov_b32 m0, s46
	s_nop 0
	global_load_lds_dwordx4 v162, s[58:59]
	s_mov_b32 m0, s47
	s_nop 0
	global_load_lds_dwordx4 v166, s[58:59]
	s_mov_b32 m0, s42
	s_nop 0
	global_load_lds_dwordx4 v160, s[36:37]
	s_mov_b32 m0, s48
	s_nop 0
	global_load_lds_dwordx4 v164, s[36:37]
	s_waitcnt vmcnt(8)
	s_waitcnt lgkmcnt(0)
	s_barrier
	s_setprio 1
	s_waitcnt lgkmcnt(6)
	v_mfma_scale_f32_16x16x128_f8f6f4 v[92:95], v[24:31], v[178:185], v[92:95], v174, v175 op_sel_hi:[0,0,0]
	v_mfma_scale_f32_16x16x128_f8f6f4 v[88:91], v[16:23], v[178:185], v[88:91], v174, v175 op_sel_hi:[0,0,0]
	s_waitcnt lgkmcnt(4)
	v_mfma_scale_f32_16x16x128_f8f6f4 v[76:79], v[24:31], v[186:193], v[76:79], v174, v175 op_sel_hi:[0,0,0]
	v_mfma_scale_f32_16x16x128_f8f6f4 v[72:75], v[16:23], v[186:193], v[72:75], v174, v175 op_sel_hi:[0,0,0]
	s_waitcnt lgkmcnt(2)
	v_mfma_scale_f32_16x16x128_f8f6f4 v[60:63], v[24:31], v[194:201], v[60:63], v174, v175 op_sel_hi:[0,0,0]
	v_mfma_scale_f32_16x16x128_f8f6f4 v[56:59], v[16:23], v[194:201], v[56:59], v174, v175 op_sel_hi:[0,0,0]
	s_waitcnt lgkmcnt(0)
	v_mfma_scale_f32_16x16x128_f8f6f4 v[44:47], v[24:31], v[202:209], v[44:47], v174, v175 op_sel_hi:[0,0,0]
	v_mfma_scale_f32_16x16x128_f8f6f4 v[40:43], v[16:23], v[202:209], v[40:43], v174, v175 op_sel_hi:[0,0,0]
	s_setprio 0
	s_setprio 1
	v_mfma_scale_f32_16x16x128_f8f6f4 v[84:87], v[8:15], v[178:185], v[84:87], v174, v175 op_sel_hi:[0,0,0]
	v_mfma_scale_f32_16x16x128_f8f6f4 v[80:83], v[0:7], v[178:185], v[80:83], v174, v175 op_sel_hi:[0,0,0]
	v_mfma_scale_f32_16x16x128_f8f6f4 v[68:71], v[8:15], v[186:193], v[68:71], v174, v175 op_sel_hi:[0,0,0]
	v_mfma_scale_f32_16x16x128_f8f6f4 v[64:67], v[0:7], v[186:193], v[64:67], v174, v175 op_sel_hi:[0,0,0]
	v_mfma_scale_f32_16x16x128_f8f6f4 v[52:55], v[8:15], v[194:201], v[52:55], v174, v175 op_sel_hi:[0,0,0]
	v_mfma_scale_f32_16x16x128_f8f6f4 v[48:51], v[0:7], v[194:201], v[48:51], v174, v175 op_sel_hi:[0,0,0]
	v_mfma_scale_f32_16x16x128_f8f6f4 v[36:39], v[8:15], v[202:209], v[36:39], v174, v175 op_sel_hi:[0,0,0]
	v_mfma_scale_f32_16x16x128_f8f6f4 v[32:35], v[0:7], v[202:209], v[32:35], v174, v175 op_sel_hi:[0,0,0]
	s_setprio 0
	s_barrier
; #define PG8_STAGE(bufoff, gbase, voff) do { _Pragma("unroll") for (int _i = 0; _i < 2; ++_i) { unsigned keep_; \
;         asm volatile("s_mov_b32 %0, m0\n\ts_mov_b32 m0, %3\n\ts_nop 0\n\tglobal_load_lds_dwordx4 %1, %2\n\ts_mov_b32 m0, %0" : "=&s"(keep_) : "v"((voff)[_i]), "s"((const char*)(gbase)), "s"(ldsb + (unsigned)((bufoff) + _i * 8192)) : "memory"); } } while (0)
; #define PG8_LDA(dst, b, h) do { _Pragma("unroll") for (int m = 0; m < 4; ++m) _Pragma("unroll") for (int k = 0; k < 2; ++k) dst[m][k] = *(const PG8_LAS bf16x8*)(lds + PG8_SA(b, h) + aoff + m * 2048 + k * 1024); } while (0)
; #define PG8_LDB(dst, b, h) do { _Pragma("unroll") for (int n = 0; n < 2; ++n) _Pragma("unroll") for (int k = 0; k < 2; ++k) dst[n][k] = *(const PG8_LAS bf16x8*)(lds + PG8_SB(b, h) + boff + n * 2048 + k * 1024); } while (0)
; #define PG8_WAIT_V(n) asm volatile("s_waitcnt vmcnt(" #n ")" ::: "memory")
; #define PG8_WAIT_L(n) asm volatile("s_waitcnt lgkmcnt(" #n ")" ::: "memory")
; #define PG8_BAR __builtin_amdgcn_s_barrier()
; #define PG8_SCHED __builtin_amdgcn_sched_barrier(0)
; template <class Epi, class Sched, bool ALIGN_EPI, bool FP8 = false>
; __device__ __forceinline__ void gemm_phase(PG8_LAS unsigned char* lds, const Gemm g, const Sched& S, const Epi& E, const int wid, const int lane) {
;     ...
;             PG8_LDB(B0, 1, 0); PG8_LDB(B1, 1, 1); PG8_SCHED; PG8_LDA(At, 1, 0); PG8_STAGE(PG8_SA(0, 1), a2 + hstepA, vc1);
;             PG8_WAIT_V(8); PG8_WAIT_L(0); PG8_BAR; PG8_MMA(0, 0, At, B0); PG8_MMA(0, 1, At, B1); PG8_BAR; PG8_SCHED;
;             PG8_LDA(At, 1, 1); PG8_STAGE(PG8_SB(1, 0), b3, voffB); PG8_STAGE(PG8_SB(1, 1), b3 + hstep, voffB); PG8_STAGE(PG8_SA(1, 0), a3, vc0);
;             PG8_WAIT_V(8); PG8_WAIT_L(0); PG8_BAR; PG8_MMA(1, 0, At, B0); PG8_MMA(1, 1, At, B1); PG8_BAR; PG8_SCHED;
	ds_read_b128 v[0:3], v176
	ds_read_b128 v[4:7], v176 offset:1024
	ds_read_b128 v[8:11], v176 offset:2048
	ds_read_b128 v[12:15], v176 offset:3072
	ds_read_b128 v[16:19], v177
	ds_read_b128 v[20:23], v177 offset:1024
	ds_read_b128 v[24:27], v177 offset:2048
	ds_read_b128 v[28:31], v177 offset:3072
	ds_read_b128 v[178:181], v173 offset:32768
	ds_read_b128 v[182:185], v173 offset:33792
	ds_read_b128 v[186:189], v173 offset:34816
	ds_read_b128 v[190:193], v173 offset:35840
	ds_read_b128 v[194:197], v173 offset:36864
	ds_read_b128 v[198:201], v173 offset:37888
	ds_read_b128 v[202:205], v173 offset:38912
	ds_read_b128 v[206:209], v173 offset:39936
	s_add_u32 s36, s36, s6
	s_addc_u32 s37, s37, s7
	s_mov_b32 m0, s49
	s_nop 0
	global_load_lds_dwordx4 v160, s[36:37]
	s_mov_b32 m0, s50
	s_nop 0
	global_load_lds_dwordx4 v164, s[36:37]
	s_waitcnt vmcnt(8)
	s_waitcnt lgkmcnt(0)
	s_barrier
	s_setprio 1
	s_waitcnt lgkmcnt(6)
	v_mfma_scale_f32_16x16x128_f8f6f4 v[156:159], v[0:7], v[178:185], v[156:159], v174, v175 op_sel_hi:[0,0,0]
	v_mfma_scale_f32_16x16x128_f8f6f4 v[152:155], v[8:15], v[178:185], v[152:155], v174, v175 op_sel_hi:[0,0,0]
	s_waitcnt lgkmcnt(4)
	v_mfma_scale_f32_16x16x128_f8f6f4 v[140:143], v[0:7], v[186:193], v[140:143], v174, v175 op_sel_hi:[0,0,0]
	v_mfma_scale_f32_16x16x128_f8f6f4 v[136:139], v[8:15], v[186:193], v[136:139], v174, v175 op_sel_hi:[0,0,0]
	s_waitcnt lgkmcnt(2)
	v_mfma_scale_f32_16x16x128_f8f6f4 v[124:127], v[0:7], v[194:201], v[124:127], v174, v175 op_sel_hi:[0,0,0]
	v_mfma_scale_f32_16x16x128_f8f6f4 v[120:123], v[8:15], v[194:201], v[120:123], v174, v175 op_sel_hi:[0,0,0]
	s_waitcnt lgkmcnt(0)
	v_mfma_scale_f32_16x16x128_f8f6f4 v[108:111], v[0:7], v[202:209], v[108:111], v174, v175 op_sel_hi:[0,0,0]
	v_mfma_scale_f32_16x16x128_f8f6f4 v[104:107], v[8:15], v[202:209], v[104:107], v174, v175 op_sel_hi:[0,0,0]
	s_setprio 0
	s_setprio 1
	v_mfma_scale_f32_16x16x128_f8f6f4 v[148:151], v[16:23], v[178:185], v[148:151], v174, v175 op_sel_hi:[0,0,0]
	v_mfma_scale_f32_16x16x128_f8f6f4 v[144:147], v[24:31], v[178:185], v[144:147], v174, v175 op_sel_hi:[0,0,0]
	v_mfma_scale_f32_16x16x128_f8f6f4 v[132:135], v[16:23], v[186:193], v[132:135], v174, v175 op_sel_hi:[0,0,0]
	v_mfma_scale_f32_16x16x128_f8f6f4 v[128:131], v[24:31], v[186:193], v[128:131], v174, v175 op_sel_hi:[0,0,0]
	v_mfma_scale_f32_16x16x128_f8f6f4 v[116:119], v[16:23], v[194:201], v[116:119], v174, v175 op_sel_hi:[0,0,0]
	v_mfma_scale_f32_16x16x128_f8f6f4 v[112:115], v[24:31], v[194:201], v[112:115], v174, v175 op_sel_hi:[0,0,0]
	v_mfma_scale_f32_16x16x128_f8f6f4 v[100:103], v[16:23], v[202:209], v[100:103], v174, v175 op_sel_hi:[0,0,0]
	v_mfma_scale_f32_16x16x128_f8f6f4 v[96:99], v[24:31], v[202:209], v[96:99], v174, v175 op_sel_hi:[0,0,0]
	s_setprio 0
	s_barrier
	ds_read_b128 v[178:181], v173 offset:49152
	ds_read_b128 v[182:185], v173 offset:50176
	ds_read_b128 v[186:189], v173 offset:51200
	ds_read_b128 v[190:193], v173 offset:52224
	ds_read_b128 v[194:197], v173 offset:53248
	ds_read_b128 v[198:201], v173 offset:54272
	ds_read_b128 v[202:205], v173 offset:55296
	ds_read_b128 v[206:209], v173 offset:56320
	s_add_u32 s34, s34, 0x80
	s_addc_u32 s35, s35, 0
	s_mov_b32 m0, s52
	s_nop 0
	global_load_lds_dwordx4 v162, s[34:35]
	s_mov_b32 m0, s53
	s_nop 0
	global_load_lds_dwordx4 v166, s[34:35]
	s_add_u32 s34, s34, s6
	s_addc_u32 s35, s35, s7
	s_mov_b32 m0, s64
	s_nop 0
	global_load_lds_dwordx4 v162, s[34:35]
	s_mov_b32 m0, s65
	s_nop 0
	global_load_lds_dwordx4 v166, s[34:35]
	s_mov_b32 m0, s54
	s_nop 0
	global_load_lds_dwordx4 v160, s[30:31]
	s_mov_b32 m0, s55
	s_nop 0
	global_load_lds_dwordx4 v164, s[30:31]
	s_waitcnt vmcnt(8)
	s_waitcnt lgkmcnt(0)
	s_barrier
	s_setprio 1
	s_waitcnt lgkmcnt(6)
	v_mfma_scale_f32_16x16x128_f8f6f4 v[92:95], v[0:7], v[178:185], v[92:95], v174, v175 op_sel_hi:[0,0,0]
	v_mfma_scale_f32_16x16x128_f8f6f4 v[88:91], v[8:15], v[178:185], v[88:91], v174, v175 op_sel_hi:[0,0,0]
	s_waitcnt lgkmcnt(4)
	v_mfma_scale_f32_16x16x128_f8f6f4 v[76:79], v[0:7], v[186:193], v[76:79], v174, v175 op_sel_hi:[0,0,0]
	v_mfma_scale_f32_16x16x128_f8f6f4 v[72:75], v[8:15], v[186:193], v[72:75], v174, v175 op_sel_hi:[0,0,0]
	s_waitcnt lgkmcnt(2)
	v_mfma_scale_f32_16x16x128_f8f6f4 v[60:63], v[0:7], v[194:201], v[60:63], v174, v175 op_sel_hi:[0,0,0]
	v_mfma_scale_f32_16x16x128_f8f6f4 v[56:59], v[8:15], v[194:201], v[56:59], v174, v175 op_sel_hi:[0,0,0]
	s_waitcnt lgkmcnt(0)
	v_mfma_scale_f32_16x16x128_f8f6f4 v[44:47], v[0:7], v[202:209], v[44:47], v174, v175 op_sel_hi:[0,0,0]
	v_mfma_scale_f32_16x16x128_f8f6f4 v[40:43], v[8:15], v[202:209], v[40:43], v174, v175 op_sel_hi:[0,0,0]
	s_setprio 0
	s_setprio 1
	v_mfma_scale_f32_16x16x128_f8f6f4 v[84:87], v[16:23], v[178:185], v[84:87], v174, v175 op_sel_hi:[0,0,0]
	v_mfma_scale_f32_16x16x128_f8f6f4 v[80:83], v[24:31], v[178:185], v[80:83], v174, v175 op_sel_hi:[0,0,0]
	v_mfma_scale_f32_16x16x128_f8f6f4 v[68:71], v[16:23], v[186:193], v[68:71], v174, v175 op_sel_hi:[0,0,0]
	v_mfma_scale_f32_16x16x128_f8f6f4 v[64:67], v[24:31], v[186:193], v[64:67], v174, v175 op_sel_hi:[0,0,0]
	v_mfma_scale_f32_16x16x128_f8f6f4 v[52:55], v[16:23], v[194:201], v[52:55], v174, v175 op_sel_hi:[0,0,0]
	v_mfma_scale_f32_16x16x128_f8f6f4 v[48:51], v[24:31], v[194:201], v[48:51], v174, v175 op_sel_hi:[0,0,0]
	v_mfma_scale_f32_16x16x128_f8f6f4 v[36:39], v[16:23], v[202:209], v[36:39], v174, v175 op_sel_hi:[0,0,0]
	v_mfma_scale_f32_16x16x128_f8f6f4 v[32:35], v[24:31], v[202:209], v[32:35], v174, v175 op_sel_hi:[0,0,0]
	s_setprio 0
	s_barrier
	s_add_u32 s84, s84, 0x100
	s_addc_u32 s85, s85, 0
	s_add_u32 s86, s86, 0x100
	s_addc_u32 s87, s87, 0
	s_add_u32 s28, s28, 0x100
	s_addc_u32 s29, s29, 0
	s_cmp_ge_i32 s33, s51
	s_mov_b32 s30, s33
	s_cbranch_scc0 .LBB0_1454

; #define PG8_STAGE(bufoff, gbase, voff) do { _Pragma("unroll") for (int _i = 0; _i < 2; ++_i) { unsigned keep_; \
;         asm volatile("s_mov_b32 %0, m0\n\ts_mov_b32 m0, %3\n\ts_nop 0\n\tglobal_load_lds_dwordx4 %1, %2\n\ts_mov_b32 m0, %0" : "=&s"(keep_) : "v"((voff)[_i]), "s"((const char*)(gbase)), "s"(ldsb + (unsigned)((bufoff) + _i * 8192)) : "memory"); } } while (0)
; #define PG8_WAIT_V(n) asm volatile("s_waitcnt vmcnt(" #n ")" ::: "memory")
; #define PG8_BAR __builtin_amdgcn_s_barrier()
; template <class Epi, class Sched, bool ALIGN_EPI, bool FP8 = false>
; __device__ __forceinline__ void gemm_phase(PG8_LAS unsigned char* lds, const Gemm g, const Sched& S, const Epi& E, const int wid, const int lane) {
;     ...
;     for (int i = 0; i < 2; ++i) { int R, C; stage_rc(tid * 16 + i * 8192, R, C); const int Rb = Epi::PERM ? ((R & ~31) + perm32(R & 31)) : R;
;         rA[i] = R; cA2[i] = (unsigned)C * 2u; voffA[i] = (unsigned)(R * KB + C * 2); voffB[i] = (unsigned)(Rb * KB + C * 2); }
;     const size_t kstep = (size_t)(BK * 2);
;     const size_t hstep = (size_t)HALF * KB;
;     const size_t hstepA = GA ? (size_t)0 : hstep;
;     const size_t tstep = 2 * hstep;
;     const unsigned ldsw = (unsigned)wid * 1024u;
;     const int aoff = lds_byte(wr * 64 + fr, fq * 8), boff = lds_byte(wc * 32 + fr, fq * 8);
;     ...
;     const char* cA = GA ? (const char*)g.A : (const char*)g.A + (size_t)cur.pm * tstep; const char* cB = (const char*)g.Bt + (size_t)cur.pn * tstep;
;     PG8_STAGE(PG8_SB(0, 0), cB, voffB); PG8_STAGE(PG8_SB(0, 1), cB + hstep, voffB); PG8_STAGE(PG8_SA(0, 0), cA, vc0); PG8_STAGE(PG8_SA(0, 1), cA + hstepA, vc1);
;     if (wr == 1) PG8_BAR;
;     PG8_WAIT_V(2); PG8_BAR;
;     PG8_STAGE(PG8_SB(1, 0), cB + kstep, voffB); PG8_STAGE(PG8_SA(1, 0), cA + kstep, vc0); PG8_STAGE(PG8_SB(1, 1), cB + hstep + kstep, voffB);
;     PG8_WAIT_V(6); PG8_BAR;
.LBB0_1621:
	v_lshlrev_b32_e32 v3, 6, v1
	v_lshlrev_b32_e32 v2, 5, v5
	v_sub_u32_e32 v3, v15, v3
	v_mov_b32_e32 v5, 1
	v_ashrrev_i16_sdwa v3, v5, sext(v3) dst_sel:DWORD dst_unused:UNUSED_PAD src0_sel:DWORD src1_sel:BYTE_0
	v_and_b32_e32 v2, 32, v2
	v_bfe_i32 v3, v3, 0, 16
	v_add_lshl_u32 v196, v2, v3, 1
	v_lshlrev_b32_e32 v3, 6, v13
	v_sub_u32_e32 v3, v12, v3
	v_lshlrev_b32_e32 v2, 5, v11
	v_ashrrev_i16_sdwa v3, v5, sext(v3) dst_sel:DWORD dst_unused:UNUSED_PAD src0_sel:DWORD src1_sel:BYTE_0
	v_and_b32_e32 v2, 32, v2
	v_bfe_i32 v3, v3, 0, 16
	v_add_lshl_u32 v198, v2, v3, 1
	s_waitcnt vmcnt(1)
	v_lshl_add_u32 v64, v0, 11, v198
	v_lshlrev_b32_e32 v0, 1, v199
	v_lshrrev_b32_e32 v2, 2, v199
	v_and_b32_e32 v3, 3, v13
	s_movk_i32 s5, 0xffe0
	v_and_b32_e32 v0, 24, v0
	v_and_b32_e32 v2, 4, v2
	v_and_or_b32 v3, v199, s5, v3
	v_or3_b32 v0, v3, v2, v0
	v_mad_u64_u32 v[200:201], s[0:1], s8, v0, v[198:199]
	v_lshlrev_b32_e32 v0, 1, v204
	v_lshrrev_b32_e32 v2, 2, v204
	v_and_b32_e32 v1, 3, v1
	v_and_b32_e32 v0, 24, v0
	v_and_b32_e32 v2, 4, v2
	v_and_or_b32 v1, v204, s5, v1
	v_or3_b32 v0, v1, v2, v0
	v_mad_u64_u32 v[202:203], s[0:1], s8, v0, v[196:197]
	s_ashr_i32 s9, s8, 31
	s_lshl_b32 s0, s80, 10
	s_lshr_b32 s4, s90, 8
	s_lshl_b64 s[16:17], s[8:9], 7
	s_lshl_b64 s[18:19], s[8:9], 8
	s_add_i32 s47, s0, 0
	s_add_u32 s20, s56, 0x41c00000
	s_addc_u32 s21, s57, 0
	s_add_u32 s48, s56, 0x1d600000
	s_addc_u32 s49, s57, 0
	s_ashr_i32 s0, s88, 31
	s_mul_i32 s0, s18, s0
	s_mul_hi_u32 s1, s18, s88
	s_add_i32 s5, s1, s0
	s_lshr_b64 s[0:1], s[8:9], 24
	s_mul_i32 s0, s0, s88
	s_add_i32 s5, s5, s0
	s_mul_i32 s0, s18, s88
	v_lshl_add_u32 v65, v8, 11, v196
	v_lshl_add_u32 v66, v4, 11, v198
	v_lshl_add_u32 v67, v6, 11, v196
	s_add_u32 s34, s48, s0
	s_addc_u32 s35, s49, s5
	s_add_i32 s51, s47, 0x10000
	s_mov_b32 m0, s51
	s_nop 0
	global_load_lds_dwordx4 v200, s[34:35]
	s_add_i32 s53, s47, 0x12000
	s_mov_b32 m0, s53
	s_nop 0
	global_load_lds_dwordx4 v202, s[34:35]
	s_add_u32 s0, s34, s16
	s_addc_u32 s1, s35, s17
	s_add_i32 s55, s47, 0x14000
	s_mov_b32 m0, s55
	s_nop 0
	global_load_lds_dwordx4 v200, s[0:1]
	s_add_i32 s64, s47, 0x16000
	s_mov_b32 m0, s64
	s_nop 0
	global_load_lds_dwordx4 v202, s[0:1]
	s_add_i32 s65, s47, 0x2000
	s_mov_b32 m0, s47
	s_nop 0
	global_load_lds_dwordx4 v64, s[20:21]
	s_add_i32 s66, s47, 0x4000
	s_mov_b32 m0, s65
	s_nop 0
	global_load_lds_dwordx4 v65, s[20:21]
	s_add_i32 s67, s47, 0x6000
	s_mov_b32 m0, s66
	s_nop 0
	global_load_lds_dwordx4 v66, s[20:21]
	s_cmp_eq_u32 s4, 1
	s_mov_b32 m0, s67
	s_nop 0
	global_load_lds_dwordx4 v67, s[20:21]
	s_mov_b32 s46, 0
	s_mov_b32 s50, 0x10000
	s_mov_b32 s52, 0x12000
	s_mov_b32 s54, 0x14000
	s_cselect_b64 s[22:23], -1, 0
	s_cmp_lg_u32 s4, 1
	s_cbranch_scc1 .LBB0_1623
	s_barrier
.LBB0_1623:
	v_and_b32_e32 v0, 15, v10
	s_add_i32 s5, 0, 0x21800
	v_lshl_or_b32 v203, s4, 6, v0
	v_ashrrev_i32_e32 v2, 6, v10
	s_lshl_b32 s4, s4, 13
	v_lshl_add_u32 v201, v197, 4, s5
	s_lshr_b32 s5, s9, 25
	v_lshl_add_u32 v4, v2, 10, s4
	s_lshl_b32 s4, s80, 5
	s_add_i32 s5, s8, s5
	s_and_b32 s9, s4, 0x60
	s_ashr_i32 s68, s5, 7
	s_lshr_b32 s4, s9, 3
	s_add_u32 s24, s56, 0x45c00000
	s_addc_u32 s25, s57, 0
	v_add_lshl_u32 v2, v2, s4, 10
	s_add_u32 s4, s56, 0x41c00080
	s_addc_u32 s5, s57, 0
	s_add_u32 s26, s34, 0x80
	s_waitcnt vmcnt(2)
	s_barrier
	s_addc_u32 s27, s35, 0
	s_add_i32 s69, s47, 0x18000
	s_mov_b32 m0, s69
	s_nop 0
	global_load_lds_dwordx4 v200, s[26:27]
	s_add_i32 s70, s47, 0x1a000
	s_add_i32 s71, s47, 0x8000
	s_add_i32 s72, s47, 0xa000
	s_mov_b32 m0, s70
	s_nop 0
	global_load_lds_dwordx4 v202, s[26:27]
	s_add_u32 s0, s0, 0x80
	s_mov_b32 m0, s71
	s_nop 0
	global_load_lds_dwordx4 v64, s[4:5]
	s_addc_u32 s1, s1, 0
	s_add_i32 s73, s47, 0x1c000
	s_add_i32 s74, s47, 0x1e000
	v_and_b32_e32 v3, 48, v10
	s_mov_b32 m0, s72
	s_nop 0
	global_load_lds_dwordx4 v65, s[4:5]
	s_cmpk_gt_i32 s8, 0x7f
	v_lshl_or_b32 v0, v0, 6, v3
	v_lshlrev_b32_e32 v3, 2, v10
	s_mov_b32 m0, s73
	s_nop 0
	global_load_lds_dwordx4 v200, s[0:1]
	s_cselect_b64 s[26:27], -1, 0
	s_add_i32 s75, s68, -2
	s_add_i32 s82, s47, 0xc000
	v_ashrrev_i32_e32 v1, 1, v10
	v_and_b32_e32 v3, 32, v3
	s_mov_b32 m0, s74
	s_nop 0
	global_load_lds_dwordx4 v202, s[0:1]
	s_cmpk_lt_u32 s90, 0x100
	v_and_b32_e32 v1, -8, v1
	v_bitop3_b32 v4, v0, v4, v3 bitop3:0xde
	v_bitop3_b32 v0, v0, v2, v3 bitop3:0xde
	s_waitcnt vmcnt(6)
	s_cselect_b64 s[28:29], -1, 0
	s_ashr_i32 s0, s76, 3
	v_add_u32_e32 v205, s9, v1
	s_mul_i32 s84, s0, s3
	v_cndmask_b32_e64 v1, 0, 1, s[6:7]
	v_add_u32_e32 v206, 0, v0
	s_add_i32 s83, s47, 0xe000
	s_add_i32 s84, s84, s44
	v_cmp_ne_u32_e64 s[0:1], 1, v1
	v_add_u32_e32 v207, 0x10000, v206
	v_add_u32_e32 v208, 0x14000, v206
	v_add_u32_e32 v209, 0, v4
	v_mov_b32_e32 v210, 0x79
	v_mov_b32_e32 v211, 0x7f
	s_barrier
	s_branch .LBB0_1626

; #define PG8_STAGE(bufoff, gbase, voff) do { _Pragma("unroll") for (int _i = 0; _i < 2; ++_i) { unsigned keep_; \
;         asm volatile("s_mov_b32 %0, m0\n\ts_mov_b32 m0, %3\n\ts_nop 0\n\tglobal_load_lds_dwordx4 %1, %2\n\ts_mov_b32 m0, %0" : "=&s"(keep_) : "v"((voff)[_i]), "s"((const char*)(gbase)), "s"(ldsb + (unsigned)((bufoff) + _i * 8192)) : "memory"); } } while (0)
; #define PG8_LDA(dst, b, h) do { _Pragma("unroll") for (int m = 0; m < 4; ++m) _Pragma("unroll") for (int k = 0; k < 2; ++k) dst[m][k] = *(const PG8_LAS bf16x8*)(lds + PG8_SA(b, h) + aoff + m * 2048 + k * 1024); } while (0)
; #define PG8_LDB(dst, b, h) do { _Pragma("unroll") for (int n = 0; n < 2; ++n) _Pragma("unroll") for (int k = 0; k < 2; ++k) dst[n][k] = *(const PG8_LAS bf16x8*)(lds + PG8_SB(b, h) + boff + n * 2048 + k * 1024); } while (0)
; #define PG8_WAIT_V(n) asm volatile("s_waitcnt vmcnt(" #n ")" ::: "memory")
; #define PG8_WAIT_L(n) asm volatile("s_waitcnt lgkmcnt(" #n ")" ::: "memory")
; #define PG8_BAR __builtin_amdgcn_s_barrier()
; #define PG8_SCHED __builtin_amdgcn_sched_barrier(0)
; template <class Epi, class Sched, bool ALIGN_EPI, bool FP8 = false>
; __device__ __forceinline__ void gemm_phase(PG8_LAS unsigned char* lds, const Gemm g, const Sched& S, const Epi& E, const int wid, const int lane) {
;     ...
;             const bool last = (t == nt - 2);
;             const char* a1 = cA + (size_t)(t + 1) * kstep;
;             const char* a2 = last ? nA : cA + (size_t)(t + 2) * kstep; const char* b2 = last ? nB : cB + (size_t)(t + 2) * kstep;
;             const char* a3 = a2 + kstep; const char* b3 = b2 + kstep;
;             PG8_LDB(B0, 0, 0); PG8_LDB(B1, 0, 1); PG8_SCHED; PG8_LDA(At, 0, 0); PG8_STAGE(PG8_SA(1, 1), a1 + hstepA, vc1);
;             if (GA && last && has_next) { const u32x4 q = *gslot; vc0[0] = q.x; vc0[1] = q.y; vc1[0] = q.z; vc1[1] = q.w; }
;             PG8_WAIT_V(8); PG8_WAIT_L(0); PG8_BAR; PG8_MMA(0, 0, At, B0); PG8_MMA(0, 1, At, B1); PG8_BAR; PG8_SCHED;
;             PG8_LDA(At, 0, 1); PG8_STAGE(PG8_SB(0, 0), b2, voffB); PG8_STAGE(PG8_SB(0, 1), b2 + hstep, voffB); PG8_STAGE(PG8_SA(0, 0), a2, vc0);
;             PG8_WAIT_V(8); PG8_WAIT_L(0); PG8_BAR; PG8_MMA(1, 0, At, B0); PG8_MMA(1, 1, At, B1); PG8_BAR; PG8_SCHED;
;             PG8_LDB(B0, 1, 0); PG8_LDB(B1, 1, 1); PG8_SCHED; PG8_LDA(At, 1, 0); PG8_STAGE(PG8_SA(0, 1), a2 + hstepA, vc1);
.LBB0_1637:
	s_add_i32 s89, s89, 2
	s_and_b64 s[8:9], s[38:39], exec
	s_cselect_b32 s9, 0, s6
	s_cselect_b32 s8, 0, s7
	s_add_u32 s40, s20, s9
	s_addc_u32 s41, s21, s8
	s_add_u32 s33, s34, s6
	s_addc_u32 s42, s35, s7
	s_add_u32 s8, s40, 0x80
	s_addc_u32 s9, s41, 0
	s_waitcnt vmcnt(8)
	s_and_b64 s[38:39], s[38:39], exec
	s_waitcnt lgkmcnt(0)
	s_cselect_b32 s43, s31, s42
	s_cselect_b32 s42, s30, s33
	s_add_u32 s38, s42, 0x80
	s_addc_u32 s39, s43, 0
	s_barrier
	s_setprio 1
	s_waitcnt lgkmcnt(6)
	v_mfma_scale_f32_16x16x128_f8f6f4 v[192:195], v[24:31], v[56:63], v[192:195], v210, v211 op_sel_hi:[0,0,0]
	v_mfma_scale_f32_16x16x128_f8f6f4 v[184:187], v[16:23], v[56:63], v[184:187], v210, v211 op_sel_hi:[0,0,0]
	s_waitcnt lgkmcnt(4)
	v_mfma_scale_f32_16x16x128_f8f6f4 v[176:179], v[24:31], v[48:55], v[176:179], v210, v211 op_sel_hi:[0,0,0]
	v_mfma_scale_f32_16x16x128_f8f6f4 v[168:171], v[16:23], v[48:55], v[168:171], v210, v211 op_sel_hi:[0,0,0]
	s_waitcnt lgkmcnt(2)
	v_mfma_scale_f32_16x16x128_f8f6f4 v[160:163], v[24:31], v[40:47], v[160:163], v210, v211 op_sel_hi:[0,0,0]
	v_mfma_scale_f32_16x16x128_f8f6f4 v[152:155], v[16:23], v[40:47], v[152:155], v210, v211 op_sel_hi:[0,0,0]
	s_waitcnt lgkmcnt(0)
	v_mfma_scale_f32_16x16x128_f8f6f4 v[144:147], v[24:31], v[32:39], v[144:147], v210, v211 op_sel_hi:[0,0,0]
	v_mfma_scale_f32_16x16x128_f8f6f4 v[136:139], v[16:23], v[32:39], v[136:139], v210, v211 op_sel_hi:[0,0,0]
	s_setprio 0
	s_setprio 1
	v_mfma_scale_f32_16x16x128_f8f6f4 v[188:191], v[8:15], v[56:63], v[188:191], v210, v211 op_sel_hi:[0,0,0]
	v_mfma_scale_f32_16x16x128_f8f6f4 v[180:183], v[0:7], v[56:63], v[180:183], v210, v211 op_sel_hi:[0,0,0]
	v_mfma_scale_f32_16x16x128_f8f6f4 v[172:175], v[8:15], v[48:55], v[172:175], v210, v211 op_sel_hi:[0,0,0]
	v_mfma_scale_f32_16x16x128_f8f6f4 v[164:167], v[0:7], v[48:55], v[164:167], v210, v211 op_sel_hi:[0,0,0]
	v_mfma_scale_f32_16x16x128_f8f6f4 v[156:159], v[8:15], v[40:47], v[156:159], v210, v211 op_sel_hi:[0,0,0]
	v_mfma_scale_f32_16x16x128_f8f6f4 v[148:151], v[0:7], v[40:47], v[148:151], v210, v211 op_sel_hi:[0,0,0]
	v_mfma_scale_f32_16x16x128_f8f6f4 v[140:143], v[8:15], v[32:39], v[140:143], v210, v211 op_sel_hi:[0,0,0]
	v_mfma_scale_f32_16x16x128_f8f6f4 v[132:135], v[0:7], v[32:39], v[132:135], v210, v211 op_sel_hi:[0,0,0]
	s_setprio 0
	s_barrier
	ds_read_b128 v[32:35], v209 offset:16384
	ds_read_b128 v[36:39], v209 offset:17408
	ds_read_b128 v[40:43], v209 offset:18432
	ds_read_b128 v[44:47], v209 offset:19456
	ds_read_b128 v[48:51], v209 offset:20480
	ds_read_b128 v[52:55], v209 offset:21504
	ds_read_b128 v[56:59], v209 offset:22528
	ds_read_b128 v[60:63], v209 offset:23552
	s_mov_b32 m0, s51
	s_nop 0
	global_load_lds_dwordx4 v200, s[42:43]
	s_mov_b32 m0, s53
	s_nop 0
	global_load_lds_dwordx4 v202, s[42:43]
	s_add_u32 s42, s42, s16
	s_addc_u32 s43, s43, s17
	s_mov_b32 m0, s55
	s_nop 0
	global_load_lds_dwordx4 v200, s[42:43]
	s_mov_b32 m0, s64
	s_nop 0
	global_load_lds_dwordx4 v202, s[42:43]
	s_mov_b32 m0, s47
	s_nop 0
	global_load_lds_dwordx4 v64, s[40:41]
	s_mov_b32 m0, s65
	s_nop 0
	global_load_lds_dwordx4 v65, s[40:41]
	s_waitcnt vmcnt(8)
	s_waitcnt lgkmcnt(0)
	s_barrier
	s_setprio 1
	s_waitcnt lgkmcnt(6)
	v_mfma_scale_f32_16x16x128_f8f6f4 v[128:131], v[24:31], v[32:39], v[128:131], v210, v211 op_sel_hi:[0,0,0]
	v_mfma_scale_f32_16x16x128_f8f6f4 v[120:123], v[16:23], v[32:39], v[120:123], v210, v211 op_sel_hi:[0,0,0]
	s_waitcnt lgkmcnt(4)
	v_mfma_scale_f32_16x16x128_f8f6f4 v[112:115], v[24:31], v[40:47], v[112:115], v210, v211 op_sel_hi:[0,0,0]
	v_mfma_scale_f32_16x16x128_f8f6f4 v[104:107], v[16:23], v[40:47], v[104:107], v210, v211 op_sel_hi:[0,0,0]
	s_waitcnt lgkmcnt(2)
	v_mfma_scale_f32_16x16x128_f8f6f4 v[96:99], v[24:31], v[48:55], v[96:99], v210, v211 op_sel_hi:[0,0,0]
	v_mfma_scale_f32_16x16x128_f8f6f4 v[88:91], v[16:23], v[48:55], v[88:91], v210, v211 op_sel_hi:[0,0,0]
	s_waitcnt lgkmcnt(0)
	v_mfma_scale_f32_16x16x128_f8f6f4 v[80:83], v[24:31], v[56:63], v[80:83], v210, v211 op_sel_hi:[0,0,0]
	v_mfma_scale_f32_16x16x128_f8f6f4 v[72:75], v[16:23], v[56:63], v[72:75], v210, v211 op_sel_hi:[0,0,0]
	s_setprio 0
	s_setprio 1
	v_mfma_scale_f32_16x16x128_f8f6f4 v[124:127], v[8:15], v[32:39], v[124:127], v210, v211 op_sel_hi:[0,0,0]
	v_mfma_scale_f32_16x16x128_f8f6f4 v[116:119], v[0:7], v[32:39], v[116:119], v210, v211 op_sel_hi:[0,0,0]
	v_mfma_scale_f32_16x16x128_f8f6f4 v[108:111], v[8:15], v[40:47], v[108:111], v210, v211 op_sel_hi:[0,0,0]
	v_mfma_scale_f32_16x16x128_f8f6f4 v[100:103], v[0:7], v[40:47], v[100:103], v210, v211 op_sel_hi:[0,0,0]
	v_mfma_scale_f32_16x16x128_f8f6f4 v[92:95], v[8:15], v[48:55], v[92:95], v210, v211 op_sel_hi:[0,0,0]
	v_mfma_scale_f32_16x16x128_f8f6f4 v[84:87], v[0:7], v[48:55], v[84:87], v210, v211 op_sel_hi:[0,0,0]
	v_mfma_scale_f32_16x16x128_f8f6f4 v[76:79], v[8:15], v[56:63], v[76:79], v210, v211 op_sel_hi:[0,0,0]
	v_mfma_scale_f32_16x16x128_f8f6f4 v[68:71], v[0:7], v[56:63], v[68:71], v210, v211 op_sel_hi:[0,0,0]
	s_setprio 0
	s_barrier
	v_add_u32_e32 v12, 0x18000, v206
	v_add_u32_e32 v28, 0x1c000, v206
	ds_read_b128 v[0:3], v12
	ds_read_b128 v[4:7], v12 offset:1024
	ds_read_b128 v[8:11], v12 offset:2048
	ds_read_b128 v[12:15], v12 offset:3072
	ds_read_b128 v[16:19], v28
	ds_read_b128 v[20:23], v28 offset:1024
	ds_read_b128 v[24:27], v28 offset:2048
	ds_read_b128 v[28:31], v28 offset:3072
	ds_read_b128 v[32:35], v209 offset:32768
	ds_read_b128 v[36:39], v209 offset:33792
	ds_read_b128 v[40:43], v209 offset:34816
	ds_read_b128 v[44:47], v209 offset:35840
	ds_read_b128 v[48:51], v209 offset:36864
	ds_read_b128 v[52:55], v209 offset:37888
	ds_read_b128 v[56:59], v209 offset:38912
	ds_read_b128 v[60:63], v209 offset:39936
	s_mov_b32 m0, s66
	s_nop 0
	global_load_lds_dwordx4 v66, s[40:41]
	s_mov_b32 m0, s67
	s_nop 0
	global_load_lds_dwordx4 v67, s[40:41]
	s_waitcnt vmcnt(8)
	s_waitcnt lgkmcnt(0)
	s_barrier
; #define PG8_STAGE(bufoff, gbase, voff) do { _Pragma("unroll") for (int _i = 0; _i < 2; ++_i) { unsigned keep_; \
;         asm volatile("s_mov_b32 %0, m0\n\ts_mov_b32 m0, %3\n\ts_nop 0\n\tglobal_load_lds_dwordx4 %1, %2\n\ts_mov_b32 m0, %0" : "=&s"(keep_) : "v"((voff)[_i]), "s"((const char*)(gbase)), "s"(ldsb + (unsigned)((bufoff) + _i * 8192)) : "memory"); } } while (0)
; #define PG8_LDA(dst, b, h) do { _Pragma("unroll") for (int m = 0; m < 4; ++m) _Pragma("unroll") for (int k = 0; k < 2; ++k) dst[m][k] = *(const PG8_LAS bf16x8*)(lds + PG8_SA(b, h) + aoff + m * 2048 + k * 1024); } while (0)
; #define PG8_LDB(dst, b, h) do { _Pragma("unroll") for (int n = 0; n < 2; ++n) _Pragma("unroll") for (int k = 0; k < 2; ++k) dst[n][k] = *(const PG8_LAS bf16x8*)(lds + PG8_SB(b, h) + boff + n * 2048 + k * 1024); } while (0)
; #define PG8_WAIT_V(n) asm volatile("s_waitcnt vmcnt(" #n ")" ::: "memory")
; #define PG8_WAIT_L(n) asm volatile("s_waitcnt lgkmcnt(" #n ")" ::: "memory")
; #define PG8_BAR __builtin_amdgcn_s_barrier()
; #define PG8_SCHED __builtin_amdgcn_sched_barrier(0)
; template <class Epi, class Sched, bool ALIGN_EPI, bool FP8 = false>
; __device__ __forceinline__ void gemm_phase(PG8_LAS unsigned char* lds, const Gemm g, const Sched& S, const Epi& E, const int wid, const int lane) {
;     ...
;         for (int t = 0; t < nt; t += 2) {
;             const bool last = (t == nt - 2);
;             const char* a1 = cA + (size_t)(t + 1) * kstep;
;             const char* a2 = last ? nA : cA + (size_t)(t + 2) * kstep; const char* b2 = last ? nB : cB + (size_t)(t + 2) * kstep;
;             const char* a3 = a2 + kstep; const char* b3 = b2 + kstep;
;             PG8_LDB(B0, 0, 0); PG8_LDB(B1, 0, 1); PG8_SCHED; PG8_LDA(At, 0, 0); PG8_STAGE(PG8_SA(1, 1), a1 + hstepA, vc1);
;             if (GA && last && has_next) { const u32x4 q = *gslot; vc0[0] = q.x; vc0[1] = q.y; vc1[0] = q.z; vc1[1] = q.w; }
;     ...
;             PG8_WAIT_V(8); PG8_WAIT_L(0); PG8_BAR; PG8_MMA(0, 0, At, B0); PG8_MMA(0, 1, At, B1); PG8_BAR; PG8_SCHED;
;             PG8_LDA(At, 1, 1); PG8_STAGE(PG8_SB(1, 0), b3, voffB); PG8_STAGE(PG8_SB(1, 1), b3 + hstep, voffB); PG8_STAGE(PG8_SA(1, 0), a3, vc0);
;             PG8_WAIT_V(8); PG8_WAIT_L(0); PG8_BAR; PG8_MMA(1, 0, At, B0); PG8_MMA(1, 1, At, B1); PG8_BAR; PG8_SCHED;
	s_setprio 1
	s_waitcnt lgkmcnt(6)
	v_mfma_scale_f32_16x16x128_f8f6f4 v[192:195], v[0:7], v[32:39], v[192:195], v210, v211 op_sel_hi:[0,0,0]
	v_mfma_scale_f32_16x16x128_f8f6f4 v[184:187], v[8:15], v[32:39], v[184:187], v210, v211 op_sel_hi:[0,0,0]
	s_waitcnt lgkmcnt(4)
	v_mfma_scale_f32_16x16x128_f8f6f4 v[176:179], v[0:7], v[40:47], v[176:179], v210, v211 op_sel_hi:[0,0,0]
	v_mfma_scale_f32_16x16x128_f8f6f4 v[168:171], v[8:15], v[40:47], v[168:171], v210, v211 op_sel_hi:[0,0,0]
	s_waitcnt lgkmcnt(2)
	v_mfma_scale_f32_16x16x128_f8f6f4 v[160:163], v[0:7], v[48:55], v[160:163], v210, v211 op_sel_hi:[0,0,0]
	v_mfma_scale_f32_16x16x128_f8f6f4 v[152:155], v[8:15], v[48:55], v[152:155], v210, v211 op_sel_hi:[0,0,0]
	s_waitcnt lgkmcnt(0)
	v_mfma_scale_f32_16x16x128_f8f6f4 v[144:147], v[0:7], v[56:63], v[144:147], v210, v211 op_sel_hi:[0,0,0]
	v_mfma_scale_f32_16x16x128_f8f6f4 v[136:139], v[8:15], v[56:63], v[136:139], v210, v211 op_sel_hi:[0,0,0]
	s_setprio 0
	s_setprio 1
	v_mfma_scale_f32_16x16x128_f8f6f4 v[188:191], v[16:23], v[32:39], v[188:191], v210, v211 op_sel_hi:[0,0,0]
	v_mfma_scale_f32_16x16x128_f8f6f4 v[180:183], v[24:31], v[32:39], v[180:183], v210, v211 op_sel_hi:[0,0,0]
	v_mfma_scale_f32_16x16x128_f8f6f4 v[172:175], v[16:23], v[40:47], v[172:175], v210, v211 op_sel_hi:[0,0,0]
	v_mfma_scale_f32_16x16x128_f8f6f4 v[164:167], v[24:31], v[40:47], v[164:167], v210, v211 op_sel_hi:[0,0,0]
	v_mfma_scale_f32_16x16x128_f8f6f4 v[156:159], v[16:23], v[48:55], v[156:159], v210, v211 op_sel_hi:[0,0,0]
	v_mfma_scale_f32_16x16x128_f8f6f4 v[148:151], v[24:31], v[48:55], v[148:151], v210, v211 op_sel_hi:[0,0,0]
	v_mfma_scale_f32_16x16x128_f8f6f4 v[140:143], v[16:23], v[56:63], v[140:143], v210, v211 op_sel_hi:[0,0,0]
	v_mfma_scale_f32_16x16x128_f8f6f4 v[132:135], v[24:31], v[56:63], v[132:135], v210, v211 op_sel_hi:[0,0,0]
	s_setprio 0
	s_barrier
	ds_read_b128 v[32:35], v209 offset:49152
	ds_read_b128 v[36:39], v209 offset:50176
	ds_read_b128 v[40:43], v209 offset:51200
	ds_read_b128 v[44:47], v209 offset:52224
	ds_read_b128 v[48:51], v209 offset:53248
	ds_read_b128 v[52:55], v209 offset:54272
	ds_read_b128 v[56:59], v209 offset:55296
	ds_read_b128 v[60:63], v209 offset:56320
	s_mov_b32 m0, s69
	s_nop 0
	global_load_lds_dwordx4 v200, s[38:39]
	s_mov_b32 m0, s70
	s_nop 0
	global_load_lds_dwordx4 v202, s[38:39]
	s_add_u32 s38, s38, s16
	s_addc_u32 s39, s39, s17
	s_mov_b32 m0, s73
	s_nop 0
	global_load_lds_dwordx4 v200, s[38:39]
	s_mov_b32 m0, s74
	s_nop 0
	global_load_lds_dwordx4 v202, s[38:39]
	s_mov_b32 m0, s71
	s_nop 0
	global_load_lds_dwordx4 v64, s[8:9]
	s_mov_b32 m0, s72
	s_nop 0
	global_load_lds_dwordx4 v65, s[8:9]
	s_waitcnt vmcnt(8)
	s_waitcnt lgkmcnt(0)
	s_barrier
	s_setprio 1
	s_waitcnt lgkmcnt(6)
	v_mfma_scale_f32_16x16x128_f8f6f4 v[128:131], v[0:7], v[32:39], v[128:131], v210, v211 op_sel_hi:[0,0,0]
	v_mfma_scale_f32_16x16x128_f8f6f4 v[120:123], v[8:15], v[32:39], v[120:123], v210, v211 op_sel_hi:[0,0,0]
	s_waitcnt lgkmcnt(4)
	v_mfma_scale_f32_16x16x128_f8f6f4 v[112:115], v[0:7], v[40:47], v[112:115], v210, v211 op_sel_hi:[0,0,0]
	v_mfma_scale_f32_16x16x128_f8f6f4 v[104:107], v[8:15], v[40:47], v[104:107], v210, v211 op_sel_hi:[0,0,0]
	s_waitcnt lgkmcnt(2)
	v_mfma_scale_f32_16x16x128_f8f6f4 v[96:99], v[0:7], v[48:55], v[96:99], v210, v211 op_sel_hi:[0,0,0]
	v_mfma_scale_f32_16x16x128_f8f6f4 v[88:91], v[8:15], v[48:55], v[88:91], v210, v211 op_sel_hi:[0,0,0]
	s_waitcnt lgkmcnt(0)
	v_mfma_scale_f32_16x16x128_f8f6f4 v[80:83], v[0:7], v[56:63], v[80:83], v210, v211 op_sel_hi:[0,0,0]
	v_mfma_scale_f32_16x16x128_f8f6f4 v[72:75], v[8:15], v[56:63], v[72:75], v210, v211 op_sel_hi:[0,0,0]
	s_setprio 0
	s_setprio 1
	v_mfma_scale_f32_16x16x128_f8f6f4 v[124:127], v[16:23], v[32:39], v[124:127], v210, v211 op_sel_hi:[0,0,0]
	v_mfma_scale_f32_16x16x128_f8f6f4 v[116:119], v[24:31], v[32:39], v[116:119], v210, v211 op_sel_hi:[0,0,0]
	v_mfma_scale_f32_16x16x128_f8f6f4 v[108:111], v[16:23], v[40:47], v[108:111], v210, v211 op_sel_hi:[0,0,0]
	v_mfma_scale_f32_16x16x128_f8f6f4 v[100:103], v[24:31], v[40:47], v[100:103], v210, v211 op_sel_hi:[0,0,0]
	v_mfma_scale_f32_16x16x128_f8f6f4 v[92:95], v[16:23], v[48:55], v[92:95], v210, v211 op_sel_hi:[0,0,0]
	v_mfma_scale_f32_16x16x128_f8f6f4 v[84:87], v[24:31], v[48:55], v[84:87], v210, v211 op_sel_hi:[0,0,0]
	v_mfma_scale_f32_16x16x128_f8f6f4 v[76:79], v[16:23], v[56:63], v[76:79], v210, v211 op_sel_hi:[0,0,0]
	v_mfma_scale_f32_16x16x128_f8f6f4 v[68:71], v[24:31], v[56:63], v[68:71], v210, v211 op_sel_hi:[0,0,0]
	s_setprio 0
	s_barrier
	s_add_u32 s6, s6, 0x100
	s_addc_u32 s7, s7, 0
	s_cmp_ge_i32 s89, s68
	s_cbranch_scc1 .LBB0_1659
.LBB0_1638:
	ds_read_b128 v[24:27], v207
	ds_read_b128 v[28:31], v207 offset:1024
	ds_read_b128 v[16:19], v207 offset:2048
	ds_read_b128 v[20:23], v207 offset:3072
	ds_read_b128 v[8:11], v208
	ds_read_b128 v[12:15], v208 offset:1024
	ds_read_b128 v[0:3], v208 offset:2048
	ds_read_b128 v[4:7], v208 offset:3072
	s_cmp_eq_u32 s75, s89
	s_cselect_b64 s[38:39], -1, 0
	s_add_u32 s8, s20, s6
	s_addc_u32 s9, s21, s7
	s_add_u32 s8, s8, 0xffffff80
	s_addc_u32 s9, s9, -1
	ds_read_b128 v[56:59], v209
	ds_read_b128 v[60:63], v209 offset:1024
	ds_read_b128 v[48:51], v209 offset:2048
	ds_read_b128 v[52:55], v209 offset:3072
	ds_read_b128 v[40:43], v209 offset:4096
	ds_read_b128 v[44:47], v209 offset:5120
	ds_read_b128 v[32:35], v209 offset:6144
	ds_read_b128 v[36:39], v209 offset:7168
	s_mov_b32 m0, s82
	s_nop 0
	global_load_lds_dwordx4 v66, s[8:9]
	s_and_b64 s[40:41], s[36:37], s[38:39]
	s_mov_b32 m0, s83
	s_nop 0
	global_load_lds_dwordx4 v67, s[8:9]
	s_andn2_b64 vcc, exec, s[40:41]
	s_cbranch_vccnz .LBB0_1637
	ds_read_b128 v[64:67], v201
	s_branch .LBB0_1637

; #define PG8_STAGE(bufoff, gbase, voff) do { _Pragma("unroll") for (int _i = 0; _i < 2; ++_i) { unsigned keep_; \
;         asm volatile("s_mov_b32 %0, m0\n\ts_mov_b32 m0, %3\n\ts_nop 0\n\tglobal_load_lds_dwordx4 %1, %2\n\ts_mov_b32 m0, %0" : "=&s"(keep_) : "v"((voff)[_i]), "s"((const char*)(gbase)), "s"(ldsb + (unsigned)((bufoff) + _i * 8192)) : "memory"); } } while (0)
; #define PG8_BAR __builtin_amdgcn_s_barrier()
; template <class Epi, class Sched, bool ALIGN_EPI, bool FP8 = false>
; __device__ __forceinline__ void gemm_phase(PG8_LAS unsigned char* lds, const Gemm g, const Sched& S, const Epi& E, const int wid, const int lane) {
;     ...
;     for (int i = 0; i < 2; ++i) { int R, C; stage_rc(tid * 16 + i * 8192, R, C); const int Rb = Epi::PERM ? ((R & ~31) + perm32(R & 31)) : R;
;         rA[i] = R; cA2[i] = (unsigned)C * 2u; voffA[i] = (unsigned)(R * KB + C * 2); voffB[i] = (unsigned)(Rb * KB + C * 2); }
;     const size_t kstep = (size_t)(BK * 2);
;     const size_t hstep = (size_t)HALF * KB;
;     const size_t hstepA = GA ? (size_t)0 : hstep;
;     const size_t tstep = 2 * hstep;
;     const unsigned ldsw = (unsigned)wid * 1024u;
;     const int aoff = lds_byte(wr * 64 + fr, fq * 8), boff = lds_byte(wc * 32 + fr, fq * 8);
;     ...
;     const char* cA = GA ? (const char*)g.A : (const char*)g.A + (size_t)cur.pm * tstep; const char* cB = (const char*)g.Bt + (size_t)cur.pn * tstep;
;     PG8_STAGE(PG8_SB(0, 0), cB, voffB); PG8_STAGE(PG8_SB(0, 1), cB + hstep, voffB); PG8_STAGE(PG8_SA(0, 0), cA, vc0); PG8_STAGE(PG8_SA(0, 1), cA + hstepA, vc1);
;     if (wr == 1) PG8_BAR;
.LBB0_1744:
	v_lshlrev_b32_e32 v0, 4, v2
	v_add_u32_e32 v1, s16, v0
	v_ashrrev_i32_e32 v3, 31, v1
	v_lshrrev_b32_e32 v3, 22, v3
	v_add_u32_e32 v3, v1, v3
	v_ashrrev_i32_e32 v3, 10, v3
	s_waitcnt vmcnt(16)
	v_mul_i32_i24_e32 v4, 0x400, v3
	v_sub_u32_e32 v4, v1, v4
	v_lshrrev_b32_e32 v5, 4, v4
	v_bitop3_b32 v4, v5, v4, 32 bitop3:0x6c
	v_ashrrev_i32_e32 v6, 31, v4
	v_lshrrev_b32_e32 v6, 26, v6
	v_add_u32_e32 v6, v4, v6
	v_ashrrev_i32_e32 v7, 6, v6
	v_and_b32_e32 v6, 0xc0, v6
	v_sub_u32_e32 v4, v4, v6
	v_mov_b32_e32 v6, 1
	v_lshlrev_b32_e32 v5, 3, v3
	v_lshlrev_b32_e32 v3, 5, v3
	v_ashrrev_i16_sdwa v4, v6, sext(v4) dst_sel:DWORD dst_unused:UNUSED_PAD src0_sel:DWORD src1_sel:BYTE_0
	v_and_b32_e32 v5, -16, v5
	v_and_b32_e32 v3, 32, v3
	v_bfe_i32 v4, v4, 0, 16
	v_add_u32_e32 v1, 0x2000, v1
	v_add_u32_e32 v5, v7, v5
	v_add_lshl_u32 v4, v3, v4, 1
	v_ashrrev_i32_e32 v3, 31, v1
	s_waitcnt vmcnt(15)
	v_lshlrev_b32_e32 v8, 1, v5
	v_lshrrev_b32_e32 v9, 2, v5
	v_and_b32_e32 v7, 3, v7
	s_movk_i32 s5, 0xffe0
	v_lshrrev_b32_e32 v3, 22, v3
	v_and_b32_e32 v8, 24, v8
	v_and_b32_e32 v9, 4, v9
	v_and_or_b32 v7, v5, s5, v7
	v_add_u32_e32 v3, v1, v3
	v_or3_b32 v7, v7, v9, v8
	v_ashrrev_i32_e32 v3, 10, v3
	v_mad_u64_u32 v[160:161], s[6:7], s4, v5, v[4:5]
	v_mad_u64_u32 v[162:163], s[6:7], s4, v7, v[4:5]
	v_mul_i32_i24_e32 v4, 0x400, v3
	v_sub_u32_e32 v1, v1, v4
	v_lshrrev_b32_e32 v4, 4, v1
	v_bitop3_b32 v1, v4, v1, 32 bitop3:0x6c
	v_ashrrev_i32_e32 v5, 31, v1
	v_lshrrev_b32_e32 v5, 26, v5
	v_lshlrev_b32_e32 v4, 3, v3
	v_add_u32_e32 v5, v1, v5
	v_and_b32_e32 v4, -16, v4
	v_ashrrev_i32_e32 v7, 6, v5
	v_add_u32_e32 v8, v7, v4
	v_and_b32_e32 v4, 0xffc0, v5
	v_sub_u32_e32 v1, v1, v4
	v_lshrrev_b16_e32 v4, 7, v1
	v_and_b32_e32 v4, 1, v4
	v_add_u16_e32 v1, v1, v4
	v_ashrrev_i16_sdwa v1, v6, sext(v1) dst_sel:DWORD dst_unused:UNUSED_PAD src0_sel:DWORD src1_sel:BYTE_0
	v_and_b32_e32 v6, 3, v7
	v_and_or_b32 v6, v8, s5, v6
	s_ashr_i32 s5, s4, 31
	v_lshlrev_b32_e32 v3, 5, v3
	v_lshlrev_b32_e32 v4, 1, v8
	v_lshrrev_b32_e32 v5, 2, v8
	s_lshr_b32 s18, s90, 8
	s_lshl_b64 s[12:13], s[4:5], 7
	s_lshl_b64 s[14:15], s[4:5], 8
	s_add_i32 s40, s16, 0
	v_and_b32_e32 v3, 32, v3
	v_bfe_i32 v1, v1, 0, 16
	v_and_b32_e32 v4, 24, v4
	v_and_b32_e32 v5, 4, v5
	s_add_u32 s41, s56, 0x45c00000
	v_or3_b32 v5, v6, v5, v4
	v_add_lshl_u32 v4, v3, v1, 1
	s_addc_u32 s42, s57, 0
	v_mad_u64_u32 v[164:165], s[6:7], s4, v8, v[4:5]
	v_mad_u64_u32 v[166:167], s[6:7], s4, v5, v[4:5]
	s_add_u32 s43, s56, 0x2da00000
	s_addc_u32 s44, s57, 0
	s_ashr_i32 s6, s74, 31
	s_mul_i32 s6, s14, s6
	s_mul_hi_u32 s7, s14, s74
	s_add_i32 s8, s7, s6
	s_lshr_b64 s[6:7], s[4:5], 24
	s_mul_i32 s7, s6, s74
	s_add_i32 s9, s8, s7
	s_ashr_i32 s7, s73, 31
	s_mul_i32 s7, s14, s7
	s_mul_hi_u32 s16, s14, s73
	s_add_i32 s7, s16, s7
	s_mul_i32 s6, s6, s73
	s_add_i32 s7, s7, s6
	s_mul_i32 s6, s14, s73
	s_add_u32 s6, s43, s6
	s_addc_u32 s7, s44, s7
	s_add_i32 s45, s40, 0x10000
	s_mov_b32 m0, s45
	s_nop 0
	global_load_lds_dwordx4 v162, s[6:7]
	s_add_i32 s46, s40, 0x12000
	s_mov_b32 m0, s46
	s_nop 0
	global_load_lds_dwordx4 v166, s[6:7]
	s_add_u32 s22, s6, s12
	s_mul_i32 s8, s14, s74
	s_addc_u32 s23, s7, s13
	s_add_i32 s47, s40, 0x14000
	s_mov_b32 m0, s47
	s_nop 0
	global_load_lds_dwordx4 v162, s[22:23]
	s_add_i32 s48, s40, 0x16000
	s_mov_b32 m0, s48
	s_nop 0
	global_load_lds_dwordx4 v166, s[22:23]
	s_add_u32 s8, s41, s8
	s_addc_u32 s9, s42, s9
	s_mov_b32 m0, s40
	s_nop 0
	global_load_lds_dwordx4 v160, s[8:9]
	s_add_i32 s49, s40, 0x2000
	s_mov_b32 m0, s49
	s_nop 0
	global_load_lds_dwordx4 v164, s[8:9]
	s_add_u32 s20, s8, s12
	s_addc_u32 s21, s9, s13
	s_add_i32 s50, s40, 0x4000
	s_mov_b32 m0, s50
	s_nop 0
	global_load_lds_dwordx4 v160, s[20:21]
	s_add_i32 s51, s40, 0x6000
	s_mov_b32 m0, s51
	s_nop 0
	global_load_lds_dwordx4 v164, s[20:21]
	s_cmp_eq_u32 s18, 1
	s_mov_b32 s39, 0
	s_cselect_b64 s[16:17], -1, 0
	s_cmp_lg_u32 s18, 1
	s_cbranch_scc1 .LBB0_1746
	s_barrier

; #define PG8_STAGE(bufoff, gbase, voff) do { _Pragma("unroll") for (int _i = 0; _i < 2; ++_i) { unsigned keep_; \
;         asm volatile("s_mov_b32 %0, m0\n\ts_mov_b32 m0, %3\n\ts_nop 0\n\tglobal_load_lds_dwordx4 %1, %2\n\ts_mov_b32 m0, %0" : "=&s"(keep_) : "v"((voff)[_i]), "s"((const char*)(gbase)), "s"(ldsb + (unsigned)((bufoff) + _i * 8192)) : "memory"); } } while (0)
; #define PG8_LDA(dst, b, h) do { _Pragma("unroll") for (int m = 0; m < 4; ++m) _Pragma("unroll") for (int k = 0; k < 2; ++k) dst[m][k] = *(const PG8_LAS bf16x8*)(lds + PG8_SA(b, h) + aoff + m * 2048 + k * 1024); } while (0)
; #define PG8_LDB(dst, b, h) do { _Pragma("unroll") for (int n = 0; n < 2; ++n) _Pragma("unroll") for (int k = 0; k < 2; ++k) dst[n][k] = *(const PG8_LAS bf16x8*)(lds + PG8_SB(b, h) + boff + n * 2048 + k * 1024); } while (0)
; #define PG8_WAIT_V(n) asm volatile("s_waitcnt vmcnt(" #n ")" ::: "memory")
; #define PG8_WAIT_L(n) asm volatile("s_waitcnt lgkmcnt(" #n ")" ::: "memory")
; #define PG8_BAR __builtin_amdgcn_s_barrier()
; #define PG8_SCHED __builtin_amdgcn_sched_barrier(0)
; template <class Epi, class Sched, bool ALIGN_EPI, bool FP8 = false>
; __device__ __forceinline__ void gemm_phase(PG8_LAS unsigned char* lds, const Gemm g, const Sched& S, const Epi& E, const int wid, const int lane) {
;     ...
;         for (int t = 0; t < nt; t += 2) {
;             const bool last = (t == nt - 2);
;             const char* a1 = cA + (size_t)(t + 1) * kstep;
;             const char* a2 = last ? nA : cA + (size_t)(t + 2) * kstep; const char* b2 = last ? nB : cB + (size_t)(t + 2) * kstep;
;             const char* a3 = a2 + kstep; const char* b3 = b2 + kstep;
;             PG8_LDB(B0, 0, 0); PG8_LDB(B1, 0, 1); PG8_SCHED; PG8_LDA(At, 0, 0); PG8_STAGE(PG8_SA(1, 1), a1 + hstepA, vc1);
;             if (GA && last && has_next) { const u32x4 q = *gslot; vc0[0] = q.x; vc0[1] = q.y; vc1[0] = q.z; vc1[1] = q.w; }
;             PG8_WAIT_V(8); PG8_WAIT_L(0); PG8_BAR; PG8_MMA(0, 0, At, B0); PG8_MMA(0, 1, At, B1); PG8_BAR; PG8_SCHED;
;             PG8_LDA(At, 0, 1); PG8_STAGE(PG8_SB(0, 0), b2, voffB); PG8_STAGE(PG8_SB(0, 1), b2 + hstep, voffB); PG8_STAGE(PG8_SA(0, 0), a2, vc0);
;             PG8_WAIT_V(8); PG8_WAIT_L(0); PG8_BAR; PG8_MMA(1, 0, At, B0); PG8_MMA(1, 1, At, B1); PG8_BAR; PG8_SCHED;
.LBB0_1762:
	ds_read_b128 v[24:27], v165
	ds_read_b128 v[28:31], v165 offset:1024
	ds_read_b128 v[16:19], v165 offset:2048
	ds_read_b128 v[20:23], v165 offset:3072
	ds_read_b128 v[8:11], v167
	ds_read_b128 v[12:15], v167 offset:1024
	ds_read_b128 v[0:3], v167 offset:2048
	ds_read_b128 v[4:7], v167 offset:3072
	s_add_i32 s33, s8, 2
	s_cmp_eq_u32 s67, s8
	s_cselect_b32 s36, s28, s75
	s_cselect_b32 s37, s29, s80
	s_cselect_b32 s34, s30, s81
	s_cselect_b32 s35, s31, s82
	s_add_u32 s8, s36, 0x80
	s_addc_u32 s9, s37, 0
	ds_read_b128 v[174:177], v169
	ds_read_b128 v[178:181], v169 offset:1024
	ds_read_b128 v[182:185], v169 offset:2048
	ds_read_b128 v[186:189], v169 offset:3072
	ds_read_b128 v[190:193], v169 offset:4096
	ds_read_b128 v[194:197], v169 offset:5120
	ds_read_b128 v[198:201], v169 offset:6144
	ds_read_b128 v[202:205], v169 offset:7168
	s_mov_b32 m0, s68
	s_nop 0
	global_load_lds_dwordx4 v160, s[6:7]
	s_mov_b32 m0, s69
	s_nop 0
	global_load_lds_dwordx4 v164, s[6:7]
	s_waitcnt vmcnt(8)
	s_waitcnt lgkmcnt(0)
	s_barrier
	s_setprio 1
	s_waitcnt lgkmcnt(6)
	v_mfma_scale_f32_16x16x128_f8f6f4 v[156:159], v[24:31], v[174:181], v[156:159], v170, v171 op_sel_hi:[0,0,0]
	v_mfma_scale_f32_16x16x128_f8f6f4 v[152:155], v[16:23], v[174:181], v[152:155], v170, v171 op_sel_hi:[0,0,0]
	s_waitcnt lgkmcnt(4)
	v_mfma_scale_f32_16x16x128_f8f6f4 v[140:143], v[24:31], v[182:189], v[140:143], v170, v171 op_sel_hi:[0,0,0]
	v_mfma_scale_f32_16x16x128_f8f6f4 v[136:139], v[16:23], v[182:189], v[136:139], v170, v171 op_sel_hi:[0,0,0]
	s_waitcnt lgkmcnt(2)
	v_mfma_scale_f32_16x16x128_f8f6f4 v[124:127], v[24:31], v[190:197], v[124:127], v170, v171 op_sel_hi:[0,0,0]
	v_mfma_scale_f32_16x16x128_f8f6f4 v[120:123], v[16:23], v[190:197], v[120:123], v170, v171 op_sel_hi:[0,0,0]
	s_waitcnt lgkmcnt(0)
	v_mfma_scale_f32_16x16x128_f8f6f4 v[108:111], v[24:31], v[198:205], v[108:111], v170, v171 op_sel_hi:[0,0,0]
	v_mfma_scale_f32_16x16x128_f8f6f4 v[104:107], v[16:23], v[198:205], v[104:107], v170, v171 op_sel_hi:[0,0,0]
	s_setprio 0
	s_setprio 1
	v_mfma_scale_f32_16x16x128_f8f6f4 v[148:151], v[8:15], v[174:181], v[148:151], v170, v171 op_sel_hi:[0,0,0]
	v_mfma_scale_f32_16x16x128_f8f6f4 v[144:147], v[0:7], v[174:181], v[144:147], v170, v171 op_sel_hi:[0,0,0]
	v_mfma_scale_f32_16x16x128_f8f6f4 v[132:135], v[8:15], v[182:189], v[132:135], v170, v171 op_sel_hi:[0,0,0]
	v_mfma_scale_f32_16x16x128_f8f6f4 v[128:131], v[0:7], v[182:189], v[128:131], v170, v171 op_sel_hi:[0,0,0]
	v_mfma_scale_f32_16x16x128_f8f6f4 v[116:119], v[8:15], v[190:197], v[116:119], v170, v171 op_sel_hi:[0,0,0]
	v_mfma_scale_f32_16x16x128_f8f6f4 v[112:115], v[0:7], v[190:197], v[112:115], v170, v171 op_sel_hi:[0,0,0]
	v_mfma_scale_f32_16x16x128_f8f6f4 v[100:103], v[8:15], v[198:205], v[100:103], v170, v171 op_sel_hi:[0,0,0]
	v_mfma_scale_f32_16x16x128_f8f6f4 v[96:99], v[0:7], v[198:205], v[96:99], v170, v171 op_sel_hi:[0,0,0]
	s_setprio 0
	s_barrier
	ds_read_b128 v[174:177], v169 offset:16384
	ds_read_b128 v[178:181], v169 offset:17408
	ds_read_b128 v[182:185], v169 offset:18432
	ds_read_b128 v[186:189], v169 offset:19456
	ds_read_b128 v[190:193], v169 offset:20480
	ds_read_b128 v[194:197], v169 offset:21504
	ds_read_b128 v[198:201], v169 offset:22528
	ds_read_b128 v[202:205], v169 offset:23552
	s_mov_b32 m0, s45
	s_nop 0
	global_load_lds_dwordx4 v162, s[34:35]
	s_mov_b32 m0, s46
	s_nop 0
	global_load_lds_dwordx4 v166, s[34:35]
	s_add_u32 s58, s34, s12
	s_addc_u32 s59, s35, s13
	s_mov_b32 m0, s47
	s_nop 0
	global_load_lds_dwordx4 v162, s[58:59]
	s_mov_b32 m0, s48
	s_nop 0
	global_load_lds_dwordx4 v166, s[58:59]
	s_mov_b32 m0, s40
	s_nop 0
	global_load_lds_dwordx4 v160, s[36:37]
	s_mov_b32 m0, s49
	s_nop 0
	global_load_lds_dwordx4 v164, s[36:37]
	s_waitcnt vmcnt(8)
	s_waitcnt lgkmcnt(0)
	s_barrier
	s_setprio 1
	s_waitcnt lgkmcnt(6)
	v_mfma_scale_f32_16x16x128_f8f6f4 v[92:95], v[24:31], v[174:181], v[92:95], v170, v171 op_sel_hi:[0,0,0]
	v_mfma_scale_f32_16x16x128_f8f6f4 v[88:91], v[16:23], v[174:181], v[88:91], v170, v171 op_sel_hi:[0,0,0]
	s_waitcnt lgkmcnt(4)
	v_mfma_scale_f32_16x16x128_f8f6f4 v[76:79], v[24:31], v[182:189], v[76:79], v170, v171 op_sel_hi:[0,0,0]
	v_mfma_scale_f32_16x16x128_f8f6f4 v[72:75], v[16:23], v[182:189], v[72:75], v170, v171 op_sel_hi:[0,0,0]
	s_waitcnt lgkmcnt(2)
	v_mfma_scale_f32_16x16x128_f8f6f4 v[60:63], v[24:31], v[190:197], v[60:63], v170, v171 op_sel_hi:[0,0,0]
	v_mfma_scale_f32_16x16x128_f8f6f4 v[56:59], v[16:23], v[190:197], v[56:59], v170, v171 op_sel_hi:[0,0,0]
	s_waitcnt lgkmcnt(0)
	v_mfma_scale_f32_16x16x128_f8f6f4 v[44:47], v[24:31], v[198:205], v[44:47], v170, v171 op_sel_hi:[0,0,0]
	v_mfma_scale_f32_16x16x128_f8f6f4 v[40:43], v[16:23], v[198:205], v[40:43], v170, v171 op_sel_hi:[0,0,0]
	s_setprio 0
	s_setprio 1
	v_mfma_scale_f32_16x16x128_f8f6f4 v[84:87], v[8:15], v[174:181], v[84:87], v170, v171 op_sel_hi:[0,0,0]
	v_mfma_scale_f32_16x16x128_f8f6f4 v[80:83], v[0:7], v[174:181], v[80:83], v170, v171 op_sel_hi:[0,0,0]
	v_mfma_scale_f32_16x16x128_f8f6f4 v[68:71], v[8:15], v[182:189], v[68:71], v170, v171 op_sel_hi:[0,0,0]
	v_mfma_scale_f32_16x16x128_f8f6f4 v[64:67], v[0:7], v[182:189], v[64:67], v170, v171 op_sel_hi:[0,0,0]
	v_mfma_scale_f32_16x16x128_f8f6f4 v[52:55], v[8:15], v[190:197], v[52:55], v170, v171 op_sel_hi:[0,0,0]
	v_mfma_scale_f32_16x16x128_f8f6f4 v[48:51], v[0:7], v[190:197], v[48:51], v170, v171 op_sel_hi:[0,0,0]
	v_mfma_scale_f32_16x16x128_f8f6f4 v[36:39], v[8:15], v[198:205], v[36:39], v170, v171 op_sel_hi:[0,0,0]
	v_mfma_scale_f32_16x16x128_f8f6f4 v[32:35], v[0:7], v[198:205], v[32:35], v170, v171 op_sel_hi:[0,0,0]
	s_setprio 0
	s_barrier
; #define PG8_STAGE(bufoff, gbase, voff) do { _Pragma("unroll") for (int _i = 0; _i < 2; ++_i) { unsigned keep_; \
;         asm volatile("s_mov_b32 %0, m0\n\ts_mov_b32 m0, %3\n\ts_nop 0\n\tglobal_load_lds_dwordx4 %1, %2\n\ts_mov_b32 m0, %0" : "=&s"(keep_) : "v"((voff)[_i]), "s"((const char*)(gbase)), "s"(ldsb + (unsigned)((bufoff) + _i * 8192)) : "memory"); } } while (0)
; #define PG8_LDA(dst, b, h) do { _Pragma("unroll") for (int m = 0; m < 4; ++m) _Pragma("unroll") for (int k = 0; k < 2; ++k) dst[m][k] = *(const PG8_LAS bf16x8*)(lds + PG8_SA(b, h) + aoff + m * 2048 + k * 1024); } while (0)
; #define PG8_LDB(dst, b, h) do { _Pragma("unroll") for (int n = 0; n < 2; ++n) _Pragma("unroll") for (int k = 0; k < 2; ++k) dst[n][k] = *(const PG8_LAS bf16x8*)(lds + PG8_SB(b, h) + boff + n * 2048 + k * 1024); } while (0)
; #define PG8_WAIT_V(n) asm volatile("s_waitcnt vmcnt(" #n ")" ::: "memory")
; #define PG8_WAIT_L(n) asm volatile("s_waitcnt lgkmcnt(" #n ")" ::: "memory")
; #define PG8_BAR __builtin_amdgcn_s_barrier()
; #define PG8_SCHED __builtin_amdgcn_sched_barrier(0)
; template <class Epi, class Sched, bool ALIGN_EPI, bool FP8 = false>
; __device__ __forceinline__ void gemm_phase(PG8_LAS unsigned char* lds, const Gemm g, const Sched& S, const Epi& E, const int wid, const int lane) {
;     ...
;             PG8_LDB(B0, 1, 0); PG8_LDB(B1, 1, 1); PG8_SCHED; PG8_LDA(At, 1, 0); PG8_STAGE(PG8_SA(0, 1), a2 + hstepA, vc1);
;             PG8_WAIT_V(8); PG8_WAIT_L(0); PG8_BAR; PG8_MMA(0, 0, At, B0); PG8_MMA(0, 1, At, B1); PG8_BAR; PG8_SCHED;
;             PG8_LDA(At, 1, 1); PG8_STAGE(PG8_SB(1, 0), b3, voffB); PG8_STAGE(PG8_SB(1, 1), b3 + hstep, voffB); PG8_STAGE(PG8_SA(1, 0), a3, vc0);
;             PG8_WAIT_V(8); PG8_WAIT_L(0); PG8_BAR; PG8_MMA(1, 0, At, B0); PG8_MMA(1, 1, At, B1); PG8_BAR; PG8_SCHED;
	ds_read_b128 v[0:3], v172
	ds_read_b128 v[4:7], v172 offset:1024
	ds_read_b128 v[8:11], v172 offset:2048
	ds_read_b128 v[12:15], v172 offset:3072
	ds_read_b128 v[16:19], v173
	ds_read_b128 v[20:23], v173 offset:1024
	ds_read_b128 v[24:27], v173 offset:2048
	ds_read_b128 v[28:31], v173 offset:3072
	ds_read_b128 v[174:177], v169 offset:32768
	ds_read_b128 v[178:181], v169 offset:33792
	ds_read_b128 v[182:185], v169 offset:34816
	ds_read_b128 v[186:189], v169 offset:35840
	ds_read_b128 v[190:193], v169 offset:36864
	ds_read_b128 v[194:197], v169 offset:37888
	ds_read_b128 v[198:201], v169 offset:38912
	ds_read_b128 v[202:205], v169 offset:39936
	s_add_u32 s36, s36, s12
	s_addc_u32 s37, s37, s13
	s_mov_b32 m0, s50
	s_nop 0
	global_load_lds_dwordx4 v160, s[36:37]
	s_mov_b32 m0, s51
	s_nop 0
	global_load_lds_dwordx4 v164, s[36:37]
	s_waitcnt vmcnt(8)
	s_waitcnt lgkmcnt(0)
	s_barrier
	s_setprio 1
	s_waitcnt lgkmcnt(6)
	v_mfma_scale_f32_16x16x128_f8f6f4 v[156:159], v[0:7], v[174:181], v[156:159], v170, v171 op_sel_hi:[0,0,0]
	v_mfma_scale_f32_16x16x128_f8f6f4 v[152:155], v[8:15], v[174:181], v[152:155], v170, v171 op_sel_hi:[0,0,0]
	s_waitcnt lgkmcnt(4)
	v_mfma_scale_f32_16x16x128_f8f6f4 v[140:143], v[0:7], v[182:189], v[140:143], v170, v171 op_sel_hi:[0,0,0]
	v_mfma_scale_f32_16x16x128_f8f6f4 v[136:139], v[8:15], v[182:189], v[136:139], v170, v171 op_sel_hi:[0,0,0]
	s_waitcnt lgkmcnt(2)
	v_mfma_scale_f32_16x16x128_f8f6f4 v[124:127], v[0:7], v[190:197], v[124:127], v170, v171 op_sel_hi:[0,0,0]
	v_mfma_scale_f32_16x16x128_f8f6f4 v[120:123], v[8:15], v[190:197], v[120:123], v170, v171 op_sel_hi:[0,0,0]
	s_waitcnt lgkmcnt(0)
	v_mfma_scale_f32_16x16x128_f8f6f4 v[108:111], v[0:7], v[198:205], v[108:111], v170, v171 op_sel_hi:[0,0,0]
	v_mfma_scale_f32_16x16x128_f8f6f4 v[104:107], v[8:15], v[198:205], v[104:107], v170, v171 op_sel_hi:[0,0,0]
	s_setprio 0
	s_setprio 1
	v_mfma_scale_f32_16x16x128_f8f6f4 v[148:151], v[16:23], v[174:181], v[148:151], v170, v171 op_sel_hi:[0,0,0]
	v_mfma_scale_f32_16x16x128_f8f6f4 v[144:147], v[24:31], v[174:181], v[144:147], v170, v171 op_sel_hi:[0,0,0]
	v_mfma_scale_f32_16x16x128_f8f6f4 v[132:135], v[16:23], v[182:189], v[132:135], v170, v171 op_sel_hi:[0,0,0]
	v_mfma_scale_f32_16x16x128_f8f6f4 v[128:131], v[24:31], v[182:189], v[128:131], v170, v171 op_sel_hi:[0,0,0]
	v_mfma_scale_f32_16x16x128_f8f6f4 v[116:119], v[16:23], v[190:197], v[116:119], v170, v171 op_sel_hi:[0,0,0]
	v_mfma_scale_f32_16x16x128_f8f6f4 v[112:115], v[24:31], v[190:197], v[112:115], v170, v171 op_sel_hi:[0,0,0]
	v_mfma_scale_f32_16x16x128_f8f6f4 v[100:103], v[16:23], v[198:205], v[100:103], v170, v171 op_sel_hi:[0,0,0]
	v_mfma_scale_f32_16x16x128_f8f6f4 v[96:99], v[24:31], v[198:205], v[96:99], v170, v171 op_sel_hi:[0,0,0]
	s_setprio 0
	s_barrier
	ds_read_b128 v[174:177], v169 offset:49152
	ds_read_b128 v[178:181], v169 offset:50176
	ds_read_b128 v[182:185], v169 offset:51200
	ds_read_b128 v[186:189], v169 offset:52224
	ds_read_b128 v[190:193], v169 offset:53248
	ds_read_b128 v[194:197], v169 offset:54272
	ds_read_b128 v[198:201], v169 offset:55296
	ds_read_b128 v[202:205], v169 offset:56320
	s_add_u32 s34, s34, 0x80
	s_addc_u32 s35, s35, 0
	s_mov_b32 m0, s53
	s_nop 0
	global_load_lds_dwordx4 v162, s[34:35]
	s_mov_b32 m0, s54
	s_nop 0
	global_load_lds_dwordx4 v166, s[34:35]
	s_add_u32 s34, s34, s12
	s_addc_u32 s35, s35, s13
	s_mov_b32 m0, s65
	s_nop 0
	global_load_lds_dwordx4 v162, s[34:35]
	s_mov_b32 m0, s66
	s_nop 0
	global_load_lds_dwordx4 v166, s[34:35]
	s_mov_b32 m0, s55
	s_nop 0
	global_load_lds_dwordx4 v160, s[8:9]
	s_mov_b32 m0, s64
	s_nop 0
	global_load_lds_dwordx4 v164, s[8:9]
	s_waitcnt vmcnt(8)
	s_waitcnt lgkmcnt(0)
	s_barrier
	s_setprio 1
	s_waitcnt lgkmcnt(6)
	v_mfma_scale_f32_16x16x128_f8f6f4 v[92:95], v[0:7], v[174:181], v[92:95], v170, v171 op_sel_hi:[0,0,0]
	v_mfma_scale_f32_16x16x128_f8f6f4 v[88:91], v[8:15], v[174:181], v[88:91], v170, v171 op_sel_hi:[0,0,0]
	s_waitcnt lgkmcnt(4)
	v_mfma_scale_f32_16x16x128_f8f6f4 v[76:79], v[0:7], v[182:189], v[76:79], v170, v171 op_sel_hi:[0,0,0]
	v_mfma_scale_f32_16x16x128_f8f6f4 v[72:75], v[8:15], v[182:189], v[72:75], v170, v171 op_sel_hi:[0,0,0]
	s_waitcnt lgkmcnt(2)
	v_mfma_scale_f32_16x16x128_f8f6f4 v[60:63], v[0:7], v[190:197], v[60:63], v170, v171 op_sel_hi:[0,0,0]
	v_mfma_scale_f32_16x16x128_f8f6f4 v[56:59], v[8:15], v[190:197], v[56:59], v170, v171 op_sel_hi:[0,0,0]
	s_waitcnt lgkmcnt(0)
	v_mfma_scale_f32_16x16x128_f8f6f4 v[44:47], v[0:7], v[198:205], v[44:47], v170, v171 op_sel_hi:[0,0,0]
	v_mfma_scale_f32_16x16x128_f8f6f4 v[40:43], v[8:15], v[198:205], v[40:43], v170, v171 op_sel_hi:[0,0,0]
	s_setprio 0
	s_setprio 1
	v_mfma_scale_f32_16x16x128_f8f6f4 v[84:87], v[16:23], v[174:181], v[84:87], v170, v171 op_sel_hi:[0,0,0]
	v_mfma_scale_f32_16x16x128_f8f6f4 v[80:83], v[24:31], v[174:181], v[80:83], v170, v171 op_sel_hi:[0,0,0]
	v_mfma_scale_f32_16x16x128_f8f6f4 v[68:71], v[16:23], v[182:189], v[68:71], v170, v171 op_sel_hi:[0,0,0]
	v_mfma_scale_f32_16x16x128_f8f6f4 v[64:67], v[24:31], v[182:189], v[64:67], v170, v171 op_sel_hi:[0,0,0]
	v_mfma_scale_f32_16x16x128_f8f6f4 v[52:55], v[16:23], v[190:197], v[52:55], v170, v171 op_sel_hi:[0,0,0]
	v_mfma_scale_f32_16x16x128_f8f6f4 v[48:51], v[24:31], v[190:197], v[48:51], v170, v171 op_sel_hi:[0,0,0]
	v_mfma_scale_f32_16x16x128_f8f6f4 v[36:39], v[16:23], v[198:205], v[36:39], v170, v171 op_sel_hi:[0,0,0]
	v_mfma_scale_f32_16x16x128_f8f6f4 v[32:35], v[24:31], v[198:205], v[32:35], v170, v171 op_sel_hi:[0,0,0]
	s_setprio 0
	s_barrier
	s_add_u32 s75, s75, 0x100
	s_addc_u32 s80, s80, 0
	s_add_u32 s81, s81, 0x100
	s_addc_u32 s82, s82, 0
	s_add_u32 s6, s6, 0x100
	s_addc_u32 s7, s7, 0
	s_cmp_ge_i32 s33, s52
	s_mov_b32 s8, s33
	s_cbranch_scc0 .LBB0_1762

; __global__ void __launch_bounds__(NWAVES * 64, 2) fwd_kernel(Args args) {
	.amdhsa_kernel _Z10fwd_kernel4Args
		.amdhsa_group_segment_fixed_size 0
		.amdhsa_private_segment_fixed_size 0
		.amdhsa_kernarg_size 448
		.amdhsa_user_sgpr_count 2
		.amdhsa_user_sgpr_dispatch_ptr 0
		.amdhsa_user_sgpr_queue_ptr 0
		.amdhsa_user_sgpr_kernarg_segment_ptr 1
		.amdhsa_user_sgpr_dispatch_id 0
		.amdhsa_user_sgpr_kernarg_preload_length 0
		.amdhsa_user_sgpr_kernarg_preload_offset 0
		.amdhsa_user_sgpr_private_segment_size 0
		.amdhsa_uses_dynamic_stack 0
		.amdhsa_enable_private_segment 0
		.amdhsa_system_sgpr_workgroup_id_x 1
		.amdhsa_system_sgpr_workgroup_id_y 0
		.amdhsa_system_sgpr_workgroup_id_z 0
		.amdhsa_system_sgpr_workgroup_info 0
		.amdhsa_system_vgpr_workitem_id 0
		.amdhsa_next_free_vgpr 249
		.amdhsa_next_free_sgpr 102
		.amdhsa_accum_offset 252
		.amdhsa_reserve_vcc 1
		.amdhsa_float_round_mode_32 0
		.amdhsa_float_round_mode_16_64 0
		.amdhsa_float_denorm_mode_32 3
		.amdhsa_float_denorm_mode_16_64 3
		.amdhsa_dx10_clamp 1
		.amdhsa_ieee_mode 1
		.amdhsa_fp16_overflow 0
		.amdhsa_tg_split 0
		.amdhsa_exception_fp_ieee_invalid_op 0
		.amdhsa_exception_fp_denorm_src 0
		.amdhsa_exception_fp_ieee_div_zero 0
		.amdhsa_exception_fp_ieee_overflow 0
		.amdhsa_exception_fp_ieee_underflow 0
		.amdhsa_exception_fp_ieee_inexact 0
		.amdhsa_exception_int_div_zero 0
	.end_amdhsa_kernel

; __global__ void __launch_bounds__(NWAVES * 64, 2) fwd_kernel(Args args) {
amdhsa.kernels:
  - .agpr_count:     0
    .args:
      - .offset:         0
        .size:           192
        .value_kind:     by_value
      - .offset:         192
        .size:           4
        .value_kind:     hidden_block_count_x
      - .offset:         196
        .size:           4
        .value_kind:     hidden_block_count_y
      - .offset:         200
        .size:           4
        .value_kind:     hidden_block_count_z
      - .offset:         204
        .size:           2
        .value_kind:     hidden_group_size_x
      - .offset:         206
        .size:           2
        .value_kind:     hidden_group_size_y
      - .offset:         208
        .size:           2
        .value_kind:     hidden_group_size_z
      - .offset:         210
        .size:           2
        .value_kind:     hidden_remainder_x
      - .offset:         212
        .size:           2
        .value_kind:     hidden_remainder_y
      - .offset:         214
        .size:           2
        .value_kind:     hidden_remainder_z
      - .offset:         232
        .size:           8
        .value_kind:     hidden_global_offset_x
      - .offset:         240
        .size:           8
        .value_kind:     hidden_global_offset_y
      - .offset:         248
        .size:           8
        .value_kind:     hidden_global_offset_z
      - .offset:         256
        .size:           2
        .value_kind:     hidden_grid_dims
      - .offset:         312
        .size:           4
        .value_kind:     hidden_dynamic_lds_size
    .group_segment_fixed_size: 0
    .kernarg_segment_align: 8
    .kernarg_segment_size: 448
    .language:       OpenCL C
    .language_version:
      - 2
      - 0
    .max_flat_workgroup_size: 512
    .name:           _Z10fwd_kernel4Args
    .private_segment_fixed_size: 0
    .sgpr_count:     108
    .sgpr_spill_count: 56
    .symbol:         _Z10fwd_kernel4Args.kd
    .uniform_work_group_size: 1
    .uses_dynamic_stack: false
    .vgpr_count:     249
    .vgpr_spill_count: 0
    .wavefront_size: 64
